# GEMM K-loops: 392 lgkmcnt waits inside MFMA segments removed (counter is provably 0 after the lgkmcnt(0)+barrier that opens each segment)
# baseline (speedup 1.0000x reference)
.LBB0_224:
	ds_read_b128 v[2:5], v169
	ds_read_b128 v[6:9], v169 offset:1024
	ds_read_b128 v[10:13], v169 offset:2048
	ds_read_b128 v[14:17], v169 offset:3072
	ds_read_b128 v[18:21], v170
	ds_read_b128 v[22:25], v170 offset:1024
	ds_read_b128 v[26:29], v170 offset:2048
	ds_read_b128 v[30:33], v170 offset:3072
	s_lshl_b32 s43, s85, 19
	s_lshl_b32 s52, s22, 19
	s_or_b32 s15, s29, 0x80
	s_or_b32 s62, s28, 0x100
	s_and_b64 s[6:7], s[38:39], exec
	s_cselect_b32 vcc_lo, s43, s29
	s_or_b32 s14, s29, 0x100
	s_and_b64 s[6:7], s[38:39], exec
	s_cselect_b32 vcc_hi, s52, s28
	s_mov_b32 m0, s79
	ds_read_b128 v[34:37], v171
	ds_read_b128 v[38:41], v171 offset:1024
	ds_read_b128 v[42:45], v171 offset:2048
	ds_read_b128 v[46:49], v171 offset:3072
	ds_read_b128 v[50:53], v171 offset:4096
	ds_read_b128 v[54:57], v171 offset:5120
	ds_read_b128 v[58:61], v171 offset:6144
	ds_read_b128 v[62:65], v171 offset:7168
	buffer_load_dwordx4 v163, s[64:67], s15 offen lds
	s_mov_b32 m0, s81
	s_or_b32 s6, s29, 0x40080
	buffer_load_dwordx4 v165, s[64:67], s15 offen lds
	s_mov_b32 m0, s80
	s_nop 0
	buffer_load_dwordx4 v163, s[64:67], s6 offen lds
	s_mov_b32 m0, s82
	s_nop 0
	buffer_load_dwordx4 v165, s[64:67], s6 offen lds
	s_waitcnt vmcnt(8)
	s_waitcnt lgkmcnt(0)
	s_barrier
	s_setprio 1
	v_mfma_scale_f32_16x16x128_f8f6f4 v[150:153], v[2:9], v[34:41], 0, v234, v234 op_sel_hi:[0,0,0]
	v_mfma_scale_f32_16x16x128_f8f6f4 v[146:149], v[10:17], v[34:41], 0, v234, v234 op_sel_hi:[0,0,0]
	s_waitcnt vmcnt(17)
	v_mfma_scale_f32_16x16x128_f8f6f4 v[134:137], v[2:9], v[42:49], 0, v234, v234 op_sel_hi:[0,0,0]
	v_mfma_scale_f32_16x16x128_f8f6f4 v[130:133], v[10:17], v[42:49], 0, v234, v234 op_sel_hi:[0,0,0]
	v_mfma_scale_f32_16x16x128_f8f6f4 v[118:121], v[2:9], v[50:57], 0, v234, v234 op_sel_hi:[0,0,0]
	v_mfma_scale_f32_16x16x128_f8f6f4 v[114:117], v[10:17], v[50:57], 0, v234, v234 op_sel_hi:[0,0,0]
	v_mfma_scale_f32_16x16x128_f8f6f4 v[98:101], v[2:9], v[58:65], 0, v234, v234 op_sel_hi:[0,0,0]
	v_mfma_scale_f32_16x16x128_f8f6f4 v[90:93], v[10:17], v[58:65], 0, v234, v234 op_sel_hi:[0,0,0]
	v_mfma_scale_f32_16x16x128_f8f6f4 v[158:161], v[18:25], v[34:41], 0, v234, v234 op_sel_hi:[0,0,0]
	v_mfma_scale_f32_16x16x128_f8f6f4 v[154:157], v[26:33], v[34:41], 0, v234, v234 op_sel_hi:[0,0,0]
	v_mfma_scale_f32_16x16x128_f8f6f4 v[142:145], v[18:25], v[42:49], 0, v234, v234 op_sel_hi:[0,0,0]
	s_waitcnt vmcnt(16)
	v_mfma_scale_f32_16x16x128_f8f6f4 v[138:141], v[26:33], v[42:49], 0, v234, v234 op_sel_hi:[0,0,0]
	v_mfma_scale_f32_16x16x128_f8f6f4 v[126:129], v[18:25], v[50:57], 0, v234, v234 op_sel_hi:[0,0,0]
	v_mfma_scale_f32_16x16x128_f8f6f4 v[122:125], v[26:33], v[50:57], 0, v234, v234 op_sel_hi:[0,0,0]
	v_mfma_scale_f32_16x16x128_f8f6f4 v[110:113], v[18:25], v[58:65], 0, v234, v234 op_sel_hi:[0,0,0]
	v_mfma_scale_f32_16x16x128_f8f6f4 v[106:109], v[26:33], v[58:65], 0, v234, v234 op_sel_hi:[0,0,0]
	s_setprio 0
	s_barrier
	s_mov_b32 m0, s9
	s_mov_b32 s6, s66
	s_mov_b32 s7, s67
	ds_read_b128 v[74:77], v171 offset:16384
	ds_read_b128 v[78:81], v171 offset:17408
	ds_read_b128 v[174:177], v171 offset:18432
	ds_read_b128 v[178:181], v171 offset:19456
	ds_read_b128 v[182:185], v171 offset:20480
	ds_read_b128 v[186:189], v171 offset:21504
	ds_read_b128 v[190:193], v171 offset:22528
	ds_read_b128 v[194:197], v171 offset:23552
	buffer_load_dwordx4 v164, s[4:7], s62 offen lds
	s_mov_b32 m0, s10
	s_or_b32 s15, s28, 0x40100
	buffer_load_dwordx4 v166, s[4:7], s62 offen lds
	s_mov_b32 m0, s11
	s_nop 0
	buffer_load_dwordx4 v164, s[4:7], s15 offen lds
	s_mov_b32 m0, s12
	s_nop 0
	buffer_load_dwordx4 v166, s[4:7], s15 offen lds
	s_waitcnt vmcnt(6)
	s_waitcnt lgkmcnt(0)
	s_barrier
	s_setprio 1
	v_mfma_scale_f32_16x16x128_f8f6f4 v[86:89], v[2:9], v[74:81], 0, v234, v234 op_sel_hi:[0,0,0]
	v_mfma_scale_f32_16x16x128_f8f6f4 v[82:85], v[10:17], v[74:81], 0, v234, v234 op_sel_hi:[0,0,0]
	v_mfma_scale_f32_16x16x128_f8f6f4 v[70:73], v[2:9], v[174:181], 0, v234, v234 op_sel_hi:[0,0,0]
	v_mfma_scale_f32_16x16x128_f8f6f4 v[66:69], v[10:17], v[174:181], 0, v234, v234 op_sel_hi:[0,0,0]
	v_mfma_scale_f32_16x16x128_f8f6f4 v[58:61], v[2:9], v[182:189], 0, v234, v234 op_sel_hi:[0,0,0]
	v_mfma_scale_f32_16x16x128_f8f6f4 v[50:53], v[10:17], v[182:189], 0, v234, v234 op_sel_hi:[0,0,0]
	v_mfma_scale_f32_16x16x128_f8f6f4 v[42:45], v[2:9], v[190:197], 0, v234, v234 op_sel_hi:[0,0,0]
	v_mfma_scale_f32_16x16x128_f8f6f4 v[34:37], v[10:17], v[190:197], 0, v234, v234 op_sel_hi:[0,0,0]
	v_mfma_scale_f32_16x16x128_f8f6f4 v[102:105], v[18:25], v[74:81], 0, v234, v234 op_sel_hi:[0,0,0]
	v_mfma_scale_f32_16x16x128_f8f6f4 v[94:97], v[26:33], v[74:81], 0, v234, v234 op_sel_hi:[0,0,0]
	v_mfma_scale_f32_16x16x128_f8f6f4 v[78:81], v[18:25], v[174:181], 0, v234, v234 op_sel_hi:[0,0,0]
	v_mfma_scale_f32_16x16x128_f8f6f4 v[74:77], v[26:33], v[174:181], 0, v234, v234 op_sel_hi:[0,0,0]
	v_mfma_scale_f32_16x16x128_f8f6f4 v[62:65], v[18:25], v[182:189], 0, v234, v234 op_sel_hi:[0,0,0]
	v_mfma_scale_f32_16x16x128_f8f6f4 v[54:57], v[26:33], v[182:189], 0, v234, v234 op_sel_hi:[0,0,0]
	v_mfma_scale_f32_16x16x128_f8f6f4 v[46:49], v[18:25], v[190:197], 0, v234, v234 op_sel_hi:[0,0,0]
	v_mfma_scale_f32_16x16x128_f8f6f4 v[38:41], v[26:33], v[190:197], 0, v234, v234 op_sel_hi:[0,0,0]
	s_setprio 0
	s_barrier
	ds_read_b128 v[26:29], v172
	ds_read_b128 v[30:33], v172 offset:1024
	ds_read_b128 v[18:21], v172 offset:2048
	ds_read_b128 v[22:25], v172 offset:3072
	ds_read_b128 v[10:13], v173
	ds_read_b128 v[14:17], v173 offset:1024
	ds_read_b128 v[2:5], v173 offset:2048
	ds_read_b128 v[6:9], v173 offset:3072
	s_mov_b32 m0, s8
	ds_read_b128 v[174:177], v171 offset:32768
	ds_read_b128 v[178:181], v171 offset:33792
	ds_read_b128 v[182:185], v171 offset:34816
	ds_read_b128 v[186:189], v171 offset:35840
	ds_read_b128 v[190:193], v171 offset:36864
	ds_read_b128 v[194:197], v171 offset:37888
	ds_read_b128 v[204:207], v171 offset:38912
	ds_read_b128 v[208:211], v171 offset:39936
	buffer_load_dwordx4 v163, s[64:67], s14 offen lds
	s_mov_b32 m0, s13
	s_nop 0
	buffer_load_dwordx4 v165, s[64:67], s14 offen lds
	s_or_b32 s14, s29, 0x40100
	s_mov_b32 m0, s20
	s_nop 0
	buffer_load_dwordx4 v163, s[64:67], s14 offen lds
	s_mov_b32 m0, s21
	s_nop 0
	buffer_load_dwordx4 v165, s[64:67], s14 offen lds
	s_waitcnt vmcnt(8)
	s_waitcnt lgkmcnt(0)
	s_barrier
	s_setprio 1
	v_mfma_scale_f32_16x16x128_f8f6f4 v[150:153], v[26:33], v[174:181], v[150:153], v234, v234 op_sel_hi:[0,0,0]
	v_mfma_scale_f32_16x16x128_f8f6f4 v[146:149], v[18:25], v[174:181], v[146:149], v234, v234 op_sel_hi:[0,0,0]
	v_mfma_scale_f32_16x16x128_f8f6f4 v[134:137], v[26:33], v[182:189], v[134:137], v234, v234 op_sel_hi:[0,0,0]
	v_mfma_scale_f32_16x16x128_f8f6f4 v[130:133], v[18:25], v[182:189], v[130:133], v234, v234 op_sel_hi:[0,0,0]
	v_mfma_scale_f32_16x16x128_f8f6f4 v[118:121], v[26:33], v[190:197], v[118:121], v234, v234 op_sel_hi:[0,0,0]
	v_mfma_scale_f32_16x16x128_f8f6f4 v[114:117], v[18:25], v[190:197], v[114:117], v234, v234 op_sel_hi:[0,0,0]
	v_mfma_scale_f32_16x16x128_f8f6f4 v[98:101], v[26:33], v[204:211], v[98:101], v234, v234 op_sel_hi:[0,0,0]
	v_mfma_scale_f32_16x16x128_f8f6f4 v[90:93], v[18:25], v[204:211], v[90:93], v234, v234 op_sel_hi:[0,0,0]
	v_mfma_scale_f32_16x16x128_f8f6f4 v[158:161], v[10:17], v[174:181], v[158:161], v234, v234 op_sel_hi:[0,0,0]
	v_mfma_scale_f32_16x16x128_f8f6f4 v[154:157], v[2:9], v[174:181], v[154:157], v234, v234 op_sel_hi:[0,0,0]
	v_mfma_scale_f32_16x16x128_f8f6f4 v[142:145], v[10:17], v[182:189], v[142:145], v234, v234 op_sel_hi:[0,0,0]
	v_mfma_scale_f32_16x16x128_f8f6f4 v[138:141], v[2:9], v[182:189], v[138:141], v234, v234 op_sel_hi:[0,0,0]
	v_mfma_scale_f32_16x16x128_f8f6f4 v[126:129], v[10:17], v[190:197], v[126:129], v234, v234 op_sel_hi:[0,0,0]
	v_mfma_scale_f32_16x16x128_f8f6f4 v[122:125], v[2:9], v[190:197], v[122:125], v234, v234 op_sel_hi:[0,0,0]
	v_mfma_scale_f32_16x16x128_f8f6f4 v[110:113], v[10:17], v[204:211], v[110:113], v234, v234 op_sel_hi:[0,0,0]
	v_mfma_scale_f32_16x16x128_f8f6f4 v[106:109], v[2:9], v[204:211], v[106:109], v234, v234 op_sel_hi:[0,0,0]
	s_setprio 0
	s_barrier
	s_mov_b32 m0, s26
	s_or_b32 s14, s28, 0x180
	ds_read_b128 v[174:177], v171 offset:49152
	ds_read_b128 v[178:181], v171 offset:50176
	ds_read_b128 v[182:185], v171 offset:51200
	ds_read_b128 v[186:189], v171 offset:52224
	ds_read_b128 v[190:193], v171 offset:53248
	ds_read_b128 v[194:197], v171 offset:54272
	ds_read_b128 v[204:207], v171 offset:55296
	ds_read_b128 v[208:211], v171 offset:56320
	buffer_load_dwordx4 v164, s[4:7], s14 offen lds
	s_mov_b32 m0, s27
	s_nop 0
	buffer_load_dwordx4 v166, s[4:7], s14 offen lds
	s_or_b32 s14, s28, 0x40180
	s_mov_b32 m0, s40
	s_nop 0
	buffer_load_dwordx4 v164, s[4:7], s14 offen lds
	s_mov_b32 m0, s76
	s_nop 0
	buffer_load_dwordx4 v166, s[4:7], s14 offen lds
	s_waitcnt vmcnt(6)
	s_waitcnt lgkmcnt(0)
	s_barrier
	s_setprio 1
	v_mfma_scale_f32_16x16x128_f8f6f4 v[86:89], v[26:33], v[174:181], v[86:89], v234, v234 op_sel_hi:[0,0,0]
	v_mfma_scale_f32_16x16x128_f8f6f4 v[82:85], v[18:25], v[174:181], v[82:85], v234, v234 op_sel_hi:[0,0,0]
	v_mfma_scale_f32_16x16x128_f8f6f4 v[70:73], v[26:33], v[182:189], v[70:73], v234, v234 op_sel_hi:[0,0,0]
	v_mfma_scale_f32_16x16x128_f8f6f4 v[66:69], v[18:25], v[182:189], v[66:69], v234, v234 op_sel_hi:[0,0,0]
	v_mfma_scale_f32_16x16x128_f8f6f4 v[58:61], v[26:33], v[190:197], v[58:61], v234, v234 op_sel_hi:[0,0,0]
	v_mfma_scale_f32_16x16x128_f8f6f4 v[50:53], v[18:25], v[190:197], v[50:53], v234, v234 op_sel_hi:[0,0,0]
	v_mfma_scale_f32_16x16x128_f8f6f4 v[42:45], v[26:33], v[204:211], v[42:45], v234, v234 op_sel_hi:[0,0,0]
	v_mfma_scale_f32_16x16x128_f8f6f4 v[34:37], v[18:25], v[204:211], v[34:37], v234, v234 op_sel_hi:[0,0,0]
	v_mfma_scale_f32_16x16x128_f8f6f4 v[102:105], v[10:17], v[174:181], v[102:105], v234, v234 op_sel_hi:[0,0,0]
	v_mfma_scale_f32_16x16x128_f8f6f4 v[94:97], v[2:9], v[174:181], v[94:97], v234, v234 op_sel_hi:[0,0,0]
	v_mfma_scale_f32_16x16x128_f8f6f4 v[78:81], v[10:17], v[182:189], v[78:81], v234, v234 op_sel_hi:[0,0,0]
	v_mfma_scale_f32_16x16x128_f8f6f4 v[74:77], v[2:9], v[182:189], v[74:77], v234, v234 op_sel_hi:[0,0,0]
	v_mfma_scale_f32_16x16x128_f8f6f4 v[62:65], v[10:17], v[190:197], v[62:65], v234, v234 op_sel_hi:[0,0,0]
	v_mfma_scale_f32_16x16x128_f8f6f4 v[54:57], v[2:9], v[190:197], v[54:57], v234, v234 op_sel_hi:[0,0,0]
	v_mfma_scale_f32_16x16x128_f8f6f4 v[46:49], v[10:17], v[204:211], v[46:49], v234, v234 op_sel_hi:[0,0,0]
	v_mfma_scale_f32_16x16x128_f8f6f4 v[38:41], v[2:9], v[204:211], v[38:41], v234, v234 op_sel_hi:[0,0,0]
	s_setprio 0
	s_barrier
	s_addk_i32 s28, 0x200
	s_add_i32 s29, s29, 0x40180
	s_mov_b32 s62, 0
.LBB0_225:
	ds_read_b128 v[2:5], v169
	ds_read_b128 v[6:9], v169 offset:1024
	ds_read_b128 v[10:13], v169 offset:2048
	ds_read_b128 v[14:17], v169 offset:3072
	ds_read_b128 v[18:21], v170
	ds_read_b128 v[22:25], v170 offset:1024
	ds_read_b128 v[26:29], v170 offset:2048
	ds_read_b128 v[30:33], v170 offset:3072
	s_add_i32 s15, s29, 0xfffc0080
	s_cmp_eq_u32 s62, 12
	s_cselect_b32 s14, vcc_hi, s28
	s_cselect_b32 s15, vcc_lo, s15
	s_add_i32 s63, s29, 0xfffc0000
	s_mov_b32 m0, s79
	ds_read_b128 v[174:177], v171
	ds_read_b128 v[178:181], v171 offset:1024
	ds_read_b128 v[182:185], v171 offset:2048
	ds_read_b128 v[186:189], v171 offset:3072
	ds_read_b128 v[190:193], v171 offset:4096
	ds_read_b128 v[194:197], v171 offset:5120
	ds_read_b128 v[204:207], v171 offset:6144
	ds_read_b128 v[208:211], v171 offset:7168
	buffer_load_dwordx4 v163, s[64:67], s63 offen lds
	s_mov_b32 m0, s81
	s_nop 0
	buffer_load_dwordx4 v165, s[64:67], s63 offen lds
	s_mov_b32 m0, s80
	s_nop 0
	buffer_load_dwordx4 v163, s[64:67], s29 offen lds
	s_mov_b32 m0, s82
	s_nop 0
	buffer_load_dwordx4 v165, s[64:67], s29 offen lds
	s_waitcnt vmcnt(8)
	s_waitcnt lgkmcnt(0)
	s_barrier
	s_setprio 1
	v_mfma_scale_f32_16x16x128_f8f6f4 v[150:153], v[2:9], v[174:181], v[150:153], v234, v234 op_sel_hi:[0,0,0]
	v_mfma_scale_f32_16x16x128_f8f6f4 v[146:149], v[10:17], v[174:181], v[146:149], v234, v234 op_sel_hi:[0,0,0]
	v_mfma_scale_f32_16x16x128_f8f6f4 v[134:137], v[2:9], v[182:189], v[134:137], v234, v234 op_sel_hi:[0,0,0]
	v_mfma_scale_f32_16x16x128_f8f6f4 v[130:133], v[10:17], v[182:189], v[130:133], v234, v234 op_sel_hi:[0,0,0]
	v_mfma_scale_f32_16x16x128_f8f6f4 v[118:121], v[2:9], v[190:197], v[118:121], v234, v234 op_sel_hi:[0,0,0]
	v_mfma_scale_f32_16x16x128_f8f6f4 v[114:117], v[10:17], v[190:197], v[114:117], v234, v234 op_sel_hi:[0,0,0]
	v_mfma_scale_f32_16x16x128_f8f6f4 v[98:101], v[2:9], v[204:211], v[98:101], v234, v234 op_sel_hi:[0,0,0]
	v_mfma_scale_f32_16x16x128_f8f6f4 v[90:93], v[10:17], v[204:211], v[90:93], v234, v234 op_sel_hi:[0,0,0]
	v_mfma_scale_f32_16x16x128_f8f6f4 v[158:161], v[18:25], v[174:181], v[158:161], v234, v234 op_sel_hi:[0,0,0]
	v_mfma_scale_f32_16x16x128_f8f6f4 v[154:157], v[26:33], v[174:181], v[154:157], v234, v234 op_sel_hi:[0,0,0]
	v_mfma_scale_f32_16x16x128_f8f6f4 v[142:145], v[18:25], v[182:189], v[142:145], v234, v234 op_sel_hi:[0,0,0]
	v_mfma_scale_f32_16x16x128_f8f6f4 v[138:141], v[26:33], v[182:189], v[138:141], v234, v234 op_sel_hi:[0,0,0]
	v_mfma_scale_f32_16x16x128_f8f6f4 v[126:129], v[18:25], v[190:197], v[126:129], v234, v234 op_sel_hi:[0,0,0]
	v_mfma_scale_f32_16x16x128_f8f6f4 v[122:125], v[26:33], v[190:197], v[122:125], v234, v234 op_sel_hi:[0,0,0]
	v_mfma_scale_f32_16x16x128_f8f6f4 v[110:113], v[18:25], v[204:211], v[110:113], v234, v234 op_sel_hi:[0,0,0]
	v_mfma_scale_f32_16x16x128_f8f6f4 v[106:109], v[26:33], v[204:211], v[106:109], v234, v234 op_sel_hi:[0,0,0]
	s_setprio 0
	s_barrier
	s_mov_b32 m0, s9
	ds_read_b128 v[174:177], v171 offset:16384
	ds_read_b128 v[178:181], v171 offset:17408
	ds_read_b128 v[182:185], v171 offset:18432
	ds_read_b128 v[186:189], v171 offset:19456
	ds_read_b128 v[190:193], v171 offset:20480
	ds_read_b128 v[194:197], v171 offset:21504
	ds_read_b128 v[204:207], v171 offset:22528
	ds_read_b128 v[208:211], v171 offset:23552
	buffer_load_dwordx4 v164, s[4:7], s14 offen lds
	s_mov_b32 m0, s10
	s_add_i32 s63, s14, 0x40000
	buffer_load_dwordx4 v166, s[4:7], s14 offen lds
	s_mov_b32 m0, s11
	s_nop 0
	buffer_load_dwordx4 v164, s[4:7], s63 offen lds
	s_mov_b32 m0, s12
	s_nop 0
	buffer_load_dwordx4 v166, s[4:7], s63 offen lds
	s_waitcnt vmcnt(6)
	s_waitcnt lgkmcnt(0)
	s_barrier
	s_setprio 1
	v_mfma_scale_f32_16x16x128_f8f6f4 v[86:89], v[2:9], v[174:181], v[86:89], v234, v234 op_sel_hi:[0,0,0]
	v_mfma_scale_f32_16x16x128_f8f6f4 v[82:85], v[10:17], v[174:181], v[82:85], v234, v234 op_sel_hi:[0,0,0]
	v_mfma_scale_f32_16x16x128_f8f6f4 v[70:73], v[2:9], v[182:189], v[70:73], v234, v234 op_sel_hi:[0,0,0]
	v_mfma_scale_f32_16x16x128_f8f6f4 v[66:69], v[10:17], v[182:189], v[66:69], v234, v234 op_sel_hi:[0,0,0]
	v_mfma_scale_f32_16x16x128_f8f6f4 v[58:61], v[2:9], v[190:197], v[58:61], v234, v234 op_sel_hi:[0,0,0]
	v_mfma_scale_f32_16x16x128_f8f6f4 v[50:53], v[10:17], v[190:197], v[50:53], v234, v234 op_sel_hi:[0,0,0]
	v_mfma_scale_f32_16x16x128_f8f6f4 v[42:45], v[2:9], v[204:211], v[42:45], v234, v234 op_sel_hi:[0,0,0]
	v_mfma_scale_f32_16x16x128_f8f6f4 v[34:37], v[10:17], v[204:211], v[34:37], v234, v234 op_sel_hi:[0,0,0]
	v_mfma_scale_f32_16x16x128_f8f6f4 v[102:105], v[18:25], v[174:181], v[102:105], v234, v234 op_sel_hi:[0,0,0]
	v_mfma_scale_f32_16x16x128_f8f6f4 v[94:97], v[26:33], v[174:181], v[94:97], v234, v234 op_sel_hi:[0,0,0]
	v_mfma_scale_f32_16x16x128_f8f6f4 v[78:81], v[18:25], v[182:189], v[78:81], v234, v234 op_sel_hi:[0,0,0]
	v_mfma_scale_f32_16x16x128_f8f6f4 v[74:77], v[26:33], v[182:189], v[74:77], v234, v234 op_sel_hi:[0,0,0]
	v_mfma_scale_f32_16x16x128_f8f6f4 v[62:65], v[18:25], v[190:197], v[62:65], v234, v234 op_sel_hi:[0,0,0]
	v_mfma_scale_f32_16x16x128_f8f6f4 v[54:57], v[26:33], v[190:197], v[54:57], v234, v234 op_sel_hi:[0,0,0]
	v_mfma_scale_f32_16x16x128_f8f6f4 v[46:49], v[18:25], v[204:211], v[46:49], v234, v234 op_sel_hi:[0,0,0]
	v_mfma_scale_f32_16x16x128_f8f6f4 v[38:41], v[26:33], v[204:211], v[38:41], v234, v234 op_sel_hi:[0,0,0]
	s_setprio 0
	s_barrier
	ds_read_b128 v[18:21], v172
	ds_read_b128 v[22:25], v172 offset:1024
	ds_read_b128 v[26:29], v172 offset:2048
	ds_read_b128 v[30:33], v172 offset:3072
	ds_read_b128 v[10:13], v173
	ds_read_b128 v[14:17], v173 offset:1024
	ds_read_b128 v[2:5], v173 offset:2048
	ds_read_b128 v[6:9], v173 offset:3072
	s_mov_b32 m0, s8
	ds_read_b128 v[174:177], v171 offset:32768
	ds_read_b128 v[178:181], v171 offset:33792
	ds_read_b128 v[182:185], v171 offset:34816
	ds_read_b128 v[186:189], v171 offset:35840
	ds_read_b128 v[190:193], v171 offset:36864
	ds_read_b128 v[194:197], v171 offset:37888
	ds_read_b128 v[204:207], v171 offset:38912
	ds_read_b128 v[208:211], v171 offset:39936
	buffer_load_dwordx4 v163, s[64:67], s15 offen lds
	s_mov_b32 m0, s13
	s_nop 0
	buffer_load_dwordx4 v165, s[64:67], s15 offen lds
	s_add_i32 s15, s15, 0x40000
	s_mov_b32 m0, s20
	s_nop 0
	buffer_load_dwordx4 v163, s[64:67], s15 offen lds
	s_mov_b32 m0, s21
	s_nop 0
	buffer_load_dwordx4 v165, s[64:67], s15 offen lds
	s_waitcnt vmcnt(8)
	s_waitcnt lgkmcnt(0)
	s_barrier
	s_setprio 1
	v_mfma_scale_f32_16x16x128_f8f6f4 v[150:153], v[18:25], v[174:181], v[150:153], v234, v234 op_sel_hi:[0,0,0]
	v_mfma_scale_f32_16x16x128_f8f6f4 v[146:149], v[26:33], v[174:181], v[146:149], v234, v234 op_sel_hi:[0,0,0]
	v_mfma_scale_f32_16x16x128_f8f6f4 v[134:137], v[18:25], v[182:189], v[134:137], v234, v234 op_sel_hi:[0,0,0]
	v_mfma_scale_f32_16x16x128_f8f6f4 v[130:133], v[26:33], v[182:189], v[130:133], v234, v234 op_sel_hi:[0,0,0]
	v_mfma_scale_f32_16x16x128_f8f6f4 v[118:121], v[18:25], v[190:197], v[118:121], v234, v234 op_sel_hi:[0,0,0]
	v_mfma_scale_f32_16x16x128_f8f6f4 v[114:117], v[26:33], v[190:197], v[114:117], v234, v234 op_sel_hi:[0,0,0]
	v_mfma_scale_f32_16x16x128_f8f6f4 v[98:101], v[18:25], v[204:211], v[98:101], v234, v234 op_sel_hi:[0,0,0]
	v_mfma_scale_f32_16x16x128_f8f6f4 v[90:93], v[26:33], v[204:211], v[90:93], v234, v234 op_sel_hi:[0,0,0]
	v_mfma_scale_f32_16x16x128_f8f6f4 v[158:161], v[10:17], v[174:181], v[158:161], v234, v234 op_sel_hi:[0,0,0]
	v_mfma_scale_f32_16x16x128_f8f6f4 v[154:157], v[2:9], v[174:181], v[154:157], v234, v234 op_sel_hi:[0,0,0]
	v_mfma_scale_f32_16x16x128_f8f6f4 v[142:145], v[10:17], v[182:189], v[142:145], v234, v234 op_sel_hi:[0,0,0]
	v_mfma_scale_f32_16x16x128_f8f6f4 v[138:141], v[2:9], v[182:189], v[138:141], v234, v234 op_sel_hi:[0,0,0]
	v_mfma_scale_f32_16x16x128_f8f6f4 v[126:129], v[10:17], v[190:197], v[126:129], v234, v234 op_sel_hi:[0,0,0]
	v_mfma_scale_f32_16x16x128_f8f6f4 v[122:125], v[2:9], v[190:197], v[122:125], v234, v234 op_sel_hi:[0,0,0]
	v_mfma_scale_f32_16x16x128_f8f6f4 v[110:113], v[10:17], v[204:211], v[110:113], v234, v234 op_sel_hi:[0,0,0]
	v_mfma_scale_f32_16x16x128_f8f6f4 v[106:109], v[2:9], v[204:211], v[106:109], v234, v234 op_sel_hi:[0,0,0]
	s_setprio 0
	s_barrier
	s_mov_b32 m0, s26
	s_or_b32 s15, s14, 0x80
	ds_read_b128 v[174:177], v171 offset:49152
	ds_read_b128 v[178:181], v171 offset:50176
	ds_read_b128 v[182:185], v171 offset:51200
	ds_read_b128 v[186:189], v171 offset:52224
	ds_read_b128 v[190:193], v171 offset:53248
	ds_read_b128 v[194:197], v171 offset:54272
	ds_read_b128 v[204:207], v171 offset:55296
	ds_read_b128 v[208:211], v171 offset:56320
	buffer_load_dwordx4 v164, s[4:7], s15 offen lds
	s_mov_b32 m0, s27
	s_add_i32 s14, s14, 0x40080
	buffer_load_dwordx4 v166, s[4:7], s15 offen lds
	s_mov_b32 m0, s40
	s_nop 0
	buffer_load_dwordx4 v164, s[4:7], s14 offen lds
	s_mov_b32 m0, s76
	s_nop 0
	buffer_load_dwordx4 v166, s[4:7], s14 offen lds
	s_waitcnt vmcnt(6)
	s_waitcnt lgkmcnt(0)
	s_barrier
	s_setprio 1
	v_mfma_scale_f32_16x16x128_f8f6f4 v[86:89], v[18:25], v[174:181], v[86:89], v234, v234 op_sel_hi:[0,0,0]
	v_mfma_scale_f32_16x16x128_f8f6f4 v[82:85], v[26:33], v[174:181], v[82:85], v234, v234 op_sel_hi:[0,0,0]
	v_mfma_scale_f32_16x16x128_f8f6f4 v[70:73], v[18:25], v[182:189], v[70:73], v234, v234 op_sel_hi:[0,0,0]
	v_mfma_scale_f32_16x16x128_f8f6f4 v[66:69], v[26:33], v[182:189], v[66:69], v234, v234 op_sel_hi:[0,0,0]
	v_mfma_scale_f32_16x16x128_f8f6f4 v[58:61], v[18:25], v[190:197], v[58:61], v234, v234 op_sel_hi:[0,0,0]
	v_mfma_scale_f32_16x16x128_f8f6f4 v[50:53], v[26:33], v[190:197], v[50:53], v234, v234 op_sel_hi:[0,0,0]
	v_mfma_scale_f32_16x16x128_f8f6f4 v[42:45], v[18:25], v[204:211], v[42:45], v234, v234 op_sel_hi:[0,0,0]
	v_mfma_scale_f32_16x16x128_f8f6f4 v[34:37], v[26:33], v[204:211], v[34:37], v234, v234 op_sel_hi:[0,0,0]
	v_mfma_scale_f32_16x16x128_f8f6f4 v[102:105], v[10:17], v[174:181], v[102:105], v234, v234 op_sel_hi:[0,0,0]
	v_mfma_scale_f32_16x16x128_f8f6f4 v[94:97], v[2:9], v[174:181], v[94:97], v234, v234 op_sel_hi:[0,0,0]
	v_mfma_scale_f32_16x16x128_f8f6f4 v[78:81], v[10:17], v[182:189], v[78:81], v234, v234 op_sel_hi:[0,0,0]
	v_mfma_scale_f32_16x16x128_f8f6f4 v[74:77], v[2:9], v[182:189], v[74:77], v234, v234 op_sel_hi:[0,0,0]
	v_mfma_scale_f32_16x16x128_f8f6f4 v[62:65], v[10:17], v[190:197], v[62:65], v234, v234 op_sel_hi:[0,0,0]
	v_mfma_scale_f32_16x16x128_f8f6f4 v[54:57], v[2:9], v[190:197], v[54:57], v234, v234 op_sel_hi:[0,0,0]
	v_mfma_scale_f32_16x16x128_f8f6f4 v[46:49], v[10:17], v[204:211], v[46:49], v234, v234 op_sel_hi:[0,0,0]
	v_mfma_scale_f32_16x16x128_f8f6f4 v[38:41], v[2:9], v[204:211], v[38:41], v234, v234 op_sel_hi:[0,0,0]
	s_setprio 0
	s_barrier
	s_add_i32 s62, s62, 2
	s_addk_i32 s28, 0x100
	s_addk_i32 s29, 0x100
	s_cmp_gt_u32 s62, 13
	s_cbranch_scc0 .LBB0_225
	s_nop 15
	s_nop 15
	s_and_b64 vcc, exec, s[36:37]
	s_cbranch_vccz .LBB0_228
	s_barrier

.LBB0_242:
	v_add_u32_e32 v130, 0x10000, v140
	v_add_u32_e32 v131, 0x14000, v140
	ds_read_b128 v[2:5], v130
	ds_read_b128 v[6:9], v130 offset:1024
	ds_read_b128 v[10:13], v130 offset:2048
	ds_read_b128 v[14:17], v130 offset:3072
	ds_read_b128 v[18:21], v131
	ds_read_b128 v[22:25], v131 offset:1024
	ds_read_b128 v[26:29], v131 offset:2048
	ds_read_b128 v[30:33], v131 offset:3072
	s_lshl_b32 s26, s21, 20
	s_lshl_b32 s27, s20, 20
	s_or_b32 s43, s15, 0x80
	s_or_b32 s52, s14, 0x100
	s_and_b64 s[2:3], s[36:37], exec
	s_cselect_b32 s28, s26, s15
	s_or_b32 s62, s15, 0x100
	s_and_b64 s[2:3], s[36:37], exec
	s_cselect_b32 s29, s27, s14
	s_mov_b32 m0, s38
	ds_read_b128 v[34:37], v141
	ds_read_b128 v[38:41], v141 offset:1024
	ds_read_b128 v[42:45], v141 offset:2048
	ds_read_b128 v[46:49], v141 offset:3072
	ds_read_b128 v[50:53], v141 offset:4096
	ds_read_b128 v[54:57], v141 offset:5120
	ds_read_b128 v[58:61], v141 offset:6144
	ds_read_b128 v[62:65], v141 offset:7168
	buffer_load_dwordx4 v134, s[64:67], s43 offen lds
	s_mov_b32 m0, s10
	s_or_b32 s2, s15, 0x80080
	buffer_load_dwordx4 v136, s[64:67], s43 offen lds
	s_mov_b32 m0, s11
	s_nop 0
	buffer_load_dwordx4 v134, s[64:67], s2 offen lds
	s_mov_b32 m0, s13
	s_nop 0
	buffer_load_dwordx4 v136, s[64:67], s2 offen lds
	s_waitcnt vmcnt(8)
	s_waitcnt lgkmcnt(0)
	s_barrier
	s_setprio 1
	v_mfma_f32_16x16x32_bf16 v[90:93], v[2:5], v[58:61], 0
	v_mfma_f32_16x16x32_bf16 v[94:97], v[6:9], v[62:65], v[90:93]
	v_mfma_f32_16x16x32_bf16 v[90:93], v[10:13], v[58:61], 0
	v_mfma_f32_16x16x32_bf16 v[66:69], v[2:5], v[34:37], 0
	v_mfma_f32_16x16x32_bf16 v[70:73], v[10:13], v[34:37], 0
	v_mfma_f32_16x16x32_bf16 v[102:105], v[14:17], v[62:65], v[90:93]
	v_mfma_f32_16x16x32_bf16 v[90:93], v[18:21], v[34:37], 0
	v_mfma_f32_16x16x32_bf16 v[34:37], v[26:29], v[34:37], 0
	v_mfma_f32_16x16x32_bf16 v[66:69], v[6:9], v[38:41], v[66:69]
	v_mfma_f32_16x16x32_bf16 v[70:73], v[14:17], v[38:41], v[70:73]
	v_mfma_f32_16x16x32_bf16 v[74:77], v[2:5], v[42:45], 0
	v_mfma_f32_16x16x32_bf16 v[78:81], v[10:13], v[42:45], 0
	v_mfma_f32_16x16x32_bf16 v[110:113], v[22:25], v[38:41], v[90:93]
	v_mfma_f32_16x16x32_bf16 v[34:37], v[30:33], v[38:41], v[34:37]
	v_mfma_f32_16x16x32_bf16 v[38:41], v[18:21], v[42:45], 0
	v_mfma_f32_16x16x32_bf16 v[42:45], v[26:29], v[42:45], 0
	v_mfma_f32_16x16x32_bf16 v[74:77], v[6:9], v[46:49], v[74:77]
	v_mfma_f32_16x16x32_bf16 v[78:81], v[14:17], v[46:49], v[78:81]
	v_mfma_f32_16x16x32_bf16 v[82:85], v[2:5], v[50:53], 0
	v_mfma_f32_16x16x32_bf16 v[86:89], v[10:13], v[50:53], 0
	v_mfma_f32_16x16x32_bf16 v[38:41], v[22:25], v[46:49], v[38:41]
	v_mfma_f32_16x16x32_bf16 v[42:45], v[30:33], v[46:49], v[42:45]
	v_mfma_f32_16x16x32_bf16 v[46:49], v[18:21], v[50:53], 0
	v_mfma_f32_16x16x32_bf16 v[50:53], v[26:29], v[50:53], 0
	v_mfma_f32_16x16x32_bf16 v[82:85], v[6:9], v[54:57], v[82:85]
	v_mfma_f32_16x16x32_bf16 v[86:89], v[14:17], v[54:57], v[86:89]
	v_mfma_f32_16x16x32_bf16 v[46:49], v[22:25], v[54:57], v[46:49]
	v_mfma_f32_16x16x32_bf16 v[50:53], v[30:33], v[54:57], v[50:53]
	v_mfma_f32_16x16x32_bf16 v[54:57], v[18:21], v[58:61], 0
	v_mfma_f32_16x16x32_bf16 v[58:61], v[26:29], v[58:61], 0
	v_mfma_f32_16x16x32_bf16 v[54:57], v[22:25], v[62:65], v[54:57]
	v_mfma_f32_16x16x32_bf16 v[58:61], v[30:33], v[62:65], v[58:61]
	s_setprio 0
	s_barrier
	s_mov_b32 m0, s39
	s_mov_b32 s2, s66
	s_mov_b32 s3, s67
	ds_read_b128 v[62:65], v141 offset:16384
	ds_read_b128 v[90:93], v141 offset:17408
	ds_read_b128 v[98:101], v141 offset:18432
	ds_read_b128 v[106:109], v141 offset:19456
	ds_read_b128 v[114:117], v141 offset:20480
	ds_read_b128 v[118:121], v141 offset:21504
	ds_read_b128 v[122:125], v141 offset:22528
	ds_read_b128 v[126:129], v141 offset:23552
	buffer_load_dwordx4 v135, s[0:3], s52 offen lds
	s_mov_b32 m0, s76
	s_or_b32 s43, s14, 0x80100
	buffer_load_dwordx4 v137, s[0:3], s52 offen lds
	s_mov_b32 m0, s77
	s_nop 0
	buffer_load_dwordx4 v135, s[0:3], s43 offen lds
	s_mov_b32 m0, s78
	s_nop 0
	buffer_load_dwordx4 v137, s[0:3], s43 offen lds
	s_waitcnt vmcnt(6)
	s_waitcnt lgkmcnt(0)
	s_barrier
	s_setprio 1
	v_mfma_f32_16x16x32_bf16 v[142:145], v[2:5], v[62:65], 0
	v_mfma_f32_16x16x32_bf16 v[150:153], v[2:5], v[98:101], 0
	v_mfma_f32_16x16x32_bf16 v[158:161], v[2:5], v[114:117], 0
	v_mfma_f32_16x16x32_bf16 v[2:5], v[2:5], v[122:125], 0
	v_mfma_f32_16x16x32_bf16 v[142:145], v[6:9], v[90:93], v[142:145]
	v_mfma_f32_16x16x32_bf16 v[146:149], v[10:13], v[62:65], 0
	v_mfma_f32_16x16x32_bf16 v[150:153], v[6:9], v[106:109], v[150:153]
	v_mfma_f32_16x16x32_bf16 v[154:157], v[10:13], v[98:101], 0
	v_mfma_f32_16x16x32_bf16 v[158:161], v[6:9], v[118:121], v[158:161]
	v_mfma_f32_16x16x32_bf16 v[162:165], v[10:13], v[114:117], 0
	v_mfma_f32_16x16x32_bf16 v[2:5], v[6:9], v[126:129], v[2:5]
	v_mfma_f32_16x16x32_bf16 v[6:9], v[10:13], v[122:125], 0
	v_mfma_f32_16x16x32_bf16 v[10:13], v[18:21], v[62:65], 0
	v_mfma_f32_16x16x32_bf16 v[146:149], v[14:17], v[90:93], v[146:149]
	v_mfma_f32_16x16x32_bf16 v[154:157], v[14:17], v[106:109], v[154:157]
	v_mfma_f32_16x16x32_bf16 v[162:165], v[14:17], v[118:121], v[162:165]
	v_mfma_f32_16x16x32_bf16 v[6:9], v[14:17], v[126:129], v[6:9]
	v_mfma_f32_16x16x32_bf16 v[14:17], v[22:25], v[90:93], v[10:13]
	v_mfma_f32_16x16x32_bf16 v[10:13], v[26:29], v[62:65], 0
	v_mfma_f32_16x16x32_bf16 v[166:169], v[30:33], v[90:93], v[10:13]
	v_mfma_f32_16x16x32_bf16 v[10:13], v[18:21], v[98:101], 0
	v_mfma_f32_16x16x32_bf16 v[170:173], v[22:25], v[106:109], v[10:13]
	v_mfma_f32_16x16x32_bf16 v[10:13], v[26:29], v[98:101], 0
	v_mfma_f32_16x16x32_bf16 v[174:177], v[30:33], v[106:109], v[10:13]
	v_mfma_f32_16x16x32_bf16 v[10:13], v[18:21], v[114:117], 0
	v_mfma_f32_16x16x32_bf16 v[178:181], v[22:25], v[118:121], v[10:13]
	v_mfma_f32_16x16x32_bf16 v[10:13], v[26:29], v[114:117], 0
	v_mfma_f32_16x16x32_bf16 v[182:185], v[30:33], v[118:121], v[10:13]
	v_mfma_f32_16x16x32_bf16 v[10:13], v[18:21], v[122:125], 0
	v_mfma_f32_16x16x32_bf16 v[186:189], v[22:25], v[126:129], v[10:13]
	v_mfma_f32_16x16x32_bf16 v[10:13], v[26:29], v[122:125], 0
	v_mfma_f32_16x16x32_bf16 v[190:193], v[30:33], v[126:129], v[10:13]
	s_setprio 0
	s_barrier
	v_add_u32_e32 v132, 0x18000, v140
	v_add_u32_e32 v133, 0x1c000, v140
	s_nop 2
	ds_read_b128 v[10:13], v132
	ds_read_b128 v[22:25], v132 offset:1024
	ds_read_b128 v[30:33], v132 offset:2048
	ds_read_b128 v[62:65], v132 offset:3072
	ds_read_b128 v[194:197], v133
	ds_read_b128 v[198:201], v133 offset:1024
	ds_read_b128 v[204:207], v133 offset:2048
	ds_read_b128 v[208:211], v133 offset:3072
	s_mov_b32 m0, s12
	ds_read_b128 v[18:21], v141 offset:32768
	ds_read_b128 v[26:29], v141 offset:33792
	ds_read_b128 v[212:215], v141 offset:34816
	ds_read_b128 v[216:219], v141 offset:35840
	ds_read_b128 v[220:223], v141 offset:36864
	ds_read_b128 v[224:227], v141 offset:37888
	ds_read_b128 v[228:231], v141 offset:38912
	ds_read_b128 v[250:253], v141 offset:39936
	buffer_load_dwordx4 v134, s[64:67], s62 offen lds
	s_mov_b32 m0, s79
	s_or_b32 s43, s15, 0x80100
	buffer_load_dwordx4 v136, s[64:67], s62 offen lds
	s_mov_b32 m0, s80
	s_nop 0
	buffer_load_dwordx4 v134, s[64:67], s43 offen lds
	s_mov_b32 m0, s81
	s_nop 0
	buffer_load_dwordx4 v136, s[64:67], s43 offen lds
	s_waitcnt vmcnt(8)
	s_waitcnt lgkmcnt(0)
	s_barrier
	s_setprio 1
	v_mfma_f32_16x16x32_bf16 v[66:69], v[10:13], v[18:21], v[66:69]
	v_mfma_f32_16x16x32_bf16 v[122:125], v[22:25], v[26:29], v[66:69]
	v_mfma_f32_16x16x32_bf16 v[66:69], v[30:33], v[18:21], v[70:73]
	v_mfma_f32_16x16x32_bf16 v[114:117], v[62:65], v[26:29], v[66:69]
	v_mfma_f32_16x16x32_bf16 v[66:69], v[10:13], v[212:215], v[74:77]
	v_mfma_f32_16x16x32_bf16 v[106:109], v[22:25], v[216:219], v[66:69]
	v_mfma_f32_16x16x32_bf16 v[66:69], v[30:33], v[212:215], v[78:81]
	v_mfma_f32_16x16x32_bf16 v[98:101], v[62:65], v[216:219], v[66:69]
	v_mfma_f32_16x16x32_bf16 v[66:69], v[10:13], v[220:223], v[82:85]
	v_mfma_f32_16x16x32_bf16 v[70:73], v[194:197], v[18:21], v[110:113]
	v_mfma_f32_16x16x32_bf16 v[18:21], v[204:207], v[18:21], v[34:37]
	v_mfma_f32_16x16x32_bf16 v[90:93], v[22:25], v[224:227], v[66:69]
	v_mfma_f32_16x16x32_bf16 v[66:69], v[30:33], v[220:223], v[86:89]
	v_mfma_f32_16x16x32_bf16 v[118:121], v[208:211], v[26:29], v[18:21]
	v_mfma_f32_16x16x32_bf16 v[18:21], v[194:197], v[212:215], v[38:41]
	v_mfma_f32_16x16x32_bf16 v[82:85], v[62:65], v[224:227], v[66:69]
	v_mfma_f32_16x16x32_bf16 v[66:69], v[10:13], v[228:231], v[94:97]
	v_mfma_f32_16x16x32_bf16 v[110:113], v[198:201], v[216:219], v[18:21]
	v_mfma_f32_16x16x32_bf16 v[18:21], v[204:207], v[212:215], v[42:45]
	v_mfma_f32_16x16x32_bf16 v[74:77], v[22:25], v[250:253], v[66:69]
	v_mfma_f32_16x16x32_bf16 v[66:69], v[30:33], v[228:231], v[102:105]
	v_mfma_f32_16x16x32_bf16 v[102:105], v[208:211], v[216:219], v[18:21]
	v_mfma_f32_16x16x32_bf16 v[18:21], v[194:197], v[220:223], v[46:49]
	v_mfma_f32_16x16x32_bf16 v[94:97], v[198:201], v[224:227], v[18:21]
	v_mfma_f32_16x16x32_bf16 v[18:21], v[204:207], v[220:223], v[50:53]
	v_mfma_f32_16x16x32_bf16 v[86:89], v[208:211], v[224:227], v[18:21]
	v_mfma_f32_16x16x32_bf16 v[18:21], v[194:197], v[228:231], v[54:57]
	v_mfma_f32_16x16x32_bf16 v[78:81], v[198:201], v[250:253], v[18:21]
	v_mfma_f32_16x16x32_bf16 v[18:21], v[204:207], v[228:231], v[58:61]
	v_mfma_f32_16x16x32_bf16 v[66:69], v[62:65], v[250:253], v[66:69]
	v_mfma_f32_16x16x32_bf16 v[126:129], v[198:201], v[26:29], v[70:73]
	v_mfma_f32_16x16x32_bf16 v[70:73], v[208:211], v[250:253], v[18:21]
	s_setprio 0
	s_barrier
	s_mov_b32 m0, s82
	s_or_b32 s43, s14, 0x180
	ds_read_b128 v[38:41], v141 offset:49152
	ds_read_b128 v[46:49], v141 offset:50176
	ds_read_b128 v[212:215], v141 offset:51200
	ds_read_b128 v[216:219], v141 offset:52224
	ds_read_b128 v[220:223], v141 offset:53248
	ds_read_b128 v[224:227], v141 offset:54272
	ds_read_b128 v[228:231], v141 offset:55296
	ds_read_b128 v[250:253], v141 offset:56320
	buffer_load_dwordx4 v135, s[0:3], s43 offen lds
	s_mov_b32 m0, s83
	s_nop 0
	buffer_load_dwordx4 v137, s[0:3], s43 offen lds
	s_or_b32 s43, s14, 0x80180
	s_mov_b32 m0, s84
	s_nop 0
	buffer_load_dwordx4 v135, s[0:3], s43 offen lds
	s_mov_b32 m0, s85
	s_nop 0
	buffer_load_dwordx4 v137, s[0:3], s43 offen lds
	s_waitcnt vmcnt(6)
	s_waitcnt lgkmcnt(0)
	s_barrier
	s_setprio 1
	v_mfma_f32_16x16x32_bf16 v[18:21], v[10:13], v[38:41], v[142:145]
	v_mfma_f32_16x16x32_bf16 v[58:61], v[22:25], v[46:49], v[18:21]
	v_mfma_f32_16x16x32_bf16 v[18:21], v[30:33], v[38:41], v[146:149]
	v_mfma_f32_16x16x32_bf16 v[50:53], v[62:65], v[46:49], v[18:21]
	v_mfma_f32_16x16x32_bf16 v[18:21], v[10:13], v[212:215], v[150:153]
	v_mfma_f32_16x16x32_bf16 v[42:45], v[22:25], v[216:219], v[18:21]
	v_mfma_f32_16x16x32_bf16 v[18:21], v[30:33], v[212:215], v[154:157]
	v_mfma_f32_16x16x32_bf16 v[34:37], v[62:65], v[216:219], v[18:21]
	v_mfma_f32_16x16x32_bf16 v[18:21], v[10:13], v[220:223], v[158:161]
	v_mfma_f32_16x16x32_bf16 v[2:5], v[10:13], v[228:231], v[2:5]
	v_mfma_f32_16x16x32_bf16 v[26:29], v[22:25], v[224:227], v[18:21]
	v_mfma_f32_16x16x32_bf16 v[18:21], v[30:33], v[220:223], v[162:165]
	v_mfma_f32_16x16x32_bf16 v[10:13], v[22:25], v[250:253], v[2:5]
	v_mfma_f32_16x16x32_bf16 v[2:5], v[30:33], v[228:231], v[6:9]
	v_mfma_f32_16x16x32_bf16 v[6:9], v[194:197], v[38:41], v[14:17]
	v_mfma_f32_16x16x32_bf16 v[18:21], v[62:65], v[224:227], v[18:21]
	v_mfma_f32_16x16x32_bf16 v[2:5], v[62:65], v[250:253], v[2:5]
	v_mfma_f32_16x16x32_bf16 v[62:65], v[198:201], v[46:49], v[6:9]
	v_mfma_f32_16x16x32_bf16 v[6:9], v[204:207], v[38:41], v[166:169]
	v_mfma_f32_16x16x32_bf16 v[54:57], v[208:211], v[46:49], v[6:9]
	v_mfma_f32_16x16x32_bf16 v[6:9], v[194:197], v[212:215], v[170:173]
	v_mfma_f32_16x16x32_bf16 v[46:49], v[198:201], v[216:219], v[6:9]
	v_mfma_f32_16x16x32_bf16 v[6:9], v[204:207], v[212:215], v[174:177]
	v_mfma_f32_16x16x32_bf16 v[38:41], v[208:211], v[216:219], v[6:9]
	v_mfma_f32_16x16x32_bf16 v[6:9], v[194:197], v[220:223], v[178:181]
	v_mfma_f32_16x16x32_bf16 v[30:33], v[198:201], v[224:227], v[6:9]
	v_mfma_f32_16x16x32_bf16 v[6:9], v[204:207], v[220:223], v[182:185]
	v_mfma_f32_16x16x32_bf16 v[22:25], v[208:211], v[224:227], v[6:9]
	v_mfma_f32_16x16x32_bf16 v[6:9], v[194:197], v[228:231], v[186:189]
	v_mfma_f32_16x16x32_bf16 v[14:17], v[198:201], v[250:253], v[6:9]
	v_mfma_f32_16x16x32_bf16 v[6:9], v[204:207], v[228:231], v[190:193]
	v_mfma_f32_16x16x32_bf16 v[6:9], v[208:211], v[250:253], v[6:9]
	s_setprio 0
	s_barrier
	s_addk_i32 s14, 0x200
	s_add_i32 s15, s15, 0x80180
	s_mov_b32 s43, 0
.LBB0_243:
	ds_read_b128 v[142:145], v130
	ds_read_b128 v[146:149], v130 offset:1024
	ds_read_b128 v[150:153], v130 offset:2048
	ds_read_b128 v[154:157], v130 offset:3072
	ds_read_b128 v[158:161], v131
	ds_read_b128 v[162:165], v131 offset:1024
	ds_read_b128 v[166:169], v131 offset:2048
	ds_read_b128 v[170:173], v131 offset:3072
	s_add_i32 s52, s15, 0xfff80080
	s_cmp_eq_u32 s43, 28
	s_cselect_b32 s62, s29, s14
	s_cselect_b32 s52, s28, s52
	s_add_i32 s63, s15, 0xfff80000
	s_mov_b32 m0, s38
	ds_read_b128 v[174:177], v141
	ds_read_b128 v[178:181], v141 offset:1024
	ds_read_b128 v[182:185], v141 offset:2048
	ds_read_b128 v[186:189], v141 offset:3072
	ds_read_b128 v[190:193], v141 offset:4096
	ds_read_b128 v[194:197], v141 offset:5120
	ds_read_b128 v[198:201], v141 offset:6144
	ds_read_b128 v[204:207], v141 offset:7168
	buffer_load_dwordx4 v134, s[64:67], s63 offen lds
	s_mov_b32 m0, s10
	s_nop 0
	buffer_load_dwordx4 v136, s[64:67], s63 offen lds
	s_mov_b32 m0, s11
	s_nop 0
	buffer_load_dwordx4 v134, s[64:67], s15 offen lds
	s_mov_b32 m0, s13
	s_nop 0
	buffer_load_dwordx4 v136, s[64:67], s15 offen lds
	s_waitcnt vmcnt(8)
	s_waitcnt lgkmcnt(0)
	s_barrier
	s_setprio 1
	v_mfma_f32_16x16x32_bf16 v[122:125], v[142:145], v[174:177], v[122:125]
	v_mfma_f32_16x16x32_bf16 v[114:117], v[150:153], v[174:177], v[114:117]
	v_mfma_f32_16x16x32_bf16 v[106:109], v[142:145], v[182:185], v[106:109]
	v_mfma_f32_16x16x32_bf16 v[98:101], v[150:153], v[182:185], v[98:101]
	v_mfma_f32_16x16x32_bf16 v[90:93], v[142:145], v[190:193], v[90:93]
	v_mfma_f32_16x16x32_bf16 v[82:85], v[150:153], v[190:193], v[82:85]
	v_mfma_f32_16x16x32_bf16 v[74:77], v[142:145], v[198:201], v[74:77]
	v_mfma_f32_16x16x32_bf16 v[66:69], v[150:153], v[198:201], v[66:69]
	v_mfma_f32_16x16x32_bf16 v[126:129], v[158:161], v[174:177], v[126:129]
	v_mfma_f32_16x16x32_bf16 v[118:121], v[166:169], v[174:177], v[118:121]
	v_mfma_f32_16x16x32_bf16 v[110:113], v[158:161], v[182:185], v[110:113]
	v_mfma_f32_16x16x32_bf16 v[102:105], v[166:169], v[182:185], v[102:105]
	v_mfma_f32_16x16x32_bf16 v[94:97], v[158:161], v[190:193], v[94:97]
	v_mfma_f32_16x16x32_bf16 v[86:89], v[166:169], v[190:193], v[86:89]
	v_mfma_f32_16x16x32_bf16 v[78:81], v[158:161], v[198:201], v[78:81]
	v_mfma_f32_16x16x32_bf16 v[70:73], v[166:169], v[198:201], v[70:73]
	v_mfma_f32_16x16x32_bf16 v[122:125], v[146:149], v[178:181], v[122:125]
	v_mfma_f32_16x16x32_bf16 v[114:117], v[154:157], v[178:181], v[114:117]
	v_mfma_f32_16x16x32_bf16 v[106:109], v[146:149], v[186:189], v[106:109]
	v_mfma_f32_16x16x32_bf16 v[98:101], v[154:157], v[186:189], v[98:101]
	v_mfma_f32_16x16x32_bf16 v[90:93], v[146:149], v[194:197], v[90:93]
	v_mfma_f32_16x16x32_bf16 v[82:85], v[154:157], v[194:197], v[82:85]
	v_mfma_f32_16x16x32_bf16 v[74:77], v[146:149], v[204:207], v[74:77]
	v_mfma_f32_16x16x32_bf16 v[66:69], v[154:157], v[204:207], v[66:69]
	v_mfma_f32_16x16x32_bf16 v[126:129], v[162:165], v[178:181], v[126:129]
	v_mfma_f32_16x16x32_bf16 v[118:121], v[170:173], v[178:181], v[118:121]
	v_mfma_f32_16x16x32_bf16 v[110:113], v[162:165], v[186:189], v[110:113]
	v_mfma_f32_16x16x32_bf16 v[102:105], v[170:173], v[186:189], v[102:105]
	v_mfma_f32_16x16x32_bf16 v[94:97], v[162:165], v[194:197], v[94:97]
	v_mfma_f32_16x16x32_bf16 v[86:89], v[170:173], v[194:197], v[86:89]
	v_mfma_f32_16x16x32_bf16 v[78:81], v[162:165], v[204:207], v[78:81]
	v_mfma_f32_16x16x32_bf16 v[70:73], v[170:173], v[204:207], v[70:73]
	s_setprio 0
	s_barrier
	s_mov_b32 m0, s39
	ds_read_b128 v[174:177], v141 offset:16384
	ds_read_b128 v[178:181], v141 offset:17408
	ds_read_b128 v[182:185], v141 offset:18432
	ds_read_b128 v[186:189], v141 offset:19456
	ds_read_b128 v[190:193], v141 offset:20480
	ds_read_b128 v[194:197], v141 offset:21504
	ds_read_b128 v[198:201], v141 offset:22528
	ds_read_b128 v[204:207], v141 offset:23552
	buffer_load_dwordx4 v135, s[0:3], s62 offen lds
	s_mov_b32 m0, s76
	s_add_i32 s63, s62, 0x80000
	buffer_load_dwordx4 v137, s[0:3], s62 offen lds
	s_mov_b32 m0, s77
	s_nop 0
	buffer_load_dwordx4 v135, s[0:3], s63 offen lds
	s_mov_b32 m0, s78
	s_nop 0
	buffer_load_dwordx4 v137, s[0:3], s63 offen lds
	s_waitcnt vmcnt(6)
	s_waitcnt lgkmcnt(0)
	s_barrier
	s_setprio 1
	v_mfma_f32_16x16x32_bf16 v[58:61], v[142:145], v[174:177], v[58:61]
	v_mfma_f32_16x16x32_bf16 v[50:53], v[150:153], v[174:177], v[50:53]
	v_mfma_f32_16x16x32_bf16 v[42:45], v[142:145], v[182:185], v[42:45]
	v_mfma_f32_16x16x32_bf16 v[34:37], v[150:153], v[182:185], v[34:37]
	v_mfma_f32_16x16x32_bf16 v[26:29], v[142:145], v[190:193], v[26:29]
	v_mfma_f32_16x16x32_bf16 v[18:21], v[150:153], v[190:193], v[18:21]
	v_mfma_f32_16x16x32_bf16 v[10:13], v[142:145], v[198:201], v[10:13]
	v_mfma_f32_16x16x32_bf16 v[2:5], v[150:153], v[198:201], v[2:5]
	v_mfma_f32_16x16x32_bf16 v[62:65], v[158:161], v[174:177], v[62:65]
	v_mfma_f32_16x16x32_bf16 v[54:57], v[166:169], v[174:177], v[54:57]
	v_mfma_f32_16x16x32_bf16 v[46:49], v[158:161], v[182:185], v[46:49]
	v_mfma_f32_16x16x32_bf16 v[38:41], v[166:169], v[182:185], v[38:41]
	v_mfma_f32_16x16x32_bf16 v[30:33], v[158:161], v[190:193], v[30:33]
	v_mfma_f32_16x16x32_bf16 v[22:25], v[166:169], v[190:193], v[22:25]
	v_mfma_f32_16x16x32_bf16 v[14:17], v[158:161], v[198:201], v[14:17]
	v_mfma_f32_16x16x32_bf16 v[6:9], v[166:169], v[198:201], v[6:9]
	v_mfma_f32_16x16x32_bf16 v[58:61], v[146:149], v[178:181], v[58:61]
	v_mfma_f32_16x16x32_bf16 v[50:53], v[154:157], v[178:181], v[50:53]
	v_mfma_f32_16x16x32_bf16 v[42:45], v[146:149], v[186:189], v[42:45]
	v_mfma_f32_16x16x32_bf16 v[34:37], v[154:157], v[186:189], v[34:37]
	v_mfma_f32_16x16x32_bf16 v[26:29], v[146:149], v[194:197], v[26:29]
	v_mfma_f32_16x16x32_bf16 v[18:21], v[154:157], v[194:197], v[18:21]
	v_mfma_f32_16x16x32_bf16 v[10:13], v[146:149], v[204:207], v[10:13]
	v_mfma_f32_16x16x32_bf16 v[2:5], v[154:157], v[204:207], v[2:5]
	v_mfma_f32_16x16x32_bf16 v[62:65], v[162:165], v[178:181], v[62:65]
	v_mfma_f32_16x16x32_bf16 v[54:57], v[170:173], v[178:181], v[54:57]
	v_mfma_f32_16x16x32_bf16 v[46:49], v[162:165], v[186:189], v[46:49]
	v_mfma_f32_16x16x32_bf16 v[38:41], v[170:173], v[186:189], v[38:41]
	v_mfma_f32_16x16x32_bf16 v[30:33], v[162:165], v[194:197], v[30:33]
	v_mfma_f32_16x16x32_bf16 v[22:25], v[170:173], v[194:197], v[22:25]
	v_mfma_f32_16x16x32_bf16 v[14:17], v[162:165], v[204:207], v[14:17]
	v_mfma_f32_16x16x32_bf16 v[6:9], v[170:173], v[204:207], v[6:9]
	s_setprio 0
	s_barrier
	ds_read_b128 v[142:145], v132
	ds_read_b128 v[146:149], v132 offset:1024
	ds_read_b128 v[150:153], v132 offset:2048
	ds_read_b128 v[154:157], v132 offset:3072
	ds_read_b128 v[158:161], v133
	ds_read_b128 v[162:165], v133 offset:1024
	ds_read_b128 v[166:169], v133 offset:2048
	ds_read_b128 v[170:173], v133 offset:3072
	s_mov_b32 m0, s12
	ds_read_b128 v[174:177], v141 offset:32768
	ds_read_b128 v[178:181], v141 offset:33792
	ds_read_b128 v[182:185], v141 offset:34816
	ds_read_b128 v[186:189], v141 offset:35840
	ds_read_b128 v[190:193], v141 offset:36864
	ds_read_b128 v[194:197], v141 offset:37888
	ds_read_b128 v[198:201], v141 offset:38912
	ds_read_b128 v[204:207], v141 offset:39936
	buffer_load_dwordx4 v134, s[64:67], s52 offen lds
	s_mov_b32 m0, s79
	s_nop 0
	buffer_load_dwordx4 v136, s[64:67], s52 offen lds
	s_add_i32 s52, s52, 0x80000
	s_mov_b32 m0, s80
	s_nop 0
	buffer_load_dwordx4 v134, s[64:67], s52 offen lds
	s_mov_b32 m0, s81
	s_nop 0
	buffer_load_dwordx4 v136, s[64:67], s52 offen lds
	s_waitcnt vmcnt(8)
	s_waitcnt lgkmcnt(0)
	s_barrier
	s_setprio 1
	v_mfma_f32_16x16x32_bf16 v[122:125], v[142:145], v[174:177], v[122:125]
	v_mfma_f32_16x16x32_bf16 v[114:117], v[150:153], v[174:177], v[114:117]
	v_mfma_f32_16x16x32_bf16 v[106:109], v[142:145], v[182:185], v[106:109]
	v_mfma_f32_16x16x32_bf16 v[98:101], v[150:153], v[182:185], v[98:101]
	v_mfma_f32_16x16x32_bf16 v[90:93], v[142:145], v[190:193], v[90:93]
	v_mfma_f32_16x16x32_bf16 v[82:85], v[150:153], v[190:193], v[82:85]
	v_mfma_f32_16x16x32_bf16 v[74:77], v[142:145], v[198:201], v[74:77]
	v_mfma_f32_16x16x32_bf16 v[66:69], v[150:153], v[198:201], v[66:69]
	v_mfma_f32_16x16x32_bf16 v[126:129], v[158:161], v[174:177], v[126:129]
	v_mfma_f32_16x16x32_bf16 v[118:121], v[166:169], v[174:177], v[118:121]
	v_mfma_f32_16x16x32_bf16 v[110:113], v[158:161], v[182:185], v[110:113]
	v_mfma_f32_16x16x32_bf16 v[102:105], v[166:169], v[182:185], v[102:105]
	v_mfma_f32_16x16x32_bf16 v[94:97], v[158:161], v[190:193], v[94:97]
	v_mfma_f32_16x16x32_bf16 v[86:89], v[166:169], v[190:193], v[86:89]
	v_mfma_f32_16x16x32_bf16 v[78:81], v[158:161], v[198:201], v[78:81]
	v_mfma_f32_16x16x32_bf16 v[70:73], v[166:169], v[198:201], v[70:73]
	v_mfma_f32_16x16x32_bf16 v[122:125], v[146:149], v[178:181], v[122:125]
	v_mfma_f32_16x16x32_bf16 v[114:117], v[154:157], v[178:181], v[114:117]
	v_mfma_f32_16x16x32_bf16 v[106:109], v[146:149], v[186:189], v[106:109]
	v_mfma_f32_16x16x32_bf16 v[98:101], v[154:157], v[186:189], v[98:101]
	v_mfma_f32_16x16x32_bf16 v[90:93], v[146:149], v[194:197], v[90:93]
	v_mfma_f32_16x16x32_bf16 v[82:85], v[154:157], v[194:197], v[82:85]
	v_mfma_f32_16x16x32_bf16 v[74:77], v[146:149], v[204:207], v[74:77]
	v_mfma_f32_16x16x32_bf16 v[66:69], v[154:157], v[204:207], v[66:69]
	v_mfma_f32_16x16x32_bf16 v[126:129], v[162:165], v[178:181], v[126:129]
	v_mfma_f32_16x16x32_bf16 v[118:121], v[170:173], v[178:181], v[118:121]
	v_mfma_f32_16x16x32_bf16 v[110:113], v[162:165], v[186:189], v[110:113]
	v_mfma_f32_16x16x32_bf16 v[102:105], v[170:173], v[186:189], v[102:105]
	v_mfma_f32_16x16x32_bf16 v[94:97], v[162:165], v[194:197], v[94:97]
	v_mfma_f32_16x16x32_bf16 v[86:89], v[170:173], v[194:197], v[86:89]
	v_mfma_f32_16x16x32_bf16 v[78:81], v[162:165], v[204:207], v[78:81]
	v_mfma_f32_16x16x32_bf16 v[70:73], v[170:173], v[204:207], v[70:73]
	s_setprio 0
	s_barrier
	s_mov_b32 m0, s82
	s_or_b32 s52, s62, 0x80
	ds_read_b128 v[174:177], v141 offset:49152
	ds_read_b128 v[178:181], v141 offset:50176
	ds_read_b128 v[182:185], v141 offset:51200
	ds_read_b128 v[186:189], v141 offset:52224
	ds_read_b128 v[190:193], v141 offset:53248
	ds_read_b128 v[194:197], v141 offset:54272
	ds_read_b128 v[198:201], v141 offset:55296
	ds_read_b128 v[204:207], v141 offset:56320
	buffer_load_dwordx4 v135, s[0:3], s52 offen lds
	s_mov_b32 m0, s83
	s_add_i32 s62, s62, 0x80080
	buffer_load_dwordx4 v137, s[0:3], s52 offen lds
	s_mov_b32 m0, s84
	s_nop 0
	buffer_load_dwordx4 v135, s[0:3], s62 offen lds
	s_mov_b32 m0, s85
	s_nop 0
	buffer_load_dwordx4 v137, s[0:3], s62 offen lds
	s_waitcnt vmcnt(6)
	s_waitcnt lgkmcnt(0)
	s_barrier
	s_setprio 1
	v_mfma_f32_16x16x32_bf16 v[58:61], v[142:145], v[174:177], v[58:61]
	v_mfma_f32_16x16x32_bf16 v[50:53], v[150:153], v[174:177], v[50:53]
	v_mfma_f32_16x16x32_bf16 v[42:45], v[142:145], v[182:185], v[42:45]
	v_mfma_f32_16x16x32_bf16 v[34:37], v[150:153], v[182:185], v[34:37]
	v_mfma_f32_16x16x32_bf16 v[26:29], v[142:145], v[190:193], v[26:29]
	v_mfma_f32_16x16x32_bf16 v[18:21], v[150:153], v[190:193], v[18:21]
	v_mfma_f32_16x16x32_bf16 v[10:13], v[142:145], v[198:201], v[10:13]
	v_mfma_f32_16x16x32_bf16 v[2:5], v[150:153], v[198:201], v[2:5]
	v_mfma_f32_16x16x32_bf16 v[62:65], v[158:161], v[174:177], v[62:65]
	v_mfma_f32_16x16x32_bf16 v[54:57], v[166:169], v[174:177], v[54:57]
	v_mfma_f32_16x16x32_bf16 v[46:49], v[158:161], v[182:185], v[46:49]
	v_mfma_f32_16x16x32_bf16 v[38:41], v[166:169], v[182:185], v[38:41]
	v_mfma_f32_16x16x32_bf16 v[30:33], v[158:161], v[190:193], v[30:33]
	v_mfma_f32_16x16x32_bf16 v[22:25], v[166:169], v[190:193], v[22:25]
	v_mfma_f32_16x16x32_bf16 v[14:17], v[158:161], v[198:201], v[14:17]
	v_mfma_f32_16x16x32_bf16 v[6:9], v[166:169], v[198:201], v[6:9]
	v_mfma_f32_16x16x32_bf16 v[58:61], v[146:149], v[178:181], v[58:61]
	v_mfma_f32_16x16x32_bf16 v[50:53], v[154:157], v[178:181], v[50:53]
	v_mfma_f32_16x16x32_bf16 v[42:45], v[146:149], v[186:189], v[42:45]
	v_mfma_f32_16x16x32_bf16 v[34:37], v[154:157], v[186:189], v[34:37]
	v_mfma_f32_16x16x32_bf16 v[26:29], v[146:149], v[194:197], v[26:29]
	v_mfma_f32_16x16x32_bf16 v[18:21], v[154:157], v[194:197], v[18:21]
	v_mfma_f32_16x16x32_bf16 v[10:13], v[146:149], v[204:207], v[10:13]
	v_mfma_f32_16x16x32_bf16 v[2:5], v[154:157], v[204:207], v[2:5]
	v_mfma_f32_16x16x32_bf16 v[62:65], v[162:165], v[178:181], v[62:65]
	v_mfma_f32_16x16x32_bf16 v[54:57], v[170:173], v[178:181], v[54:57]
	v_mfma_f32_16x16x32_bf16 v[46:49], v[162:165], v[186:189], v[46:49]
	v_mfma_f32_16x16x32_bf16 v[38:41], v[170:173], v[186:189], v[38:41]
	v_mfma_f32_16x16x32_bf16 v[30:33], v[162:165], v[194:197], v[30:33]
	v_mfma_f32_16x16x32_bf16 v[22:25], v[170:173], v[194:197], v[22:25]
	v_mfma_f32_16x16x32_bf16 v[14:17], v[162:165], v[204:207], v[14:17]
	v_mfma_f32_16x16x32_bf16 v[6:9], v[170:173], v[204:207], v[6:9]
	s_setprio 0
	s_barrier
	s_add_i32 s43, s43, 2
	s_addk_i32 s14, 0x100
	s_addk_i32 s15, 0x100
	s_cmp_gt_u32 s43, 29
	s_cbranch_scc0 .LBB0_243
	s_and_b64 vcc, exec, s[6:7]
	s_cbranch_vccz .LBB0_246
	s_barrier

.LBB0_261:
	v_add_u32_e32 v130, 0x10000, v138
	v_add_u32_e32 v131, 0x14000, v138
	ds_read_b128 v[2:5], v130
	ds_read_b128 v[6:9], v130 offset:1024
	ds_read_b128 v[10:13], v130 offset:2048
	ds_read_b128 v[14:17], v130 offset:3072
	ds_read_b128 v[18:21], v131
	ds_read_b128 v[22:25], v131 offset:1024
	ds_read_b128 v[26:29], v131 offset:2048
	ds_read_b128 v[30:33], v131 offset:3072
	s_mul_i32 s63, s22, s9
	s_and_b64 s[2:3], s[38:39], exec
	s_cselect_b32 s29, s63, s84
	s_add_i32 vcc_lo, s83, 0x100
	s_add_i32 s15, s84, 0x100
	s_and_b64 s[2:3], s[30:31], exec
	s_mul_i32 s14, s28, s9
	s_cselect_b32 s15, s29, s15
	s_and_b64 s[2:3], s[38:39], exec
	s_cselect_b32 s62, s14, s83
	s_and_b64 s[2:3], s[30:31], exec
	s_cselect_b32 vcc_lo, s62, vcc_lo
	s_add_i32 s2, s83, 0x80
	s_mov_b32 m0, s78
	ds_read_b128 v[34:37], v139
	ds_read_b128 v[38:41], v139 offset:1024
	ds_read_b128 v[42:45], v139 offset:2048
	ds_read_b128 v[46:49], v139 offset:3072
	ds_read_b128 v[50:53], v139 offset:4096
	ds_read_b128 v[54:57], v139 offset:5120
	ds_read_b128 v[58:61], v139 offset:6144
	ds_read_b128 v[62:65], v139 offset:7168
	buffer_load_dwordx4 v132, s[64:67], s2 offen lds
	s_mov_b32 m0, s80
	s_nop 0
	buffer_load_dwordx4 v134, s[64:67], s2 offen lds
	s_add_i32 s2, s2, s8
	s_mov_b32 m0, s79
	s_nop 0
	buffer_load_dwordx4 v132, s[64:67], s2 offen lds
	s_mov_b32 m0, s81
	s_nop 0
	buffer_load_dwordx4 v134, s[64:67], s2 offen lds
	s_waitcnt vmcnt(8)
	s_waitcnt lgkmcnt(0)
	s_barrier
	s_setprio 1
	v_mfma_f32_16x16x32_bf16 v[90:93], v[2:5], v[58:61], 0
	v_mfma_f32_16x16x32_bf16 v[98:101], v[6:9], v[62:65], v[90:93]
	v_mfma_f32_16x16x32_bf16 v[90:93], v[10:13], v[58:61], 0
	v_mfma_f32_16x16x32_bf16 v[66:69], v[2:5], v[34:37], 0
	v_mfma_f32_16x16x32_bf16 v[70:73], v[10:13], v[34:37], 0
	v_mfma_f32_16x16x32_bf16 v[102:105], v[14:17], v[62:65], v[90:93]
	v_mfma_f32_16x16x32_bf16 v[90:93], v[18:21], v[34:37], 0
	v_mfma_f32_16x16x32_bf16 v[34:37], v[26:29], v[34:37], 0
	v_mfma_f32_16x16x32_bf16 v[66:69], v[6:9], v[38:41], v[66:69]
	v_mfma_f32_16x16x32_bf16 v[70:73], v[14:17], v[38:41], v[70:73]
	v_mfma_f32_16x16x32_bf16 v[74:77], v[2:5], v[42:45], 0
	v_mfma_f32_16x16x32_bf16 v[78:81], v[10:13], v[42:45], 0
	v_mfma_f32_16x16x32_bf16 v[114:117], v[22:25], v[38:41], v[90:93]
	v_mfma_f32_16x16x32_bf16 v[34:37], v[30:33], v[38:41], v[34:37]
	v_mfma_f32_16x16x32_bf16 v[38:41], v[18:21], v[42:45], 0
	v_mfma_f32_16x16x32_bf16 v[42:45], v[26:29], v[42:45], 0
	v_mfma_f32_16x16x32_bf16 v[74:77], v[6:9], v[46:49], v[74:77]
	v_mfma_f32_16x16x32_bf16 v[78:81], v[14:17], v[46:49], v[78:81]
	v_mfma_f32_16x16x32_bf16 v[82:85], v[2:5], v[50:53], 0
	v_mfma_f32_16x16x32_bf16 v[86:89], v[10:13], v[50:53], 0
	v_mfma_f32_16x16x32_bf16 v[38:41], v[22:25], v[46:49], v[38:41]
	v_mfma_f32_16x16x32_bf16 v[42:45], v[30:33], v[46:49], v[42:45]
	v_mfma_f32_16x16x32_bf16 v[46:49], v[18:21], v[50:53], 0
	v_mfma_f32_16x16x32_bf16 v[50:53], v[26:29], v[50:53], 0
	v_mfma_f32_16x16x32_bf16 v[82:85], v[6:9], v[54:57], v[82:85]
	v_mfma_f32_16x16x32_bf16 v[86:89], v[14:17], v[54:57], v[86:89]
	v_mfma_f32_16x16x32_bf16 v[46:49], v[22:25], v[54:57], v[46:49]
	v_mfma_f32_16x16x32_bf16 v[50:53], v[30:33], v[54:57], v[50:53]
	v_mfma_f32_16x16x32_bf16 v[54:57], v[18:21], v[58:61], 0
	v_mfma_f32_16x16x32_bf16 v[58:61], v[26:29], v[58:61], 0
	v_mfma_f32_16x16x32_bf16 v[54:57], v[22:25], v[62:65], v[54:57]
	v_mfma_f32_16x16x32_bf16 v[62:65], v[30:33], v[62:65], v[58:61]
	s_setprio 0
	s_barrier
	s_mov_b32 m0, s11
	s_mov_b32 s2, s66
	s_mov_b32 s3, s67
	s_nop 0
	ds_read_b128 v[58:61], v139 offset:16384
	ds_read_b128 v[90:93], v139 offset:17408
	ds_read_b128 v[94:97], v139 offset:18432
	ds_read_b128 v[106:109], v139 offset:19456
	ds_read_b128 v[110:113], v139 offset:20480
	ds_read_b128 v[118:121], v139 offset:21504
	ds_read_b128 v[122:125], v139 offset:22528
	ds_read_b128 v[126:129], v139 offset:23552
	buffer_load_dwordx4 v133, s[0:3], s15 offen lds
	s_mov_b32 m0, s12
	s_add_i32 vcc_hi, s15, s8
	buffer_load_dwordx4 v135, s[0:3], s15 offen lds
	s_mov_b32 m0, s13
	s_nop 0
	buffer_load_dwordx4 v133, s[0:3], vcc_hi offen lds
	s_mov_b32 m0, s20
	s_nop 0
	buffer_load_dwordx4 v135, s[0:3], vcc_hi offen lds
	s_waitcnt vmcnt(6)
	s_waitcnt lgkmcnt(0)
	s_barrier
	s_setprio 1
	v_mfma_f32_16x16x32_bf16 v[140:143], v[2:5], v[58:61], 0
	v_mfma_f32_16x16x32_bf16 v[150:153], v[2:5], v[94:97], 0
	v_mfma_f32_16x16x32_bf16 v[158:161], v[2:5], v[110:113], 0
	v_mfma_f32_16x16x32_bf16 v[2:5], v[2:5], v[122:125], 0
	v_mfma_f32_16x16x32_bf16 v[142:145], v[6:9], v[90:93], v[140:143]
	v_mfma_f32_16x16x32_bf16 v[146:149], v[10:13], v[58:61], 0
	v_mfma_f32_16x16x32_bf16 v[150:153], v[6:9], v[106:109], v[150:153]
	v_mfma_f32_16x16x32_bf16 v[154:157], v[10:13], v[94:97], 0
	v_mfma_f32_16x16x32_bf16 v[158:161], v[6:9], v[118:121], v[158:161]
	v_mfma_f32_16x16x32_bf16 v[162:165], v[10:13], v[110:113], 0
	v_mfma_f32_16x16x32_bf16 v[2:5], v[6:9], v[126:129], v[2:5]
	v_mfma_f32_16x16x32_bf16 v[6:9], v[10:13], v[122:125], 0
	v_mfma_f32_16x16x32_bf16 v[10:13], v[18:21], v[58:61], 0
	v_mfma_f32_16x16x32_bf16 v[166:169], v[22:25], v[90:93], v[10:13]
	v_mfma_f32_16x16x32_bf16 v[10:13], v[26:29], v[58:61], 0
	v_mfma_f32_16x16x32_bf16 v[170:173], v[30:33], v[90:93], v[10:13]
	v_mfma_f32_16x16x32_bf16 v[10:13], v[18:21], v[94:97], 0
	v_mfma_f32_16x16x32_bf16 v[174:177], v[22:25], v[106:109], v[10:13]
	v_mfma_f32_16x16x32_bf16 v[10:13], v[26:29], v[94:97], 0
	v_mfma_f32_16x16x32_bf16 v[178:181], v[30:33], v[106:109], v[10:13]
	v_mfma_f32_16x16x32_bf16 v[10:13], v[18:21], v[110:113], 0
	v_mfma_f32_16x16x32_bf16 v[182:185], v[22:25], v[118:121], v[10:13]
	v_mfma_f32_16x16x32_bf16 v[10:13], v[26:29], v[110:113], 0
	v_mfma_f32_16x16x32_bf16 v[186:189], v[30:33], v[118:121], v[10:13]
	v_mfma_f32_16x16x32_bf16 v[10:13], v[18:21], v[122:125], 0
	v_mfma_f32_16x16x32_bf16 v[6:9], v[14:17], v[126:129], v[6:9]
	v_mfma_f32_16x16x32_bf16 v[190:193], v[22:25], v[126:129], v[10:13]
	v_mfma_f32_16x16x32_bf16 v[10:13], v[26:29], v[122:125], 0
	v_mfma_f32_16x16x32_bf16 v[146:149], v[14:17], v[90:93], v[146:149]
	v_mfma_f32_16x16x32_bf16 v[154:157], v[14:17], v[106:109], v[154:157]
	v_mfma_f32_16x16x32_bf16 v[162:165], v[14:17], v[118:121], v[162:165]
	v_mfma_f32_16x16x32_bf16 v[194:197], v[30:33], v[126:129], v[10:13]
	s_setprio 0
	s_barrier
	v_add_u32_e32 v140, 0x18000, v138
	v_add_u32_e32 v141, 0x1c000, v138
	ds_read_b128 v[10:13], v140
	ds_read_b128 v[14:17], v140 offset:1024
	ds_read_b128 v[18:21], v140 offset:2048
	ds_read_b128 v[22:25], v140 offset:3072
	ds_read_b128 v[198:201], v141
	ds_read_b128 v[204:207], v141 offset:1024
	ds_read_b128 v[208:211], v141 offset:2048
	ds_read_b128 v[212:215], v141 offset:3072
	s_mov_b32 m0, s10
	ds_read_b128 v[26:29], v139 offset:32768
	ds_read_b128 v[30:33], v139 offset:33792
	ds_read_b128 v[58:61], v139 offset:34816
	ds_read_b128 v[216:219], v139 offset:35840
	ds_read_b128 v[220:223], v139 offset:36864
	ds_read_b128 v[224:227], v139 offset:37888
	ds_read_b128 v[228:231], v139 offset:38912
	ds_read_b128 v[250:253], v139 offset:39936
	buffer_load_dwordx4 v132, s[64:67], vcc_lo offen lds
	s_mov_b32 m0, s21
	s_nop 0
	buffer_load_dwordx4 v134, s[64:67], vcc_lo offen lds
	s_add_i32 vcc_lo, vcc_lo, s8
	s_mov_b32 m0, s26
	s_nop 0
	buffer_load_dwordx4 v132, s[64:67], vcc_lo offen lds
	s_mov_b32 m0, s27
	s_nop 0
	buffer_load_dwordx4 v134, s[64:67], vcc_lo offen lds
	s_waitcnt vmcnt(8)
	s_waitcnt lgkmcnt(0)
	s_barrier
	s_setprio 1
	v_mfma_f32_16x16x32_bf16 v[66:69], v[10:13], v[26:29], v[66:69]
	v_mfma_f32_16x16x32_bf16 v[126:129], v[14:17], v[30:33], v[66:69]
	v_mfma_f32_16x16x32_bf16 v[66:69], v[18:21], v[26:29], v[70:73]
	v_mfma_f32_16x16x32_bf16 v[118:121], v[22:25], v[30:33], v[66:69]
	v_mfma_f32_16x16x32_bf16 v[66:69], v[10:13], v[58:61], v[74:77]
	v_mfma_f32_16x16x32_bf16 v[110:113], v[14:17], v[216:219], v[66:69]
	v_mfma_f32_16x16x32_bf16 v[66:69], v[18:21], v[58:61], v[78:81]
	v_mfma_f32_16x16x32_bf16 v[106:109], v[22:25], v[216:219], v[66:69]
	v_mfma_f32_16x16x32_bf16 v[66:69], v[10:13], v[220:223], v[82:85]
	v_mfma_f32_16x16x32_bf16 v[94:97], v[14:17], v[224:227], v[66:69]
	v_mfma_f32_16x16x32_bf16 v[66:69], v[18:21], v[220:223], v[86:89]
	v_mfma_f32_16x16x32_bf16 v[70:73], v[198:201], v[26:29], v[114:117]
	v_mfma_f32_16x16x32_bf16 v[26:29], v[208:211], v[26:29], v[34:37]
	v_mfma_f32_16x16x32_bf16 v[90:93], v[22:25], v[224:227], v[66:69]
	v_mfma_f32_16x16x32_bf16 v[66:69], v[10:13], v[228:231], v[98:101]
	v_mfma_f32_16x16x32_bf16 v[114:117], v[212:215], v[30:33], v[26:29]
	v_mfma_f32_16x16x32_bf16 v[26:29], v[198:201], v[58:61], v[38:41]
	v_mfma_f32_16x16x32_bf16 v[74:77], v[14:17], v[250:253], v[66:69]
	v_mfma_f32_16x16x32_bf16 v[66:69], v[18:21], v[228:231], v[102:105]
	v_mfma_f32_16x16x32_bf16 v[102:105], v[204:207], v[216:219], v[26:29]
	v_mfma_f32_16x16x32_bf16 v[26:29], v[208:211], v[58:61], v[42:45]
	v_mfma_f32_16x16x32_bf16 v[98:101], v[212:215], v[216:219], v[26:29]
	v_mfma_f32_16x16x32_bf16 v[26:29], v[198:201], v[220:223], v[46:49]
	v_mfma_f32_16x16x32_bf16 v[86:89], v[204:207], v[224:227], v[26:29]
	v_mfma_f32_16x16x32_bf16 v[26:29], v[208:211], v[220:223], v[50:53]
	v_mfma_f32_16x16x32_bf16 v[82:85], v[212:215], v[224:227], v[26:29]
	v_mfma_f32_16x16x32_bf16 v[26:29], v[198:201], v[228:231], v[54:57]
	v_mfma_f32_16x16x32_bf16 v[58:61], v[204:207], v[250:253], v[26:29]
	v_mfma_f32_16x16x32_bf16 v[26:29], v[208:211], v[228:231], v[62:65]
	v_mfma_f32_16x16x32_bf16 v[66:69], v[22:25], v[250:253], v[66:69]
	v_mfma_f32_16x16x32_bf16 v[122:125], v[204:207], v[30:33], v[70:73]
	v_mfma_f32_16x16x32_bf16 v[50:53], v[212:215], v[250:253], v[26:29]
	s_setprio 0
	s_barrier
	s_mov_b32 m0, s40
	s_addk_i32 s15, 0x80
	ds_read_b128 v[34:37], v139 offset:49152
	ds_read_b128 v[38:41], v139 offset:50176
	ds_read_b128 v[216:219], v139 offset:51200
	ds_read_b128 v[220:223], v139 offset:52224
	ds_read_b128 v[224:227], v139 offset:53248
	ds_read_b128 v[228:231], v139 offset:54272
	ds_read_b128 v[250:253], v139 offset:55296
	ds_read_b128 v[244:247], v139 offset:56320
	buffer_load_dwordx4 v133, s[0:3], s15 offen lds
	s_mov_b32 m0, s43
	s_nop 0
	buffer_load_dwordx4 v135, s[0:3], s15 offen lds
	s_add_i32 s15, s15, s8
	s_mov_b32 m0, s52
	s_nop 0
	buffer_load_dwordx4 v133, s[0:3], s15 offen lds
	s_mov_b32 m0, s72
	s_nop 0
	buffer_load_dwordx4 v135, s[0:3], s15 offen lds
	s_waitcnt vmcnt(6)
	s_waitcnt lgkmcnt(0)
	s_barrier
	s_setprio 1
	v_mfma_f32_16x16x32_bf16 v[26:29], v[10:13], v[34:37], v[142:145]
	v_mfma_f32_16x16x32_bf16 v[78:81], v[14:17], v[38:41], v[26:29]
	v_mfma_f32_16x16x32_bf16 v[26:29], v[18:21], v[34:37], v[146:149]
	v_mfma_f32_16x16x32_bf16 v[70:73], v[22:25], v[38:41], v[26:29]
	v_mfma_f32_16x16x32_bf16 v[26:29], v[10:13], v[216:219], v[150:153]
	v_mfma_f32_16x16x32_bf16 v[46:49], v[14:17], v[220:223], v[26:29]
	v_mfma_f32_16x16x32_bf16 v[26:29], v[18:21], v[216:219], v[154:157]
	v_mfma_f32_16x16x32_bf16 v[42:45], v[22:25], v[220:223], v[26:29]
	v_mfma_f32_16x16x32_bf16 v[26:29], v[10:13], v[224:227], v[158:161]
	v_mfma_f32_16x16x32_bf16 v[2:5], v[10:13], v[250:253], v[2:5]
	v_mfma_f32_16x16x32_bf16 v[30:33], v[14:17], v[228:231], v[26:29]
	v_mfma_f32_16x16x32_bf16 v[14:17], v[14:17], v[244:247], v[2:5]
	v_mfma_f32_16x16x32_bf16 v[2:5], v[18:21], v[250:253], v[6:9]
	v_mfma_f32_16x16x32_bf16 v[10:13], v[22:25], v[244:247], v[2:5]
	v_mfma_f32_16x16x32_bf16 v[2:5], v[198:201], v[34:37], v[166:169]
	v_mfma_f32_16x16x32_bf16 v[62:65], v[204:207], v[38:41], v[2:5]
	v_mfma_f32_16x16x32_bf16 v[2:5], v[208:211], v[34:37], v[170:173]
	v_mfma_f32_16x16x32_bf16 v[54:57], v[212:215], v[38:41], v[2:5]
	v_mfma_f32_16x16x32_bf16 v[2:5], v[198:201], v[216:219], v[174:177]
	v_mfma_f32_16x16x32_bf16 v[38:41], v[204:207], v[220:223], v[2:5]
	v_mfma_f32_16x16x32_bf16 v[2:5], v[208:211], v[216:219], v[178:181]
	v_mfma_f32_16x16x32_bf16 v[26:29], v[18:21], v[224:227], v[162:165]
	v_mfma_f32_16x16x32_bf16 v[34:37], v[212:215], v[220:223], v[2:5]
	v_mfma_f32_16x16x32_bf16 v[2:5], v[198:201], v[224:227], v[182:185]
	v_mfma_f32_16x16x32_bf16 v[26:29], v[22:25], v[228:231], v[26:29]
	v_mfma_f32_16x16x32_bf16 v[22:25], v[204:207], v[228:231], v[2:5]
	v_mfma_f32_16x16x32_bf16 v[2:5], v[208:211], v[224:227], v[186:189]
	v_mfma_f32_16x16x32_bf16 v[18:21], v[212:215], v[228:231], v[2:5]
	v_mfma_f32_16x16x32_bf16 v[2:5], v[198:201], v[250:253], v[190:193]
	v_mfma_f32_16x16x32_bf16 v[6:9], v[204:207], v[244:247], v[2:5]
	v_mfma_f32_16x16x32_bf16 v[2:5], v[208:211], v[250:253], v[194:197]
	v_mfma_f32_16x16x32_bf16 v[2:5], v[212:215], v[244:247], v[2:5]
	s_setprio 0
	s_barrier
	s_andn2_b64 vcc, exec, s[34:35]
	s_cbranch_vccnz .LBB0_264
	s_add_i32 s15, s84, 0x200
	s_addk_i32 s83, 0x180
	s_mov_b32 s84, 4
.LBB0_263:
	ds_read_b128 v[142:145], v130
	ds_read_b128 v[146:149], v130 offset:1024
	ds_read_b128 v[150:153], v130 offset:2048
	ds_read_b128 v[154:157], v130 offset:3072
	ds_read_b128 v[158:161], v131
	ds_read_b128 v[162:165], v131 offset:1024
	ds_read_b128 v[166:169], v131 offset:2048
	ds_read_b128 v[170:173], v131 offset:3072
	s_add_i32 s2, s83, 0x80
	s_cmp_eq_u32 s73, s84
	s_cselect_b32 s42, s29, s15
	s_cselect_b32 vcc_hi, s62, s2
	s_mov_b32 m0, s78
	ds_read_b128 v[174:177], v139
	ds_read_b128 v[178:181], v139 offset:1024
	ds_read_b128 v[182:185], v139 offset:2048
	ds_read_b128 v[186:189], v139 offset:3072
	ds_read_b128 v[190:193], v139 offset:4096
	ds_read_b128 v[194:197], v139 offset:5120
	ds_read_b128 v[198:201], v139 offset:6144
	ds_read_b128 v[204:207], v139 offset:7168
	buffer_load_dwordx4 v132, s[64:67], s83 offen lds
	s_mov_b32 m0, s80
	s_add_i32 s2, s8, s83
	buffer_load_dwordx4 v134, s[64:67], s83 offen lds
	s_mov_b32 m0, s79
	s_nop 0
	buffer_load_dwordx4 v132, s[64:67], s2 offen lds
	s_mov_b32 m0, s81
	s_nop 0
	buffer_load_dwordx4 v134, s[64:67], s2 offen lds
	s_waitcnt vmcnt(8)
	s_waitcnt lgkmcnt(0)
	s_barrier
	s_setprio 1
	v_mfma_f32_16x16x32_bf16 v[126:129], v[142:145], v[174:177], v[126:129]
	v_mfma_f32_16x16x32_bf16 v[118:121], v[150:153], v[174:177], v[118:121]
	v_mfma_f32_16x16x32_bf16 v[110:113], v[142:145], v[182:185], v[110:113]
	v_mfma_f32_16x16x32_bf16 v[106:109], v[150:153], v[182:185], v[106:109]
	v_mfma_f32_16x16x32_bf16 v[94:97], v[142:145], v[190:193], v[94:97]
	v_mfma_f32_16x16x32_bf16 v[90:93], v[150:153], v[190:193], v[90:93]
	v_mfma_f32_16x16x32_bf16 v[74:77], v[142:145], v[198:201], v[74:77]
	v_mfma_f32_16x16x32_bf16 v[66:69], v[150:153], v[198:201], v[66:69]
	v_mfma_f32_16x16x32_bf16 v[122:125], v[158:161], v[174:177], v[122:125]
	v_mfma_f32_16x16x32_bf16 v[114:117], v[166:169], v[174:177], v[114:117]
	v_mfma_f32_16x16x32_bf16 v[102:105], v[158:161], v[182:185], v[102:105]
	v_mfma_f32_16x16x32_bf16 v[98:101], v[166:169], v[182:185], v[98:101]
	v_mfma_f32_16x16x32_bf16 v[86:89], v[158:161], v[190:193], v[86:89]
	v_mfma_f32_16x16x32_bf16 v[82:85], v[166:169], v[190:193], v[82:85]
	v_mfma_f32_16x16x32_bf16 v[58:61], v[158:161], v[198:201], v[58:61]
	v_mfma_f32_16x16x32_bf16 v[50:53], v[166:169], v[198:201], v[50:53]
	v_mfma_f32_16x16x32_bf16 v[126:129], v[146:149], v[178:181], v[126:129]
	v_mfma_f32_16x16x32_bf16 v[118:121], v[154:157], v[178:181], v[118:121]
	v_mfma_f32_16x16x32_bf16 v[110:113], v[146:149], v[186:189], v[110:113]
	v_mfma_f32_16x16x32_bf16 v[106:109], v[154:157], v[186:189], v[106:109]
	v_mfma_f32_16x16x32_bf16 v[94:97], v[146:149], v[194:197], v[94:97]
	v_mfma_f32_16x16x32_bf16 v[90:93], v[154:157], v[194:197], v[90:93]
	v_mfma_f32_16x16x32_bf16 v[74:77], v[146:149], v[204:207], v[74:77]
	v_mfma_f32_16x16x32_bf16 v[66:69], v[154:157], v[204:207], v[66:69]
	v_mfma_f32_16x16x32_bf16 v[122:125], v[162:165], v[178:181], v[122:125]
	v_mfma_f32_16x16x32_bf16 v[114:117], v[170:173], v[178:181], v[114:117]
	v_mfma_f32_16x16x32_bf16 v[102:105], v[162:165], v[186:189], v[102:105]
	v_mfma_f32_16x16x32_bf16 v[98:101], v[170:173], v[186:189], v[98:101]
	v_mfma_f32_16x16x32_bf16 v[86:89], v[162:165], v[194:197], v[86:89]
	v_mfma_f32_16x16x32_bf16 v[82:85], v[170:173], v[194:197], v[82:85]
	v_mfma_f32_16x16x32_bf16 v[58:61], v[162:165], v[204:207], v[58:61]
	v_mfma_f32_16x16x32_bf16 v[50:53], v[170:173], v[204:207], v[50:53]
	s_setprio 0
	s_barrier
	s_mov_b32 m0, s11
	s_mov_b32 s2, s66
	s_mov_b32 s3, s67
	ds_read_b128 v[174:177], v139 offset:16384
	ds_read_b128 v[178:181], v139 offset:17408
	ds_read_b128 v[182:185], v139 offset:18432
	ds_read_b128 v[186:189], v139 offset:19456
	ds_read_b128 v[190:193], v139 offset:20480
	ds_read_b128 v[194:197], v139 offset:21504
	ds_read_b128 v[198:201], v139 offset:22528
	ds_read_b128 v[204:207], v139 offset:23552
	buffer_load_dwordx4 v133, s[0:3], s42 offen lds
	s_mov_b32 m0, s12
	s_add_i32 vcc_lo, s42, s8
	buffer_load_dwordx4 v135, s[0:3], s42 offen lds
	s_mov_b32 m0, s13
	s_nop 0
	buffer_load_dwordx4 v133, s[0:3], vcc_lo offen lds
	s_mov_b32 m0, s20
	s_nop 0
	buffer_load_dwordx4 v135, s[0:3], vcc_lo offen lds
	s_waitcnt vmcnt(6)
	s_waitcnt lgkmcnt(0)
	s_barrier
	s_setprio 1
	v_mfma_f32_16x16x32_bf16 v[78:81], v[142:145], v[174:177], v[78:81]
	v_mfma_f32_16x16x32_bf16 v[70:73], v[150:153], v[174:177], v[70:73]
	v_mfma_f32_16x16x32_bf16 v[46:49], v[142:145], v[182:185], v[46:49]
	v_mfma_f32_16x16x32_bf16 v[42:45], v[150:153], v[182:185], v[42:45]
	v_mfma_f32_16x16x32_bf16 v[30:33], v[142:145], v[190:193], v[30:33]
	v_mfma_f32_16x16x32_bf16 v[26:29], v[150:153], v[190:193], v[26:29]
	v_mfma_f32_16x16x32_bf16 v[14:17], v[142:145], v[198:201], v[14:17]
	v_mfma_f32_16x16x32_bf16 v[10:13], v[150:153], v[198:201], v[10:13]
	v_mfma_f32_16x16x32_bf16 v[62:65], v[158:161], v[174:177], v[62:65]
	v_mfma_f32_16x16x32_bf16 v[54:57], v[166:169], v[174:177], v[54:57]
	v_mfma_f32_16x16x32_bf16 v[38:41], v[158:161], v[182:185], v[38:41]
	v_mfma_f32_16x16x32_bf16 v[34:37], v[166:169], v[182:185], v[34:37]
	v_mfma_f32_16x16x32_bf16 v[22:25], v[158:161], v[190:193], v[22:25]
	v_mfma_f32_16x16x32_bf16 v[18:21], v[166:169], v[190:193], v[18:21]
	v_mfma_f32_16x16x32_bf16 v[6:9], v[158:161], v[198:201], v[6:9]
	v_mfma_f32_16x16x32_bf16 v[2:5], v[166:169], v[198:201], v[2:5]
	v_mfma_f32_16x16x32_bf16 v[78:81], v[146:149], v[178:181], v[78:81]
	v_mfma_f32_16x16x32_bf16 v[70:73], v[154:157], v[178:181], v[70:73]
	v_mfma_f32_16x16x32_bf16 v[46:49], v[146:149], v[186:189], v[46:49]
	v_mfma_f32_16x16x32_bf16 v[42:45], v[154:157], v[186:189], v[42:45]
	v_mfma_f32_16x16x32_bf16 v[30:33], v[146:149], v[194:197], v[30:33]
	v_mfma_f32_16x16x32_bf16 v[26:29], v[154:157], v[194:197], v[26:29]
	v_mfma_f32_16x16x32_bf16 v[14:17], v[146:149], v[204:207], v[14:17]
	v_mfma_f32_16x16x32_bf16 v[10:13], v[154:157], v[204:207], v[10:13]
	v_mfma_f32_16x16x32_bf16 v[62:65], v[162:165], v[178:181], v[62:65]
	v_mfma_f32_16x16x32_bf16 v[54:57], v[170:173], v[178:181], v[54:57]
	v_mfma_f32_16x16x32_bf16 v[38:41], v[162:165], v[186:189], v[38:41]
	v_mfma_f32_16x16x32_bf16 v[34:37], v[170:173], v[186:189], v[34:37]
	v_mfma_f32_16x16x32_bf16 v[22:25], v[162:165], v[194:197], v[22:25]
	v_mfma_f32_16x16x32_bf16 v[18:21], v[170:173], v[194:197], v[18:21]
	v_mfma_f32_16x16x32_bf16 v[6:9], v[162:165], v[204:207], v[6:9]
	v_mfma_f32_16x16x32_bf16 v[2:5], v[170:173], v[204:207], v[2:5]
	s_setprio 0
	s_barrier
	ds_read_b128 v[142:145], v140
	ds_read_b128 v[146:149], v140 offset:1024
	ds_read_b128 v[150:153], v140 offset:2048
	ds_read_b128 v[154:157], v140 offset:3072
	ds_read_b128 v[158:161], v141
	ds_read_b128 v[162:165], v141 offset:1024
	ds_read_b128 v[166:169], v141 offset:2048
	ds_read_b128 v[170:173], v141 offset:3072
	s_mov_b32 m0, s10
	ds_read_b128 v[174:177], v139 offset:32768
	ds_read_b128 v[178:181], v139 offset:33792
	ds_read_b128 v[182:185], v139 offset:34816
	ds_read_b128 v[186:189], v139 offset:35840
	ds_read_b128 v[190:193], v139 offset:36864
	ds_read_b128 v[194:197], v139 offset:37888
	ds_read_b128 v[198:201], v139 offset:38912
	ds_read_b128 v[204:207], v139 offset:39936
	buffer_load_dwordx4 v132, s[64:67], vcc_hi offen lds
	s_mov_b32 m0, s21
	s_nop 0
	buffer_load_dwordx4 v134, s[64:67], vcc_hi offen lds
	s_add_i32 vcc_hi, vcc_hi, s8
	s_mov_b32 m0, s26
	s_nop 0
	buffer_load_dwordx4 v132, s[64:67], vcc_hi offen lds
	s_mov_b32 m0, s27
	s_nop 0
	buffer_load_dwordx4 v134, s[64:67], vcc_hi offen lds
	s_waitcnt vmcnt(8)
	s_waitcnt lgkmcnt(0)
	s_barrier
	s_setprio 1
	v_mfma_f32_16x16x32_bf16 v[126:129], v[142:145], v[174:177], v[126:129]
	v_mfma_f32_16x16x32_bf16 v[118:121], v[150:153], v[174:177], v[118:121]
	v_mfma_f32_16x16x32_bf16 v[110:113], v[142:145], v[182:185], v[110:113]
	v_mfma_f32_16x16x32_bf16 v[106:109], v[150:153], v[182:185], v[106:109]
	v_mfma_f32_16x16x32_bf16 v[94:97], v[142:145], v[190:193], v[94:97]
	v_mfma_f32_16x16x32_bf16 v[90:93], v[150:153], v[190:193], v[90:93]
	v_mfma_f32_16x16x32_bf16 v[74:77], v[142:145], v[198:201], v[74:77]
	v_mfma_f32_16x16x32_bf16 v[66:69], v[150:153], v[198:201], v[66:69]
	v_mfma_f32_16x16x32_bf16 v[122:125], v[158:161], v[174:177], v[122:125]
	v_mfma_f32_16x16x32_bf16 v[114:117], v[166:169], v[174:177], v[114:117]
	v_mfma_f32_16x16x32_bf16 v[102:105], v[158:161], v[182:185], v[102:105]
	v_mfma_f32_16x16x32_bf16 v[98:101], v[166:169], v[182:185], v[98:101]
	v_mfma_f32_16x16x32_bf16 v[86:89], v[158:161], v[190:193], v[86:89]
	v_mfma_f32_16x16x32_bf16 v[82:85], v[166:169], v[190:193], v[82:85]
	v_mfma_f32_16x16x32_bf16 v[58:61], v[158:161], v[198:201], v[58:61]
	v_mfma_f32_16x16x32_bf16 v[50:53], v[166:169], v[198:201], v[50:53]
	v_mfma_f32_16x16x32_bf16 v[126:129], v[146:149], v[178:181], v[126:129]
	v_mfma_f32_16x16x32_bf16 v[118:121], v[154:157], v[178:181], v[118:121]
	v_mfma_f32_16x16x32_bf16 v[110:113], v[146:149], v[186:189], v[110:113]
	v_mfma_f32_16x16x32_bf16 v[106:109], v[154:157], v[186:189], v[106:109]
	v_mfma_f32_16x16x32_bf16 v[94:97], v[146:149], v[194:197], v[94:97]
	v_mfma_f32_16x16x32_bf16 v[90:93], v[154:157], v[194:197], v[90:93]
	v_mfma_f32_16x16x32_bf16 v[74:77], v[146:149], v[204:207], v[74:77]
	v_mfma_f32_16x16x32_bf16 v[66:69], v[154:157], v[204:207], v[66:69]
	v_mfma_f32_16x16x32_bf16 v[122:125], v[162:165], v[178:181], v[122:125]
	v_mfma_f32_16x16x32_bf16 v[114:117], v[170:173], v[178:181], v[114:117]
	v_mfma_f32_16x16x32_bf16 v[102:105], v[162:165], v[186:189], v[102:105]
	v_mfma_f32_16x16x32_bf16 v[98:101], v[170:173], v[186:189], v[98:101]
	v_mfma_f32_16x16x32_bf16 v[86:89], v[162:165], v[194:197], v[86:89]
	v_mfma_f32_16x16x32_bf16 v[82:85], v[170:173], v[194:197], v[82:85]
	v_mfma_f32_16x16x32_bf16 v[58:61], v[162:165], v[204:207], v[58:61]
	v_mfma_f32_16x16x32_bf16 v[50:53], v[170:173], v[204:207], v[50:53]
	s_setprio 0
	s_barrier
	s_mov_b32 m0, s40
	s_addk_i32 s42, 0x80
	ds_read_b128 v[174:177], v139 offset:49152
	ds_read_b128 v[178:181], v139 offset:50176
	ds_read_b128 v[182:185], v139 offset:51200
	ds_read_b128 v[186:189], v139 offset:52224
	ds_read_b128 v[190:193], v139 offset:53248
	ds_read_b128 v[194:197], v139 offset:54272
	ds_read_b128 v[198:201], v139 offset:55296
	ds_read_b128 v[204:207], v139 offset:56320
	buffer_load_dwordx4 v133, s[0:3], s42 offen lds
	s_mov_b32 m0, s43
	s_nop 0
	buffer_load_dwordx4 v135, s[0:3], s42 offen lds
	s_add_i32 s42, s42, s8
	s_mov_b32 m0, s52
	s_nop 0
	buffer_load_dwordx4 v133, s[0:3], s42 offen lds
	s_mov_b32 m0, s72
	s_nop 0
	buffer_load_dwordx4 v135, s[0:3], s42 offen lds
	s_waitcnt vmcnt(6)
	s_waitcnt lgkmcnt(0)
	s_barrier
	s_setprio 1
	v_mfma_f32_16x16x32_bf16 v[78:81], v[142:145], v[174:177], v[78:81]
	v_mfma_f32_16x16x32_bf16 v[70:73], v[150:153], v[174:177], v[70:73]
	v_mfma_f32_16x16x32_bf16 v[46:49], v[142:145], v[182:185], v[46:49]
	v_mfma_f32_16x16x32_bf16 v[42:45], v[150:153], v[182:185], v[42:45]
	v_mfma_f32_16x16x32_bf16 v[30:33], v[142:145], v[190:193], v[30:33]
	v_mfma_f32_16x16x32_bf16 v[26:29], v[150:153], v[190:193], v[26:29]
	v_mfma_f32_16x16x32_bf16 v[14:17], v[142:145], v[198:201], v[14:17]
	v_mfma_f32_16x16x32_bf16 v[10:13], v[150:153], v[198:201], v[10:13]
	v_mfma_f32_16x16x32_bf16 v[62:65], v[158:161], v[174:177], v[62:65]
	v_mfma_f32_16x16x32_bf16 v[54:57], v[166:169], v[174:177], v[54:57]
	v_mfma_f32_16x16x32_bf16 v[38:41], v[158:161], v[182:185], v[38:41]
	v_mfma_f32_16x16x32_bf16 v[34:37], v[166:169], v[182:185], v[34:37]
	v_mfma_f32_16x16x32_bf16 v[22:25], v[158:161], v[190:193], v[22:25]
	v_mfma_f32_16x16x32_bf16 v[18:21], v[166:169], v[190:193], v[18:21]
	v_mfma_f32_16x16x32_bf16 v[6:9], v[158:161], v[198:201], v[6:9]
	v_mfma_f32_16x16x32_bf16 v[2:5], v[166:169], v[198:201], v[2:5]
	v_mfma_f32_16x16x32_bf16 v[78:81], v[146:149], v[178:181], v[78:81]
	v_mfma_f32_16x16x32_bf16 v[70:73], v[154:157], v[178:181], v[70:73]
	v_mfma_f32_16x16x32_bf16 v[46:49], v[146:149], v[186:189], v[46:49]
	v_mfma_f32_16x16x32_bf16 v[42:45], v[154:157], v[186:189], v[42:45]
	v_mfma_f32_16x16x32_bf16 v[30:33], v[146:149], v[194:197], v[30:33]
	v_mfma_f32_16x16x32_bf16 v[26:29], v[154:157], v[194:197], v[26:29]
	v_mfma_f32_16x16x32_bf16 v[14:17], v[146:149], v[204:207], v[14:17]
	v_mfma_f32_16x16x32_bf16 v[10:13], v[154:157], v[204:207], v[10:13]
	v_mfma_f32_16x16x32_bf16 v[62:65], v[162:165], v[178:181], v[62:65]
	v_mfma_f32_16x16x32_bf16 v[54:57], v[170:173], v[178:181], v[54:57]
	v_mfma_f32_16x16x32_bf16 v[38:41], v[162:165], v[186:189], v[38:41]
	v_mfma_f32_16x16x32_bf16 v[34:37], v[170:173], v[186:189], v[34:37]
	v_mfma_f32_16x16x32_bf16 v[22:25], v[162:165], v[194:197], v[22:25]
	v_mfma_f32_16x16x32_bf16 v[18:21], v[170:173], v[194:197], v[18:21]
	v_mfma_f32_16x16x32_bf16 v[6:9], v[162:165], v[204:207], v[6:9]
	v_mfma_f32_16x16x32_bf16 v[2:5], v[170:173], v[204:207], v[2:5]
	s_setprio 0
	s_barrier
	s_add_i32 s2, s84, 2
	s_addk_i32 s15, 0x100
	s_addk_i32 s83, 0x100
	s_cmp_ge_i32 s84, s73
	s_mov_b32 s84, s2
	s_cbranch_scc0 .LBB0_263

.LBB0_333:
	v_add_u32_e32 v105, 0x10000, v103
	s_waitcnt vmcnt(18)
	v_add_u32_e32 v170, 0x14000, v103
	ds_read_b128 v[2:5], v105
	ds_read_b128 v[6:9], v105 offset:1024
	ds_read_b128 v[10:13], v105 offset:2048
	ds_read_b128 v[14:17], v105 offset:3072
	ds_read_b128 v[18:21], v170
	ds_read_b128 v[22:25], v170 offset:1024
	ds_read_b128 v[26:29], v170 offset:2048
	ds_read_b128 v[30:33], v170 offset:3072
	s_or_b32 s77, s46, 0x80
	s_or_b32 s78, s13, 0x100
	s_mul_i32 s62, s60, 0x160000
	s_and_b64 s[6:7], s[36:37], exec
	s_cselect_b32 s72, s62, s46
	s_or_b32 s76, s46, 0x100
	s_mul_i32 s63, s59, 0x160000
	s_and_b64 s[6:7], s[36:37], exec
	s_cselect_b32 s73, s63, s13
	s_mov_b32 m0, s54
	ds_read_b128 v[42:45], v104
	ds_read_b128 v[46:49], v104 offset:1024
	ds_read_b128 v[50:53], v104 offset:2048
	ds_read_b128 v[54:57], v104 offset:3072
	ds_read_b128 v[58:61], v104 offset:4096
	ds_read_b128 v[62:65], v104 offset:5120
	ds_read_b128 v[90:93], v104 offset:6144
	ds_read_b128 v[94:97], v104 offset:7168
	buffer_load_dwordx4 v99, s[64:67], s77 offen lds
	s_mov_b32 m0, s56
	s_add_i32 s6, s46, 0xb0080
	buffer_load_dwordx4 v101, s[64:67], s77 offen lds
	s_mov_b32 m0, s55
	s_nop 0
	buffer_load_dwordx4 v99, s[64:67], s6 offen lds
	s_mov_b32 m0, s57
	s_nop 0
	buffer_load_dwordx4 v101, s[64:67], s6 offen lds
	s_waitcnt vmcnt(8)
	s_waitcnt lgkmcnt(0)
	s_barrier
	s_setprio 1
	v_mfma_scale_f32_16x16x128_f8f6f4 v[34:37], v[2:9], v[42:49], 0, v237, v237 op_sel_hi:[0,0,0]
	v_mfma_scale_f32_16x16x128_f8f6f4 v[38:41], v[10:17], v[42:49], 0, v237, v237 op_sel_hi:[0,0,0]
	v_mfma_scale_f32_16x16x128_f8f6f4 v[70:73], v[2:9], v[50:57], 0, v237, v237 op_sel_hi:[0,0,0]
	v_mfma_scale_f32_16x16x128_f8f6f4 v[66:69], v[10:17], v[50:57], 0, v237, v237 op_sel_hi:[0,0,0]
	v_mfma_scale_f32_16x16x128_f8f6f4 v[78:81], v[2:9], v[58:65], 0, v237, v237 op_sel_hi:[0,0,0]
	v_mfma_scale_f32_16x16x128_f8f6f4 v[74:77], v[10:17], v[58:65], 0, v237, v237 op_sel_hi:[0,0,0]
	v_mfma_scale_f32_16x16x128_f8f6f4 v[118:121], v[2:9], v[90:97], 0, v237, v237 op_sel_hi:[0,0,0]
	v_mfma_scale_f32_16x16x128_f8f6f4 v[114:117], v[10:17], v[90:97], 0, v237, v237 op_sel_hi:[0,0,0]
	v_mfma_scale_f32_16x16x128_f8f6f4 v[82:85], v[18:25], v[42:49], 0, v237, v237 op_sel_hi:[0,0,0]
	v_mfma_scale_f32_16x16x128_f8f6f4 v[86:89], v[26:33], v[42:49], 0, v237, v237 op_sel_hi:[0,0,0]
	s_waitcnt vmcnt(21)
	v_mfma_scale_f32_16x16x128_f8f6f4 v[166:169], v[18:25], v[50:57], 0, v237, v237 op_sel_hi:[0,0,0]
	s_waitcnt vmcnt(20)
	v_mfma_scale_f32_16x16x128_f8f6f4 v[162:165], v[26:33], v[50:57], 0, v237, v237 op_sel_hi:[0,0,0]
	v_mfma_scale_f32_16x16x128_f8f6f4 v[158:161], v[18:25], v[58:65], 0, v237, v237 op_sel_hi:[0,0,0]
	v_mfma_scale_f32_16x16x128_f8f6f4 v[154:157], v[26:33], v[58:65], 0, v237, v237 op_sel_hi:[0,0,0]
	v_mfma_scale_f32_16x16x128_f8f6f4 v[126:129], v[18:25], v[90:97], 0, v237, v237 op_sel_hi:[0,0,0]
	v_mfma_scale_f32_16x16x128_f8f6f4 v[122:125], v[26:33], v[90:97], 0, v237, v237 op_sel_hi:[0,0,0]
	s_setprio 0
	s_barrier
	s_mov_b32 m0, s12
	s_mov_b32 s6, s66
	s_mov_b32 s7, s67
	ds_read_b128 v[106:109], v104 offset:16384
	ds_read_b128 v[110:113], v104 offset:17408
	s_waitcnt vmcnt(16)
	ds_read_b128 v[138:141], v104 offset:18432
	ds_read_b128 v[142:145], v104 offset:19456
	ds_read_b128 v[172:175], v104 offset:20480
	ds_read_b128 v[176:179], v104 offset:21504
	ds_read_b128 v[180:183], v104 offset:22528
	ds_read_b128 v[184:187], v104 offset:23552
	buffer_load_dwordx4 v100, s[4:7], s78 offen lds
	s_mov_b32 m0, s20
	s_add_i32 s77, s13, 0xb0100
	buffer_load_dwordx4 v102, s[4:7], s78 offen lds
	s_mov_b32 m0, s21
	s_nop 0
	buffer_load_dwordx4 v100, s[4:7], s77 offen lds
	s_mov_b32 m0, s40
	s_nop 0
	buffer_load_dwordx4 v102, s[4:7], s77 offen lds
	s_waitcnt vmcnt(6)
	s_waitcnt lgkmcnt(0)
	s_barrier
	s_setprio 1
	v_mfma_scale_f32_16x16x128_f8f6f4 v[46:49], v[2:9], v[106:113], 0, v237, v237 op_sel_hi:[0,0,0]
	v_mfma_scale_f32_16x16x128_f8f6f4 v[42:45], v[10:17], v[106:113], 0, v237, v237 op_sel_hi:[0,0,0]
	v_mfma_scale_f32_16x16x128_f8f6f4 v[54:57], v[2:9], v[138:145], 0, v237, v237 op_sel_hi:[0,0,0]
	v_mfma_scale_f32_16x16x128_f8f6f4 v[50:53], v[10:17], v[138:145], 0, v237, v237 op_sel_hi:[0,0,0]
	v_mfma_scale_f32_16x16x128_f8f6f4 v[94:97], v[2:9], v[172:179], 0, v237, v237 op_sel_hi:[0,0,0]
	v_mfma_scale_f32_16x16x128_f8f6f4 v[90:93], v[10:17], v[172:179], 0, v237, v237 op_sel_hi:[0,0,0]
	v_mfma_scale_f32_16x16x128_f8f6f4 v[134:137], v[2:9], v[180:187], 0, v237, v237 op_sel_hi:[0,0,0]
	v_mfma_scale_f32_16x16x128_f8f6f4 v[130:133], v[10:17], v[180:187], 0, v237, v237 op_sel_hi:[0,0,0]
	v_mfma_scale_f32_16x16x128_f8f6f4 v[62:65], v[18:25], v[106:113], 0, v237, v237 op_sel_hi:[0,0,0]
	v_mfma_scale_f32_16x16x128_f8f6f4 v[58:61], v[26:33], v[106:113], 0, v237, v237 op_sel_hi:[0,0,0]
	v_mfma_scale_f32_16x16x128_f8f6f4 v[110:113], v[18:25], v[138:145], 0, v237, v237 op_sel_hi:[0,0,0]
	v_mfma_scale_f32_16x16x128_f8f6f4 v[106:109], v[26:33], v[138:145], 0, v237, v237 op_sel_hi:[0,0,0]
	v_mfma_scale_f32_16x16x128_f8f6f4 v[150:153], v[18:25], v[172:179], 0, v237, v237 op_sel_hi:[0,0,0]
	v_mfma_scale_f32_16x16x128_f8f6f4 v[146:149], v[26:33], v[172:179], 0, v237, v237 op_sel_hi:[0,0,0]
	v_mfma_scale_f32_16x16x128_f8f6f4 v[142:145], v[18:25], v[180:187], 0, v237, v237 op_sel_hi:[0,0,0]
	v_mfma_scale_f32_16x16x128_f8f6f4 v[138:141], v[26:33], v[180:187], 0, v237, v237 op_sel_hi:[0,0,0]
	s_setprio 0
	s_barrier
	v_add_u32_e32 v171, 0x18000, v103
	v_add_u32_e32 v172, 0x1c000, v103
	ds_read_b128 v[26:29], v171
	ds_read_b128 v[30:33], v171 offset:1024
	ds_read_b128 v[18:21], v171 offset:2048
	ds_read_b128 v[22:25], v171 offset:3072
	ds_read_b128 v[10:13], v172
	ds_read_b128 v[14:17], v172 offset:1024
	ds_read_b128 v[2:5], v172 offset:2048
	ds_read_b128 v[6:9], v172 offset:3072
	s_mov_b32 m0, s11
	ds_read_b128 v[174:177], v104 offset:32768
	ds_read_b128 v[178:181], v104 offset:33792
	ds_read_b128 v[182:185], v104 offset:34816
	ds_read_b128 v[186:189], v104 offset:35840
	ds_read_b128 v[190:193], v104 offset:36864
	ds_read_b128 v[194:197], v104 offset:37888
	ds_read_b128 v[204:207], v104 offset:38912
	ds_read_b128 v[208:211], v104 offset:39936
	buffer_load_dwordx4 v99, s[64:67], s76 offen lds
	s_mov_b32 m0, s45
	s_nop 0
	buffer_load_dwordx4 v101, s[64:67], s76 offen lds
	s_add_i32 s76, s46, 0xb0100
	s_mov_b32 m0, s47
	s_nop 0
	buffer_load_dwordx4 v99, s[64:67], s76 offen lds
	s_mov_b32 m0, s48
	s_nop 0
	buffer_load_dwordx4 v101, s[64:67], s76 offen lds
	s_waitcnt vmcnt(8)
	s_waitcnt lgkmcnt(0)
	s_barrier
	s_setprio 1
	v_mfma_scale_f32_16x16x128_f8f6f4 v[34:37], v[26:33], v[174:181], v[34:37], v237, v237 op_sel_hi:[0,0,0]
	v_mfma_scale_f32_16x16x128_f8f6f4 v[38:41], v[18:25], v[174:181], v[38:41], v237, v237 op_sel_hi:[0,0,0]
	v_mfma_scale_f32_16x16x128_f8f6f4 v[70:73], v[26:33], v[182:189], v[70:73], v237, v237 op_sel_hi:[0,0,0]
	v_mfma_scale_f32_16x16x128_f8f6f4 v[66:69], v[18:25], v[182:189], v[66:69], v237, v237 op_sel_hi:[0,0,0]
	v_mfma_scale_f32_16x16x128_f8f6f4 v[78:81], v[26:33], v[190:197], v[78:81], v237, v237 op_sel_hi:[0,0,0]
	v_mfma_scale_f32_16x16x128_f8f6f4 v[74:77], v[18:25], v[190:197], v[74:77], v237, v237 op_sel_hi:[0,0,0]
	v_mfma_scale_f32_16x16x128_f8f6f4 v[118:121], v[26:33], v[204:211], v[118:121], v237, v237 op_sel_hi:[0,0,0]
	v_mfma_scale_f32_16x16x128_f8f6f4 v[114:117], v[18:25], v[204:211], v[114:117], v237, v237 op_sel_hi:[0,0,0]
	v_mfma_scale_f32_16x16x128_f8f6f4 v[82:85], v[10:17], v[174:181], v[82:85], v237, v237 op_sel_hi:[0,0,0]
	v_mfma_scale_f32_16x16x128_f8f6f4 v[86:89], v[2:9], v[174:181], v[86:89], v237, v237 op_sel_hi:[0,0,0]
	v_mfma_scale_f32_16x16x128_f8f6f4 v[166:169], v[10:17], v[182:189], v[166:169], v237, v237 op_sel_hi:[0,0,0]
	v_mfma_scale_f32_16x16x128_f8f6f4 v[162:165], v[2:9], v[182:189], v[162:165], v237, v237 op_sel_hi:[0,0,0]
	v_mfma_scale_f32_16x16x128_f8f6f4 v[158:161], v[10:17], v[190:197], v[158:161], v237, v237 op_sel_hi:[0,0,0]
	v_mfma_scale_f32_16x16x128_f8f6f4 v[154:157], v[2:9], v[190:197], v[154:157], v237, v237 op_sel_hi:[0,0,0]
	v_mfma_scale_f32_16x16x128_f8f6f4 v[126:129], v[10:17], v[204:211], v[126:129], v237, v237 op_sel_hi:[0,0,0]
	v_mfma_scale_f32_16x16x128_f8f6f4 v[122:125], v[2:9], v[204:211], v[122:125], v237, v237 op_sel_hi:[0,0,0]
	s_setprio 0
	s_barrier
	s_mov_b32 m0, s50
	s_or_b32 s76, s13, 0x180
	ds_read_b128 v[174:177], v104 offset:49152
	ds_read_b128 v[178:181], v104 offset:50176
	ds_read_b128 v[182:185], v104 offset:51200
	ds_read_b128 v[186:189], v104 offset:52224
	ds_read_b128 v[190:193], v104 offset:53248
	ds_read_b128 v[194:197], v104 offset:54272
	ds_read_b128 v[204:207], v104 offset:55296
	ds_read_b128 v[208:211], v104 offset:56320
	buffer_load_dwordx4 v100, s[4:7], s76 offen lds
	s_mov_b32 m0, s51
	s_nop 0
	buffer_load_dwordx4 v102, s[4:7], s76 offen lds
	s_add_i32 s76, s13, 0xb0180
	s_mov_b32 m0, s52
	s_nop 0
	buffer_load_dwordx4 v100, s[4:7], s76 offen lds
	s_mov_b32 m0, s53
	s_nop 0
	buffer_load_dwordx4 v102, s[4:7], s76 offen lds
	s_waitcnt vmcnt(6)
	s_waitcnt lgkmcnt(0)
	s_barrier
	s_setprio 1
	v_mfma_scale_f32_16x16x128_f8f6f4 v[46:49], v[26:33], v[174:181], v[46:49], v237, v237 op_sel_hi:[0,0,0]
	v_mfma_scale_f32_16x16x128_f8f6f4 v[42:45], v[18:25], v[174:181], v[42:45], v237, v237 op_sel_hi:[0,0,0]
	v_mfma_scale_f32_16x16x128_f8f6f4 v[54:57], v[26:33], v[182:189], v[54:57], v237, v237 op_sel_hi:[0,0,0]
	v_mfma_scale_f32_16x16x128_f8f6f4 v[50:53], v[18:25], v[182:189], v[50:53], v237, v237 op_sel_hi:[0,0,0]
	v_mfma_scale_f32_16x16x128_f8f6f4 v[94:97], v[26:33], v[190:197], v[94:97], v237, v237 op_sel_hi:[0,0,0]
	v_mfma_scale_f32_16x16x128_f8f6f4 v[90:93], v[18:25], v[190:197], v[90:93], v237, v237 op_sel_hi:[0,0,0]
	v_mfma_scale_f32_16x16x128_f8f6f4 v[134:137], v[26:33], v[204:211], v[134:137], v237, v237 op_sel_hi:[0,0,0]
	v_mfma_scale_f32_16x16x128_f8f6f4 v[130:133], v[18:25], v[204:211], v[130:133], v237, v237 op_sel_hi:[0,0,0]
	v_mfma_scale_f32_16x16x128_f8f6f4 v[62:65], v[10:17], v[174:181], v[62:65], v237, v237 op_sel_hi:[0,0,0]
	v_mfma_scale_f32_16x16x128_f8f6f4 v[58:61], v[2:9], v[174:181], v[58:61], v237, v237 op_sel_hi:[0,0,0]
	v_mfma_scale_f32_16x16x128_f8f6f4 v[110:113], v[10:17], v[182:189], v[110:113], v237, v237 op_sel_hi:[0,0,0]
	v_mfma_scale_f32_16x16x128_f8f6f4 v[106:109], v[2:9], v[182:189], v[106:109], v237, v237 op_sel_hi:[0,0,0]
	v_mfma_scale_f32_16x16x128_f8f6f4 v[150:153], v[10:17], v[190:197], v[150:153], v237, v237 op_sel_hi:[0,0,0]
	v_mfma_scale_f32_16x16x128_f8f6f4 v[146:149], v[2:9], v[190:197], v[146:149], v237, v237 op_sel_hi:[0,0,0]
	v_mfma_scale_f32_16x16x128_f8f6f4 v[142:145], v[10:17], v[204:211], v[142:145], v237, v237 op_sel_hi:[0,0,0]
	v_mfma_scale_f32_16x16x128_f8f6f4 v[138:141], v[2:9], v[204:211], v[138:141], v237, v237 op_sel_hi:[0,0,0]
	s_setprio 0
	s_barrier
	s_mov_b32 s76, 0
	s_movk_i32 s77, 0xec00
.LBB0_334:
	ds_read_b128 v[2:5], v105
	ds_read_b128 v[6:9], v105 offset:1024
	ds_read_b128 v[10:13], v105 offset:2048
	ds_read_b128 v[14:17], v105 offset:3072
	ds_read_b128 v[18:21], v170
	ds_read_b128 v[22:25], v170 offset:1024
	ds_read_b128 v[26:29], v170 offset:2048
	ds_read_b128 v[30:33], v170 offset:3072
	s_add_i32 s80, s46, s77
	s_add_i32 s78, s13, s77
	s_add_i32 s79, s80, 0x1600
	s_addk_i32 s78, 0x1600
	s_cmp_eq_u32 s77, 0
	s_cselect_b32 s78, s73, s78
	s_cselect_b32 s79, s72, s79
	s_add_i32 s81, s80, 0x1580
	s_mov_b32 m0, s54
	ds_read_b128 v[174:177], v104
	ds_read_b128 v[178:181], v104 offset:1024
	ds_read_b128 v[182:185], v104 offset:2048
	ds_read_b128 v[186:189], v104 offset:3072
	ds_read_b128 v[190:193], v104 offset:4096
	ds_read_b128 v[194:197], v104 offset:5120
	ds_read_b128 v[204:207], v104 offset:6144
	ds_read_b128 v[208:211], v104 offset:7168
	buffer_load_dwordx4 v99, s[64:67], s81 offen lds
	s_mov_b32 m0, s56
	s_add_i32 s80, s80, 0xb1580
	buffer_load_dwordx4 v101, s[64:67], s81 offen lds
	s_mov_b32 m0, s55
	s_nop 0
	buffer_load_dwordx4 v99, s[64:67], s80 offen lds
	s_mov_b32 m0, s57
	s_nop 0
	buffer_load_dwordx4 v101, s[64:67], s80 offen lds
	s_waitcnt vmcnt(8)
	s_waitcnt lgkmcnt(0)
	s_barrier
	s_setprio 1
	v_mfma_scale_f32_16x16x128_f8f6f4 v[34:37], v[2:9], v[174:181], v[34:37], v237, v237 op_sel_hi:[0,0,0]
	v_mfma_scale_f32_16x16x128_f8f6f4 v[38:41], v[10:17], v[174:181], v[38:41], v237, v237 op_sel_hi:[0,0,0]
	v_mfma_scale_f32_16x16x128_f8f6f4 v[70:73], v[2:9], v[182:189], v[70:73], v237, v237 op_sel_hi:[0,0,0]
	v_mfma_scale_f32_16x16x128_f8f6f4 v[66:69], v[10:17], v[182:189], v[66:69], v237, v237 op_sel_hi:[0,0,0]
	v_mfma_scale_f32_16x16x128_f8f6f4 v[78:81], v[2:9], v[190:197], v[78:81], v237, v237 op_sel_hi:[0,0,0]
	v_mfma_scale_f32_16x16x128_f8f6f4 v[74:77], v[10:17], v[190:197], v[74:77], v237, v237 op_sel_hi:[0,0,0]
	v_mfma_scale_f32_16x16x128_f8f6f4 v[118:121], v[2:9], v[204:211], v[118:121], v237, v237 op_sel_hi:[0,0,0]
	v_mfma_scale_f32_16x16x128_f8f6f4 v[114:117], v[10:17], v[204:211], v[114:117], v237, v237 op_sel_hi:[0,0,0]
	v_mfma_scale_f32_16x16x128_f8f6f4 v[82:85], v[18:25], v[174:181], v[82:85], v237, v237 op_sel_hi:[0,0,0]
	v_mfma_scale_f32_16x16x128_f8f6f4 v[86:89], v[26:33], v[174:181], v[86:89], v237, v237 op_sel_hi:[0,0,0]
	v_mfma_scale_f32_16x16x128_f8f6f4 v[166:169], v[18:25], v[182:189], v[166:169], v237, v237 op_sel_hi:[0,0,0]
	v_mfma_scale_f32_16x16x128_f8f6f4 v[162:165], v[26:33], v[182:189], v[162:165], v237, v237 op_sel_hi:[0,0,0]
	v_mfma_scale_f32_16x16x128_f8f6f4 v[158:161], v[18:25], v[190:197], v[158:161], v237, v237 op_sel_hi:[0,0,0]
	v_mfma_scale_f32_16x16x128_f8f6f4 v[154:157], v[26:33], v[190:197], v[154:157], v237, v237 op_sel_hi:[0,0,0]
	v_mfma_scale_f32_16x16x128_f8f6f4 v[126:129], v[18:25], v[204:211], v[126:129], v237, v237 op_sel_hi:[0,0,0]
	v_mfma_scale_f32_16x16x128_f8f6f4 v[122:125], v[26:33], v[204:211], v[122:125], v237, v237 op_sel_hi:[0,0,0]
	s_setprio 0
	s_barrier
	s_mov_b32 m0, s12
	ds_read_b128 v[174:177], v104 offset:16384
	ds_read_b128 v[178:181], v104 offset:17408
	ds_read_b128 v[182:185], v104 offset:18432
	ds_read_b128 v[186:189], v104 offset:19456
	ds_read_b128 v[190:193], v104 offset:20480
	ds_read_b128 v[194:197], v104 offset:21504
	ds_read_b128 v[204:207], v104 offset:22528
	ds_read_b128 v[208:211], v104 offset:23552
	buffer_load_dwordx4 v100, s[4:7], s78 offen lds
	s_mov_b32 m0, s20
	s_add_i32 s80, s78, 0xb0000
	buffer_load_dwordx4 v102, s[4:7], s78 offen lds
	s_mov_b32 m0, s21
	s_nop 0
	buffer_load_dwordx4 v100, s[4:7], s80 offen lds
	s_mov_b32 m0, s40
	s_nop 0
	buffer_load_dwordx4 v102, s[4:7], s80 offen lds
	s_waitcnt vmcnt(6)
	s_waitcnt lgkmcnt(0)
	s_barrier
	s_setprio 1
	v_mfma_scale_f32_16x16x128_f8f6f4 v[46:49], v[2:9], v[174:181], v[46:49], v237, v237 op_sel_hi:[0,0,0]
	v_mfma_scale_f32_16x16x128_f8f6f4 v[42:45], v[10:17], v[174:181], v[42:45], v237, v237 op_sel_hi:[0,0,0]
	v_mfma_scale_f32_16x16x128_f8f6f4 v[54:57], v[2:9], v[182:189], v[54:57], v237, v237 op_sel_hi:[0,0,0]
	v_mfma_scale_f32_16x16x128_f8f6f4 v[50:53], v[10:17], v[182:189], v[50:53], v237, v237 op_sel_hi:[0,0,0]
	v_mfma_scale_f32_16x16x128_f8f6f4 v[94:97], v[2:9], v[190:197], v[94:97], v237, v237 op_sel_hi:[0,0,0]
	v_mfma_scale_f32_16x16x128_f8f6f4 v[90:93], v[10:17], v[190:197], v[90:93], v237, v237 op_sel_hi:[0,0,0]
	v_mfma_scale_f32_16x16x128_f8f6f4 v[134:137], v[2:9], v[204:211], v[134:137], v237, v237 op_sel_hi:[0,0,0]
	v_mfma_scale_f32_16x16x128_f8f6f4 v[130:133], v[10:17], v[204:211], v[130:133], v237, v237 op_sel_hi:[0,0,0]
	v_mfma_scale_f32_16x16x128_f8f6f4 v[62:65], v[18:25], v[174:181], v[62:65], v237, v237 op_sel_hi:[0,0,0]
	v_mfma_scale_f32_16x16x128_f8f6f4 v[58:61], v[26:33], v[174:181], v[58:61], v237, v237 op_sel_hi:[0,0,0]
	v_mfma_scale_f32_16x16x128_f8f6f4 v[110:113], v[18:25], v[182:189], v[110:113], v237, v237 op_sel_hi:[0,0,0]
	v_mfma_scale_f32_16x16x128_f8f6f4 v[106:109], v[26:33], v[182:189], v[106:109], v237, v237 op_sel_hi:[0,0,0]
	v_mfma_scale_f32_16x16x128_f8f6f4 v[150:153], v[18:25], v[190:197], v[150:153], v237, v237 op_sel_hi:[0,0,0]
	v_mfma_scale_f32_16x16x128_f8f6f4 v[146:149], v[26:33], v[190:197], v[146:149], v237, v237 op_sel_hi:[0,0,0]
	v_mfma_scale_f32_16x16x128_f8f6f4 v[142:145], v[18:25], v[204:211], v[142:145], v237, v237 op_sel_hi:[0,0,0]
	v_mfma_scale_f32_16x16x128_f8f6f4 v[138:141], v[26:33], v[204:211], v[138:141], v237, v237 op_sel_hi:[0,0,0]
	s_setprio 0
	s_barrier
	ds_read_b128 v[18:21], v171
	ds_read_b128 v[22:25], v171 offset:1024
	ds_read_b128 v[26:29], v171 offset:2048
	ds_read_b128 v[30:33], v171 offset:3072
	ds_read_b128 v[10:13], v172
	ds_read_b128 v[14:17], v172 offset:1024
	ds_read_b128 v[2:5], v172 offset:2048
	ds_read_b128 v[6:9], v172 offset:3072
	s_mov_b32 m0, s11
	ds_read_b128 v[174:177], v104 offset:32768
	ds_read_b128 v[178:181], v104 offset:33792
	ds_read_b128 v[182:185], v104 offset:34816
	ds_read_b128 v[186:189], v104 offset:35840
	ds_read_b128 v[190:193], v104 offset:36864
	ds_read_b128 v[194:197], v104 offset:37888
	ds_read_b128 v[204:207], v104 offset:38912
	ds_read_b128 v[208:211], v104 offset:39936
	buffer_load_dwordx4 v99, s[64:67], s79 offen lds
	s_mov_b32 m0, s45
	s_nop 0
	buffer_load_dwordx4 v101, s[64:67], s79 offen lds
	s_add_i32 s79, s79, 0xb0000
	s_mov_b32 m0, s47
	s_nop 0
	buffer_load_dwordx4 v99, s[64:67], s79 offen lds
	s_mov_b32 m0, s48
	s_nop 0
	buffer_load_dwordx4 v101, s[64:67], s79 offen lds
	s_waitcnt vmcnt(8)
	s_waitcnt lgkmcnt(0)
	s_barrier
	s_setprio 1
	v_mfma_scale_f32_16x16x128_f8f6f4 v[34:37], v[18:25], v[174:181], v[34:37], v237, v237 op_sel_hi:[0,0,0]
	v_mfma_scale_f32_16x16x128_f8f6f4 v[38:41], v[26:33], v[174:181], v[38:41], v237, v237 op_sel_hi:[0,0,0]
	v_mfma_scale_f32_16x16x128_f8f6f4 v[70:73], v[18:25], v[182:189], v[70:73], v237, v237 op_sel_hi:[0,0,0]
	v_mfma_scale_f32_16x16x128_f8f6f4 v[66:69], v[26:33], v[182:189], v[66:69], v237, v237 op_sel_hi:[0,0,0]
	v_mfma_scale_f32_16x16x128_f8f6f4 v[78:81], v[18:25], v[190:197], v[78:81], v237, v237 op_sel_hi:[0,0,0]
	v_mfma_scale_f32_16x16x128_f8f6f4 v[74:77], v[26:33], v[190:197], v[74:77], v237, v237 op_sel_hi:[0,0,0]
	v_mfma_scale_f32_16x16x128_f8f6f4 v[118:121], v[18:25], v[204:211], v[118:121], v237, v237 op_sel_hi:[0,0,0]
	v_mfma_scale_f32_16x16x128_f8f6f4 v[114:117], v[26:33], v[204:211], v[114:117], v237, v237 op_sel_hi:[0,0,0]
	v_mfma_scale_f32_16x16x128_f8f6f4 v[82:85], v[10:17], v[174:181], v[82:85], v237, v237 op_sel_hi:[0,0,0]
	v_mfma_scale_f32_16x16x128_f8f6f4 v[86:89], v[2:9], v[174:181], v[86:89], v237, v237 op_sel_hi:[0,0,0]
	v_mfma_scale_f32_16x16x128_f8f6f4 v[166:169], v[10:17], v[182:189], v[166:169], v237, v237 op_sel_hi:[0,0,0]
	v_mfma_scale_f32_16x16x128_f8f6f4 v[162:165], v[2:9], v[182:189], v[162:165], v237, v237 op_sel_hi:[0,0,0]
	v_mfma_scale_f32_16x16x128_f8f6f4 v[158:161], v[10:17], v[190:197], v[158:161], v237, v237 op_sel_hi:[0,0,0]
	v_mfma_scale_f32_16x16x128_f8f6f4 v[154:157], v[2:9], v[190:197], v[154:157], v237, v237 op_sel_hi:[0,0,0]
	v_mfma_scale_f32_16x16x128_f8f6f4 v[126:129], v[10:17], v[204:211], v[126:129], v237, v237 op_sel_hi:[0,0,0]
	v_mfma_scale_f32_16x16x128_f8f6f4 v[122:125], v[2:9], v[204:211], v[122:125], v237, v237 op_sel_hi:[0,0,0]
	s_setprio 0
	s_barrier
	s_mov_b32 m0, s50
	s_or_b32 s79, s78, 0x80
	ds_read_b128 v[174:177], v104 offset:49152
	ds_read_b128 v[178:181], v104 offset:50176
	ds_read_b128 v[182:185], v104 offset:51200
	ds_read_b128 v[186:189], v104 offset:52224
	ds_read_b128 v[190:193], v104 offset:53248
	ds_read_b128 v[194:197], v104 offset:54272
	ds_read_b128 v[204:207], v104 offset:55296
	ds_read_b128 v[208:211], v104 offset:56320
	buffer_load_dwordx4 v100, s[4:7], s79 offen lds
	s_mov_b32 m0, s51
	s_add_i32 s78, s78, 0xb0080
	buffer_load_dwordx4 v102, s[4:7], s79 offen lds
	s_mov_b32 m0, s52
	s_nop 0
	buffer_load_dwordx4 v100, s[4:7], s78 offen lds
	s_mov_b32 m0, s53
	s_nop 0
	buffer_load_dwordx4 v102, s[4:7], s78 offen lds
	s_waitcnt vmcnt(6)
	s_waitcnt lgkmcnt(0)
	s_barrier
	s_setprio 1
	v_mfma_scale_f32_16x16x128_f8f6f4 v[46:49], v[18:25], v[174:181], v[46:49], v237, v237 op_sel_hi:[0,0,0]
	v_mfma_scale_f32_16x16x128_f8f6f4 v[42:45], v[26:33], v[174:181], v[42:45], v237, v237 op_sel_hi:[0,0,0]
	v_mfma_scale_f32_16x16x128_f8f6f4 v[54:57], v[18:25], v[182:189], v[54:57], v237, v237 op_sel_hi:[0,0,0]
	v_mfma_scale_f32_16x16x128_f8f6f4 v[50:53], v[26:33], v[182:189], v[50:53], v237, v237 op_sel_hi:[0,0,0]
	v_mfma_scale_f32_16x16x128_f8f6f4 v[94:97], v[18:25], v[190:197], v[94:97], v237, v237 op_sel_hi:[0,0,0]
	v_mfma_scale_f32_16x16x128_f8f6f4 v[90:93], v[26:33], v[190:197], v[90:93], v237, v237 op_sel_hi:[0,0,0]
	v_mfma_scale_f32_16x16x128_f8f6f4 v[134:137], v[18:25], v[204:211], v[134:137], v237, v237 op_sel_hi:[0,0,0]
	v_mfma_scale_f32_16x16x128_f8f6f4 v[130:133], v[26:33], v[204:211], v[130:133], v237, v237 op_sel_hi:[0,0,0]
	v_mfma_scale_f32_16x16x128_f8f6f4 v[62:65], v[10:17], v[174:181], v[62:65], v237, v237 op_sel_hi:[0,0,0]
	v_mfma_scale_f32_16x16x128_f8f6f4 v[58:61], v[2:9], v[174:181], v[58:61], v237, v237 op_sel_hi:[0,0,0]
	v_mfma_scale_f32_16x16x128_f8f6f4 v[110:113], v[10:17], v[182:189], v[110:113], v237, v237 op_sel_hi:[0,0,0]
	v_mfma_scale_f32_16x16x128_f8f6f4 v[106:109], v[2:9], v[182:189], v[106:109], v237, v237 op_sel_hi:[0,0,0]
	v_mfma_scale_f32_16x16x128_f8f6f4 v[150:153], v[10:17], v[190:197], v[150:153], v237, v237 op_sel_hi:[0,0,0]
	v_mfma_scale_f32_16x16x128_f8f6f4 v[146:149], v[2:9], v[190:197], v[146:149], v237, v237 op_sel_hi:[0,0,0]
	v_mfma_scale_f32_16x16x128_f8f6f4 v[142:145], v[10:17], v[204:211], v[142:145], v237, v237 op_sel_hi:[0,0,0]
	v_mfma_scale_f32_16x16x128_f8f6f4 v[138:141], v[2:9], v[204:211], v[138:141], v237, v237 op_sel_hi:[0,0,0]
	s_setprio 0
	s_barrier
	s_add_i32 s76, s76, 2
	s_addk_i32 s77, 0x100
	s_cmp_gt_u32 s76, 41
	s_cbranch_scc0 .LBB0_334
	s_nop 15
	s_nop 15
	s_and_b64 vcc, exec, s[36:37]
	s_cbranch_vccz .LBB0_330
	s_mov_b32 s10, s59
	s_mov_b32 s0, s60
	s_mov_b32 s13, s63
	s_mov_b32 s46, s62
	s_mov_b32 s58, s61
	s_branch .LBB0_330

.LBB0_411:
	v_add_u32_e32 v137, 0x10000, v135
	v_add_u32_e32 v170, 0x14000, v135
	ds_read_b128 v[2:5], v137
	ds_read_b128 v[6:9], v137 offset:1024
	ds_read_b128 v[10:13], v137 offset:2048
	ds_read_b128 v[14:17], v137 offset:3072
	ds_read_b128 v[18:21], v170
	ds_read_b128 v[22:25], v170 offset:1024
	ds_read_b128 v[26:29], v170 offset:2048
	ds_read_b128 v[30:33], v170 offset:3072
	s_or_b32 s63, s37, 0x80
	s_or_b32 s72, s13, 0x100
	s_mul_i32 s58, s56, 0x160000
	s_and_b64 s[6:7], s[28:29], exec
	s_cselect_b32 s60, s58, s37
	s_or_b32 s62, s37, 0x100
	s_mul_i32 s59, s55, 0x160000
	s_and_b64 s[6:7], s[28:29], exec
	s_cselect_b32 s61, s59, s13
	s_mov_b32 m0, s50
	ds_read_b128 v[66:69], v136
	ds_read_b128 v[70:73], v136 offset:1024
	ds_read_b128 v[74:77], v136 offset:2048
	ds_read_b128 v[78:81], v136 offset:3072
	ds_read_b128 v[82:85], v136 offset:4096
	ds_read_b128 v[86:89], v136 offset:5120
	ds_read_b128 v[122:125], v136 offset:6144
	ds_read_b128 v[126:129], v136 offset:7168
	buffer_load_dwordx4 v131, s[64:67], s63 offen lds
	s_mov_b32 m0, s52
	s_add_i32 s6, s37, 0xb0080
	buffer_load_dwordx4 v133, s[64:67], s63 offen lds
	s_mov_b32 m0, s51
	s_nop 0
	buffer_load_dwordx4 v131, s[64:67], s6 offen lds
	s_mov_b32 m0, s53
	s_nop 0
	buffer_load_dwordx4 v133, s[64:67], s6 offen lds
	s_waitcnt vmcnt(8)
	s_waitcnt lgkmcnt(0)
	s_barrier
	s_setprio 1
	v_mfma_scale_f32_16x16x128_f8f6f4 v[114:117], v[2:9], v[66:73], 0, v237, v237 op_sel_hi:[0,0,0]
	v_mfma_scale_f32_16x16x128_f8f6f4 v[118:121], v[10:17], v[66:73], 0, v237, v237 op_sel_hi:[0,0,0]
	v_mfma_scale_f32_16x16x128_f8f6f4 v[54:57], v[2:9], v[74:81], 0, v237, v237 op_sel_hi:[0,0,0]
	v_mfma_scale_f32_16x16x128_f8f6f4 v[50:53], v[10:17], v[74:81], 0, v237, v237 op_sel_hi:[0,0,0]
	v_mfma_scale_f32_16x16x128_f8f6f4 v[46:49], v[2:9], v[82:89], 0, v237, v237 op_sel_hi:[0,0,0]
	v_mfma_scale_f32_16x16x128_f8f6f4 v[42:45], v[10:17], v[82:89], 0, v237, v237 op_sel_hi:[0,0,0]
	v_mfma_scale_f32_16x16x128_f8f6f4 v[38:41], v[2:9], v[122:129], 0, v237, v237 op_sel_hi:[0,0,0]
	v_mfma_scale_f32_16x16x128_f8f6f4 v[34:37], v[10:17], v[122:129], 0, v237, v237 op_sel_hi:[0,0,0]
	v_mfma_scale_f32_16x16x128_f8f6f4 v[58:61], v[18:25], v[66:73], 0, v237, v237 op_sel_hi:[0,0,0]
	v_mfma_scale_f32_16x16x128_f8f6f4 v[62:65], v[26:33], v[66:73], 0, v237, v237 op_sel_hi:[0,0,0]
	v_mfma_scale_f32_16x16x128_f8f6f4 v[110:113], v[18:25], v[74:81], 0, v237, v237 op_sel_hi:[0,0,0]
	v_mfma_scale_f32_16x16x128_f8f6f4 v[106:109], v[26:33], v[74:81], 0, v237, v237 op_sel_hi:[0,0,0]
	v_mfma_scale_f32_16x16x128_f8f6f4 v[102:105], v[18:25], v[82:89], 0, v237, v237 op_sel_hi:[0,0,0]
	v_mfma_scale_f32_16x16x128_f8f6f4 v[98:101], v[26:33], v[82:89], 0, v237, v237 op_sel_hi:[0,0,0]
	v_mfma_scale_f32_16x16x128_f8f6f4 v[162:165], v[18:25], v[122:129], 0, v237, v237 op_sel_hi:[0,0,0]
	v_mfma_scale_f32_16x16x128_f8f6f4 v[94:97], v[26:33], v[122:129], 0, v237, v237 op_sel_hi:[0,0,0]
	s_setprio 0
	s_barrier
	s_mov_b32 m0, s12
	s_mov_b32 s6, s66
	s_mov_b32 s7, s67
	ds_read_b128 v[122:125], v136 offset:16384
	ds_read_b128 v[126:129], v136 offset:17408
	s_waitcnt vmcnt(16)
	ds_read_b128 v[138:141], v136 offset:18432
	ds_read_b128 v[142:145], v136 offset:19456
	ds_read_b128 v[172:175], v136 offset:20480
	ds_read_b128 v[176:179], v136 offset:21504
	ds_read_b128 v[180:183], v136 offset:22528
	ds_read_b128 v[184:187], v136 offset:23552
	buffer_load_dwordx4 v132, s[4:7], s72 offen lds
	s_mov_b32 m0, s31
	s_add_i32 s63, s13, 0xb0100
	buffer_load_dwordx4 v134, s[4:7], s72 offen lds
	s_mov_b32 m0, s34
	s_nop 0
	buffer_load_dwordx4 v132, s[4:7], s63 offen lds
	s_mov_b32 m0, s35
	s_nop 0
	buffer_load_dwordx4 v134, s[4:7], s63 offen lds
	s_waitcnt vmcnt(6)
	s_waitcnt lgkmcnt(0)
	s_barrier
	s_setprio 1
	v_mfma_scale_f32_16x16x128_f8f6f4 v[154:157], v[2:9], v[122:129], 0, v237, v237 op_sel_hi:[0,0,0]
	v_mfma_scale_f32_16x16x128_f8f6f4 v[90:93], v[10:17], v[122:129], 0, v237, v237 op_sel_hi:[0,0,0]
	v_mfma_scale_f32_16x16x128_f8f6f4 v[86:89], v[2:9], v[138:145], 0, v237, v237 op_sel_hi:[0,0,0]
	v_mfma_scale_f32_16x16x128_f8f6f4 v[82:85], v[10:17], v[138:145], 0, v237, v237 op_sel_hi:[0,0,0]
	v_mfma_scale_f32_16x16x128_f8f6f4 v[78:81], v[2:9], v[172:179], 0, v237, v237 op_sel_hi:[0,0,0]
	v_mfma_scale_f32_16x16x128_f8f6f4 v[74:77], v[10:17], v[172:179], 0, v237, v237 op_sel_hi:[0,0,0]
	v_mfma_scale_f32_16x16x128_f8f6f4 v[70:73], v[2:9], v[180:187], 0, v237, v237 op_sel_hi:[0,0,0]
	v_mfma_scale_f32_16x16x128_f8f6f4 v[66:69], v[10:17], v[180:187], 0, v237, v237 op_sel_hi:[0,0,0]
	v_mfma_scale_f32_16x16x128_f8f6f4 v[166:169], v[18:25], v[122:129], 0, v237, v237 op_sel_hi:[0,0,0]
	v_mfma_scale_f32_16x16x128_f8f6f4 v[158:161], v[26:33], v[122:129], 0, v237, v237 op_sel_hi:[0,0,0]
	v_mfma_scale_f32_16x16x128_f8f6f4 v[150:153], v[18:25], v[138:145], 0, v237, v237 op_sel_hi:[0,0,0]
	v_mfma_scale_f32_16x16x128_f8f6f4 v[146:149], v[26:33], v[138:145], 0, v237, v237 op_sel_hi:[0,0,0]
	v_mfma_scale_f32_16x16x128_f8f6f4 v[142:145], v[18:25], v[172:179], 0, v237, v237 op_sel_hi:[0,0,0]
	v_mfma_scale_f32_16x16x128_f8f6f4 v[138:141], v[26:33], v[172:179], 0, v237, v237 op_sel_hi:[0,0,0]
	v_mfma_scale_f32_16x16x128_f8f6f4 v[126:129], v[18:25], v[180:187], 0, v237, v237 op_sel_hi:[0,0,0]
	v_mfma_scale_f32_16x16x128_f8f6f4 v[122:125], v[26:33], v[180:187], 0, v237, v237 op_sel_hi:[0,0,0]
	s_setprio 0
	s_barrier
	v_add_u32_e32 v171, 0x18000, v135
	v_add_u32_e32 v172, 0x1c000, v135
	ds_read_b128 v[26:29], v171
	ds_read_b128 v[30:33], v171 offset:1024
	ds_read_b128 v[18:21], v171 offset:2048
	ds_read_b128 v[22:25], v171 offset:3072
	ds_read_b128 v[10:13], v172
	ds_read_b128 v[14:17], v172 offset:1024
	ds_read_b128 v[2:5], v172 offset:2048
	ds_read_b128 v[6:9], v172 offset:3072
	s_mov_b32 m0, s11
	ds_read_b128 v[174:177], v136 offset:32768
	ds_read_b128 v[178:181], v136 offset:33792
	ds_read_b128 v[182:185], v136 offset:34816
	ds_read_b128 v[186:189], v136 offset:35840
	ds_read_b128 v[190:193], v136 offset:36864
	ds_read_b128 v[194:197], v136 offset:37888
	ds_read_b128 v[204:207], v136 offset:38912
	ds_read_b128 v[208:211], v136 offset:39936
	buffer_load_dwordx4 v131, s[64:67], s62 offen lds
	s_mov_b32 m0, s36
	s_nop 0
	buffer_load_dwordx4 v133, s[64:67], s62 offen lds
	s_add_i32 s62, s37, 0xb0100
	s_mov_b32 m0, s40
	s_nop 0
	buffer_load_dwordx4 v131, s[64:67], s62 offen lds
	s_mov_b32 m0, s44
	s_nop 0
	buffer_load_dwordx4 v133, s[64:67], s62 offen lds
	s_waitcnt vmcnt(8)
	s_waitcnt lgkmcnt(0)
	s_barrier
	s_setprio 1
	v_mfma_scale_f32_16x16x128_f8f6f4 v[114:117], v[26:33], v[174:181], v[114:117], v237, v237 op_sel_hi:[0,0,0]
	v_mfma_scale_f32_16x16x128_f8f6f4 v[118:121], v[18:25], v[174:181], v[118:121], v237, v237 op_sel_hi:[0,0,0]
	v_mfma_scale_f32_16x16x128_f8f6f4 v[54:57], v[26:33], v[182:189], v[54:57], v237, v237 op_sel_hi:[0,0,0]
	v_mfma_scale_f32_16x16x128_f8f6f4 v[50:53], v[18:25], v[182:189], v[50:53], v237, v237 op_sel_hi:[0,0,0]
	v_mfma_scale_f32_16x16x128_f8f6f4 v[46:49], v[26:33], v[190:197], v[46:49], v237, v237 op_sel_hi:[0,0,0]
	v_mfma_scale_f32_16x16x128_f8f6f4 v[42:45], v[18:25], v[190:197], v[42:45], v237, v237 op_sel_hi:[0,0,0]
	v_mfma_scale_f32_16x16x128_f8f6f4 v[38:41], v[26:33], v[204:211], v[38:41], v237, v237 op_sel_hi:[0,0,0]
	v_mfma_scale_f32_16x16x128_f8f6f4 v[34:37], v[18:25], v[204:211], v[34:37], v237, v237 op_sel_hi:[0,0,0]
	v_mfma_scale_f32_16x16x128_f8f6f4 v[58:61], v[10:17], v[174:181], v[58:61], v237, v237 op_sel_hi:[0,0,0]
	v_mfma_scale_f32_16x16x128_f8f6f4 v[62:65], v[2:9], v[174:181], v[62:65], v237, v237 op_sel_hi:[0,0,0]
	v_mfma_scale_f32_16x16x128_f8f6f4 v[110:113], v[10:17], v[182:189], v[110:113], v237, v237 op_sel_hi:[0,0,0]
	v_mfma_scale_f32_16x16x128_f8f6f4 v[106:109], v[2:9], v[182:189], v[106:109], v237, v237 op_sel_hi:[0,0,0]
	v_mfma_scale_f32_16x16x128_f8f6f4 v[102:105], v[10:17], v[190:197], v[102:105], v237, v237 op_sel_hi:[0,0,0]
	v_mfma_scale_f32_16x16x128_f8f6f4 v[98:101], v[2:9], v[190:197], v[98:101], v237, v237 op_sel_hi:[0,0,0]
	v_mfma_scale_f32_16x16x128_f8f6f4 v[162:165], v[10:17], v[204:211], v[162:165], v237, v237 op_sel_hi:[0,0,0]
	v_mfma_scale_f32_16x16x128_f8f6f4 v[94:97], v[2:9], v[204:211], v[94:97], v237, v237 op_sel_hi:[0,0,0]
	s_setprio 0
	s_barrier
	s_mov_b32 m0, s46
	s_or_b32 s62, s13, 0x180
	ds_read_b128 v[174:177], v136 offset:49152
	ds_read_b128 v[178:181], v136 offset:50176
	ds_read_b128 v[182:185], v136 offset:51200
	ds_read_b128 v[186:189], v136 offset:52224
	ds_read_b128 v[190:193], v136 offset:53248
	ds_read_b128 v[194:197], v136 offset:54272
	ds_read_b128 v[204:207], v136 offset:55296
	ds_read_b128 v[208:211], v136 offset:56320
	buffer_load_dwordx4 v132, s[4:7], s62 offen lds
	s_mov_b32 m0, s47
	s_nop 0
	buffer_load_dwordx4 v134, s[4:7], s62 offen lds
	s_add_i32 s62, s13, 0xb0180
	s_mov_b32 m0, s48
	s_nop 0
	buffer_load_dwordx4 v132, s[4:7], s62 offen lds
	s_mov_b32 m0, s49
	s_nop 0
	buffer_load_dwordx4 v134, s[4:7], s62 offen lds
	s_waitcnt vmcnt(6)
	s_waitcnt lgkmcnt(0)
	s_barrier
	s_setprio 1
	v_mfma_scale_f32_16x16x128_f8f6f4 v[154:157], v[26:33], v[174:181], v[154:157], v237, v237 op_sel_hi:[0,0,0]
	v_mfma_scale_f32_16x16x128_f8f6f4 v[90:93], v[18:25], v[174:181], v[90:93], v237, v237 op_sel_hi:[0,0,0]
	v_mfma_scale_f32_16x16x128_f8f6f4 v[86:89], v[26:33], v[182:189], v[86:89], v237, v237 op_sel_hi:[0,0,0]
	v_mfma_scale_f32_16x16x128_f8f6f4 v[82:85], v[18:25], v[182:189], v[82:85], v237, v237 op_sel_hi:[0,0,0]
	v_mfma_scale_f32_16x16x128_f8f6f4 v[78:81], v[26:33], v[190:197], v[78:81], v237, v237 op_sel_hi:[0,0,0]
	v_mfma_scale_f32_16x16x128_f8f6f4 v[74:77], v[18:25], v[190:197], v[74:77], v237, v237 op_sel_hi:[0,0,0]
	v_mfma_scale_f32_16x16x128_f8f6f4 v[70:73], v[26:33], v[204:211], v[70:73], v237, v237 op_sel_hi:[0,0,0]
	v_mfma_scale_f32_16x16x128_f8f6f4 v[66:69], v[18:25], v[204:211], v[66:69], v237, v237 op_sel_hi:[0,0,0]
	v_mfma_scale_f32_16x16x128_f8f6f4 v[166:169], v[10:17], v[174:181], v[166:169], v237, v237 op_sel_hi:[0,0,0]
	v_mfma_scale_f32_16x16x128_f8f6f4 v[158:161], v[2:9], v[174:181], v[158:161], v237, v237 op_sel_hi:[0,0,0]
	v_mfma_scale_f32_16x16x128_f8f6f4 v[150:153], v[10:17], v[182:189], v[150:153], v237, v237 op_sel_hi:[0,0,0]
	v_mfma_scale_f32_16x16x128_f8f6f4 v[146:149], v[2:9], v[182:189], v[146:149], v237, v237 op_sel_hi:[0,0,0]
	v_mfma_scale_f32_16x16x128_f8f6f4 v[142:145], v[10:17], v[190:197], v[142:145], v237, v237 op_sel_hi:[0,0,0]
	v_mfma_scale_f32_16x16x128_f8f6f4 v[138:141], v[2:9], v[190:197], v[138:141], v237, v237 op_sel_hi:[0,0,0]
	v_mfma_scale_f32_16x16x128_f8f6f4 v[126:129], v[10:17], v[204:211], v[126:129], v237, v237 op_sel_hi:[0,0,0]
	v_mfma_scale_f32_16x16x128_f8f6f4 v[122:125], v[2:9], v[204:211], v[122:125], v237, v237 op_sel_hi:[0,0,0]
	s_setprio 0
	s_barrier
	s_mov_b32 s62, 0
	s_movk_i32 s63, 0xec00
.LBB0_412:
	ds_read_b128 v[2:5], v137
	ds_read_b128 v[6:9], v137 offset:1024
	ds_read_b128 v[10:13], v137 offset:2048
	ds_read_b128 v[14:17], v137 offset:3072
	ds_read_b128 v[18:21], v170
	ds_read_b128 v[22:25], v170 offset:1024
	ds_read_b128 v[26:29], v170 offset:2048
	ds_read_b128 v[30:33], v170 offset:3072
	s_add_i32 s76, s37, s63
	s_add_i32 s72, s13, s63
	s_add_i32 s73, s76, 0x1600
	s_addk_i32 s72, 0x1600
	s_cmp_eq_u32 s63, 0
	s_cselect_b32 s72, s61, s72
	s_cselect_b32 s73, s60, s73
	s_add_i32 s77, s76, 0x1580
	s_mov_b32 m0, s50
	ds_read_b128 v[174:177], v136
	ds_read_b128 v[178:181], v136 offset:1024
	ds_read_b128 v[182:185], v136 offset:2048
	ds_read_b128 v[186:189], v136 offset:3072
	ds_read_b128 v[190:193], v136 offset:4096
	ds_read_b128 v[194:197], v136 offset:5120
	ds_read_b128 v[204:207], v136 offset:6144
	ds_read_b128 v[208:211], v136 offset:7168
	buffer_load_dwordx4 v131, s[64:67], s77 offen lds
	s_mov_b32 m0, s52
	s_add_i32 s76, s76, 0xb1580
	buffer_load_dwordx4 v133, s[64:67], s77 offen lds
	s_mov_b32 m0, s51
	s_nop 0
	buffer_load_dwordx4 v131, s[64:67], s76 offen lds
	s_mov_b32 m0, s53
	s_nop 0
	buffer_load_dwordx4 v133, s[64:67], s76 offen lds
	s_waitcnt vmcnt(8)
	s_waitcnt lgkmcnt(0)
	s_barrier
	s_setprio 1
	v_mfma_scale_f32_16x16x128_f8f6f4 v[114:117], v[2:9], v[174:181], v[114:117], v237, v237 op_sel_hi:[0,0,0]
	v_mfma_scale_f32_16x16x128_f8f6f4 v[118:121], v[10:17], v[174:181], v[118:121], v237, v237 op_sel_hi:[0,0,0]
	v_mfma_scale_f32_16x16x128_f8f6f4 v[54:57], v[2:9], v[182:189], v[54:57], v237, v237 op_sel_hi:[0,0,0]
	v_mfma_scale_f32_16x16x128_f8f6f4 v[50:53], v[10:17], v[182:189], v[50:53], v237, v237 op_sel_hi:[0,0,0]
	v_mfma_scale_f32_16x16x128_f8f6f4 v[46:49], v[2:9], v[190:197], v[46:49], v237, v237 op_sel_hi:[0,0,0]
	v_mfma_scale_f32_16x16x128_f8f6f4 v[42:45], v[10:17], v[190:197], v[42:45], v237, v237 op_sel_hi:[0,0,0]
	v_mfma_scale_f32_16x16x128_f8f6f4 v[38:41], v[2:9], v[204:211], v[38:41], v237, v237 op_sel_hi:[0,0,0]
	v_mfma_scale_f32_16x16x128_f8f6f4 v[34:37], v[10:17], v[204:211], v[34:37], v237, v237 op_sel_hi:[0,0,0]
	v_mfma_scale_f32_16x16x128_f8f6f4 v[58:61], v[18:25], v[174:181], v[58:61], v237, v237 op_sel_hi:[0,0,0]
	v_mfma_scale_f32_16x16x128_f8f6f4 v[62:65], v[26:33], v[174:181], v[62:65], v237, v237 op_sel_hi:[0,0,0]
	v_mfma_scale_f32_16x16x128_f8f6f4 v[110:113], v[18:25], v[182:189], v[110:113], v237, v237 op_sel_hi:[0,0,0]
	v_mfma_scale_f32_16x16x128_f8f6f4 v[106:109], v[26:33], v[182:189], v[106:109], v237, v237 op_sel_hi:[0,0,0]
	v_mfma_scale_f32_16x16x128_f8f6f4 v[102:105], v[18:25], v[190:197], v[102:105], v237, v237 op_sel_hi:[0,0,0]
	v_mfma_scale_f32_16x16x128_f8f6f4 v[98:101], v[26:33], v[190:197], v[98:101], v237, v237 op_sel_hi:[0,0,0]
	v_mfma_scale_f32_16x16x128_f8f6f4 v[162:165], v[18:25], v[204:211], v[162:165], v237, v237 op_sel_hi:[0,0,0]
	v_mfma_scale_f32_16x16x128_f8f6f4 v[94:97], v[26:33], v[204:211], v[94:97], v237, v237 op_sel_hi:[0,0,0]
	s_setprio 0
	s_barrier
	s_mov_b32 m0, s12
	ds_read_b128 v[174:177], v136 offset:16384
	ds_read_b128 v[178:181], v136 offset:17408
	ds_read_b128 v[182:185], v136 offset:18432
	ds_read_b128 v[186:189], v136 offset:19456
	ds_read_b128 v[190:193], v136 offset:20480
	ds_read_b128 v[194:197], v136 offset:21504
	ds_read_b128 v[204:207], v136 offset:22528
	ds_read_b128 v[208:211], v136 offset:23552
	buffer_load_dwordx4 v132, s[4:7], s72 offen lds
	s_mov_b32 m0, s31
	s_add_i32 s76, s72, 0xb0000
	buffer_load_dwordx4 v134, s[4:7], s72 offen lds
	s_mov_b32 m0, s34
	s_nop 0
	buffer_load_dwordx4 v132, s[4:7], s76 offen lds
	s_mov_b32 m0, s35
	s_nop 0
	buffer_load_dwordx4 v134, s[4:7], s76 offen lds
	s_waitcnt vmcnt(6)
	s_waitcnt lgkmcnt(0)
	s_barrier
	s_setprio 1
	v_mfma_scale_f32_16x16x128_f8f6f4 v[154:157], v[2:9], v[174:181], v[154:157], v237, v237 op_sel_hi:[0,0,0]
	v_mfma_scale_f32_16x16x128_f8f6f4 v[90:93], v[10:17], v[174:181], v[90:93], v237, v237 op_sel_hi:[0,0,0]
	v_mfma_scale_f32_16x16x128_f8f6f4 v[86:89], v[2:9], v[182:189], v[86:89], v237, v237 op_sel_hi:[0,0,0]
	v_mfma_scale_f32_16x16x128_f8f6f4 v[82:85], v[10:17], v[182:189], v[82:85], v237, v237 op_sel_hi:[0,0,0]
	v_mfma_scale_f32_16x16x128_f8f6f4 v[78:81], v[2:9], v[190:197], v[78:81], v237, v237 op_sel_hi:[0,0,0]
	v_mfma_scale_f32_16x16x128_f8f6f4 v[74:77], v[10:17], v[190:197], v[74:77], v237, v237 op_sel_hi:[0,0,0]
	v_mfma_scale_f32_16x16x128_f8f6f4 v[70:73], v[2:9], v[204:211], v[70:73], v237, v237 op_sel_hi:[0,0,0]
	v_mfma_scale_f32_16x16x128_f8f6f4 v[66:69], v[10:17], v[204:211], v[66:69], v237, v237 op_sel_hi:[0,0,0]
	v_mfma_scale_f32_16x16x128_f8f6f4 v[166:169], v[18:25], v[174:181], v[166:169], v237, v237 op_sel_hi:[0,0,0]
	v_mfma_scale_f32_16x16x128_f8f6f4 v[158:161], v[26:33], v[174:181], v[158:161], v237, v237 op_sel_hi:[0,0,0]
	v_mfma_scale_f32_16x16x128_f8f6f4 v[150:153], v[18:25], v[182:189], v[150:153], v237, v237 op_sel_hi:[0,0,0]
	v_mfma_scale_f32_16x16x128_f8f6f4 v[146:149], v[26:33], v[182:189], v[146:149], v237, v237 op_sel_hi:[0,0,0]
	v_mfma_scale_f32_16x16x128_f8f6f4 v[142:145], v[18:25], v[190:197], v[142:145], v237, v237 op_sel_hi:[0,0,0]
	v_mfma_scale_f32_16x16x128_f8f6f4 v[138:141], v[26:33], v[190:197], v[138:141], v237, v237 op_sel_hi:[0,0,0]
	v_mfma_scale_f32_16x16x128_f8f6f4 v[126:129], v[18:25], v[204:211], v[126:129], v237, v237 op_sel_hi:[0,0,0]
	v_mfma_scale_f32_16x16x128_f8f6f4 v[122:125], v[26:33], v[204:211], v[122:125], v237, v237 op_sel_hi:[0,0,0]
	s_setprio 0
	s_barrier
	ds_read_b128 v[18:21], v171
	ds_read_b128 v[22:25], v171 offset:1024
	ds_read_b128 v[26:29], v171 offset:2048
	ds_read_b128 v[30:33], v171 offset:3072
	ds_read_b128 v[10:13], v172
	ds_read_b128 v[14:17], v172 offset:1024
	ds_read_b128 v[2:5], v172 offset:2048
	ds_read_b128 v[6:9], v172 offset:3072
	s_mov_b32 m0, s11
	ds_read_b128 v[174:177], v136 offset:32768
	ds_read_b128 v[178:181], v136 offset:33792
	ds_read_b128 v[182:185], v136 offset:34816
	ds_read_b128 v[186:189], v136 offset:35840
	ds_read_b128 v[190:193], v136 offset:36864
	ds_read_b128 v[194:197], v136 offset:37888
	ds_read_b128 v[204:207], v136 offset:38912
	ds_read_b128 v[208:211], v136 offset:39936
	buffer_load_dwordx4 v131, s[64:67], s73 offen lds
	s_mov_b32 m0, s36
	s_nop 0
	buffer_load_dwordx4 v133, s[64:67], s73 offen lds
	s_add_i32 s73, s73, 0xb0000
	s_mov_b32 m0, s40
	s_nop 0
	buffer_load_dwordx4 v131, s[64:67], s73 offen lds
	s_mov_b32 m0, s44
	s_nop 0
	buffer_load_dwordx4 v133, s[64:67], s73 offen lds
	s_waitcnt vmcnt(8)
	s_waitcnt lgkmcnt(0)
	s_barrier
	s_setprio 1
	v_mfma_scale_f32_16x16x128_f8f6f4 v[114:117], v[18:25], v[174:181], v[114:117], v237, v237 op_sel_hi:[0,0,0]
	v_mfma_scale_f32_16x16x128_f8f6f4 v[118:121], v[26:33], v[174:181], v[118:121], v237, v237 op_sel_hi:[0,0,0]
	v_mfma_scale_f32_16x16x128_f8f6f4 v[54:57], v[18:25], v[182:189], v[54:57], v237, v237 op_sel_hi:[0,0,0]
	v_mfma_scale_f32_16x16x128_f8f6f4 v[50:53], v[26:33], v[182:189], v[50:53], v237, v237 op_sel_hi:[0,0,0]
	v_mfma_scale_f32_16x16x128_f8f6f4 v[46:49], v[18:25], v[190:197], v[46:49], v237, v237 op_sel_hi:[0,0,0]
	v_mfma_scale_f32_16x16x128_f8f6f4 v[42:45], v[26:33], v[190:197], v[42:45], v237, v237 op_sel_hi:[0,0,0]
	v_mfma_scale_f32_16x16x128_f8f6f4 v[38:41], v[18:25], v[204:211], v[38:41], v237, v237 op_sel_hi:[0,0,0]
	v_mfma_scale_f32_16x16x128_f8f6f4 v[34:37], v[26:33], v[204:211], v[34:37], v237, v237 op_sel_hi:[0,0,0]
	v_mfma_scale_f32_16x16x128_f8f6f4 v[58:61], v[10:17], v[174:181], v[58:61], v237, v237 op_sel_hi:[0,0,0]
	v_mfma_scale_f32_16x16x128_f8f6f4 v[62:65], v[2:9], v[174:181], v[62:65], v237, v237 op_sel_hi:[0,0,0]
	v_mfma_scale_f32_16x16x128_f8f6f4 v[110:113], v[10:17], v[182:189], v[110:113], v237, v237 op_sel_hi:[0,0,0]
	v_mfma_scale_f32_16x16x128_f8f6f4 v[106:109], v[2:9], v[182:189], v[106:109], v237, v237 op_sel_hi:[0,0,0]
	v_mfma_scale_f32_16x16x128_f8f6f4 v[102:105], v[10:17], v[190:197], v[102:105], v237, v237 op_sel_hi:[0,0,0]
	v_mfma_scale_f32_16x16x128_f8f6f4 v[98:101], v[2:9], v[190:197], v[98:101], v237, v237 op_sel_hi:[0,0,0]
	v_mfma_scale_f32_16x16x128_f8f6f4 v[162:165], v[10:17], v[204:211], v[162:165], v237, v237 op_sel_hi:[0,0,0]
	v_mfma_scale_f32_16x16x128_f8f6f4 v[94:97], v[2:9], v[204:211], v[94:97], v237, v237 op_sel_hi:[0,0,0]
	s_setprio 0
	s_barrier
	s_mov_b32 m0, s46
	s_or_b32 s73, s72, 0x80
	ds_read_b128 v[174:177], v136 offset:49152
	ds_read_b128 v[178:181], v136 offset:50176
	ds_read_b128 v[182:185], v136 offset:51200
	ds_read_b128 v[186:189], v136 offset:52224
	ds_read_b128 v[190:193], v136 offset:53248
	ds_read_b128 v[194:197], v136 offset:54272
	ds_read_b128 v[204:207], v136 offset:55296
	ds_read_b128 v[208:211], v136 offset:56320
	buffer_load_dwordx4 v132, s[4:7], s73 offen lds
	s_mov_b32 m0, s47
	s_add_i32 s72, s72, 0xb0080
	buffer_load_dwordx4 v134, s[4:7], s73 offen lds
	s_mov_b32 m0, s48
	s_nop 0
	buffer_load_dwordx4 v132, s[4:7], s72 offen lds
	s_mov_b32 m0, s49
	s_nop 0
	buffer_load_dwordx4 v134, s[4:7], s72 offen lds
	s_waitcnt vmcnt(6)
	s_waitcnt lgkmcnt(0)
	s_barrier
	s_setprio 1
	v_mfma_scale_f32_16x16x128_f8f6f4 v[154:157], v[18:25], v[174:181], v[154:157], v237, v237 op_sel_hi:[0,0,0]
	v_mfma_scale_f32_16x16x128_f8f6f4 v[90:93], v[26:33], v[174:181], v[90:93], v237, v237 op_sel_hi:[0,0,0]
	v_mfma_scale_f32_16x16x128_f8f6f4 v[86:89], v[18:25], v[182:189], v[86:89], v237, v237 op_sel_hi:[0,0,0]
	v_mfma_scale_f32_16x16x128_f8f6f4 v[82:85], v[26:33], v[182:189], v[82:85], v237, v237 op_sel_hi:[0,0,0]
	v_mfma_scale_f32_16x16x128_f8f6f4 v[78:81], v[18:25], v[190:197], v[78:81], v237, v237 op_sel_hi:[0,0,0]
	v_mfma_scale_f32_16x16x128_f8f6f4 v[74:77], v[26:33], v[190:197], v[74:77], v237, v237 op_sel_hi:[0,0,0]
	v_mfma_scale_f32_16x16x128_f8f6f4 v[70:73], v[18:25], v[204:211], v[70:73], v237, v237 op_sel_hi:[0,0,0]
	v_mfma_scale_f32_16x16x128_f8f6f4 v[66:69], v[26:33], v[204:211], v[66:69], v237, v237 op_sel_hi:[0,0,0]
	v_mfma_scale_f32_16x16x128_f8f6f4 v[166:169], v[10:17], v[174:181], v[166:169], v237, v237 op_sel_hi:[0,0,0]
	v_mfma_scale_f32_16x16x128_f8f6f4 v[158:161], v[2:9], v[174:181], v[158:161], v237, v237 op_sel_hi:[0,0,0]
	v_mfma_scale_f32_16x16x128_f8f6f4 v[150:153], v[10:17], v[182:189], v[150:153], v237, v237 op_sel_hi:[0,0,0]
	v_mfma_scale_f32_16x16x128_f8f6f4 v[146:149], v[2:9], v[182:189], v[146:149], v237, v237 op_sel_hi:[0,0,0]
	v_mfma_scale_f32_16x16x128_f8f6f4 v[142:145], v[10:17], v[190:197], v[142:145], v237, v237 op_sel_hi:[0,0,0]
	v_mfma_scale_f32_16x16x128_f8f6f4 v[138:141], v[2:9], v[190:197], v[138:141], v237, v237 op_sel_hi:[0,0,0]
	v_mfma_scale_f32_16x16x128_f8f6f4 v[126:129], v[10:17], v[204:211], v[126:129], v237, v237 op_sel_hi:[0,0,0]
	v_mfma_scale_f32_16x16x128_f8f6f4 v[122:125], v[2:9], v[204:211], v[122:125], v237, v237 op_sel_hi:[0,0,0]
	s_setprio 0
	s_barrier
	s_add_i32 s62, s62, 2
	s_addk_i32 s63, 0x100
	s_cmp_gt_u32 s62, 41
	s_cbranch_scc0 .LBB0_412
	s_nop 15
	s_nop 15
	s_and_b64 vcc, exec, s[28:29]
	s_cbranch_vccz .LBB0_408
	s_mov_b32 s10, s55
	s_mov_b32 s0, s56
	s_mov_b32 s13, s59
	s_mov_b32 s37, s58
	s_mov_b32 s54, s57
	s_branch .LBB0_408

.LBB0_572:
	v_add_u32_e32 v137, 0x10000, v135
	s_waitcnt vmcnt(12)
	v_add_u32_e32 v138, 0x14000, v135
	ds_read_b128 v[2:5], v137
	ds_read_b128 v[6:9], v137 offset:1024
	ds_read_b128 v[10:13], v137 offset:2048
	ds_read_b128 v[14:17], v137 offset:3072
	ds_read_b128 v[18:21], v138
	ds_read_b128 v[22:25], v138 offset:1024
	ds_read_b128 v[26:29], v138 offset:2048
	ds_read_b128 v[30:33], v138 offset:3072
	s_or_b32 s58, s35, 0x80
	s_or_b32 s59, s28, 0x100
	s_mul_i32 s54, s52, 0x2c0000
	s_and_b64 s[6:7], s[26:27], exec
	s_cselect_b32 s56, s54, s35
	s_or_b32 s60, s35, 0x100
	s_mul_i32 s55, s51, 0x2c0000
	s_and_b64 s[6:7], s[26:27], exec
	s_cselect_b32 s57, s55, s28
	s_mov_b32 m0, s46
	ds_read_b128 v[34:37], v136
	ds_read_b128 v[38:41], v136 offset:1024
	ds_read_b128 v[42:45], v136 offset:2048
	ds_read_b128 v[46:49], v136 offset:3072
	ds_read_b128 v[50:53], v136 offset:4096
	ds_read_b128 v[54:57], v136 offset:5120
	ds_read_b128 v[58:61], v136 offset:6144
	ds_read_b128 v[62:65], v136 offset:7168
	buffer_load_dwordx4 v127, s[64:67], s58 offen lds
	s_mov_b32 m0, s48
	s_add_i32 s6, s35, 0x160080
	buffer_load_dwordx4 v129, s[64:67], s58 offen lds
	s_mov_b32 m0, s47
	s_nop 0
	buffer_load_dwordx4 v127, s[64:67], s6 offen lds
	s_mov_b32 m0, s49
	s_nop 0
	buffer_load_dwordx4 v129, s[64:67], s6 offen lds
	s_waitcnt vmcnt(8)
	s_waitcnt lgkmcnt(0)
	s_barrier
	s_setprio 1
	v_mfma_f32_16x16x32_bf16 v[66:69], v[2:5], v[34:37], 0
	v_mfma_f32_16x16x32_bf16 v[70:73], v[10:13], v[34:37], 0
	v_mfma_f32_16x16x32_bf16 v[98:101], v[18:21], v[34:37], 0
	v_mfma_f32_16x16x32_bf16 v[34:37], v[26:29], v[34:37], 0
	v_mfma_f32_16x16x32_bf16 v[66:69], v[6:9], v[38:41], v[66:69]
	v_mfma_f32_16x16x32_bf16 v[70:73], v[14:17], v[38:41], v[70:73]
	v_mfma_f32_16x16x32_bf16 v[74:77], v[2:5], v[42:45], 0
	v_mfma_f32_16x16x32_bf16 v[78:81], v[10:13], v[42:45], 0
	v_mfma_f32_16x16x32_bf16 v[130:133], v[22:25], v[38:41], v[98:101]
	v_mfma_f32_16x16x32_bf16 v[34:37], v[30:33], v[38:41], v[34:37]
	v_mfma_f32_16x16x32_bf16 v[38:41], v[18:21], v[42:45], 0
	v_mfma_f32_16x16x32_bf16 v[42:45], v[26:29], v[42:45], 0
	v_mfma_f32_16x16x32_bf16 v[74:77], v[6:9], v[46:49], v[74:77]
	v_mfma_f32_16x16x32_bf16 v[78:81], v[14:17], v[46:49], v[78:81]
	v_mfma_f32_16x16x32_bf16 v[82:85], v[2:5], v[50:53], 0
	v_mfma_f32_16x16x32_bf16 v[86:89], v[10:13], v[50:53], 0
	v_mfma_f32_16x16x32_bf16 v[38:41], v[22:25], v[46:49], v[38:41]
	v_mfma_f32_16x16x32_bf16 v[42:45], v[30:33], v[46:49], v[42:45]
	v_mfma_f32_16x16x32_bf16 v[46:49], v[18:21], v[50:53], 0
	v_mfma_f32_16x16x32_bf16 v[50:53], v[26:29], v[50:53], 0
	v_mfma_f32_16x16x32_bf16 v[82:85], v[6:9], v[54:57], v[82:85]
	v_mfma_f32_16x16x32_bf16 v[86:89], v[14:17], v[54:57], v[86:89]
	v_mfma_f32_16x16x32_bf16 v[90:93], v[2:5], v[58:61], 0
	v_mfma_f32_16x16x32_bf16 v[94:97], v[10:13], v[58:61], 0
	v_mfma_f32_16x16x32_bf16 v[46:49], v[22:25], v[54:57], v[46:49]
	v_mfma_f32_16x16x32_bf16 v[50:53], v[30:33], v[54:57], v[50:53]
	v_mfma_f32_16x16x32_bf16 v[54:57], v[18:21], v[58:61], 0
	v_mfma_f32_16x16x32_bf16 v[58:61], v[26:29], v[58:61], 0
	v_mfma_f32_16x16x32_bf16 v[90:93], v[6:9], v[62:65], v[90:93]
	v_mfma_f32_16x16x32_bf16 v[94:97], v[14:17], v[62:65], v[94:97]
	v_mfma_f32_16x16x32_bf16 v[54:57], v[22:25], v[62:65], v[54:57]
	v_mfma_f32_16x16x32_bf16 v[58:61], v[30:33], v[62:65], v[58:61]
	s_setprio 0
	s_barrier
	s_mov_b32 m0, s13
	s_mov_b32 s6, s66
	s_mov_b32 s7, s67
	ds_read_b128 v[62:65], v136 offset:16384
	ds_read_b128 v[98:101], v136 offset:17408
	ds_read_b128 v[102:105], v136 offset:18432
	ds_read_b128 v[106:109], v136 offset:19456
	ds_read_b128 v[110:113], v136 offset:20480
	ds_read_b128 v[114:117], v136 offset:21504
	ds_read_b128 v[118:121], v136 offset:22528
	ds_read_b128 v[122:125], v136 offset:23552
	buffer_load_dwordx4 v128, s[4:7], s59 offen lds
	s_mov_b32 m0, s29
	s_add_i32 s58, s28, 0x160100
	buffer_load_dwordx4 v134, s[4:7], s59 offen lds
	s_mov_b32 m0, s30
	s_nop 0
	buffer_load_dwordx4 v128, s[4:7], s58 offen lds
	s_mov_b32 m0, s31
	s_nop 0
	buffer_load_dwordx4 v134, s[4:7], s58 offen lds
	s_waitcnt vmcnt(6)
	s_waitcnt lgkmcnt(0)
	s_barrier
	s_setprio 1
	v_mfma_f32_16x16x32_bf16 v[140:143], v[2:5], v[62:65], 0
	v_mfma_f32_16x16x32_bf16 v[150:153], v[2:5], v[102:105], 0
	v_mfma_f32_16x16x32_bf16 v[158:161], v[2:5], v[110:113], 0
	v_mfma_f32_16x16x32_bf16 v[2:5], v[2:5], v[118:121], 0
	v_mfma_f32_16x16x32_bf16 v[166:169], v[6:9], v[122:125], v[2:5]
	v_mfma_f32_16x16x32_bf16 v[2:5], v[10:13], v[118:121], 0
	v_mfma_f32_16x16x32_bf16 v[170:173], v[14:17], v[122:125], v[2:5]
	v_mfma_f32_16x16x32_bf16 v[2:5], v[18:21], v[62:65], 0
	v_mfma_f32_16x16x32_bf16 v[174:177], v[22:25], v[98:101], v[2:5]
	v_mfma_f32_16x16x32_bf16 v[2:5], v[26:29], v[62:65], 0
	v_mfma_f32_16x16x32_bf16 v[146:149], v[10:13], v[62:65], 0
	v_mfma_f32_16x16x32_bf16 v[62:65], v[30:33], v[98:101], v[2:5]
	v_mfma_f32_16x16x32_bf16 v[2:5], v[18:21], v[102:105], 0
	v_mfma_f32_16x16x32_bf16 v[178:181], v[22:25], v[106:109], v[2:5]
	v_mfma_f32_16x16x32_bf16 v[2:5], v[26:29], v[102:105], 0
	v_mfma_f32_16x16x32_bf16 v[182:185], v[30:33], v[106:109], v[2:5]
	v_mfma_f32_16x16x32_bf16 v[2:5], v[18:21], v[110:113], 0
	v_mfma_f32_16x16x32_bf16 v[186:189], v[22:25], v[114:117], v[2:5]
	v_mfma_f32_16x16x32_bf16 v[2:5], v[26:29], v[110:113], 0
	v_mfma_f32_16x16x32_bf16 v[190:193], v[30:33], v[114:117], v[2:5]
	v_mfma_f32_16x16x32_bf16 v[2:5], v[18:21], v[118:121], 0
	v_mfma_f32_16x16x32_bf16 v[154:157], v[10:13], v[102:105], 0
	v_mfma_f32_16x16x32_bf16 v[162:165], v[10:13], v[110:113], 0
	v_mfma_f32_16x16x32_bf16 v[194:197], v[22:25], v[122:125], v[2:5]
	v_mfma_f32_16x16x32_bf16 v[2:5], v[26:29], v[118:121], 0
	v_mfma_f32_16x16x32_bf16 v[142:145], v[6:9], v[98:101], v[140:143]
	v_mfma_f32_16x16x32_bf16 v[146:149], v[14:17], v[98:101], v[146:149]
	v_mfma_f32_16x16x32_bf16 v[150:153], v[6:9], v[106:109], v[150:153]
	v_mfma_f32_16x16x32_bf16 v[154:157], v[14:17], v[106:109], v[154:157]
	v_mfma_f32_16x16x32_bf16 v[158:161], v[6:9], v[114:117], v[158:161]
	v_mfma_f32_16x16x32_bf16 v[162:165], v[14:17], v[114:117], v[162:165]
	v_mfma_f32_16x16x32_bf16 v[198:201], v[30:33], v[122:125], v[2:5]
	s_setprio 0
	s_barrier
	v_add_u32_e32 v139, 0x18000, v135
	v_add_u32_e32 v140, 0x1c000, v135
	ds_read_b128 v[26:29], v139
	ds_read_b128 v[204:207], v139 offset:1024
	ds_read_b128 v[208:211], v139 offset:2048
	ds_read_b128 v[212:215], v139 offset:3072
	ds_read_b128 v[216:219], v140
	ds_read_b128 v[220:223], v140 offset:1024
	ds_read_b128 v[224:227], v140 offset:2048
	ds_read_b128 v[228:231], v140 offset:3072
	s_mov_b32 m0, s12
	ds_read_b128 v[6:9], v136 offset:32768
	ds_read_b128 v[10:13], v136 offset:33792
	ds_read_b128 v[14:17], v136 offset:34816
	ds_read_b128 v[18:21], v136 offset:35840
	ds_read_b128 v[22:25], v136 offset:36864
	ds_read_b128 v[244:247], v136 offset:37888
	ds_read_b128 v[250:253], v136 offset:38912
	ds_read_b128 v[238:241], v136 offset:39936
	buffer_load_dwordx4 v127, s[64:67], s60 offen lds
	s_mov_b32 m0, s34
	s_add_i32 s58, s35, 0x160100
	buffer_load_dwordx4 v129, s[64:67], s60 offen lds
	s_mov_b32 m0, s36
	s_nop 0
	buffer_load_dwordx4 v127, s[64:67], s58 offen lds
	s_mov_b32 m0, s37
	s_nop 0
	buffer_load_dwordx4 v129, s[64:67], s58 offen lds
	s_waitcnt vmcnt(8)
	s_waitcnt lgkmcnt(0)
	s_barrier
	s_setprio 1
	v_mfma_f32_16x16x32_bf16 v[2:5], v[26:29], v[6:9], v[66:69]
	v_mfma_f32_16x16x32_bf16 v[122:125], v[204:207], v[10:13], v[2:5]
	v_mfma_f32_16x16x32_bf16 v[2:5], v[208:211], v[6:9], v[70:73]
	v_mfma_f32_16x16x32_bf16 v[30:33], v[216:219], v[6:9], v[130:133]
	v_mfma_f32_16x16x32_bf16 v[6:9], v[224:227], v[6:9], v[34:37]
	v_mfma_f32_16x16x32_bf16 v[118:121], v[212:215], v[10:13], v[2:5]
	v_mfma_f32_16x16x32_bf16 v[2:5], v[26:29], v[14:17], v[74:77]
	v_mfma_f32_16x16x32_bf16 v[34:37], v[228:231], v[10:13], v[6:9]
	v_mfma_f32_16x16x32_bf16 v[6:9], v[216:219], v[14:17], v[38:41]
	v_mfma_f32_16x16x32_bf16 v[114:117], v[204:207], v[18:21], v[2:5]
	v_mfma_f32_16x16x32_bf16 v[2:5], v[208:211], v[14:17], v[78:81]
	v_mfma_f32_16x16x32_bf16 v[30:33], v[220:223], v[10:13], v[30:33]
	v_mfma_f32_16x16x32_bf16 v[10:13], v[220:223], v[18:21], v[6:9]
	v_mfma_f32_16x16x32_bf16 v[6:9], v[224:227], v[14:17], v[42:45]
	v_mfma_f32_16x16x32_bf16 v[110:113], v[212:215], v[18:21], v[2:5]
	v_mfma_f32_16x16x32_bf16 v[2:5], v[26:29], v[22:25], v[82:85]
	v_mfma_f32_16x16x32_bf16 v[14:17], v[228:231], v[18:21], v[6:9]
	v_mfma_f32_16x16x32_bf16 v[6:9], v[216:219], v[22:25], v[46:49]
	v_mfma_f32_16x16x32_bf16 v[98:101], v[204:207], v[244:247], v[2:5]
	v_mfma_f32_16x16x32_bf16 v[2:5], v[208:211], v[22:25], v[86:89]
	v_mfma_f32_16x16x32_bf16 v[18:21], v[220:223], v[244:247], v[6:9]
	v_mfma_f32_16x16x32_bf16 v[6:9], v[224:227], v[22:25], v[50:53]
	v_mfma_f32_16x16x32_bf16 v[106:109], v[212:215], v[244:247], v[2:5]
	v_mfma_f32_16x16x32_bf16 v[2:5], v[26:29], v[250:253], v[90:93]
	v_mfma_f32_16x16x32_bf16 v[22:25], v[228:231], v[244:247], v[6:9]
	v_mfma_f32_16x16x32_bf16 v[6:9], v[216:219], v[250:253], v[54:57]
	v_mfma_f32_16x16x32_bf16 v[102:105], v[204:207], v[238:241], v[2:5]
	v_mfma_f32_16x16x32_bf16 v[2:5], v[208:211], v[250:253], v[94:97]
	v_mfma_f32_16x16x32_bf16 v[94:97], v[220:223], v[238:241], v[6:9]
	v_mfma_f32_16x16x32_bf16 v[6:9], v[224:227], v[250:253], v[58:61]
	v_mfma_f32_16x16x32_bf16 v[2:5], v[212:215], v[238:241], v[2:5]
	v_mfma_f32_16x16x32_bf16 v[6:9], v[228:231], v[238:241], v[6:9]
	s_setprio 0
	s_barrier
	s_mov_b32 m0, s42
	s_or_b32 s58, s28, 0x180
	ds_read_b128 v[38:41], v136 offset:49152
	ds_read_b128 v[46:49], v136 offset:50176
	ds_read_b128 v[54:57], v136 offset:51200
	ds_read_b128 v[86:89], v136 offset:52224
	ds_read_b128 v[130:133], v136 offset:53248
	ds_read_b128 v[238:241], v136 offset:54272
	ds_read_b128 v[244:247], v136 offset:55296
	ds_read_b128 v[250:253], v136 offset:56320
	buffer_load_dwordx4 v128, s[4:7], s58 offen lds
	s_mov_b32 m0, s43
	s_nop 0
	buffer_load_dwordx4 v134, s[4:7], s58 offen lds
	s_add_i32 s58, s28, 0x160180
	s_mov_b32 m0, s44
	s_nop 0
	buffer_load_dwordx4 v128, s[4:7], s58 offen lds
	s_mov_b32 m0, s45
	s_nop 0
	buffer_load_dwordx4 v134, s[4:7], s58 offen lds
	s_waitcnt vmcnt(6)
	s_waitcnt lgkmcnt(0)
	s_barrier
	s_setprio 1
	v_mfma_f32_16x16x32_bf16 v[42:45], v[26:29], v[38:41], v[142:145]
	v_mfma_f32_16x16x32_bf16 v[74:77], v[204:207], v[46:49], v[42:45]
	v_mfma_f32_16x16x32_bf16 v[42:45], v[208:211], v[38:41], v[146:149]
	v_mfma_f32_16x16x32_bf16 v[82:85], v[212:215], v[46:49], v[42:45]
	v_mfma_f32_16x16x32_bf16 v[42:45], v[26:29], v[54:57], v[150:153]
	v_mfma_f32_16x16x32_bf16 v[66:69], v[204:207], v[86:89], v[42:45]
	v_mfma_f32_16x16x32_bf16 v[42:45], v[208:211], v[54:57], v[154:157]
	v_mfma_f32_16x16x32_bf16 v[70:73], v[212:215], v[86:89], v[42:45]
	v_mfma_f32_16x16x32_bf16 v[42:45], v[26:29], v[130:133], v[158:161]
	v_mfma_f32_16x16x32_bf16 v[26:29], v[26:29], v[244:247], v[166:169]
	v_mfma_f32_16x16x32_bf16 v[90:93], v[204:207], v[238:241], v[42:45]
	v_mfma_f32_16x16x32_bf16 v[42:45], v[208:211], v[130:133], v[162:165]
	v_mfma_f32_16x16x32_bf16 v[78:81], v[204:207], v[250:253], v[26:29]
	v_mfma_f32_16x16x32_bf16 v[26:29], v[208:211], v[244:247], v[170:173]
	v_mfma_f32_16x16x32_bf16 v[50:53], v[212:215], v[238:241], v[42:45]
	v_mfma_f32_16x16x32_bf16 v[42:45], v[212:215], v[250:253], v[26:29]
	v_mfma_f32_16x16x32_bf16 v[26:29], v[216:219], v[38:41], v[174:177]
	v_mfma_f32_16x16x32_bf16 v[38:41], v[224:227], v[38:41], v[62:65]
	v_mfma_f32_16x16x32_bf16 v[26:29], v[220:223], v[46:49], v[26:29]
	v_mfma_f32_16x16x32_bf16 v[38:41], v[228:231], v[46:49], v[38:41]
	v_mfma_f32_16x16x32_bf16 v[46:49], v[216:219], v[54:57], v[178:181]
	v_mfma_f32_16x16x32_bf16 v[58:61], v[220:223], v[86:89], v[46:49]
	v_mfma_f32_16x16x32_bf16 v[46:49], v[224:227], v[54:57], v[182:185]
	v_mfma_f32_16x16x32_bf16 v[62:65], v[228:231], v[86:89], v[46:49]
	v_mfma_f32_16x16x32_bf16 v[46:49], v[216:219], v[130:133], v[186:189]
	v_mfma_f32_16x16x32_bf16 v[86:89], v[220:223], v[238:241], v[46:49]
	v_mfma_f32_16x16x32_bf16 v[46:49], v[224:227], v[130:133], v[190:193]
	v_mfma_f32_16x16x32_bf16 v[54:57], v[228:231], v[238:241], v[46:49]
	v_mfma_f32_16x16x32_bf16 v[46:49], v[216:219], v[244:247], v[194:197]
	v_mfma_f32_16x16x32_bf16 v[130:133], v[220:223], v[250:253], v[46:49]
	v_mfma_f32_16x16x32_bf16 v[46:49], v[224:227], v[244:247], v[198:201]
	v_mfma_f32_16x16x32_bf16 v[46:49], v[228:231], v[250:253], v[46:49]
	s_setprio 0
	s_barrier
	s_mov_b32 s58, 0
	s_movk_i32 s59, 0xd600
.LBB0_573:
	ds_read_b128 v[142:145], v137
	ds_read_b128 v[146:149], v137 offset:1024
	ds_read_b128 v[150:153], v137 offset:2048
	ds_read_b128 v[154:157], v137 offset:3072
	ds_read_b128 v[158:161], v138
	ds_read_b128 v[162:165], v138 offset:1024
	ds_read_b128 v[166:169], v138 offset:2048
	ds_read_b128 v[170:173], v138 offset:3072
	s_add_i32 s61, s35, s59
	s_add_i32 s60, s28, s59
	s_add_i32 s62, s61, 0x2c00
	s_addk_i32 s60, 0x2c00
	s_cmp_eq_u32 s59, 0
	s_cselect_b32 s60, s57, s60
	s_cselect_b32 s62, s56, s62
	s_add_i32 s63, s61, 0x2b80
	s_mov_b32 m0, s46
	ds_read_b128 v[174:177], v136
	ds_read_b128 v[178:181], v136 offset:1024
	ds_read_b128 v[182:185], v136 offset:2048
	ds_read_b128 v[186:189], v136 offset:3072
	ds_read_b128 v[190:193], v136 offset:4096
	ds_read_b128 v[194:197], v136 offset:5120
	ds_read_b128 v[198:201], v136 offset:6144
	ds_read_b128 v[204:207], v136 offset:7168
	buffer_load_dwordx4 v127, s[64:67], s63 offen lds
	s_mov_b32 m0, s48
	s_add_i32 s61, s61, 0x162b80
	buffer_load_dwordx4 v129, s[64:67], s63 offen lds
	s_mov_b32 m0, s47
	s_nop 0
	buffer_load_dwordx4 v127, s[64:67], s61 offen lds
	s_mov_b32 m0, s49
	s_nop 0
	buffer_load_dwordx4 v129, s[64:67], s61 offen lds
	s_waitcnt vmcnt(8)
	s_waitcnt lgkmcnt(0)
	s_barrier
	s_setprio 1
	v_mfma_f32_16x16x32_bf16 v[122:125], v[142:145], v[174:177], v[122:125]
	v_mfma_f32_16x16x32_bf16 v[118:121], v[150:153], v[174:177], v[118:121]
	v_mfma_f32_16x16x32_bf16 v[114:117], v[142:145], v[182:185], v[114:117]
	v_mfma_f32_16x16x32_bf16 v[110:113], v[150:153], v[182:185], v[110:113]
	v_mfma_f32_16x16x32_bf16 v[98:101], v[142:145], v[190:193], v[98:101]
	v_mfma_f32_16x16x32_bf16 v[106:109], v[150:153], v[190:193], v[106:109]
	v_mfma_f32_16x16x32_bf16 v[102:105], v[142:145], v[198:201], v[102:105]
	v_mfma_f32_16x16x32_bf16 v[2:5], v[150:153], v[198:201], v[2:5]
	v_mfma_f32_16x16x32_bf16 v[30:33], v[158:161], v[174:177], v[30:33]
	v_mfma_f32_16x16x32_bf16 v[34:37], v[166:169], v[174:177], v[34:37]
	v_mfma_f32_16x16x32_bf16 v[10:13], v[158:161], v[182:185], v[10:13]
	v_mfma_f32_16x16x32_bf16 v[14:17], v[166:169], v[182:185], v[14:17]
	v_mfma_f32_16x16x32_bf16 v[18:21], v[158:161], v[190:193], v[18:21]
	v_mfma_f32_16x16x32_bf16 v[22:25], v[166:169], v[190:193], v[22:25]
	v_mfma_f32_16x16x32_bf16 v[94:97], v[158:161], v[198:201], v[94:97]
	v_mfma_f32_16x16x32_bf16 v[6:9], v[166:169], v[198:201], v[6:9]
	v_mfma_f32_16x16x32_bf16 v[122:125], v[146:149], v[178:181], v[122:125]
	v_mfma_f32_16x16x32_bf16 v[118:121], v[154:157], v[178:181], v[118:121]
	v_mfma_f32_16x16x32_bf16 v[114:117], v[146:149], v[186:189], v[114:117]
	v_mfma_f32_16x16x32_bf16 v[110:113], v[154:157], v[186:189], v[110:113]
	v_mfma_f32_16x16x32_bf16 v[98:101], v[146:149], v[194:197], v[98:101]
	v_mfma_f32_16x16x32_bf16 v[106:109], v[154:157], v[194:197], v[106:109]
	v_mfma_f32_16x16x32_bf16 v[102:105], v[146:149], v[204:207], v[102:105]
	v_mfma_f32_16x16x32_bf16 v[2:5], v[154:157], v[204:207], v[2:5]
	v_mfma_f32_16x16x32_bf16 v[30:33], v[162:165], v[178:181], v[30:33]
	v_mfma_f32_16x16x32_bf16 v[34:37], v[170:173], v[178:181], v[34:37]
	v_mfma_f32_16x16x32_bf16 v[10:13], v[162:165], v[186:189], v[10:13]
	v_mfma_f32_16x16x32_bf16 v[14:17], v[170:173], v[186:189], v[14:17]
	v_mfma_f32_16x16x32_bf16 v[18:21], v[162:165], v[194:197], v[18:21]
	v_mfma_f32_16x16x32_bf16 v[22:25], v[170:173], v[194:197], v[22:25]
	v_mfma_f32_16x16x32_bf16 v[94:97], v[162:165], v[204:207], v[94:97]
	v_mfma_f32_16x16x32_bf16 v[6:9], v[170:173], v[204:207], v[6:9]
	s_setprio 0
	s_barrier
	s_mov_b32 m0, s13
	ds_read_b128 v[174:177], v136 offset:16384
	ds_read_b128 v[178:181], v136 offset:17408
	ds_read_b128 v[182:185], v136 offset:18432
	ds_read_b128 v[186:189], v136 offset:19456
	ds_read_b128 v[190:193], v136 offset:20480
	ds_read_b128 v[194:197], v136 offset:21504
	ds_read_b128 v[198:201], v136 offset:22528
	ds_read_b128 v[204:207], v136 offset:23552
	buffer_load_dwordx4 v128, s[4:7], s60 offen lds
	s_mov_b32 m0, s29
	s_add_i32 s61, s60, 0x160000
	buffer_load_dwordx4 v134, s[4:7], s60 offen lds
	s_mov_b32 m0, s30
	s_nop 0
	buffer_load_dwordx4 v128, s[4:7], s61 offen lds
	s_mov_b32 m0, s31
	s_nop 0
	buffer_load_dwordx4 v134, s[4:7], s61 offen lds
	s_waitcnt vmcnt(6)
	s_waitcnt lgkmcnt(0)
	s_barrier
	s_setprio 1
	v_mfma_f32_16x16x32_bf16 v[74:77], v[142:145], v[174:177], v[74:77]
	v_mfma_f32_16x16x32_bf16 v[82:85], v[150:153], v[174:177], v[82:85]
	v_mfma_f32_16x16x32_bf16 v[66:69], v[142:145], v[182:185], v[66:69]
	v_mfma_f32_16x16x32_bf16 v[70:73], v[150:153], v[182:185], v[70:73]
	v_mfma_f32_16x16x32_bf16 v[90:93], v[142:145], v[190:193], v[90:93]
	v_mfma_f32_16x16x32_bf16 v[50:53], v[150:153], v[190:193], v[50:53]
	v_mfma_f32_16x16x32_bf16 v[78:81], v[142:145], v[198:201], v[78:81]
	v_mfma_f32_16x16x32_bf16 v[42:45], v[150:153], v[198:201], v[42:45]
	v_mfma_f32_16x16x32_bf16 v[26:29], v[158:161], v[174:177], v[26:29]
	v_mfma_f32_16x16x32_bf16 v[38:41], v[166:169], v[174:177], v[38:41]
	v_mfma_f32_16x16x32_bf16 v[58:61], v[158:161], v[182:185], v[58:61]
	v_mfma_f32_16x16x32_bf16 v[62:65], v[166:169], v[182:185], v[62:65]
	v_mfma_f32_16x16x32_bf16 v[86:89], v[158:161], v[190:193], v[86:89]
	v_mfma_f32_16x16x32_bf16 v[54:57], v[166:169], v[190:193], v[54:57]
	v_mfma_f32_16x16x32_bf16 v[130:133], v[158:161], v[198:201], v[130:133]
	v_mfma_f32_16x16x32_bf16 v[46:49], v[166:169], v[198:201], v[46:49]
	v_mfma_f32_16x16x32_bf16 v[74:77], v[146:149], v[178:181], v[74:77]
	v_mfma_f32_16x16x32_bf16 v[82:85], v[154:157], v[178:181], v[82:85]
	v_mfma_f32_16x16x32_bf16 v[66:69], v[146:149], v[186:189], v[66:69]
	v_mfma_f32_16x16x32_bf16 v[70:73], v[154:157], v[186:189], v[70:73]
	v_mfma_f32_16x16x32_bf16 v[90:93], v[146:149], v[194:197], v[90:93]
	v_mfma_f32_16x16x32_bf16 v[50:53], v[154:157], v[194:197], v[50:53]
	v_mfma_f32_16x16x32_bf16 v[78:81], v[146:149], v[204:207], v[78:81]
	v_mfma_f32_16x16x32_bf16 v[42:45], v[154:157], v[204:207], v[42:45]
	v_mfma_f32_16x16x32_bf16 v[26:29], v[162:165], v[178:181], v[26:29]
	v_mfma_f32_16x16x32_bf16 v[38:41], v[170:173], v[178:181], v[38:41]
	v_mfma_f32_16x16x32_bf16 v[58:61], v[162:165], v[186:189], v[58:61]
	v_mfma_f32_16x16x32_bf16 v[62:65], v[170:173], v[186:189], v[62:65]
	v_mfma_f32_16x16x32_bf16 v[86:89], v[162:165], v[194:197], v[86:89]
	v_mfma_f32_16x16x32_bf16 v[54:57], v[170:173], v[194:197], v[54:57]
	v_mfma_f32_16x16x32_bf16 v[130:133], v[162:165], v[204:207], v[130:133]
	v_mfma_f32_16x16x32_bf16 v[46:49], v[170:173], v[204:207], v[46:49]
	s_setprio 0
	s_barrier
	ds_read_b128 v[142:145], v139
	ds_read_b128 v[146:149], v139 offset:1024
	ds_read_b128 v[150:153], v139 offset:2048
	ds_read_b128 v[154:157], v139 offset:3072
	ds_read_b128 v[158:161], v140
	ds_read_b128 v[162:165], v140 offset:1024
	ds_read_b128 v[166:169], v140 offset:2048
	ds_read_b128 v[170:173], v140 offset:3072
	s_mov_b32 m0, s12
	ds_read_b128 v[174:177], v136 offset:32768
	ds_read_b128 v[178:181], v136 offset:33792
	ds_read_b128 v[182:185], v136 offset:34816
	ds_read_b128 v[186:189], v136 offset:35840
	ds_read_b128 v[190:193], v136 offset:36864
	ds_read_b128 v[194:197], v136 offset:37888
	ds_read_b128 v[198:201], v136 offset:38912
	ds_read_b128 v[204:207], v136 offset:39936
	buffer_load_dwordx4 v127, s[64:67], s62 offen lds
	s_mov_b32 m0, s34
	s_nop 0
	buffer_load_dwordx4 v129, s[64:67], s62 offen lds
	s_add_i32 s62, s62, 0x160000
	s_mov_b32 m0, s36
	s_nop 0
	buffer_load_dwordx4 v127, s[64:67], s62 offen lds
	s_mov_b32 m0, s37
	s_nop 0
	buffer_load_dwordx4 v129, s[64:67], s62 offen lds
	s_waitcnt vmcnt(8)
	s_waitcnt lgkmcnt(0)
	s_barrier
	s_setprio 1
	v_mfma_f32_16x16x32_bf16 v[122:125], v[142:145], v[174:177], v[122:125]
	v_mfma_f32_16x16x32_bf16 v[118:121], v[150:153], v[174:177], v[118:121]
	v_mfma_f32_16x16x32_bf16 v[114:117], v[142:145], v[182:185], v[114:117]
	v_mfma_f32_16x16x32_bf16 v[110:113], v[150:153], v[182:185], v[110:113]
	v_mfma_f32_16x16x32_bf16 v[98:101], v[142:145], v[190:193], v[98:101]
	v_mfma_f32_16x16x32_bf16 v[106:109], v[150:153], v[190:193], v[106:109]
	v_mfma_f32_16x16x32_bf16 v[102:105], v[142:145], v[198:201], v[102:105]
	v_mfma_f32_16x16x32_bf16 v[2:5], v[150:153], v[198:201], v[2:5]
	v_mfma_f32_16x16x32_bf16 v[30:33], v[158:161], v[174:177], v[30:33]
	v_mfma_f32_16x16x32_bf16 v[34:37], v[166:169], v[174:177], v[34:37]
	v_mfma_f32_16x16x32_bf16 v[10:13], v[158:161], v[182:185], v[10:13]
	v_mfma_f32_16x16x32_bf16 v[14:17], v[166:169], v[182:185], v[14:17]
	v_mfma_f32_16x16x32_bf16 v[18:21], v[158:161], v[190:193], v[18:21]
	v_mfma_f32_16x16x32_bf16 v[22:25], v[166:169], v[190:193], v[22:25]
	v_mfma_f32_16x16x32_bf16 v[94:97], v[158:161], v[198:201], v[94:97]
	v_mfma_f32_16x16x32_bf16 v[6:9], v[166:169], v[198:201], v[6:9]
	v_mfma_f32_16x16x32_bf16 v[122:125], v[146:149], v[178:181], v[122:125]
	v_mfma_f32_16x16x32_bf16 v[118:121], v[154:157], v[178:181], v[118:121]
	v_mfma_f32_16x16x32_bf16 v[114:117], v[146:149], v[186:189], v[114:117]
	v_mfma_f32_16x16x32_bf16 v[110:113], v[154:157], v[186:189], v[110:113]
	v_mfma_f32_16x16x32_bf16 v[98:101], v[146:149], v[194:197], v[98:101]
	v_mfma_f32_16x16x32_bf16 v[106:109], v[154:157], v[194:197], v[106:109]
	v_mfma_f32_16x16x32_bf16 v[102:105], v[146:149], v[204:207], v[102:105]
	v_mfma_f32_16x16x32_bf16 v[2:5], v[154:157], v[204:207], v[2:5]
	v_mfma_f32_16x16x32_bf16 v[30:33], v[162:165], v[178:181], v[30:33]
	v_mfma_f32_16x16x32_bf16 v[34:37], v[170:173], v[178:181], v[34:37]
	v_mfma_f32_16x16x32_bf16 v[10:13], v[162:165], v[186:189], v[10:13]
	v_mfma_f32_16x16x32_bf16 v[14:17], v[170:173], v[186:189], v[14:17]
	v_mfma_f32_16x16x32_bf16 v[18:21], v[162:165], v[194:197], v[18:21]
	v_mfma_f32_16x16x32_bf16 v[22:25], v[170:173], v[194:197], v[22:25]
	v_mfma_f32_16x16x32_bf16 v[94:97], v[162:165], v[204:207], v[94:97]
	v_mfma_f32_16x16x32_bf16 v[6:9], v[170:173], v[204:207], v[6:9]
	s_setprio 0
	s_barrier
	s_mov_b32 m0, s42
	s_or_b32 s61, s60, 0x80
	ds_read_b128 v[174:177], v136 offset:49152
	ds_read_b128 v[178:181], v136 offset:50176
	ds_read_b128 v[182:185], v136 offset:51200
	ds_read_b128 v[186:189], v136 offset:52224
	ds_read_b128 v[190:193], v136 offset:53248
	ds_read_b128 v[194:197], v136 offset:54272
	ds_read_b128 v[198:201], v136 offset:55296
	ds_read_b128 v[204:207], v136 offset:56320
	buffer_load_dwordx4 v128, s[4:7], s61 offen lds
	s_mov_b32 m0, s43
	s_add_i32 s60, s60, 0x160080
	buffer_load_dwordx4 v134, s[4:7], s61 offen lds
	s_mov_b32 m0, s44
	s_nop 0
	buffer_load_dwordx4 v128, s[4:7], s60 offen lds
	s_mov_b32 m0, s45
	s_nop 0
	buffer_load_dwordx4 v134, s[4:7], s60 offen lds
	s_waitcnt vmcnt(6)
	s_waitcnt lgkmcnt(0)
	s_barrier
	s_setprio 1
	v_mfma_f32_16x16x32_bf16 v[74:77], v[142:145], v[174:177], v[74:77]
	v_mfma_f32_16x16x32_bf16 v[82:85], v[150:153], v[174:177], v[82:85]
	v_mfma_f32_16x16x32_bf16 v[66:69], v[142:145], v[182:185], v[66:69]
	v_mfma_f32_16x16x32_bf16 v[70:73], v[150:153], v[182:185], v[70:73]
	v_mfma_f32_16x16x32_bf16 v[90:93], v[142:145], v[190:193], v[90:93]
	v_mfma_f32_16x16x32_bf16 v[50:53], v[150:153], v[190:193], v[50:53]
	v_mfma_f32_16x16x32_bf16 v[78:81], v[142:145], v[198:201], v[78:81]
	v_mfma_f32_16x16x32_bf16 v[42:45], v[150:153], v[198:201], v[42:45]
	v_mfma_f32_16x16x32_bf16 v[26:29], v[158:161], v[174:177], v[26:29]
	v_mfma_f32_16x16x32_bf16 v[38:41], v[166:169], v[174:177], v[38:41]
	v_mfma_f32_16x16x32_bf16 v[58:61], v[158:161], v[182:185], v[58:61]
	v_mfma_f32_16x16x32_bf16 v[62:65], v[166:169], v[182:185], v[62:65]
	v_mfma_f32_16x16x32_bf16 v[86:89], v[158:161], v[190:193], v[86:89]
	v_mfma_f32_16x16x32_bf16 v[54:57], v[166:169], v[190:193], v[54:57]
	v_mfma_f32_16x16x32_bf16 v[130:133], v[158:161], v[198:201], v[130:133]
	v_mfma_f32_16x16x32_bf16 v[46:49], v[166:169], v[198:201], v[46:49]
	v_mfma_f32_16x16x32_bf16 v[74:77], v[146:149], v[178:181], v[74:77]
	v_mfma_f32_16x16x32_bf16 v[82:85], v[154:157], v[178:181], v[82:85]
	v_mfma_f32_16x16x32_bf16 v[66:69], v[146:149], v[186:189], v[66:69]
	v_mfma_f32_16x16x32_bf16 v[70:73], v[154:157], v[186:189], v[70:73]
	v_mfma_f32_16x16x32_bf16 v[90:93], v[146:149], v[194:197], v[90:93]
	v_mfma_f32_16x16x32_bf16 v[50:53], v[154:157], v[194:197], v[50:53]
	v_mfma_f32_16x16x32_bf16 v[78:81], v[146:149], v[204:207], v[78:81]
	v_mfma_f32_16x16x32_bf16 v[42:45], v[154:157], v[204:207], v[42:45]
	v_mfma_f32_16x16x32_bf16 v[26:29], v[162:165], v[178:181], v[26:29]
	v_mfma_f32_16x16x32_bf16 v[38:41], v[170:173], v[178:181], v[38:41]
	v_mfma_f32_16x16x32_bf16 v[58:61], v[162:165], v[186:189], v[58:61]
	v_mfma_f32_16x16x32_bf16 v[62:65], v[170:173], v[186:189], v[62:65]
	v_mfma_f32_16x16x32_bf16 v[86:89], v[162:165], v[194:197], v[86:89]
	v_mfma_f32_16x16x32_bf16 v[54:57], v[170:173], v[194:197], v[54:57]
	v_mfma_f32_16x16x32_bf16 v[130:133], v[162:165], v[204:207], v[130:133]
	v_mfma_f32_16x16x32_bf16 v[46:49], v[170:173], v[204:207], v[46:49]
	s_setprio 0
	s_barrier
	s_add_i32 s58, s58, 2
	s_addk_i32 s59, 0x100
	s_cmpk_gt_u32 s58, 0x55
	s_cbranch_scc0 .LBB0_573
	s_and_b64 vcc, exec, s[26:27]
	s_cbranch_vccz .LBB0_569
	s_mov_b32 s11, s51
	s_mov_b32 s0, s52
	s_mov_b32 s28, s55
	s_mov_b32 s35, s54
	s_mov_b32 s50, s53
	s_branch .LBB0_569

.LBB0_674:
	v_add_u32_e32 v169, 0x10000, v167
	v_add_u32_e32 v170, 0x14000, v167
	ds_read_b128 v[2:5], v169
	ds_read_b128 v[6:9], v169 offset:1024
	ds_read_b128 v[10:13], v169 offset:2048
	ds_read_b128 v[14:17], v169 offset:3072
	ds_read_b128 v[18:21], v170
	ds_read_b128 v[22:25], v170 offset:1024
	ds_read_b128 v[26:29], v170 offset:2048
	ds_read_b128 v[30:33], v170 offset:3072
	s_add_i32 s54, s26, 0x200
	s_lshl_b32 s52, s50, 19
	s_lshl_b32 s53, s49, 19
	s_or_b32 s58, s36, 0x80
	s_or_b32 s59, s26, 0x100
	s_and_b64 s[2:3], s[24:25], exec
	s_cselect_b32 s55, s52, s36
	s_or_b32 s57, s36, 0x100
	s_and_b64 s[2:3], s[24:25], exec
	s_cselect_b32 s56, s53, s26
	s_mov_b32 m0, s44
	ds_read_b128 v[34:37], v168
	ds_read_b128 v[38:41], v168 offset:1024
	ds_read_b128 v[42:45], v168 offset:2048
	ds_read_b128 v[46:49], v168 offset:3072
	ds_read_b128 v[50:53], v168 offset:4096
	ds_read_b128 v[54:57], v168 offset:5120
	ds_read_b128 v[66:69], v168 offset:6144
	ds_read_b128 v[70:73], v168 offset:7168
	buffer_load_dwordx4 v163, s[64:67], s58 offen lds
	s_mov_b32 m0, s46
	s_or_b32 s2, s36, 0x40080
	buffer_load_dwordx4 v165, s[64:67], s58 offen lds
	s_mov_b32 m0, s45
	s_nop 0
	buffer_load_dwordx4 v163, s[64:67], s2 offen lds
	s_mov_b32 m0, s47
	s_nop 0
	buffer_load_dwordx4 v165, s[64:67], s2 offen lds
	s_waitcnt vmcnt(8)
	s_waitcnt lgkmcnt(0)
	s_barrier
	s_setprio 1
	v_mfma_scale_f32_16x16x128_f8f6f4 v[62:65], v[2:9], v[34:41], 0, v234, v234 op_sel_hi:[0,0,0]
	v_mfma_scale_f32_16x16x128_f8f6f4 v[58:61], v[10:17], v[34:41], 0, v234, v234 op_sel_hi:[0,0,0]
	v_mfma_scale_f32_16x16x128_f8f6f4 v[78:81], v[2:9], v[42:49], 0, v234, v234 op_sel_hi:[0,0,0]
	v_mfma_scale_f32_16x16x128_f8f6f4 v[74:77], v[10:17], v[42:49], 0, v234, v234 op_sel_hi:[0,0,0]
	v_mfma_scale_f32_16x16x128_f8f6f4 v[94:97], v[2:9], v[50:57], 0, v234, v234 op_sel_hi:[0,0,0]
	v_mfma_scale_f32_16x16x128_f8f6f4 v[90:93], v[10:17], v[50:57], 0, v234, v234 op_sel_hi:[0,0,0]
	v_mfma_scale_f32_16x16x128_f8f6f4 v[106:109], v[2:9], v[66:73], 0, v234, v234 op_sel_hi:[0,0,0]
	v_mfma_scale_f32_16x16x128_f8f6f4 v[102:105], v[10:17], v[66:73], 0, v234, v234 op_sel_hi:[0,0,0]
	v_mfma_scale_f32_16x16x128_f8f6f4 v[158:161], v[18:25], v[34:41], 0, v234, v234 op_sel_hi:[0,0,0]
	v_mfma_scale_f32_16x16x128_f8f6f4 v[154:157], v[26:33], v[34:41], 0, v234, v234 op_sel_hi:[0,0,0]
	v_mfma_scale_f32_16x16x128_f8f6f4 v[150:153], v[18:25], v[42:49], 0, v234, v234 op_sel_hi:[0,0,0]
	v_mfma_scale_f32_16x16x128_f8f6f4 v[146:149], v[26:33], v[42:49], 0, v234, v234 op_sel_hi:[0,0,0]
	v_mfma_scale_f32_16x16x128_f8f6f4 v[142:145], v[18:25], v[50:57], 0, v234, v234 op_sel_hi:[0,0,0]
	s_waitcnt vmcnt(16)
	v_mfma_scale_f32_16x16x128_f8f6f4 v[138:141], v[26:33], v[50:57], 0, v234, v234 op_sel_hi:[0,0,0]
	v_mfma_scale_f32_16x16x128_f8f6f4 v[134:137], v[18:25], v[66:73], 0, v234, v234 op_sel_hi:[0,0,0]
	v_mfma_scale_f32_16x16x128_f8f6f4 v[130:133], v[26:33], v[66:73], 0, v234, v234 op_sel_hi:[0,0,0]
	s_setprio 0
	s_barrier
	s_mov_b32 m0, s11
	s_mov_b32 s2, s66
	s_mov_b32 s3, s67
	ds_read_b128 v[42:45], v168 offset:16384
	ds_read_b128 v[46:49], v168 offset:17408
	ds_read_b128 v[50:53], v168 offset:18432
	ds_read_b128 v[54:57], v168 offset:19456
	ds_read_b128 v[66:69], v168 offset:20480
	ds_read_b128 v[70:73], v168 offset:21504
	ds_read_b128 v[172:175], v168 offset:22528
	ds_read_b128 v[176:179], v168 offset:23552
	buffer_load_dwordx4 v164, s[0:3], s59 offen lds
	s_mov_b32 m0, s30
	s_or_b32 s58, s26, 0x40100
	buffer_load_dwordx4 v166, s[0:3], s59 offen lds
	s_mov_b32 m0, s31
	s_nop 0
	buffer_load_dwordx4 v164, s[0:3], s58 offen lds
	s_mov_b32 m0, s34
	s_nop 0
	buffer_load_dwordx4 v166, s[0:3], s58 offen lds
	s_waitcnt vmcnt(6)
	s_waitcnt lgkmcnt(0)
	s_barrier
	s_setprio 1
	v_mfma_scale_f32_16x16x128_f8f6f4 v[118:121], v[2:9], v[42:49], 0, v234, v234 op_sel_hi:[0,0,0]
	v_mfma_scale_f32_16x16x128_f8f6f4 v[114:117], v[10:17], v[42:49], 0, v234, v234 op_sel_hi:[0,0,0]
	v_mfma_scale_f32_16x16x128_f8f6f4 v[126:129], v[2:9], v[50:57], 0, v234, v234 op_sel_hi:[0,0,0]
	v_mfma_scale_f32_16x16x128_f8f6f4 v[122:125], v[10:17], v[50:57], 0, v234, v234 op_sel_hi:[0,0,0]
	v_mfma_scale_f32_16x16x128_f8f6f4 v[110:113], v[2:9], v[66:73], 0, v234, v234 op_sel_hi:[0,0,0]
	v_mfma_scale_f32_16x16x128_f8f6f4 v[98:101], v[10:17], v[66:73], 0, v234, v234 op_sel_hi:[0,0,0]
	v_mfma_scale_f32_16x16x128_f8f6f4 v[86:89], v[2:9], v[172:179], 0, v234, v234 op_sel_hi:[0,0,0]
	v_mfma_scale_f32_16x16x128_f8f6f4 v[82:85], v[10:17], v[172:179], 0, v234, v234 op_sel_hi:[0,0,0]
	v_mfma_scale_f32_16x16x128_f8f6f4 v[38:41], v[18:25], v[42:49], 0, v234, v234 op_sel_hi:[0,0,0]
	v_mfma_scale_f32_16x16x128_f8f6f4 v[34:37], v[26:33], v[42:49], 0, v234, v234 op_sel_hi:[0,0,0]
	v_mfma_scale_f32_16x16x128_f8f6f4 v[46:49], v[18:25], v[50:57], 0, v234, v234 op_sel_hi:[0,0,0]
	v_mfma_scale_f32_16x16x128_f8f6f4 v[42:45], v[26:33], v[50:57], 0, v234, v234 op_sel_hi:[0,0,0]
	v_mfma_scale_f32_16x16x128_f8f6f4 v[54:57], v[18:25], v[66:73], 0, v234, v234 op_sel_hi:[0,0,0]
	v_mfma_scale_f32_16x16x128_f8f6f4 v[50:53], v[26:33], v[66:73], 0, v234, v234 op_sel_hi:[0,0,0]
	v_mfma_scale_f32_16x16x128_f8f6f4 v[70:73], v[18:25], v[172:179], 0, v234, v234 op_sel_hi:[0,0,0]
	v_mfma_scale_f32_16x16x128_f8f6f4 v[66:69], v[26:33], v[172:179], 0, v234, v234 op_sel_hi:[0,0,0]
	s_setprio 0
	s_barrier
	v_add_u32_e32 v171, 0x18000, v167
	v_add_u32_e32 v172, 0x1c000, v167
	ds_read_b128 v[26:29], v171
	ds_read_b128 v[30:33], v171 offset:1024
	ds_read_b128 v[18:21], v171 offset:2048
	ds_read_b128 v[22:25], v171 offset:3072
	ds_read_b128 v[10:13], v172
	ds_read_b128 v[14:17], v172 offset:1024
	ds_read_b128 v[2:5], v172 offset:2048
	ds_read_b128 v[6:9], v172 offset:3072
	s_mov_b32 m0, s10
	ds_read_b128 v[174:177], v168 offset:32768
	ds_read_b128 v[178:181], v168 offset:33792
	ds_read_b128 v[182:185], v168 offset:34816
	ds_read_b128 v[186:189], v168 offset:35840
	ds_read_b128 v[190:193], v168 offset:36864
	ds_read_b128 v[194:197], v168 offset:37888
	ds_read_b128 v[204:207], v168 offset:38912
	ds_read_b128 v[208:211], v168 offset:39936
	buffer_load_dwordx4 v163, s[64:67], s57 offen lds
	s_mov_b32 m0, s35
	s_nop 0
	buffer_load_dwordx4 v165, s[64:67], s57 offen lds
	s_or_b32 s57, s36, 0x40100
	s_mov_b32 m0, s37
	s_nop 0
	buffer_load_dwordx4 v163, s[64:67], s57 offen lds
	s_mov_b32 m0, s38
	s_nop 0
	buffer_load_dwordx4 v165, s[64:67], s57 offen lds
	s_waitcnt vmcnt(8)
	s_waitcnt lgkmcnt(0)
	s_barrier
	s_setprio 1
	v_mfma_scale_f32_16x16x128_f8f6f4 v[62:65], v[26:33], v[174:181], v[62:65], v234, v234 op_sel_hi:[0,0,0]
	v_mfma_scale_f32_16x16x128_f8f6f4 v[58:61], v[18:25], v[174:181], v[58:61], v234, v234 op_sel_hi:[0,0,0]
	v_mfma_scale_f32_16x16x128_f8f6f4 v[78:81], v[26:33], v[182:189], v[78:81], v234, v234 op_sel_hi:[0,0,0]
	v_mfma_scale_f32_16x16x128_f8f6f4 v[74:77], v[18:25], v[182:189], v[74:77], v234, v234 op_sel_hi:[0,0,0]
	v_mfma_scale_f32_16x16x128_f8f6f4 v[94:97], v[26:33], v[190:197], v[94:97], v234, v234 op_sel_hi:[0,0,0]
	v_mfma_scale_f32_16x16x128_f8f6f4 v[90:93], v[18:25], v[190:197], v[90:93], v234, v234 op_sel_hi:[0,0,0]
	v_mfma_scale_f32_16x16x128_f8f6f4 v[106:109], v[26:33], v[204:211], v[106:109], v234, v234 op_sel_hi:[0,0,0]
	v_mfma_scale_f32_16x16x128_f8f6f4 v[102:105], v[18:25], v[204:211], v[102:105], v234, v234 op_sel_hi:[0,0,0]
	v_mfma_scale_f32_16x16x128_f8f6f4 v[158:161], v[10:17], v[174:181], v[158:161], v234, v234 op_sel_hi:[0,0,0]
	v_mfma_scale_f32_16x16x128_f8f6f4 v[154:157], v[2:9], v[174:181], v[154:157], v234, v234 op_sel_hi:[0,0,0]
	v_mfma_scale_f32_16x16x128_f8f6f4 v[150:153], v[10:17], v[182:189], v[150:153], v234, v234 op_sel_hi:[0,0,0]
	v_mfma_scale_f32_16x16x128_f8f6f4 v[146:149], v[2:9], v[182:189], v[146:149], v234, v234 op_sel_hi:[0,0,0]
	v_mfma_scale_f32_16x16x128_f8f6f4 v[142:145], v[10:17], v[190:197], v[142:145], v234, v234 op_sel_hi:[0,0,0]
	v_mfma_scale_f32_16x16x128_f8f6f4 v[138:141], v[2:9], v[190:197], v[138:141], v234, v234 op_sel_hi:[0,0,0]
	v_mfma_scale_f32_16x16x128_f8f6f4 v[134:137], v[10:17], v[204:211], v[134:137], v234, v234 op_sel_hi:[0,0,0]
	v_mfma_scale_f32_16x16x128_f8f6f4 v[130:133], v[2:9], v[204:211], v[130:133], v234, v234 op_sel_hi:[0,0,0]
	s_setprio 0
	s_barrier
	s_mov_b32 m0, s40
	s_or_b32 s57, s26, 0x180
	ds_read_b128 v[174:177], v168 offset:49152
	ds_read_b128 v[178:181], v168 offset:50176
	ds_read_b128 v[182:185], v168 offset:51200
	ds_read_b128 v[186:189], v168 offset:52224
	ds_read_b128 v[190:193], v168 offset:53248
	ds_read_b128 v[194:197], v168 offset:54272
	ds_read_b128 v[204:207], v168 offset:55296
	ds_read_b128 v[208:211], v168 offset:56320
	buffer_load_dwordx4 v164, s[0:3], s57 offen lds
	s_mov_b32 m0, s41
	s_nop 0
	buffer_load_dwordx4 v166, s[0:3], s57 offen lds
	s_or_b32 s57, s26, 0x40180
	s_mov_b32 m0, s42
	s_nop 0
	buffer_load_dwordx4 v164, s[0:3], s57 offen lds
	s_mov_b32 m0, s43
	s_nop 0
	buffer_load_dwordx4 v166, s[0:3], s57 offen lds
	s_waitcnt vmcnt(6)
	s_waitcnt lgkmcnt(0)
	s_barrier
	s_setprio 1
	v_mfma_scale_f32_16x16x128_f8f6f4 v[118:121], v[26:33], v[174:181], v[118:121], v234, v234 op_sel_hi:[0,0,0]
	v_mfma_scale_f32_16x16x128_f8f6f4 v[114:117], v[18:25], v[174:181], v[114:117], v234, v234 op_sel_hi:[0,0,0]
	v_mfma_scale_f32_16x16x128_f8f6f4 v[126:129], v[26:33], v[182:189], v[126:129], v234, v234 op_sel_hi:[0,0,0]
	v_mfma_scale_f32_16x16x128_f8f6f4 v[122:125], v[18:25], v[182:189], v[122:125], v234, v234 op_sel_hi:[0,0,0]
	v_mfma_scale_f32_16x16x128_f8f6f4 v[110:113], v[26:33], v[190:197], v[110:113], v234, v234 op_sel_hi:[0,0,0]
	v_mfma_scale_f32_16x16x128_f8f6f4 v[98:101], v[18:25], v[190:197], v[98:101], v234, v234 op_sel_hi:[0,0,0]
	v_mfma_scale_f32_16x16x128_f8f6f4 v[86:89], v[26:33], v[204:211], v[86:89], v234, v234 op_sel_hi:[0,0,0]
	v_mfma_scale_f32_16x16x128_f8f6f4 v[82:85], v[18:25], v[204:211], v[82:85], v234, v234 op_sel_hi:[0,0,0]
	v_mfma_scale_f32_16x16x128_f8f6f4 v[38:41], v[10:17], v[174:181], v[38:41], v234, v234 op_sel_hi:[0,0,0]
	v_mfma_scale_f32_16x16x128_f8f6f4 v[34:37], v[2:9], v[174:181], v[34:37], v234, v234 op_sel_hi:[0,0,0]
	v_mfma_scale_f32_16x16x128_f8f6f4 v[46:49], v[10:17], v[182:189], v[46:49], v234, v234 op_sel_hi:[0,0,0]
	v_mfma_scale_f32_16x16x128_f8f6f4 v[42:45], v[2:9], v[182:189], v[42:45], v234, v234 op_sel_hi:[0,0,0]
	v_mfma_scale_f32_16x16x128_f8f6f4 v[54:57], v[10:17], v[190:197], v[54:57], v234, v234 op_sel_hi:[0,0,0]
	v_mfma_scale_f32_16x16x128_f8f6f4 v[50:53], v[2:9], v[190:197], v[50:53], v234, v234 op_sel_hi:[0,0,0]
	v_mfma_scale_f32_16x16x128_f8f6f4 v[70:73], v[10:17], v[204:211], v[70:73], v234, v234 op_sel_hi:[0,0,0]
	v_mfma_scale_f32_16x16x128_f8f6f4 v[66:69], v[2:9], v[204:211], v[66:69], v234, v234 op_sel_hi:[0,0,0]
	s_setprio 0
	s_barrier
	s_mov_b32 s57, 0
	s_mov_b32 s58, 0
.LBB0_675:
	ds_read_b128 v[2:5], v169
	ds_read_b128 v[6:9], v169 offset:1024
	ds_read_b128 v[10:13], v169 offset:2048
	ds_read_b128 v[14:17], v169 offset:3072
	ds_read_b128 v[18:21], v170
	ds_read_b128 v[22:25], v170 offset:1024
	ds_read_b128 v[26:29], v170 offset:2048
	ds_read_b128 v[30:33], v170 offset:3072
	s_add_i32 s61, s36, s57
	s_add_i32 s62, s61, 0x100
	s_add_i32 s60, s61, 0x200
	s_add_i32 s59, s54, s57
	s_cmpk_eq_i32 s57, 0x600
	s_cselect_b32 s59, s56, s59
	s_cselect_b32 s60, s55, s60
	s_addk_i32 s61, 0x180
	s_mov_b32 m0, s44
	ds_read_b128 v[174:177], v168
	ds_read_b128 v[178:181], v168 offset:1024
	ds_read_b128 v[182:185], v168 offset:2048
	ds_read_b128 v[186:189], v168 offset:3072
	ds_read_b128 v[190:193], v168 offset:4096
	ds_read_b128 v[194:197], v168 offset:5120
	ds_read_b128 v[204:207], v168 offset:6144
	ds_read_b128 v[208:211], v168 offset:7168
	buffer_load_dwordx4 v163, s[64:67], s61 offen lds
	s_mov_b32 m0, s46
	s_nop 0
	buffer_load_dwordx4 v165, s[64:67], s61 offen lds
	s_or_b32 s61, s62, 0x40080
	s_mov_b32 m0, s45
	s_nop 0
	buffer_load_dwordx4 v163, s[64:67], s61 offen lds
	s_mov_b32 m0, s47
	s_nop 0
	buffer_load_dwordx4 v165, s[64:67], s61 offen lds
	s_waitcnt vmcnt(8)
	s_waitcnt lgkmcnt(0)
	s_barrier
	s_setprio 1
	v_mfma_scale_f32_16x16x128_f8f6f4 v[62:65], v[2:9], v[174:181], v[62:65], v234, v234 op_sel_hi:[0,0,0]
	v_mfma_scale_f32_16x16x128_f8f6f4 v[58:61], v[10:17], v[174:181], v[58:61], v234, v234 op_sel_hi:[0,0,0]
	v_mfma_scale_f32_16x16x128_f8f6f4 v[78:81], v[2:9], v[182:189], v[78:81], v234, v234 op_sel_hi:[0,0,0]
	v_mfma_scale_f32_16x16x128_f8f6f4 v[74:77], v[10:17], v[182:189], v[74:77], v234, v234 op_sel_hi:[0,0,0]
	v_mfma_scale_f32_16x16x128_f8f6f4 v[94:97], v[2:9], v[190:197], v[94:97], v234, v234 op_sel_hi:[0,0,0]
	v_mfma_scale_f32_16x16x128_f8f6f4 v[90:93], v[10:17], v[190:197], v[90:93], v234, v234 op_sel_hi:[0,0,0]
	v_mfma_scale_f32_16x16x128_f8f6f4 v[106:109], v[2:9], v[204:211], v[106:109], v234, v234 op_sel_hi:[0,0,0]
	v_mfma_scale_f32_16x16x128_f8f6f4 v[102:105], v[10:17], v[204:211], v[102:105], v234, v234 op_sel_hi:[0,0,0]
	v_mfma_scale_f32_16x16x128_f8f6f4 v[158:161], v[18:25], v[174:181], v[158:161], v234, v234 op_sel_hi:[0,0,0]
	v_mfma_scale_f32_16x16x128_f8f6f4 v[154:157], v[26:33], v[174:181], v[154:157], v234, v234 op_sel_hi:[0,0,0]
	v_mfma_scale_f32_16x16x128_f8f6f4 v[150:153], v[18:25], v[182:189], v[150:153], v234, v234 op_sel_hi:[0,0,0]
	v_mfma_scale_f32_16x16x128_f8f6f4 v[146:149], v[26:33], v[182:189], v[146:149], v234, v234 op_sel_hi:[0,0,0]
	v_mfma_scale_f32_16x16x128_f8f6f4 v[142:145], v[18:25], v[190:197], v[142:145], v234, v234 op_sel_hi:[0,0,0]
	v_mfma_scale_f32_16x16x128_f8f6f4 v[138:141], v[26:33], v[190:197], v[138:141], v234, v234 op_sel_hi:[0,0,0]
	v_mfma_scale_f32_16x16x128_f8f6f4 v[134:137], v[18:25], v[204:211], v[134:137], v234, v234 op_sel_hi:[0,0,0]
	v_mfma_scale_f32_16x16x128_f8f6f4 v[130:133], v[26:33], v[204:211], v[130:133], v234, v234 op_sel_hi:[0,0,0]
	s_setprio 0
	s_barrier
	s_mov_b32 m0, s11
	ds_read_b128 v[174:177], v168 offset:16384
	ds_read_b128 v[178:181], v168 offset:17408
	ds_read_b128 v[182:185], v168 offset:18432
	ds_read_b128 v[186:189], v168 offset:19456
	ds_read_b128 v[190:193], v168 offset:20480
	ds_read_b128 v[194:197], v168 offset:21504
	ds_read_b128 v[204:207], v168 offset:22528
	ds_read_b128 v[208:211], v168 offset:23552
	buffer_load_dwordx4 v164, s[0:3], s59 offen lds
	s_mov_b32 m0, s30
	s_or_b32 s61, s59, 0x40000
	buffer_load_dwordx4 v166, s[0:3], s59 offen lds
	s_mov_b32 m0, s31
	s_nop 0
	buffer_load_dwordx4 v164, s[0:3], s61 offen lds
	s_mov_b32 m0, s34
	s_nop 0
	buffer_load_dwordx4 v166, s[0:3], s61 offen lds
	s_waitcnt vmcnt(6)
	s_waitcnt lgkmcnt(0)
	s_barrier
	s_setprio 1
	v_mfma_scale_f32_16x16x128_f8f6f4 v[118:121], v[2:9], v[174:181], v[118:121], v234, v234 op_sel_hi:[0,0,0]
	v_mfma_scale_f32_16x16x128_f8f6f4 v[114:117], v[10:17], v[174:181], v[114:117], v234, v234 op_sel_hi:[0,0,0]
	v_mfma_scale_f32_16x16x128_f8f6f4 v[126:129], v[2:9], v[182:189], v[126:129], v234, v234 op_sel_hi:[0,0,0]
	v_mfma_scale_f32_16x16x128_f8f6f4 v[122:125], v[10:17], v[182:189], v[122:125], v234, v234 op_sel_hi:[0,0,0]
	v_mfma_scale_f32_16x16x128_f8f6f4 v[110:113], v[2:9], v[190:197], v[110:113], v234, v234 op_sel_hi:[0,0,0]
	v_mfma_scale_f32_16x16x128_f8f6f4 v[98:101], v[10:17], v[190:197], v[98:101], v234, v234 op_sel_hi:[0,0,0]
	v_mfma_scale_f32_16x16x128_f8f6f4 v[86:89], v[2:9], v[204:211], v[86:89], v234, v234 op_sel_hi:[0,0,0]
	v_mfma_scale_f32_16x16x128_f8f6f4 v[82:85], v[10:17], v[204:211], v[82:85], v234, v234 op_sel_hi:[0,0,0]
	v_mfma_scale_f32_16x16x128_f8f6f4 v[38:41], v[18:25], v[174:181], v[38:41], v234, v234 op_sel_hi:[0,0,0]
	v_mfma_scale_f32_16x16x128_f8f6f4 v[34:37], v[26:33], v[174:181], v[34:37], v234, v234 op_sel_hi:[0,0,0]
	v_mfma_scale_f32_16x16x128_f8f6f4 v[46:49], v[18:25], v[182:189], v[46:49], v234, v234 op_sel_hi:[0,0,0]
	v_mfma_scale_f32_16x16x128_f8f6f4 v[42:45], v[26:33], v[182:189], v[42:45], v234, v234 op_sel_hi:[0,0,0]
	v_mfma_scale_f32_16x16x128_f8f6f4 v[54:57], v[18:25], v[190:197], v[54:57], v234, v234 op_sel_hi:[0,0,0]
	v_mfma_scale_f32_16x16x128_f8f6f4 v[50:53], v[26:33], v[190:197], v[50:53], v234, v234 op_sel_hi:[0,0,0]
	v_mfma_scale_f32_16x16x128_f8f6f4 v[70:73], v[18:25], v[204:211], v[70:73], v234, v234 op_sel_hi:[0,0,0]
	v_mfma_scale_f32_16x16x128_f8f6f4 v[66:69], v[26:33], v[204:211], v[66:69], v234, v234 op_sel_hi:[0,0,0]
	s_setprio 0
	s_barrier
	ds_read_b128 v[18:21], v171
	ds_read_b128 v[22:25], v171 offset:1024
	ds_read_b128 v[26:29], v171 offset:2048
	ds_read_b128 v[30:33], v171 offset:3072
	ds_read_b128 v[10:13], v172
	ds_read_b128 v[14:17], v172 offset:1024
	ds_read_b128 v[2:5], v172 offset:2048
	ds_read_b128 v[6:9], v172 offset:3072
	s_mov_b32 m0, s10
	ds_read_b128 v[174:177], v168 offset:32768
	ds_read_b128 v[178:181], v168 offset:33792
	ds_read_b128 v[182:185], v168 offset:34816
	ds_read_b128 v[186:189], v168 offset:35840
	ds_read_b128 v[190:193], v168 offset:36864
	ds_read_b128 v[194:197], v168 offset:37888
	ds_read_b128 v[204:207], v168 offset:38912
	ds_read_b128 v[208:211], v168 offset:39936
	buffer_load_dwordx4 v163, s[64:67], s60 offen lds
	s_mov_b32 m0, s35
	s_nop 0
	buffer_load_dwordx4 v165, s[64:67], s60 offen lds
	s_bitset1_b32 s60, 18
	s_mov_b32 m0, s37
	s_nop 0
	buffer_load_dwordx4 v163, s[64:67], s60 offen lds
	s_mov_b32 m0, s38
	s_nop 0
	buffer_load_dwordx4 v165, s[64:67], s60 offen lds
	s_waitcnt vmcnt(8)
	s_waitcnt lgkmcnt(0)
	s_barrier
	s_setprio 1
	v_mfma_scale_f32_16x16x128_f8f6f4 v[62:65], v[18:25], v[174:181], v[62:65], v234, v234 op_sel_hi:[0,0,0]
	v_mfma_scale_f32_16x16x128_f8f6f4 v[58:61], v[26:33], v[174:181], v[58:61], v234, v234 op_sel_hi:[0,0,0]
	v_mfma_scale_f32_16x16x128_f8f6f4 v[78:81], v[18:25], v[182:189], v[78:81], v234, v234 op_sel_hi:[0,0,0]
	v_mfma_scale_f32_16x16x128_f8f6f4 v[74:77], v[26:33], v[182:189], v[74:77], v234, v234 op_sel_hi:[0,0,0]
	v_mfma_scale_f32_16x16x128_f8f6f4 v[94:97], v[18:25], v[190:197], v[94:97], v234, v234 op_sel_hi:[0,0,0]
	v_mfma_scale_f32_16x16x128_f8f6f4 v[90:93], v[26:33], v[190:197], v[90:93], v234, v234 op_sel_hi:[0,0,0]
	v_mfma_scale_f32_16x16x128_f8f6f4 v[106:109], v[18:25], v[204:211], v[106:109], v234, v234 op_sel_hi:[0,0,0]
	v_mfma_scale_f32_16x16x128_f8f6f4 v[102:105], v[26:33], v[204:211], v[102:105], v234, v234 op_sel_hi:[0,0,0]
	v_mfma_scale_f32_16x16x128_f8f6f4 v[158:161], v[10:17], v[174:181], v[158:161], v234, v234 op_sel_hi:[0,0,0]
	v_mfma_scale_f32_16x16x128_f8f6f4 v[154:157], v[2:9], v[174:181], v[154:157], v234, v234 op_sel_hi:[0,0,0]
	v_mfma_scale_f32_16x16x128_f8f6f4 v[150:153], v[10:17], v[182:189], v[150:153], v234, v234 op_sel_hi:[0,0,0]
	v_mfma_scale_f32_16x16x128_f8f6f4 v[146:149], v[2:9], v[182:189], v[146:149], v234, v234 op_sel_hi:[0,0,0]
	v_mfma_scale_f32_16x16x128_f8f6f4 v[142:145], v[10:17], v[190:197], v[142:145], v234, v234 op_sel_hi:[0,0,0]
	v_mfma_scale_f32_16x16x128_f8f6f4 v[138:141], v[2:9], v[190:197], v[138:141], v234, v234 op_sel_hi:[0,0,0]
	v_mfma_scale_f32_16x16x128_f8f6f4 v[134:137], v[10:17], v[204:211], v[134:137], v234, v234 op_sel_hi:[0,0,0]
	v_mfma_scale_f32_16x16x128_f8f6f4 v[130:133], v[2:9], v[204:211], v[130:133], v234, v234 op_sel_hi:[0,0,0]
	s_setprio 0
	s_barrier
	s_mov_b32 m0, s40
	s_or_b32 s60, s59, 0x80
	ds_read_b128 v[174:177], v168 offset:49152
	ds_read_b128 v[178:181], v168 offset:50176
	ds_read_b128 v[182:185], v168 offset:51200
	ds_read_b128 v[186:189], v168 offset:52224
	ds_read_b128 v[190:193], v168 offset:53248
	ds_read_b128 v[194:197], v168 offset:54272
	ds_read_b128 v[204:207], v168 offset:55296
	ds_read_b128 v[208:211], v168 offset:56320
	buffer_load_dwordx4 v164, s[0:3], s60 offen lds
	s_mov_b32 m0, s41
	s_or_b32 s59, s59, 0x40080
	buffer_load_dwordx4 v166, s[0:3], s60 offen lds
	s_mov_b32 m0, s42
	s_nop 0
	buffer_load_dwordx4 v164, s[0:3], s59 offen lds
	s_mov_b32 m0, s43
	s_nop 0
	buffer_load_dwordx4 v166, s[0:3], s59 offen lds
	s_waitcnt vmcnt(6)
	s_waitcnt lgkmcnt(0)
	s_barrier
	s_setprio 1
	v_mfma_scale_f32_16x16x128_f8f6f4 v[118:121], v[18:25], v[174:181], v[118:121], v234, v234 op_sel_hi:[0,0,0]
	v_mfma_scale_f32_16x16x128_f8f6f4 v[114:117], v[26:33], v[174:181], v[114:117], v234, v234 op_sel_hi:[0,0,0]
	v_mfma_scale_f32_16x16x128_f8f6f4 v[126:129], v[18:25], v[182:189], v[126:129], v234, v234 op_sel_hi:[0,0,0]
	v_mfma_scale_f32_16x16x128_f8f6f4 v[122:125], v[26:33], v[182:189], v[122:125], v234, v234 op_sel_hi:[0,0,0]
	v_mfma_scale_f32_16x16x128_f8f6f4 v[110:113], v[18:25], v[190:197], v[110:113], v234, v234 op_sel_hi:[0,0,0]
	v_mfma_scale_f32_16x16x128_f8f6f4 v[98:101], v[26:33], v[190:197], v[98:101], v234, v234 op_sel_hi:[0,0,0]
	v_mfma_scale_f32_16x16x128_f8f6f4 v[86:89], v[18:25], v[204:211], v[86:89], v234, v234 op_sel_hi:[0,0,0]
	v_mfma_scale_f32_16x16x128_f8f6f4 v[82:85], v[26:33], v[204:211], v[82:85], v234, v234 op_sel_hi:[0,0,0]
	v_mfma_scale_f32_16x16x128_f8f6f4 v[38:41], v[10:17], v[174:181], v[38:41], v234, v234 op_sel_hi:[0,0,0]
	v_mfma_scale_f32_16x16x128_f8f6f4 v[34:37], v[2:9], v[174:181], v[34:37], v234, v234 op_sel_hi:[0,0,0]
	v_mfma_scale_f32_16x16x128_f8f6f4 v[46:49], v[10:17], v[182:189], v[46:49], v234, v234 op_sel_hi:[0,0,0]
	v_mfma_scale_f32_16x16x128_f8f6f4 v[42:45], v[2:9], v[182:189], v[42:45], v234, v234 op_sel_hi:[0,0,0]
	v_mfma_scale_f32_16x16x128_f8f6f4 v[54:57], v[10:17], v[190:197], v[54:57], v234, v234 op_sel_hi:[0,0,0]
	v_mfma_scale_f32_16x16x128_f8f6f4 v[50:53], v[2:9], v[190:197], v[50:53], v234, v234 op_sel_hi:[0,0,0]
	v_mfma_scale_f32_16x16x128_f8f6f4 v[70:73], v[10:17], v[204:211], v[70:73], v234, v234 op_sel_hi:[0,0,0]
	v_mfma_scale_f32_16x16x128_f8f6f4 v[66:69], v[2:9], v[204:211], v[66:69], v234, v234 op_sel_hi:[0,0,0]
	s_setprio 0
	s_barrier
	s_add_i32 s58, s58, 2
	s_addk_i32 s57, 0x100
	s_cmp_gt_u32 s58, 13
	s_cbranch_scc0 .LBB0_675
	s_nop 15
	s_nop 15
	s_and_b64 vcc, exec, s[24:25]
	s_cbranch_vccz .LBB0_671
	s_mov_b32 s9, s49
	s_mov_b32 s20, s50
	s_mov_b32 s26, s53
	s_mov_b32 s36, s52
	s_mov_b32 s48, s51
	s_branch .LBB0_671

.LBB0_844:
	v_add_u32_e32 v130, 0x10000, v137
	v_add_u32_e32 v131, 0x14000, v137
	ds_read_b128 v[2:5], v130
	ds_read_b128 v[6:9], v130 offset:1024
	ds_read_b128 v[10:13], v130 offset:2048
	ds_read_b128 v[14:17], v130 offset:3072
	ds_read_b128 v[18:21], v131
	ds_read_b128 v[22:25], v131 offset:1024
	ds_read_b128 v[26:29], v131 offset:2048
	ds_read_b128 v[30:33], v131 offset:3072
	s_lshl_b32 s18, s51, 20
	s_lshl_b32 s19, s49, 20
	s_or_b32 s58, s53, 0x80
	s_or_b32 s60, s52, 0x100
	s_and_b64 s[6:7], s[30:31], exec
	s_cselect_b32 vcc_lo, s18, s53
	s_or_b32 s61, s53, 0x100
	s_and_b64 s[6:7], s[30:31], exec
	s_cselect_b32 vcc_hi, s19, s52
	s_mov_b32 m0, s79
	ds_read_b128 v[34:37], v138
	ds_read_b128 v[38:41], v138 offset:1024
	ds_read_b128 v[42:45], v138 offset:2048
	ds_read_b128 v[46:49], v138 offset:3072
	ds_read_b128 v[50:53], v138 offset:4096
	ds_read_b128 v[54:57], v138 offset:5120
	ds_read_b128 v[58:61], v138 offset:6144
	ds_read_b128 v[62:65], v138 offset:7168
	buffer_load_dwordx4 v0, s[64:67], s58 offen lds
	s_mov_b32 m0, s81
	s_or_b32 s6, s53, 0x80080
	buffer_load_dwordx4 v133, s[64:67], s58 offen lds
	s_mov_b32 m0, s80
	s_nop 0
	buffer_load_dwordx4 v0, s[64:67], s6 offen lds
	s_mov_b32 m0, s82
	s_nop 0
	buffer_load_dwordx4 v133, s[64:67], s6 offen lds
	s_waitcnt vmcnt(8)
	s_waitcnt lgkmcnt(0)
	s_barrier
	s_setprio 1
	v_mfma_f32_16x16x32_bf16 v[94:97], v[10:13], v[58:61], 0
	v_mfma_f32_16x16x32_bf16 v[66:69], v[2:5], v[34:37], 0
	v_mfma_f32_16x16x32_bf16 v[70:73], v[10:13], v[34:37], 0
	v_mfma_f32_16x16x32_bf16 v[98:101], v[14:17], v[62:65], v[94:97]
	v_mfma_f32_16x16x32_bf16 v[94:97], v[18:21], v[34:37], 0
	v_mfma_f32_16x16x32_bf16 v[34:37], v[26:29], v[34:37], 0
	v_mfma_f32_16x16x32_bf16 v[66:69], v[6:9], v[38:41], v[66:69]
	v_mfma_f32_16x16x32_bf16 v[70:73], v[14:17], v[38:41], v[70:73]
	v_mfma_f32_16x16x32_bf16 v[74:77], v[2:5], v[42:45], 0
	v_mfma_f32_16x16x32_bf16 v[78:81], v[10:13], v[42:45], 0
	v_mfma_f32_16x16x32_bf16 v[106:109], v[22:25], v[38:41], v[94:97]
	v_mfma_f32_16x16x32_bf16 v[34:37], v[30:33], v[38:41], v[34:37]
	v_mfma_f32_16x16x32_bf16 v[38:41], v[18:21], v[42:45], 0
	v_mfma_f32_16x16x32_bf16 v[42:45], v[26:29], v[42:45], 0
	v_mfma_f32_16x16x32_bf16 v[74:77], v[6:9], v[46:49], v[74:77]
	v_mfma_f32_16x16x32_bf16 v[78:81], v[14:17], v[46:49], v[78:81]
	v_mfma_f32_16x16x32_bf16 v[82:85], v[2:5], v[50:53], 0
	v_mfma_f32_16x16x32_bf16 v[86:89], v[10:13], v[50:53], 0
	v_mfma_f32_16x16x32_bf16 v[38:41], v[22:25], v[46:49], v[38:41]
	v_mfma_f32_16x16x32_bf16 v[42:45], v[30:33], v[46:49], v[42:45]
	v_mfma_f32_16x16x32_bf16 v[46:49], v[18:21], v[50:53], 0
	v_mfma_f32_16x16x32_bf16 v[50:53], v[26:29], v[50:53], 0
	v_mfma_f32_16x16x32_bf16 v[82:85], v[6:9], v[54:57], v[82:85]
	v_mfma_f32_16x16x32_bf16 v[86:89], v[14:17], v[54:57], v[86:89]
	v_mfma_f32_16x16x32_bf16 v[90:93], v[2:5], v[58:61], 0
	v_mfma_f32_16x16x32_bf16 v[46:49], v[22:25], v[54:57], v[46:49]
	v_mfma_f32_16x16x32_bf16 v[50:53], v[30:33], v[54:57], v[50:53]
	v_mfma_f32_16x16x32_bf16 v[54:57], v[18:21], v[58:61], 0
	v_mfma_f32_16x16x32_bf16 v[90:93], v[6:9], v[62:65], v[90:93]
	v_mfma_f32_16x16x32_bf16 v[142:145], v[22:25], v[62:65], v[54:57]
	v_mfma_f32_16x16x32_bf16 v[54:57], v[26:29], v[58:61], 0
	v_mfma_f32_16x16x32_bf16 v[146:149], v[30:33], v[62:65], v[54:57]
	s_setprio 0
	s_barrier
	s_mov_b32 m0, s15
	s_mov_b32 s6, s66
	s_mov_b32 s7, s67
	s_nop 1
	ds_read_b128 v[54:57], v138 offset:16384
	ds_read_b128 v[58:61], v138 offset:17408
	ds_read_b128 v[62:65], v138 offset:18432
	ds_read_b128 v[94:97], v138 offset:19456
	ds_read_b128 v[102:105], v138 offset:20480
	ds_read_b128 v[110:113], v138 offset:21504
	ds_read_b128 v[114:117], v138 offset:22528
	ds_read_b128 v[118:121], v138 offset:23552
	buffer_load_dwordx4 v132, s[4:7], s60 offen lds
	s_mov_b32 m0, s16
	s_or_b32 s58, s52, 0x80100
	buffer_load_dwordx4 v134, s[4:7], s60 offen lds
	s_mov_b32 m0, s17
	s_nop 0
	buffer_load_dwordx4 v132, s[4:7], s58 offen lds
	s_mov_b32 m0, s20
	s_nop 0
	buffer_load_dwordx4 v134, s[4:7], s58 offen lds
	s_waitcnt vmcnt(6)
	s_waitcnt lgkmcnt(0)
	s_barrier
	s_setprio 1
	v_mfma_f32_16x16x32_bf16 v[122:125], v[2:5], v[54:57], 0
	v_mfma_f32_16x16x32_bf16 v[150:153], v[6:9], v[58:61], v[122:125]
	v_mfma_f32_16x16x32_bf16 v[122:125], v[10:13], v[54:57], 0
	v_mfma_f32_16x16x32_bf16 v[154:157], v[14:17], v[58:61], v[122:125]
	v_mfma_f32_16x16x32_bf16 v[122:125], v[2:5], v[62:65], 0
	v_mfma_f32_16x16x32_bf16 v[158:161], v[6:9], v[94:97], v[122:125]
	v_mfma_f32_16x16x32_bf16 v[122:125], v[10:13], v[62:65], 0
	v_mfma_f32_16x16x32_bf16 v[162:165], v[14:17], v[94:97], v[122:125]
	v_mfma_f32_16x16x32_bf16 v[122:125], v[2:5], v[102:105], 0
	v_mfma_f32_16x16x32_bf16 v[2:5], v[2:5], v[114:117], 0
	v_mfma_f32_16x16x32_bf16 v[166:169], v[6:9], v[110:113], v[122:125]
	v_mfma_f32_16x16x32_bf16 v[122:125], v[10:13], v[102:105], 0
	v_mfma_f32_16x16x32_bf16 v[2:5], v[6:9], v[118:121], v[2:5]
	v_mfma_f32_16x16x32_bf16 v[6:9], v[10:13], v[114:117], 0
	v_mfma_f32_16x16x32_bf16 v[170:173], v[14:17], v[110:113], v[122:125]
	v_mfma_f32_16x16x32_bf16 v[6:9], v[14:17], v[118:121], v[6:9]
	v_mfma_f32_16x16x32_bf16 v[14:17], v[26:29], v[54:57], 0
	v_mfma_f32_16x16x32_bf16 v[174:177], v[30:33], v[58:61], v[14:17]
	v_mfma_f32_16x16x32_bf16 v[14:17], v[18:21], v[62:65], 0
	v_mfma_f32_16x16x32_bf16 v[178:181], v[22:25], v[94:97], v[14:17]
	v_mfma_f32_16x16x32_bf16 v[14:17], v[26:29], v[62:65], 0
	v_mfma_f32_16x16x32_bf16 v[182:185], v[30:33], v[94:97], v[14:17]
	v_mfma_f32_16x16x32_bf16 v[14:17], v[18:21], v[102:105], 0
	v_mfma_f32_16x16x32_bf16 v[186:189], v[22:25], v[110:113], v[14:17]
	v_mfma_f32_16x16x32_bf16 v[14:17], v[26:29], v[102:105], 0
	v_mfma_f32_16x16x32_bf16 v[10:13], v[18:21], v[54:57], 0
	v_mfma_f32_16x16x32_bf16 v[190:193], v[30:33], v[110:113], v[14:17]
	v_mfma_f32_16x16x32_bf16 v[14:17], v[18:21], v[114:117], 0
	v_mfma_f32_16x16x32_bf16 v[10:13], v[22:25], v[58:61], v[10:13]
	v_mfma_f32_16x16x32_bf16 v[194:197], v[22:25], v[118:121], v[14:17]
	v_mfma_f32_16x16x32_bf16 v[14:17], v[26:29], v[114:117], 0
	v_mfma_f32_16x16x32_bf16 v[198:201], v[30:33], v[118:121], v[14:17]
	s_setprio 0
	s_barrier
	v_add_u32_e32 v139, 0x18000, v137
	v_add_u32_e32 v140, 0x1c000, v137
	s_nop 2
	ds_read_b128 v[14:17], v139
	ds_read_b128 v[18:21], v139 offset:1024
	ds_read_b128 v[26:29], v139 offset:2048
	ds_read_b128 v[204:207], v139 offset:3072
	ds_read_b128 v[208:211], v140
	ds_read_b128 v[212:215], v140 offset:1024
	ds_read_b128 v[216:219], v140 offset:2048
	ds_read_b128 v[220:223], v140 offset:3072
	s_mov_b32 m0, s14
	ds_read_b128 v[22:25], v138 offset:32768
	ds_read_b128 v[30:33], v138 offset:33792
	ds_read_b128 v[58:61], v138 offset:34816
	ds_read_b128 v[224:227], v138 offset:35840
	ds_read_b128 v[228:231], v138 offset:36864
	ds_read_b128 v[238:241], v138 offset:37888
	ds_read_b128 v[244:247], v138 offset:38912
	ds_read_b128 v[250:253], v138 offset:39936
	buffer_load_dwordx4 v0, s[64:67], s61 offen lds
	s_mov_b32 m0, s21
	s_or_b32 s58, s53, 0x80100
	buffer_load_dwordx4 v133, s[64:67], s61 offen lds
	s_mov_b32 m0, s46
	s_nop 0
	buffer_load_dwordx4 v0, s[64:67], s58 offen lds
	s_mov_b32 m0, s47
	s_nop 0
	buffer_load_dwordx4 v133, s[64:67], s58 offen lds
	s_waitcnt vmcnt(8)
	s_waitcnt lgkmcnt(0)
	s_barrier
	s_setprio 1
	v_mfma_f32_16x16x32_bf16 v[54:57], v[14:17], v[22:25], v[66:69]
	v_mfma_f32_16x16x32_bf16 v[126:129], v[18:21], v[30:33], v[54:57]
	v_mfma_f32_16x16x32_bf16 v[54:57], v[26:29], v[22:25], v[70:73]
	v_mfma_f32_16x16x32_bf16 v[118:121], v[204:207], v[30:33], v[54:57]
	v_mfma_f32_16x16x32_bf16 v[54:57], v[14:17], v[58:61], v[74:77]
	v_mfma_f32_16x16x32_bf16 v[110:113], v[18:21], v[224:227], v[54:57]
	v_mfma_f32_16x16x32_bf16 v[54:57], v[26:29], v[58:61], v[78:81]
	v_mfma_f32_16x16x32_bf16 v[102:105], v[204:207], v[224:227], v[54:57]
	v_mfma_f32_16x16x32_bf16 v[54:57], v[14:17], v[228:231], v[82:85]
	v_mfma_f32_16x16x32_bf16 v[66:69], v[208:211], v[22:25], v[106:109]
	v_mfma_f32_16x16x32_bf16 v[22:25], v[216:219], v[22:25], v[34:37]
	v_mfma_f32_16x16x32_bf16 v[94:97], v[18:21], v[238:241], v[54:57]
	v_mfma_f32_16x16x32_bf16 v[54:57], v[26:29], v[228:231], v[86:89]
	v_mfma_f32_16x16x32_bf16 v[114:117], v[220:223], v[30:33], v[22:25]
	v_mfma_f32_16x16x32_bf16 v[22:25], v[208:211], v[58:61], v[38:41]
	v_mfma_f32_16x16x32_bf16 v[86:89], v[204:207], v[238:241], v[54:57]
	v_mfma_f32_16x16x32_bf16 v[54:57], v[14:17], v[244:247], v[90:93]
	v_mfma_f32_16x16x32_bf16 v[106:109], v[212:215], v[224:227], v[22:25]
	v_mfma_f32_16x16x32_bf16 v[22:25], v[216:219], v[58:61], v[42:45]
	v_mfma_f32_16x16x32_bf16 v[62:65], v[18:21], v[250:253], v[54:57]
	v_mfma_f32_16x16x32_bf16 v[54:57], v[26:29], v[244:247], v[98:101]
	v_mfma_f32_16x16x32_bf16 v[98:101], v[220:223], v[224:227], v[22:25]
	v_mfma_f32_16x16x32_bf16 v[22:25], v[208:211], v[228:231], v[46:49]
	v_mfma_f32_16x16x32_bf16 v[90:93], v[212:215], v[238:241], v[22:25]
	v_mfma_f32_16x16x32_bf16 v[22:25], v[216:219], v[228:231], v[50:53]
	v_mfma_f32_16x16x32_bf16 v[82:85], v[220:223], v[238:241], v[22:25]
	v_mfma_f32_16x16x32_bf16 v[22:25], v[208:211], v[244:247], v[142:145]
	v_mfma_f32_16x16x32_bf16 v[58:61], v[212:215], v[250:253], v[22:25]
	v_mfma_f32_16x16x32_bf16 v[22:25], v[216:219], v[244:247], v[146:149]
	v_mfma_f32_16x16x32_bf16 v[54:57], v[204:207], v[250:253], v[54:57]
	v_mfma_f32_16x16x32_bf16 v[122:125], v[212:215], v[30:33], v[66:69]
	v_mfma_f32_16x16x32_bf16 v[50:53], v[220:223], v[250:253], v[22:25]
	s_setprio 0
	s_barrier
	s_mov_b32 m0, s55
	s_or_b32 s58, s52, 0x180
	ds_read_b128 v[34:37], v138 offset:49152
	ds_read_b128 v[42:45], v138 offset:50176
	ds_read_b128 v[142:145], v138 offset:51200
	ds_read_b128 v[146:149], v138 offset:52224
	ds_read_b128 v[224:227], v138 offset:53248
	ds_read_b128 v[228:231], v138 offset:54272
	ds_read_b128 v[238:241], v138 offset:55296
	ds_read_b128 v[244:247], v138 offset:56320
	buffer_load_dwordx4 v132, s[4:7], s58 offen lds
	s_mov_b32 m0, s56
	s_nop 0
	buffer_load_dwordx4 v134, s[4:7], s58 offen lds
	s_or_b32 s58, s52, 0x80180
	s_mov_b32 m0, s63
	s_nop 0
	buffer_load_dwordx4 v132, s[4:7], s58 offen lds
	s_mov_b32 m0, s76
	s_nop 0
	buffer_load_dwordx4 v134, s[4:7], s58 offen lds
	s_waitcnt vmcnt(6)
	s_waitcnt lgkmcnt(0)
	s_barrier
	s_setprio 1
	v_mfma_f32_16x16x32_bf16 v[22:25], v[14:17], v[34:37], v[150:153]
	v_mfma_f32_16x16x32_bf16 v[78:81], v[18:21], v[42:45], v[22:25]
	v_mfma_f32_16x16x32_bf16 v[22:25], v[26:29], v[34:37], v[154:157]
	v_mfma_f32_16x16x32_bf16 v[70:73], v[204:207], v[42:45], v[22:25]
	v_mfma_f32_16x16x32_bf16 v[22:25], v[14:17], v[142:145], v[158:161]
	v_mfma_f32_16x16x32_bf16 v[46:49], v[18:21], v[146:149], v[22:25]
	v_mfma_f32_16x16x32_bf16 v[22:25], v[26:29], v[142:145], v[162:165]
	v_mfma_f32_16x16x32_bf16 v[2:5], v[14:17], v[238:241], v[2:5]
	v_mfma_f32_16x16x32_bf16 v[38:41], v[204:207], v[146:149], v[22:25]
	v_mfma_f32_16x16x32_bf16 v[22:25], v[14:17], v[224:227], v[166:169]
	v_mfma_f32_16x16x32_bf16 v[14:17], v[18:21], v[244:247], v[2:5]
	v_mfma_f32_16x16x32_bf16 v[2:5], v[26:29], v[238:241], v[6:9]
	v_mfma_f32_16x16x32_bf16 v[6:9], v[204:207], v[244:247], v[2:5]
	v_mfma_f32_16x16x32_bf16 v[2:5], v[208:211], v[34:37], v[10:13]
	v_mfma_f32_16x16x32_bf16 v[74:77], v[212:215], v[42:45], v[2:5]
	v_mfma_f32_16x16x32_bf16 v[2:5], v[216:219], v[34:37], v[174:177]
	v_mfma_f32_16x16x32_bf16 v[66:69], v[220:223], v[42:45], v[2:5]
	v_mfma_f32_16x16x32_bf16 v[2:5], v[208:211], v[142:145], v[178:181]
	v_mfma_f32_16x16x32_bf16 v[42:45], v[212:215], v[146:149], v[2:5]
	v_mfma_f32_16x16x32_bf16 v[2:5], v[216:219], v[142:145], v[182:185]
	v_mfma_f32_16x16x32_bf16 v[34:37], v[220:223], v[146:149], v[2:5]
	v_mfma_f32_16x16x32_bf16 v[2:5], v[208:211], v[224:227], v[186:189]
	v_mfma_f32_16x16x32_bf16 v[30:33], v[18:21], v[228:231], v[22:25]
	v_mfma_f32_16x16x32_bf16 v[22:25], v[26:29], v[224:227], v[170:173]
	v_mfma_f32_16x16x32_bf16 v[26:29], v[212:215], v[228:231], v[2:5]
	v_mfma_f32_16x16x32_bf16 v[2:5], v[216:219], v[224:227], v[190:193]
	v_mfma_f32_16x16x32_bf16 v[18:21], v[220:223], v[228:231], v[2:5]
	v_mfma_f32_16x16x32_bf16 v[2:5], v[208:211], v[238:241], v[194:197]
	v_mfma_f32_16x16x32_bf16 v[10:13], v[212:215], v[244:247], v[2:5]
	v_mfma_f32_16x16x32_bf16 v[2:5], v[216:219], v[238:241], v[198:201]
	v_mfma_f32_16x16x32_bf16 v[22:25], v[204:207], v[228:231], v[22:25]
	v_mfma_f32_16x16x32_bf16 v[2:5], v[220:223], v[244:247], v[2:5]
	s_setprio 0
	s_barrier
	s_addk_i32 s52, 0x200
	s_add_i32 s53, s53, 0x80180
	s_mov_b32 s58, 0
.LBB0_845:
	ds_read_b128 v[142:145], v130
	ds_read_b128 v[146:149], v130 offset:1024
	ds_read_b128 v[150:153], v130 offset:2048
	ds_read_b128 v[154:157], v130 offset:3072
	ds_read_b128 v[158:161], v131
	ds_read_b128 v[162:165], v131 offset:1024
	ds_read_b128 v[166:169], v131 offset:2048
	ds_read_b128 v[170:173], v131 offset:3072
	s_add_i32 s60, s53, 0xfff80080
	s_cmp_eq_u32 s58, 28
	s_cselect_b32 s61, vcc_hi, s52
	s_cselect_b32 s60, vcc_lo, s60
	s_add_i32 s62, s53, 0xfff80000
	s_mov_b32 m0, s79
	ds_read_b128 v[174:177], v138
	ds_read_b128 v[178:181], v138 offset:1024
	ds_read_b128 v[182:185], v138 offset:2048
	ds_read_b128 v[186:189], v138 offset:3072
	ds_read_b128 v[190:193], v138 offset:4096
	ds_read_b128 v[194:197], v138 offset:5120
	ds_read_b128 v[198:201], v138 offset:6144
	ds_read_b128 v[204:207], v138 offset:7168
	buffer_load_dwordx4 v0, s[64:67], s62 offen lds
	s_mov_b32 m0, s81
	s_nop 0
	buffer_load_dwordx4 v133, s[64:67], s62 offen lds
	s_mov_b32 m0, s80
	s_nop 0
	buffer_load_dwordx4 v0, s[64:67], s53 offen lds
	s_mov_b32 m0, s82
	s_nop 0
	buffer_load_dwordx4 v133, s[64:67], s53 offen lds
	s_waitcnt vmcnt(8)
	s_waitcnt lgkmcnt(0)
	s_barrier
	s_setprio 1
	v_mfma_f32_16x16x32_bf16 v[126:129], v[142:145], v[174:177], v[126:129]
	v_mfma_f32_16x16x32_bf16 v[118:121], v[150:153], v[174:177], v[118:121]
	v_mfma_f32_16x16x32_bf16 v[110:113], v[142:145], v[182:185], v[110:113]
	v_mfma_f32_16x16x32_bf16 v[102:105], v[150:153], v[182:185], v[102:105]
	v_mfma_f32_16x16x32_bf16 v[94:97], v[142:145], v[190:193], v[94:97]
	v_mfma_f32_16x16x32_bf16 v[86:89], v[150:153], v[190:193], v[86:89]
	v_mfma_f32_16x16x32_bf16 v[62:65], v[142:145], v[198:201], v[62:65]
	v_mfma_f32_16x16x32_bf16 v[54:57], v[150:153], v[198:201], v[54:57]
	v_mfma_f32_16x16x32_bf16 v[122:125], v[158:161], v[174:177], v[122:125]
	v_mfma_f32_16x16x32_bf16 v[114:117], v[166:169], v[174:177], v[114:117]
	v_mfma_f32_16x16x32_bf16 v[106:109], v[158:161], v[182:185], v[106:109]
	v_mfma_f32_16x16x32_bf16 v[98:101], v[166:169], v[182:185], v[98:101]
	v_mfma_f32_16x16x32_bf16 v[90:93], v[158:161], v[190:193], v[90:93]
	v_mfma_f32_16x16x32_bf16 v[82:85], v[166:169], v[190:193], v[82:85]
	v_mfma_f32_16x16x32_bf16 v[58:61], v[158:161], v[198:201], v[58:61]
	v_mfma_f32_16x16x32_bf16 v[50:53], v[166:169], v[198:201], v[50:53]
	v_mfma_f32_16x16x32_bf16 v[126:129], v[146:149], v[178:181], v[126:129]
	v_mfma_f32_16x16x32_bf16 v[118:121], v[154:157], v[178:181], v[118:121]
	v_mfma_f32_16x16x32_bf16 v[110:113], v[146:149], v[186:189], v[110:113]
	v_mfma_f32_16x16x32_bf16 v[102:105], v[154:157], v[186:189], v[102:105]
	v_mfma_f32_16x16x32_bf16 v[94:97], v[146:149], v[194:197], v[94:97]
	v_mfma_f32_16x16x32_bf16 v[86:89], v[154:157], v[194:197], v[86:89]
	v_mfma_f32_16x16x32_bf16 v[62:65], v[146:149], v[204:207], v[62:65]
	v_mfma_f32_16x16x32_bf16 v[54:57], v[154:157], v[204:207], v[54:57]
	v_mfma_f32_16x16x32_bf16 v[122:125], v[162:165], v[178:181], v[122:125]
	v_mfma_f32_16x16x32_bf16 v[114:117], v[170:173], v[178:181], v[114:117]
	v_mfma_f32_16x16x32_bf16 v[106:109], v[162:165], v[186:189], v[106:109]
	v_mfma_f32_16x16x32_bf16 v[98:101], v[170:173], v[186:189], v[98:101]
	v_mfma_f32_16x16x32_bf16 v[90:93], v[162:165], v[194:197], v[90:93]
	v_mfma_f32_16x16x32_bf16 v[82:85], v[170:173], v[194:197], v[82:85]
	v_mfma_f32_16x16x32_bf16 v[58:61], v[162:165], v[204:207], v[58:61]
	v_mfma_f32_16x16x32_bf16 v[50:53], v[170:173], v[204:207], v[50:53]
	s_setprio 0
	s_barrier
	s_mov_b32 m0, s15
	ds_read_b128 v[174:177], v138 offset:16384
	ds_read_b128 v[178:181], v138 offset:17408
	ds_read_b128 v[182:185], v138 offset:18432
	ds_read_b128 v[186:189], v138 offset:19456
	ds_read_b128 v[190:193], v138 offset:20480
	ds_read_b128 v[194:197], v138 offset:21504
	ds_read_b128 v[198:201], v138 offset:22528
	ds_read_b128 v[204:207], v138 offset:23552
	buffer_load_dwordx4 v132, s[4:7], s61 offen lds
	s_mov_b32 m0, s16
	s_add_i32 s62, s61, 0x80000
	buffer_load_dwordx4 v134, s[4:7], s61 offen lds
	s_mov_b32 m0, s17
	s_nop 0
	buffer_load_dwordx4 v132, s[4:7], s62 offen lds
	s_mov_b32 m0, s20
	s_nop 0
	buffer_load_dwordx4 v134, s[4:7], s62 offen lds
	s_waitcnt vmcnt(6)
	s_waitcnt lgkmcnt(0)
	s_barrier
	s_setprio 1
	v_mfma_f32_16x16x32_bf16 v[78:81], v[142:145], v[174:177], v[78:81]
	v_mfma_f32_16x16x32_bf16 v[70:73], v[150:153], v[174:177], v[70:73]
	v_mfma_f32_16x16x32_bf16 v[46:49], v[142:145], v[182:185], v[46:49]
	v_mfma_f32_16x16x32_bf16 v[38:41], v[150:153], v[182:185], v[38:41]
	v_mfma_f32_16x16x32_bf16 v[30:33], v[142:145], v[190:193], v[30:33]
	v_mfma_f32_16x16x32_bf16 v[22:25], v[150:153], v[190:193], v[22:25]
	v_mfma_f32_16x16x32_bf16 v[14:17], v[142:145], v[198:201], v[14:17]
	v_mfma_f32_16x16x32_bf16 v[6:9], v[150:153], v[198:201], v[6:9]
	v_mfma_f32_16x16x32_bf16 v[74:77], v[158:161], v[174:177], v[74:77]
	v_mfma_f32_16x16x32_bf16 v[66:69], v[166:169], v[174:177], v[66:69]
	v_mfma_f32_16x16x32_bf16 v[42:45], v[158:161], v[182:185], v[42:45]
	v_mfma_f32_16x16x32_bf16 v[34:37], v[166:169], v[182:185], v[34:37]
	v_mfma_f32_16x16x32_bf16 v[26:29], v[158:161], v[190:193], v[26:29]
	v_mfma_f32_16x16x32_bf16 v[18:21], v[166:169], v[190:193], v[18:21]
	v_mfma_f32_16x16x32_bf16 v[10:13], v[158:161], v[198:201], v[10:13]
	v_mfma_f32_16x16x32_bf16 v[2:5], v[166:169], v[198:201], v[2:5]
	v_mfma_f32_16x16x32_bf16 v[78:81], v[146:149], v[178:181], v[78:81]
	v_mfma_f32_16x16x32_bf16 v[70:73], v[154:157], v[178:181], v[70:73]
	v_mfma_f32_16x16x32_bf16 v[46:49], v[146:149], v[186:189], v[46:49]
	v_mfma_f32_16x16x32_bf16 v[38:41], v[154:157], v[186:189], v[38:41]
	v_mfma_f32_16x16x32_bf16 v[30:33], v[146:149], v[194:197], v[30:33]
	v_mfma_f32_16x16x32_bf16 v[22:25], v[154:157], v[194:197], v[22:25]
	v_mfma_f32_16x16x32_bf16 v[14:17], v[146:149], v[204:207], v[14:17]
	v_mfma_f32_16x16x32_bf16 v[6:9], v[154:157], v[204:207], v[6:9]
	v_mfma_f32_16x16x32_bf16 v[74:77], v[162:165], v[178:181], v[74:77]
	v_mfma_f32_16x16x32_bf16 v[66:69], v[170:173], v[178:181], v[66:69]
	v_mfma_f32_16x16x32_bf16 v[42:45], v[162:165], v[186:189], v[42:45]
	v_mfma_f32_16x16x32_bf16 v[34:37], v[170:173], v[186:189], v[34:37]
	v_mfma_f32_16x16x32_bf16 v[26:29], v[162:165], v[194:197], v[26:29]
	v_mfma_f32_16x16x32_bf16 v[18:21], v[170:173], v[194:197], v[18:21]
	v_mfma_f32_16x16x32_bf16 v[10:13], v[162:165], v[204:207], v[10:13]
	v_mfma_f32_16x16x32_bf16 v[2:5], v[170:173], v[204:207], v[2:5]
	s_setprio 0
	s_barrier
	ds_read_b128 v[142:145], v139
	ds_read_b128 v[146:149], v139 offset:1024
	ds_read_b128 v[150:153], v139 offset:2048
	ds_read_b128 v[154:157], v139 offset:3072
	ds_read_b128 v[158:161], v140
	ds_read_b128 v[162:165], v140 offset:1024
	ds_read_b128 v[166:169], v140 offset:2048
	ds_read_b128 v[170:173], v140 offset:3072
	s_mov_b32 m0, s14
	ds_read_b128 v[174:177], v138 offset:32768
	ds_read_b128 v[178:181], v138 offset:33792
	ds_read_b128 v[182:185], v138 offset:34816
	ds_read_b128 v[186:189], v138 offset:35840
	ds_read_b128 v[190:193], v138 offset:36864
	ds_read_b128 v[194:197], v138 offset:37888
	ds_read_b128 v[198:201], v138 offset:38912
	ds_read_b128 v[204:207], v138 offset:39936
	buffer_load_dwordx4 v0, s[64:67], s60 offen lds
	s_mov_b32 m0, s21
	s_nop 0
	buffer_load_dwordx4 v133, s[64:67], s60 offen lds
	s_add_i32 s60, s60, 0x80000
	s_mov_b32 m0, s46
	s_nop 0
	buffer_load_dwordx4 v0, s[64:67], s60 offen lds
	s_mov_b32 m0, s47
	s_nop 0
	buffer_load_dwordx4 v133, s[64:67], s60 offen lds
	s_waitcnt vmcnt(8)
	s_waitcnt lgkmcnt(0)
	s_barrier
	s_setprio 1
	v_mfma_f32_16x16x32_bf16 v[126:129], v[142:145], v[174:177], v[126:129]
	v_mfma_f32_16x16x32_bf16 v[118:121], v[150:153], v[174:177], v[118:121]
	v_mfma_f32_16x16x32_bf16 v[110:113], v[142:145], v[182:185], v[110:113]
	v_mfma_f32_16x16x32_bf16 v[102:105], v[150:153], v[182:185], v[102:105]
	v_mfma_f32_16x16x32_bf16 v[94:97], v[142:145], v[190:193], v[94:97]
	v_mfma_f32_16x16x32_bf16 v[86:89], v[150:153], v[190:193], v[86:89]
	v_mfma_f32_16x16x32_bf16 v[62:65], v[142:145], v[198:201], v[62:65]
	v_mfma_f32_16x16x32_bf16 v[54:57], v[150:153], v[198:201], v[54:57]
	v_mfma_f32_16x16x32_bf16 v[122:125], v[158:161], v[174:177], v[122:125]
	v_mfma_f32_16x16x32_bf16 v[114:117], v[166:169], v[174:177], v[114:117]
	v_mfma_f32_16x16x32_bf16 v[106:109], v[158:161], v[182:185], v[106:109]
	v_mfma_f32_16x16x32_bf16 v[98:101], v[166:169], v[182:185], v[98:101]
	v_mfma_f32_16x16x32_bf16 v[90:93], v[158:161], v[190:193], v[90:93]
	v_mfma_f32_16x16x32_bf16 v[82:85], v[166:169], v[190:193], v[82:85]
	v_mfma_f32_16x16x32_bf16 v[58:61], v[158:161], v[198:201], v[58:61]
	v_mfma_f32_16x16x32_bf16 v[50:53], v[166:169], v[198:201], v[50:53]
	v_mfma_f32_16x16x32_bf16 v[126:129], v[146:149], v[178:181], v[126:129]
	v_mfma_f32_16x16x32_bf16 v[118:121], v[154:157], v[178:181], v[118:121]
	v_mfma_f32_16x16x32_bf16 v[110:113], v[146:149], v[186:189], v[110:113]
	v_mfma_f32_16x16x32_bf16 v[102:105], v[154:157], v[186:189], v[102:105]
	v_mfma_f32_16x16x32_bf16 v[94:97], v[146:149], v[194:197], v[94:97]
	v_mfma_f32_16x16x32_bf16 v[86:89], v[154:157], v[194:197], v[86:89]
	v_mfma_f32_16x16x32_bf16 v[62:65], v[146:149], v[204:207], v[62:65]
	v_mfma_f32_16x16x32_bf16 v[54:57], v[154:157], v[204:207], v[54:57]
	v_mfma_f32_16x16x32_bf16 v[122:125], v[162:165], v[178:181], v[122:125]
	v_mfma_f32_16x16x32_bf16 v[114:117], v[170:173], v[178:181], v[114:117]
	v_mfma_f32_16x16x32_bf16 v[106:109], v[162:165], v[186:189], v[106:109]
	v_mfma_f32_16x16x32_bf16 v[98:101], v[170:173], v[186:189], v[98:101]
	v_mfma_f32_16x16x32_bf16 v[90:93], v[162:165], v[194:197], v[90:93]
	v_mfma_f32_16x16x32_bf16 v[82:85], v[170:173], v[194:197], v[82:85]
	v_mfma_f32_16x16x32_bf16 v[58:61], v[162:165], v[204:207], v[58:61]
	v_mfma_f32_16x16x32_bf16 v[50:53], v[170:173], v[204:207], v[50:53]
	s_setprio 0
	s_barrier
	s_mov_b32 m0, s55
	s_or_b32 s60, s61, 0x80
	ds_read_b128 v[174:177], v138 offset:49152
	ds_read_b128 v[178:181], v138 offset:50176
	ds_read_b128 v[182:185], v138 offset:51200
	ds_read_b128 v[186:189], v138 offset:52224
	ds_read_b128 v[190:193], v138 offset:53248
	ds_read_b128 v[194:197], v138 offset:54272
	ds_read_b128 v[198:201], v138 offset:55296
	ds_read_b128 v[204:207], v138 offset:56320
	buffer_load_dwordx4 v132, s[4:7], s60 offen lds
	s_mov_b32 m0, s56
	s_add_i32 s61, s61, 0x80080
	buffer_load_dwordx4 v134, s[4:7], s60 offen lds
	s_mov_b32 m0, s63
	s_nop 0
	buffer_load_dwordx4 v132, s[4:7], s61 offen lds
	s_mov_b32 m0, s76
	s_nop 0
	buffer_load_dwordx4 v134, s[4:7], s61 offen lds
	s_waitcnt vmcnt(6)
	s_waitcnt lgkmcnt(0)
	s_barrier
	s_setprio 1
	v_mfma_f32_16x16x32_bf16 v[78:81], v[142:145], v[174:177], v[78:81]
	v_mfma_f32_16x16x32_bf16 v[70:73], v[150:153], v[174:177], v[70:73]
	v_mfma_f32_16x16x32_bf16 v[46:49], v[142:145], v[182:185], v[46:49]
	v_mfma_f32_16x16x32_bf16 v[38:41], v[150:153], v[182:185], v[38:41]
	v_mfma_f32_16x16x32_bf16 v[30:33], v[142:145], v[190:193], v[30:33]
	v_mfma_f32_16x16x32_bf16 v[22:25], v[150:153], v[190:193], v[22:25]
	v_mfma_f32_16x16x32_bf16 v[14:17], v[142:145], v[198:201], v[14:17]
	v_mfma_f32_16x16x32_bf16 v[6:9], v[150:153], v[198:201], v[6:9]
	v_mfma_f32_16x16x32_bf16 v[74:77], v[158:161], v[174:177], v[74:77]
	v_mfma_f32_16x16x32_bf16 v[66:69], v[166:169], v[174:177], v[66:69]
	v_mfma_f32_16x16x32_bf16 v[42:45], v[158:161], v[182:185], v[42:45]
	v_mfma_f32_16x16x32_bf16 v[34:37], v[166:169], v[182:185], v[34:37]
	v_mfma_f32_16x16x32_bf16 v[26:29], v[158:161], v[190:193], v[26:29]
	v_mfma_f32_16x16x32_bf16 v[18:21], v[166:169], v[190:193], v[18:21]
	v_mfma_f32_16x16x32_bf16 v[10:13], v[158:161], v[198:201], v[10:13]
	v_mfma_f32_16x16x32_bf16 v[2:5], v[166:169], v[198:201], v[2:5]
	v_mfma_f32_16x16x32_bf16 v[78:81], v[146:149], v[178:181], v[78:81]
	v_mfma_f32_16x16x32_bf16 v[70:73], v[154:157], v[178:181], v[70:73]
	v_mfma_f32_16x16x32_bf16 v[46:49], v[146:149], v[186:189], v[46:49]
	v_mfma_f32_16x16x32_bf16 v[38:41], v[154:157], v[186:189], v[38:41]
	v_mfma_f32_16x16x32_bf16 v[30:33], v[146:149], v[194:197], v[30:33]
	v_mfma_f32_16x16x32_bf16 v[22:25], v[154:157], v[194:197], v[22:25]
	v_mfma_f32_16x16x32_bf16 v[14:17], v[146:149], v[204:207], v[14:17]
	v_mfma_f32_16x16x32_bf16 v[6:9], v[154:157], v[204:207], v[6:9]
	v_mfma_f32_16x16x32_bf16 v[74:77], v[162:165], v[178:181], v[74:77]
	v_mfma_f32_16x16x32_bf16 v[66:69], v[170:173], v[178:181], v[66:69]
	v_mfma_f32_16x16x32_bf16 v[42:45], v[162:165], v[186:189], v[42:45]
	v_mfma_f32_16x16x32_bf16 v[34:37], v[170:173], v[186:189], v[34:37]
	v_mfma_f32_16x16x32_bf16 v[26:29], v[162:165], v[194:197], v[26:29]
	v_mfma_f32_16x16x32_bf16 v[18:21], v[170:173], v[194:197], v[18:21]
	v_mfma_f32_16x16x32_bf16 v[10:13], v[162:165], v[204:207], v[10:13]
	v_mfma_f32_16x16x32_bf16 v[2:5], v[170:173], v[204:207], v[2:5]
	s_setprio 0
	s_barrier
	s_add_i32 s58, s58, 2
	s_addk_i32 s52, 0x100
	s_addk_i32 s53, 0x100
	s_cmp_gt_u32 s58, 29
	s_cbranch_scc0 .LBB0_845
	s_and_b64 vcc, exec, s[28:29]
	s_cbranch_vccz .LBB0_848
	s_barrier

.LBB0_871:
	v_add_u32_e32 v169, 0x10000, v167
	v_add_u32_e32 v170, 0x14000, v167
	ds_read_b128 v[2:5], v169
	ds_read_b128 v[6:9], v169 offset:1024
	ds_read_b128 v[10:13], v169 offset:2048
	ds_read_b128 v[14:17], v169 offset:3072
	ds_read_b128 v[18:21], v170
	ds_read_b128 v[22:25], v170 offset:1024
	ds_read_b128 v[26:29], v170 offset:2048
	ds_read_b128 v[30:33], v170 offset:3072
	s_lshl_b32 s47, s14, 19
	s_lshl_b32 s55, s56, 19
	s_or_b32 s51, s19, 0x80
	s_or_b32 s52, s18, 0x100
	s_and_b64 s[6:7], s[28:29], exec
	s_cselect_b32 s15, s47, s19
	s_or_b32 s49, s19, 0x100
	s_and_b64 s[6:7], s[28:29], exec
	s_cselect_b32 vcc_lo, s55, s18
	s_mov_b32 m0, s30
	ds_read_b128 v[34:37], v168
	ds_read_b128 v[38:41], v168 offset:1024
	ds_read_b128 v[42:45], v168 offset:2048
	ds_read_b128 v[46:49], v168 offset:3072
	ds_read_b128 v[50:53], v168 offset:4096
	ds_read_b128 v[54:57], v168 offset:5120
	ds_read_b128 v[58:61], v168 offset:6144
	ds_read_b128 v[62:65], v168 offset:7168
	buffer_load_dwordx4 v0, s[64:67], s51 offen lds
	s_mov_b32 m0, s16
	s_or_b32 s6, s19, 0x40080
	buffer_load_dwordx4 v163, s[64:67], s51 offen lds
	s_mov_b32 m0, s17
	s_nop 0
	buffer_load_dwordx4 v0, s[64:67], s6 offen lds
	s_mov_b32 m0, s21
	s_nop 0
	buffer_load_dwordx4 v163, s[64:67], s6 offen lds
	s_waitcnt vmcnt(8)
	s_waitcnt lgkmcnt(0)
	s_barrier
	s_setprio 1
	s_waitcnt vmcnt(16)
	v_mfma_scale_f32_16x16x128_f8f6f4 v[138:141], v[2:9], v[34:41], 0, v234, v234 op_sel_hi:[0,0,0]
	v_mfma_scale_f32_16x16x128_f8f6f4 v[146:149], v[10:17], v[34:41], 0, v234, v234 op_sel_hi:[0,0,0]
	v_mfma_scale_f32_16x16x128_f8f6f4 v[134:137], v[2:9], v[42:49], 0, v234, v234 op_sel_hi:[0,0,0]
	v_mfma_scale_f32_16x16x128_f8f6f4 v[130:133], v[10:17], v[42:49], 0, v234, v234 op_sel_hi:[0,0,0]
	v_mfma_scale_f32_16x16x128_f8f6f4 v[110:113], v[2:9], v[50:57], 0, v234, v234 op_sel_hi:[0,0,0]
	v_mfma_scale_f32_16x16x128_f8f6f4 v[102:105], v[10:17], v[50:57], 0, v234, v234 op_sel_hi:[0,0,0]
	v_mfma_scale_f32_16x16x128_f8f6f4 v[78:81], v[2:9], v[58:65], 0, v234, v234 op_sel_hi:[0,0,0]
	v_mfma_scale_f32_16x16x128_f8f6f4 v[70:73], v[10:17], v[58:65], 0, v234, v234 op_sel_hi:[0,0,0]
	v_mfma_scale_f32_16x16x128_f8f6f4 v[154:157], v[18:25], v[34:41], 0, v234, v234 op_sel_hi:[0,0,0]
	v_mfma_scale_f32_16x16x128_f8f6f4 v[158:161], v[26:33], v[34:41], 0, v234, v234 op_sel_hi:[0,0,0]
	v_mfma_scale_f32_16x16x128_f8f6f4 v[150:153], v[18:25], v[42:49], 0, v234, v234 op_sel_hi:[0,0,0]
	v_mfma_scale_f32_16x16x128_f8f6f4 v[142:145], v[26:33], v[42:49], 0, v234, v234 op_sel_hi:[0,0,0]
	v_mfma_scale_f32_16x16x128_f8f6f4 v[126:129], v[18:25], v[50:57], 0, v234, v234 op_sel_hi:[0,0,0]
	v_mfma_scale_f32_16x16x128_f8f6f4 v[118:121], v[26:33], v[50:57], 0, v234, v234 op_sel_hi:[0,0,0]
	v_mfma_scale_f32_16x16x128_f8f6f4 v[94:97], v[18:25], v[58:65], 0, v234, v234 op_sel_hi:[0,0,0]
	v_mfma_scale_f32_16x16x128_f8f6f4 v[86:89], v[26:33], v[58:65], 0, v234, v234 op_sel_hi:[0,0,0]
	s_setprio 0
	s_barrier
	s_mov_b32 m0, s31
	s_mov_b32 s6, s66
	s_mov_b32 s7, s67
	ds_read_b128 v[34:37], v168 offset:16384
	ds_read_b128 v[38:41], v168 offset:17408
	ds_read_b128 v[172:175], v168 offset:18432
	ds_read_b128 v[176:179], v168 offset:19456
	ds_read_b128 v[180:183], v168 offset:20480
	ds_read_b128 v[184:187], v168 offset:21504
	ds_read_b128 v[188:191], v168 offset:22528
	ds_read_b128 v[192:195], v168 offset:23552
	buffer_load_dwordx4 v162, s[4:7], s52 offen lds
	s_mov_b32 m0, s73
	s_or_b32 s51, s18, 0x40100
	buffer_load_dwordx4 v164, s[4:7], s52 offen lds
	s_mov_b32 m0, s76
	s_nop 0
	buffer_load_dwordx4 v162, s[4:7], s51 offen lds
	s_mov_b32 m0, s77
	s_nop 0
	buffer_load_dwordx4 v164, s[4:7], s51 offen lds
	s_waitcnt vmcnt(6)
	s_waitcnt lgkmcnt(0)
	s_barrier
	s_setprio 1
	v_mfma_scale_f32_16x16x128_f8f6f4 v[106:109], v[2:9], v[34:41], 0, v234, v234 op_sel_hi:[0,0,0]
	v_mfma_scale_f32_16x16x128_f8f6f4 v[98:101], v[10:17], v[34:41], 0, v234, v234 op_sel_hi:[0,0,0]
	v_mfma_scale_f32_16x16x128_f8f6f4 v[74:77], v[2:9], v[172:179], 0, v234, v234 op_sel_hi:[0,0,0]
	v_mfma_scale_f32_16x16x128_f8f6f4 v[66:69], v[10:17], v[172:179], 0, v234, v234 op_sel_hi:[0,0,0]
	v_mfma_scale_f32_16x16x128_f8f6f4 v[62:65], v[2:9], v[180:187], 0, v234, v234 op_sel_hi:[0,0,0]
	v_mfma_scale_f32_16x16x128_f8f6f4 v[54:57], v[10:17], v[180:187], 0, v234, v234 op_sel_hi:[0,0,0]
	v_mfma_scale_f32_16x16x128_f8f6f4 v[46:49], v[2:9], v[188:195], 0, v234, v234 op_sel_hi:[0,0,0]
	v_mfma_scale_f32_16x16x128_f8f6f4 v[42:45], v[10:17], v[188:195], 0, v234, v234 op_sel_hi:[0,0,0]
	v_mfma_scale_f32_16x16x128_f8f6f4 v[122:125], v[18:25], v[34:41], 0, v234, v234 op_sel_hi:[0,0,0]
	v_mfma_scale_f32_16x16x128_f8f6f4 v[114:117], v[26:33], v[34:41], 0, v234, v234 op_sel_hi:[0,0,0]
	v_mfma_scale_f32_16x16x128_f8f6f4 v[90:93], v[18:25], v[172:179], 0, v234, v234 op_sel_hi:[0,0,0]
	v_mfma_scale_f32_16x16x128_f8f6f4 v[82:85], v[26:33], v[172:179], 0, v234, v234 op_sel_hi:[0,0,0]
	v_mfma_scale_f32_16x16x128_f8f6f4 v[58:61], v[18:25], v[180:187], 0, v234, v234 op_sel_hi:[0,0,0]
	v_mfma_scale_f32_16x16x128_f8f6f4 v[50:53], v[26:33], v[180:187], 0, v234, v234 op_sel_hi:[0,0,0]
	v_mfma_scale_f32_16x16x128_f8f6f4 v[38:41], v[18:25], v[188:195], 0, v234, v234 op_sel_hi:[0,0,0]
	v_mfma_scale_f32_16x16x128_f8f6f4 v[34:37], v[26:33], v[188:195], 0, v234, v234 op_sel_hi:[0,0,0]
	s_setprio 0
	s_barrier
	v_add_u32_e32 v171, 0x18000, v167
	v_add_u32_e32 v172, 0x1c000, v167
	ds_read_b128 v[26:29], v171
	ds_read_b128 v[30:33], v171 offset:1024
	ds_read_b128 v[18:21], v171 offset:2048
	ds_read_b128 v[22:25], v171 offset:3072
	ds_read_b128 v[10:13], v172
	ds_read_b128 v[14:17], v172 offset:1024
	ds_read_b128 v[2:5], v172 offset:2048
	ds_read_b128 v[6:9], v172 offset:3072
	s_mov_b32 m0, s20
	ds_read_b128 v[174:177], v168 offset:32768
	ds_read_b128 v[178:181], v168 offset:33792
	ds_read_b128 v[182:185], v168 offset:34816
	ds_read_b128 v[186:189], v168 offset:35840
	ds_read_b128 v[190:193], v168 offset:36864
	ds_read_b128 v[194:197], v168 offset:37888
	ds_read_b128 v[204:207], v168 offset:38912
	ds_read_b128 v[208:211], v168 offset:39936
	buffer_load_dwordx4 v0, s[64:67], s49 offen lds
	s_mov_b32 m0, s78
	s_nop 0
	buffer_load_dwordx4 v163, s[64:67], s49 offen lds
	s_or_b32 s49, s19, 0x40100
	s_mov_b32 m0, s79
	s_nop 0
	buffer_load_dwordx4 v0, s[64:67], s49 offen lds
	s_mov_b32 m0, s80
	s_nop 0
	buffer_load_dwordx4 v163, s[64:67], s49 offen lds
	s_waitcnt vmcnt(8)
	s_waitcnt lgkmcnt(0)
	s_barrier
	s_setprio 1
	v_mfma_scale_f32_16x16x128_f8f6f4 v[138:141], v[26:33], v[174:181], v[138:141], v234, v234 op_sel_hi:[0,0,0]
	v_mfma_scale_f32_16x16x128_f8f6f4 v[146:149], v[18:25], v[174:181], v[146:149], v234, v234 op_sel_hi:[0,0,0]
	v_mfma_scale_f32_16x16x128_f8f6f4 v[134:137], v[26:33], v[182:189], v[134:137], v234, v234 op_sel_hi:[0,0,0]
	v_mfma_scale_f32_16x16x128_f8f6f4 v[130:133], v[18:25], v[182:189], v[130:133], v234, v234 op_sel_hi:[0,0,0]
	v_mfma_scale_f32_16x16x128_f8f6f4 v[110:113], v[26:33], v[190:197], v[110:113], v234, v234 op_sel_hi:[0,0,0]
	v_mfma_scale_f32_16x16x128_f8f6f4 v[102:105], v[18:25], v[190:197], v[102:105], v234, v234 op_sel_hi:[0,0,0]
	v_mfma_scale_f32_16x16x128_f8f6f4 v[78:81], v[26:33], v[204:211], v[78:81], v234, v234 op_sel_hi:[0,0,0]
	v_mfma_scale_f32_16x16x128_f8f6f4 v[70:73], v[18:25], v[204:211], v[70:73], v234, v234 op_sel_hi:[0,0,0]
	v_mfma_scale_f32_16x16x128_f8f6f4 v[154:157], v[10:17], v[174:181], v[154:157], v234, v234 op_sel_hi:[0,0,0]
	v_mfma_scale_f32_16x16x128_f8f6f4 v[158:161], v[2:9], v[174:181], v[158:161], v234, v234 op_sel_hi:[0,0,0]
	v_mfma_scale_f32_16x16x128_f8f6f4 v[150:153], v[10:17], v[182:189], v[150:153], v234, v234 op_sel_hi:[0,0,0]
	v_mfma_scale_f32_16x16x128_f8f6f4 v[142:145], v[2:9], v[182:189], v[142:145], v234, v234 op_sel_hi:[0,0,0]
	v_mfma_scale_f32_16x16x128_f8f6f4 v[126:129], v[10:17], v[190:197], v[126:129], v234, v234 op_sel_hi:[0,0,0]
	v_mfma_scale_f32_16x16x128_f8f6f4 v[118:121], v[2:9], v[190:197], v[118:121], v234, v234 op_sel_hi:[0,0,0]
	v_mfma_scale_f32_16x16x128_f8f6f4 v[94:97], v[10:17], v[204:211], v[94:97], v234, v234 op_sel_hi:[0,0,0]
	v_mfma_scale_f32_16x16x128_f8f6f4 v[86:89], v[2:9], v[204:211], v[86:89], v234, v234 op_sel_hi:[0,0,0]
	s_setprio 0
	s_barrier
	s_mov_b32 m0, s81
	s_or_b32 s49, s18, 0x180
	ds_read_b128 v[174:177], v168 offset:49152
	ds_read_b128 v[178:181], v168 offset:50176
	ds_read_b128 v[182:185], v168 offset:51200
	ds_read_b128 v[186:189], v168 offset:52224
	ds_read_b128 v[190:193], v168 offset:53248
	ds_read_b128 v[194:197], v168 offset:54272
	ds_read_b128 v[204:207], v168 offset:55296
	ds_read_b128 v[208:211], v168 offset:56320
	buffer_load_dwordx4 v162, s[4:7], s49 offen lds
	s_mov_b32 m0, s82
	s_nop 0
	buffer_load_dwordx4 v164, s[4:7], s49 offen lds
	s_or_b32 s49, s18, 0x40180
	s_mov_b32 m0, s83
	s_nop 0
	buffer_load_dwordx4 v162, s[4:7], s49 offen lds
	s_mov_b32 m0, s84
	s_nop 0
	buffer_load_dwordx4 v164, s[4:7], s49 offen lds
	s_waitcnt vmcnt(6)
	s_waitcnt lgkmcnt(0)
	s_barrier
	s_setprio 1
	v_mfma_scale_f32_16x16x128_f8f6f4 v[106:109], v[26:33], v[174:181], v[106:109], v234, v234 op_sel_hi:[0,0,0]
	v_mfma_scale_f32_16x16x128_f8f6f4 v[98:101], v[18:25], v[174:181], v[98:101], v234, v234 op_sel_hi:[0,0,0]
	v_mfma_scale_f32_16x16x128_f8f6f4 v[74:77], v[26:33], v[182:189], v[74:77], v234, v234 op_sel_hi:[0,0,0]
	v_mfma_scale_f32_16x16x128_f8f6f4 v[66:69], v[18:25], v[182:189], v[66:69], v234, v234 op_sel_hi:[0,0,0]
	v_mfma_scale_f32_16x16x128_f8f6f4 v[62:65], v[26:33], v[190:197], v[62:65], v234, v234 op_sel_hi:[0,0,0]
	v_mfma_scale_f32_16x16x128_f8f6f4 v[54:57], v[18:25], v[190:197], v[54:57], v234, v234 op_sel_hi:[0,0,0]
	v_mfma_scale_f32_16x16x128_f8f6f4 v[46:49], v[26:33], v[204:211], v[46:49], v234, v234 op_sel_hi:[0,0,0]
	v_mfma_scale_f32_16x16x128_f8f6f4 v[42:45], v[18:25], v[204:211], v[42:45], v234, v234 op_sel_hi:[0,0,0]
	v_mfma_scale_f32_16x16x128_f8f6f4 v[122:125], v[10:17], v[174:181], v[122:125], v234, v234 op_sel_hi:[0,0,0]
	v_mfma_scale_f32_16x16x128_f8f6f4 v[114:117], v[2:9], v[174:181], v[114:117], v234, v234 op_sel_hi:[0,0,0]
	v_mfma_scale_f32_16x16x128_f8f6f4 v[90:93], v[10:17], v[182:189], v[90:93], v234, v234 op_sel_hi:[0,0,0]
	v_mfma_scale_f32_16x16x128_f8f6f4 v[82:85], v[2:9], v[182:189], v[82:85], v234, v234 op_sel_hi:[0,0,0]
	v_mfma_scale_f32_16x16x128_f8f6f4 v[58:61], v[10:17], v[190:197], v[58:61], v234, v234 op_sel_hi:[0,0,0]
	v_mfma_scale_f32_16x16x128_f8f6f4 v[50:53], v[2:9], v[190:197], v[50:53], v234, v234 op_sel_hi:[0,0,0]
	v_mfma_scale_f32_16x16x128_f8f6f4 v[38:41], v[10:17], v[204:211], v[38:41], v234, v234 op_sel_hi:[0,0,0]
	v_mfma_scale_f32_16x16x128_f8f6f4 v[34:37], v[2:9], v[204:211], v[34:37], v234, v234 op_sel_hi:[0,0,0]
	s_setprio 0
	s_barrier
	s_addk_i32 s18, 0x200
	s_add_i32 s19, s19, 0x40180
	s_mov_b32 s49, 0
.LBB0_872:
	ds_read_b128 v[2:5], v169
	ds_read_b128 v[6:9], v169 offset:1024
	ds_read_b128 v[10:13], v169 offset:2048
	ds_read_b128 v[14:17], v169 offset:3072
	ds_read_b128 v[18:21], v170
	ds_read_b128 v[22:25], v170 offset:1024
	ds_read_b128 v[26:29], v170 offset:2048
	ds_read_b128 v[30:33], v170 offset:3072
	s_add_i32 s52, s19, 0xfffc0080
	s_cmp_eq_u32 s49, 12
	s_cselect_b32 s51, vcc_lo, s18
	s_cselect_b32 s52, s15, s52
	s_add_i32 s53, s19, 0xfffc0000
	s_mov_b32 m0, s30
	ds_read_b128 v[174:177], v168
	ds_read_b128 v[178:181], v168 offset:1024
	ds_read_b128 v[182:185], v168 offset:2048
	ds_read_b128 v[186:189], v168 offset:3072
	ds_read_b128 v[190:193], v168 offset:4096
	ds_read_b128 v[194:197], v168 offset:5120
	ds_read_b128 v[204:207], v168 offset:6144
	ds_read_b128 v[208:211], v168 offset:7168
	buffer_load_dwordx4 v0, s[64:67], s53 offen lds
	s_mov_b32 m0, s16
	s_nop 0
	buffer_load_dwordx4 v163, s[64:67], s53 offen lds
	s_mov_b32 m0, s17
	s_nop 0
	buffer_load_dwordx4 v0, s[64:67], s19 offen lds
	s_mov_b32 m0, s21
	s_nop 0
	buffer_load_dwordx4 v163, s[64:67], s19 offen lds
	s_waitcnt vmcnt(8)
	s_waitcnt lgkmcnt(0)
	s_barrier
	s_setprio 1
	v_mfma_scale_f32_16x16x128_f8f6f4 v[138:141], v[2:9], v[174:181], v[138:141], v234, v234 op_sel_hi:[0,0,0]
	v_mfma_scale_f32_16x16x128_f8f6f4 v[146:149], v[10:17], v[174:181], v[146:149], v234, v234 op_sel_hi:[0,0,0]
	v_mfma_scale_f32_16x16x128_f8f6f4 v[134:137], v[2:9], v[182:189], v[134:137], v234, v234 op_sel_hi:[0,0,0]
	v_mfma_scale_f32_16x16x128_f8f6f4 v[130:133], v[10:17], v[182:189], v[130:133], v234, v234 op_sel_hi:[0,0,0]
	v_mfma_scale_f32_16x16x128_f8f6f4 v[110:113], v[2:9], v[190:197], v[110:113], v234, v234 op_sel_hi:[0,0,0]
	v_mfma_scale_f32_16x16x128_f8f6f4 v[102:105], v[10:17], v[190:197], v[102:105], v234, v234 op_sel_hi:[0,0,0]
	v_mfma_scale_f32_16x16x128_f8f6f4 v[78:81], v[2:9], v[204:211], v[78:81], v234, v234 op_sel_hi:[0,0,0]
	v_mfma_scale_f32_16x16x128_f8f6f4 v[70:73], v[10:17], v[204:211], v[70:73], v234, v234 op_sel_hi:[0,0,0]
	v_mfma_scale_f32_16x16x128_f8f6f4 v[154:157], v[18:25], v[174:181], v[154:157], v234, v234 op_sel_hi:[0,0,0]
	v_mfma_scale_f32_16x16x128_f8f6f4 v[158:161], v[26:33], v[174:181], v[158:161], v234, v234 op_sel_hi:[0,0,0]
	v_mfma_scale_f32_16x16x128_f8f6f4 v[150:153], v[18:25], v[182:189], v[150:153], v234, v234 op_sel_hi:[0,0,0]
	v_mfma_scale_f32_16x16x128_f8f6f4 v[142:145], v[26:33], v[182:189], v[142:145], v234, v234 op_sel_hi:[0,0,0]
	v_mfma_scale_f32_16x16x128_f8f6f4 v[126:129], v[18:25], v[190:197], v[126:129], v234, v234 op_sel_hi:[0,0,0]
	v_mfma_scale_f32_16x16x128_f8f6f4 v[118:121], v[26:33], v[190:197], v[118:121], v234, v234 op_sel_hi:[0,0,0]
	v_mfma_scale_f32_16x16x128_f8f6f4 v[94:97], v[18:25], v[204:211], v[94:97], v234, v234 op_sel_hi:[0,0,0]
	v_mfma_scale_f32_16x16x128_f8f6f4 v[86:89], v[26:33], v[204:211], v[86:89], v234, v234 op_sel_hi:[0,0,0]
	s_setprio 0
	s_barrier
	s_mov_b32 m0, s31
	ds_read_b128 v[174:177], v168 offset:16384
	ds_read_b128 v[178:181], v168 offset:17408
	ds_read_b128 v[182:185], v168 offset:18432
	ds_read_b128 v[186:189], v168 offset:19456
	ds_read_b128 v[190:193], v168 offset:20480
	ds_read_b128 v[194:197], v168 offset:21504
	ds_read_b128 v[204:207], v168 offset:22528
	ds_read_b128 v[208:211], v168 offset:23552
	buffer_load_dwordx4 v162, s[4:7], s51 offen lds
	s_mov_b32 m0, s73
	s_add_i32 s53, s51, 0x40000
	buffer_load_dwordx4 v164, s[4:7], s51 offen lds
	s_mov_b32 m0, s76
	s_nop 0
	buffer_load_dwordx4 v162, s[4:7], s53 offen lds
	s_mov_b32 m0, s77
	s_nop 0
	buffer_load_dwordx4 v164, s[4:7], s53 offen lds
	s_waitcnt vmcnt(6)
	s_waitcnt lgkmcnt(0)
	s_barrier
	s_setprio 1
	v_mfma_scale_f32_16x16x128_f8f6f4 v[106:109], v[2:9], v[174:181], v[106:109], v234, v234 op_sel_hi:[0,0,0]
	v_mfma_scale_f32_16x16x128_f8f6f4 v[98:101], v[10:17], v[174:181], v[98:101], v234, v234 op_sel_hi:[0,0,0]
	v_mfma_scale_f32_16x16x128_f8f6f4 v[74:77], v[2:9], v[182:189], v[74:77], v234, v234 op_sel_hi:[0,0,0]
	v_mfma_scale_f32_16x16x128_f8f6f4 v[66:69], v[10:17], v[182:189], v[66:69], v234, v234 op_sel_hi:[0,0,0]
	v_mfma_scale_f32_16x16x128_f8f6f4 v[62:65], v[2:9], v[190:197], v[62:65], v234, v234 op_sel_hi:[0,0,0]
	v_mfma_scale_f32_16x16x128_f8f6f4 v[54:57], v[10:17], v[190:197], v[54:57], v234, v234 op_sel_hi:[0,0,0]
	v_mfma_scale_f32_16x16x128_f8f6f4 v[46:49], v[2:9], v[204:211], v[46:49], v234, v234 op_sel_hi:[0,0,0]
	v_mfma_scale_f32_16x16x128_f8f6f4 v[42:45], v[10:17], v[204:211], v[42:45], v234, v234 op_sel_hi:[0,0,0]
	v_mfma_scale_f32_16x16x128_f8f6f4 v[122:125], v[18:25], v[174:181], v[122:125], v234, v234 op_sel_hi:[0,0,0]
	v_mfma_scale_f32_16x16x128_f8f6f4 v[114:117], v[26:33], v[174:181], v[114:117], v234, v234 op_sel_hi:[0,0,0]
	v_mfma_scale_f32_16x16x128_f8f6f4 v[90:93], v[18:25], v[182:189], v[90:93], v234, v234 op_sel_hi:[0,0,0]
	v_mfma_scale_f32_16x16x128_f8f6f4 v[82:85], v[26:33], v[182:189], v[82:85], v234, v234 op_sel_hi:[0,0,0]
	v_mfma_scale_f32_16x16x128_f8f6f4 v[58:61], v[18:25], v[190:197], v[58:61], v234, v234 op_sel_hi:[0,0,0]
	v_mfma_scale_f32_16x16x128_f8f6f4 v[50:53], v[26:33], v[190:197], v[50:53], v234, v234 op_sel_hi:[0,0,0]
	v_mfma_scale_f32_16x16x128_f8f6f4 v[38:41], v[18:25], v[204:211], v[38:41], v234, v234 op_sel_hi:[0,0,0]
	v_mfma_scale_f32_16x16x128_f8f6f4 v[34:37], v[26:33], v[204:211], v[34:37], v234, v234 op_sel_hi:[0,0,0]
	s_setprio 0
	s_barrier
	ds_read_b128 v[18:21], v171
	ds_read_b128 v[22:25], v171 offset:1024
	ds_read_b128 v[26:29], v171 offset:2048
	ds_read_b128 v[30:33], v171 offset:3072
	ds_read_b128 v[10:13], v172
	ds_read_b128 v[14:17], v172 offset:1024
	ds_read_b128 v[2:5], v172 offset:2048
	ds_read_b128 v[6:9], v172 offset:3072
	s_mov_b32 m0, s20
	ds_read_b128 v[174:177], v168 offset:32768
	ds_read_b128 v[178:181], v168 offset:33792
	ds_read_b128 v[182:185], v168 offset:34816
	ds_read_b128 v[186:189], v168 offset:35840
	ds_read_b128 v[190:193], v168 offset:36864
	ds_read_b128 v[194:197], v168 offset:37888
	ds_read_b128 v[204:207], v168 offset:38912
	ds_read_b128 v[208:211], v168 offset:39936
	buffer_load_dwordx4 v0, s[64:67], s52 offen lds
	s_mov_b32 m0, s78
	s_nop 0
	buffer_load_dwordx4 v163, s[64:67], s52 offen lds
	s_add_i32 s52, s52, 0x40000
	s_mov_b32 m0, s79
	s_nop 0
	buffer_load_dwordx4 v0, s[64:67], s52 offen lds
	s_mov_b32 m0, s80
	s_nop 0
	buffer_load_dwordx4 v163, s[64:67], s52 offen lds
	s_waitcnt vmcnt(8)
	s_waitcnt lgkmcnt(0)
	s_barrier
	s_setprio 1
	v_mfma_scale_f32_16x16x128_f8f6f4 v[138:141], v[18:25], v[174:181], v[138:141], v234, v234 op_sel_hi:[0,0,0]
	v_mfma_scale_f32_16x16x128_f8f6f4 v[146:149], v[26:33], v[174:181], v[146:149], v234, v234 op_sel_hi:[0,0,0]
	v_mfma_scale_f32_16x16x128_f8f6f4 v[134:137], v[18:25], v[182:189], v[134:137], v234, v234 op_sel_hi:[0,0,0]
	v_mfma_scale_f32_16x16x128_f8f6f4 v[130:133], v[26:33], v[182:189], v[130:133], v234, v234 op_sel_hi:[0,0,0]
	v_mfma_scale_f32_16x16x128_f8f6f4 v[110:113], v[18:25], v[190:197], v[110:113], v234, v234 op_sel_hi:[0,0,0]
	v_mfma_scale_f32_16x16x128_f8f6f4 v[102:105], v[26:33], v[190:197], v[102:105], v234, v234 op_sel_hi:[0,0,0]
	v_mfma_scale_f32_16x16x128_f8f6f4 v[78:81], v[18:25], v[204:211], v[78:81], v234, v234 op_sel_hi:[0,0,0]
	v_mfma_scale_f32_16x16x128_f8f6f4 v[70:73], v[26:33], v[204:211], v[70:73], v234, v234 op_sel_hi:[0,0,0]
	v_mfma_scale_f32_16x16x128_f8f6f4 v[154:157], v[10:17], v[174:181], v[154:157], v234, v234 op_sel_hi:[0,0,0]
	v_mfma_scale_f32_16x16x128_f8f6f4 v[158:161], v[2:9], v[174:181], v[158:161], v234, v234 op_sel_hi:[0,0,0]
	v_mfma_scale_f32_16x16x128_f8f6f4 v[150:153], v[10:17], v[182:189], v[150:153], v234, v234 op_sel_hi:[0,0,0]
	v_mfma_scale_f32_16x16x128_f8f6f4 v[142:145], v[2:9], v[182:189], v[142:145], v234, v234 op_sel_hi:[0,0,0]
	v_mfma_scale_f32_16x16x128_f8f6f4 v[126:129], v[10:17], v[190:197], v[126:129], v234, v234 op_sel_hi:[0,0,0]
	v_mfma_scale_f32_16x16x128_f8f6f4 v[118:121], v[2:9], v[190:197], v[118:121], v234, v234 op_sel_hi:[0,0,0]
	v_mfma_scale_f32_16x16x128_f8f6f4 v[94:97], v[10:17], v[204:211], v[94:97], v234, v234 op_sel_hi:[0,0,0]
	v_mfma_scale_f32_16x16x128_f8f6f4 v[86:89], v[2:9], v[204:211], v[86:89], v234, v234 op_sel_hi:[0,0,0]
	s_setprio 0
	s_barrier
	s_mov_b32 m0, s81
	s_or_b32 s52, s51, 0x80
	ds_read_b128 v[174:177], v168 offset:49152
	ds_read_b128 v[178:181], v168 offset:50176
	ds_read_b128 v[182:185], v168 offset:51200
	ds_read_b128 v[186:189], v168 offset:52224
	ds_read_b128 v[190:193], v168 offset:53248
	ds_read_b128 v[194:197], v168 offset:54272
	ds_read_b128 v[204:207], v168 offset:55296
	ds_read_b128 v[208:211], v168 offset:56320
	buffer_load_dwordx4 v162, s[4:7], s52 offen lds
	s_mov_b32 m0, s82
	s_add_i32 s51, s51, 0x40080
	buffer_load_dwordx4 v164, s[4:7], s52 offen lds
	s_mov_b32 m0, s83
	s_nop 0
	buffer_load_dwordx4 v162, s[4:7], s51 offen lds
	s_mov_b32 m0, s84
	s_nop 0
	buffer_load_dwordx4 v164, s[4:7], s51 offen lds
	s_waitcnt vmcnt(6)
	s_waitcnt lgkmcnt(0)
	s_barrier
	s_setprio 1
	v_mfma_scale_f32_16x16x128_f8f6f4 v[106:109], v[18:25], v[174:181], v[106:109], v234, v234 op_sel_hi:[0,0,0]
	v_mfma_scale_f32_16x16x128_f8f6f4 v[98:101], v[26:33], v[174:181], v[98:101], v234, v234 op_sel_hi:[0,0,0]
	v_mfma_scale_f32_16x16x128_f8f6f4 v[74:77], v[18:25], v[182:189], v[74:77], v234, v234 op_sel_hi:[0,0,0]
	v_mfma_scale_f32_16x16x128_f8f6f4 v[66:69], v[26:33], v[182:189], v[66:69], v234, v234 op_sel_hi:[0,0,0]
	v_mfma_scale_f32_16x16x128_f8f6f4 v[62:65], v[18:25], v[190:197], v[62:65], v234, v234 op_sel_hi:[0,0,0]
	v_mfma_scale_f32_16x16x128_f8f6f4 v[54:57], v[26:33], v[190:197], v[54:57], v234, v234 op_sel_hi:[0,0,0]
	v_mfma_scale_f32_16x16x128_f8f6f4 v[46:49], v[18:25], v[204:211], v[46:49], v234, v234 op_sel_hi:[0,0,0]
	v_mfma_scale_f32_16x16x128_f8f6f4 v[42:45], v[26:33], v[204:211], v[42:45], v234, v234 op_sel_hi:[0,0,0]
	v_mfma_scale_f32_16x16x128_f8f6f4 v[122:125], v[10:17], v[174:181], v[122:125], v234, v234 op_sel_hi:[0,0,0]
	v_mfma_scale_f32_16x16x128_f8f6f4 v[114:117], v[2:9], v[174:181], v[114:117], v234, v234 op_sel_hi:[0,0,0]
	v_mfma_scale_f32_16x16x128_f8f6f4 v[90:93], v[10:17], v[182:189], v[90:93], v234, v234 op_sel_hi:[0,0,0]
	v_mfma_scale_f32_16x16x128_f8f6f4 v[82:85], v[2:9], v[182:189], v[82:85], v234, v234 op_sel_hi:[0,0,0]
	v_mfma_scale_f32_16x16x128_f8f6f4 v[58:61], v[10:17], v[190:197], v[58:61], v234, v234 op_sel_hi:[0,0,0]
	v_mfma_scale_f32_16x16x128_f8f6f4 v[50:53], v[2:9], v[190:197], v[50:53], v234, v234 op_sel_hi:[0,0,0]
	v_mfma_scale_f32_16x16x128_f8f6f4 v[38:41], v[10:17], v[204:211], v[38:41], v234, v234 op_sel_hi:[0,0,0]
	v_mfma_scale_f32_16x16x128_f8f6f4 v[34:37], v[2:9], v[204:211], v[34:37], v234, v234 op_sel_hi:[0,0,0]
	s_setprio 0
	s_barrier
	s_add_i32 s49, s49, 2
	s_addk_i32 s18, 0x100
	s_addk_i32 s19, 0x100
	s_cmp_gt_u32 s49, 13
	s_cbranch_scc0 .LBB0_872
	s_nop 15
	s_nop 15
	s_and_b64 vcc, exec, s[26:27]
	s_cbranch_vccz .LBB0_875
	s_barrier

.LBB0_1796:
	v_add_u32_e32 v137, 0x10000, v135
	v_add_u32_e32 v138, 0x14000, v135
	ds_read_b128 v[2:5], v137
	ds_read_b128 v[6:9], v137 offset:1024
	ds_read_b128 v[10:13], v137 offset:2048
	ds_read_b128 v[14:17], v137 offset:3072
	ds_read_b128 v[18:21], v138
	ds_read_b128 v[22:25], v138 offset:1024
	ds_read_b128 v[26:29], v138 offset:2048
	ds_read_b128 v[30:33], v138 offset:3072
	s_add_i32 s59, s36, 0x200
	s_lshl_b32 s57, s55, 20
	s_lshl_b32 s58, s54, 20
	s_or_b32 s0, s41, 0x80
	s_or_b32 s62, s36, 0x100
	s_and_b64 s[2:3], s[22:23], exec
	s_cselect_b32 s60, s57, s41
	s_or_b32 s63, s41, 0x100
	s_and_b64 s[2:3], s[22:23], exec
	s_cselect_b32 s61, s58, s36
	s_mov_b32 m0, s49
	ds_read_b128 v[34:37], v136
	ds_read_b128 v[38:41], v136 offset:1024
	ds_read_b128 v[42:45], v136 offset:2048
	ds_read_b128 v[46:49], v136 offset:3072
	ds_read_b128 v[50:53], v136 offset:4096
	ds_read_b128 v[54:57], v136 offset:5120
	ds_read_b128 v[58:61], v136 offset:6144
	ds_read_b128 v[62:65], v136 offset:7168
	buffer_load_dwordx4 v131, s[64:67], s0 offen lds
	s_mov_b32 m0, s51
	s_nop 0
	buffer_load_dwordx4 v133, s[64:67], s0 offen lds
	s_or_b32 s0, s41, 0x80080
	s_mov_b32 m0, s50
	s_nop 0
	buffer_load_dwordx4 v131, s[64:67], s0 offen lds
	s_mov_b32 m0, s52
	s_nop 0
	buffer_load_dwordx4 v133, s[64:67], s0 offen lds
	s_waitcnt vmcnt(8)
	s_waitcnt lgkmcnt(0)
	s_barrier
	s_setprio 1
	v_mfma_f32_16x16x32_bf16 v[66:69], v[2:5], v[34:37], 0
	v_mfma_f32_16x16x32_bf16 v[70:73], v[10:13], v[34:37], 0
	v_mfma_f32_16x16x32_bf16 v[98:101], v[18:21], v[34:37], 0
	v_mfma_f32_16x16x32_bf16 v[34:37], v[26:29], v[34:37], 0
	v_mfma_f32_16x16x32_bf16 v[118:121], v[6:9], v[38:41], v[66:69]
	v_mfma_f32_16x16x32_bf16 v[70:73], v[14:17], v[38:41], v[70:73]
	v_mfma_f32_16x16x32_bf16 v[74:77], v[2:5], v[42:45], 0
	v_mfma_f32_16x16x32_bf16 v[78:81], v[10:13], v[42:45], 0
	v_mfma_f32_16x16x32_bf16 v[142:145], v[22:25], v[38:41], v[98:101]
	v_mfma_f32_16x16x32_bf16 v[34:37], v[30:33], v[38:41], v[34:37]
	v_mfma_f32_16x16x32_bf16 v[38:41], v[18:21], v[42:45], 0
	v_mfma_f32_16x16x32_bf16 v[42:45], v[26:29], v[42:45], 0
	v_mfma_f32_16x16x32_bf16 v[74:77], v[6:9], v[46:49], v[74:77]
	v_mfma_f32_16x16x32_bf16 v[78:81], v[14:17], v[46:49], v[78:81]
	v_mfma_f32_16x16x32_bf16 v[82:85], v[2:5], v[50:53], 0
	v_mfma_f32_16x16x32_bf16 v[86:89], v[10:13], v[50:53], 0
	v_mfma_f32_16x16x32_bf16 v[38:41], v[22:25], v[46:49], v[38:41]
	v_mfma_f32_16x16x32_bf16 v[42:45], v[30:33], v[46:49], v[42:45]
	v_mfma_f32_16x16x32_bf16 v[46:49], v[18:21], v[50:53], 0
	v_mfma_f32_16x16x32_bf16 v[50:53], v[26:29], v[50:53], 0
	v_mfma_f32_16x16x32_bf16 v[90:93], v[2:5], v[58:61], 0
	v_mfma_f32_16x16x32_bf16 v[94:97], v[10:13], v[58:61], 0
	v_mfma_f32_16x16x32_bf16 v[146:149], v[30:33], v[54:57], v[50:53]
	v_mfma_f32_16x16x32_bf16 v[50:53], v[18:21], v[58:61], 0
	v_mfma_f32_16x16x32_bf16 v[82:85], v[6:9], v[54:57], v[82:85]
	v_mfma_f32_16x16x32_bf16 v[86:89], v[14:17], v[54:57], v[86:89]
	v_mfma_f32_16x16x32_bf16 v[90:93], v[6:9], v[62:65], v[90:93]
	v_mfma_f32_16x16x32_bf16 v[94:97], v[14:17], v[62:65], v[94:97]
	v_mfma_f32_16x16x32_bf16 v[46:49], v[22:25], v[54:57], v[46:49]
	v_mfma_f32_16x16x32_bf16 v[150:153], v[22:25], v[62:65], v[50:53]
	v_mfma_f32_16x16x32_bf16 v[50:53], v[26:29], v[58:61], 0
	v_mfma_f32_16x16x32_bf16 v[154:157], v[30:33], v[62:65], v[50:53]
	s_setprio 0
	s_barrier
	s_mov_b32 m0, s35
	s_mov_b32 s0, s4
	s_mov_b32 s2, s66
	s_mov_b32 s3, s67
	s_nop 0
	ds_read_b128 v[50:53], v136 offset:16384
	ds_read_b128 v[54:57], v136 offset:17408
	ds_read_b128 v[58:61], v136 offset:18432
	ds_read_b128 v[62:65], v136 offset:19456
	ds_read_b128 v[98:101], v136 offset:20480
	ds_read_b128 v[102:105], v136 offset:21504
	ds_read_b128 v[106:109], v136 offset:22528
	ds_read_b128 v[110:113], v136 offset:23552
	buffer_load_dwordx4 v132, s[0:3], s62 offen lds
	s_mov_b32 m0, s37
	s_nop 0
	buffer_load_dwordx4 v134, s[0:3], s62 offen lds
	s_or_b32 s62, s36, 0x80100
	s_mov_b32 m0, s38
	s_nop 0
	buffer_load_dwordx4 v132, s[0:3], s62 offen lds
	s_mov_b32 m0, s39
	s_nop 0
	buffer_load_dwordx4 v134, s[0:3], s62 offen lds
	s_waitcnt vmcnt(6)
	s_waitcnt lgkmcnt(0)
	s_barrier
	s_setprio 1
	v_mfma_f32_16x16x32_bf16 v[114:117], v[2:5], v[50:53], 0
	v_mfma_f32_16x16x32_bf16 v[158:161], v[6:9], v[54:57], v[114:117]
	v_mfma_f32_16x16x32_bf16 v[114:117], v[10:13], v[50:53], 0
	v_mfma_f32_16x16x32_bf16 v[162:165], v[14:17], v[54:57], v[114:117]
	v_mfma_f32_16x16x32_bf16 v[114:117], v[2:5], v[58:61], 0
	v_mfma_f32_16x16x32_bf16 v[166:169], v[6:9], v[62:65], v[114:117]
	v_mfma_f32_16x16x32_bf16 v[114:117], v[10:13], v[58:61], 0
	v_mfma_f32_16x16x32_bf16 v[170:173], v[14:17], v[62:65], v[114:117]
	v_mfma_f32_16x16x32_bf16 v[114:117], v[2:5], v[98:101], 0
	v_mfma_f32_16x16x32_bf16 v[2:5], v[2:5], v[106:109], 0
	v_mfma_f32_16x16x32_bf16 v[174:177], v[6:9], v[102:105], v[114:117]
	v_mfma_f32_16x16x32_bf16 v[114:117], v[10:13], v[98:101], 0
	v_mfma_f32_16x16x32_bf16 v[2:5], v[6:9], v[110:113], v[2:5]
	v_mfma_f32_16x16x32_bf16 v[6:9], v[10:13], v[106:109], 0
	v_mfma_f32_16x16x32_bf16 v[178:181], v[14:17], v[102:105], v[114:117]
	v_mfma_f32_16x16x32_bf16 v[6:9], v[14:17], v[110:113], v[6:9]
	v_mfma_f32_16x16x32_bf16 v[10:13], v[18:21], v[50:53], 0
	v_mfma_f32_16x16x32_bf16 v[14:17], v[26:29], v[50:53], 0
	v_mfma_f32_16x16x32_bf16 v[50:53], v[18:21], v[58:61], 0
	v_mfma_f32_16x16x32_bf16 v[182:185], v[22:25], v[62:65], v[50:53]
	v_mfma_f32_16x16x32_bf16 v[50:53], v[26:29], v[58:61], 0
	v_mfma_f32_16x16x32_bf16 v[186:189], v[30:33], v[62:65], v[50:53]
	v_mfma_f32_16x16x32_bf16 v[50:53], v[18:21], v[98:101], 0
	v_mfma_f32_16x16x32_bf16 v[18:21], v[18:21], v[106:109], 0
	v_mfma_f32_16x16x32_bf16 v[10:13], v[22:25], v[54:57], v[10:13]
	v_mfma_f32_16x16x32_bf16 v[14:17], v[30:33], v[54:57], v[14:17]
	v_mfma_f32_16x16x32_bf16 v[190:193], v[22:25], v[102:105], v[50:53]
	v_mfma_f32_16x16x32_bf16 v[50:53], v[26:29], v[98:101], 0
	v_mfma_f32_16x16x32_bf16 v[198:201], v[22:25], v[110:113], v[18:21]
	v_mfma_f32_16x16x32_bf16 v[18:21], v[26:29], v[106:109], 0
	v_mfma_f32_16x16x32_bf16 v[194:197], v[30:33], v[102:105], v[50:53]
	v_mfma_f32_16x16x32_bf16 v[204:207], v[30:33], v[110:113], v[18:21]
	s_setprio 0
	s_barrier
	v_add_u32_e32 v139, 0x18000, v135
	v_add_u32_e32 v140, 0x1c000, v135
	s_nop 1
	ds_read_b128 v[18:21], v139
	ds_read_b128 v[22:25], v139 offset:1024
	ds_read_b128 v[26:29], v139 offset:2048
	ds_read_b128 v[30:33], v139 offset:3072
	ds_read_b128 v[208:211], v140
	ds_read_b128 v[212:215], v140 offset:1024
	ds_read_b128 v[216:219], v140 offset:2048
	ds_read_b128 v[220:223], v140 offset:3072
	s_mov_b32 m0, s34
	ds_read_b128 v[50:53], v136 offset:32768
	ds_read_b128 v[54:57], v136 offset:33792
	ds_read_b128 v[224:227], v136 offset:34816
	ds_read_b128 v[228:231], v136 offset:35840
	ds_read_b128 v[238:241], v136 offset:36864
	ds_read_b128 v[244:247], v136 offset:37888
	ds_read_b128 v[250:253], v136 offset:38912
	ds_read_b128 v[66:69], v136 offset:39936
	buffer_load_dwordx4 v131, s[64:67], s63 offen lds
	s_mov_b32 m0, s40
	s_or_b32 s62, s41, 0x80100
	buffer_load_dwordx4 v133, s[64:67], s63 offen lds
	s_mov_b32 m0, s42
	s_nop 0
	buffer_load_dwordx4 v131, s[64:67], s62 offen lds
	s_mov_b32 m0, s43
	s_nop 0
	buffer_load_dwordx4 v133, s[64:67], s62 offen lds
	s_waitcnt vmcnt(8)
	s_waitcnt lgkmcnt(0)
	s_barrier
	s_setprio 1
	v_mfma_f32_16x16x32_bf16 v[58:61], v[18:21], v[50:53], v[118:121]
	v_mfma_f32_16x16x32_bf16 v[122:125], v[22:25], v[54:57], v[58:61]
	v_mfma_f32_16x16x32_bf16 v[58:61], v[26:29], v[50:53], v[70:73]
	v_mfma_f32_16x16x32_bf16 v[126:129], v[30:33], v[54:57], v[58:61]
	v_mfma_f32_16x16x32_bf16 v[58:61], v[18:21], v[224:227], v[74:77]
	v_mfma_f32_16x16x32_bf16 v[114:117], v[22:25], v[228:231], v[58:61]
	v_mfma_f32_16x16x32_bf16 v[58:61], v[26:29], v[224:227], v[78:81]
	v_mfma_f32_16x16x32_bf16 v[118:121], v[30:33], v[228:231], v[58:61]
	v_mfma_f32_16x16x32_bf16 v[58:61], v[18:21], v[238:241], v[82:85]
	v_mfma_f32_16x16x32_bf16 v[110:113], v[22:25], v[244:247], v[58:61]
	v_mfma_f32_16x16x32_bf16 v[58:61], v[26:29], v[238:241], v[86:89]
	v_mfma_f32_16x16x32_bf16 v[106:109], v[30:33], v[244:247], v[58:61]
	v_mfma_f32_16x16x32_bf16 v[58:61], v[18:21], v[250:253], v[90:93]
	v_mfma_f32_16x16x32_bf16 v[34:37], v[216:219], v[50:53], v[34:37]
	v_mfma_f32_16x16x32_bf16 v[98:101], v[22:25], v[66:69], v[58:61]
	v_mfma_f32_16x16x32_bf16 v[58:61], v[26:29], v[250:253], v[94:97]
	v_mfma_f32_16x16x32_bf16 v[62:65], v[220:223], v[54:57], v[34:37]
	v_mfma_f32_16x16x32_bf16 v[34:37], v[208:211], v[224:227], v[38:41]
	v_mfma_f32_16x16x32_bf16 v[102:105], v[30:33], v[66:69], v[58:61]
	v_mfma_f32_16x16x32_bf16 v[58:61], v[208:211], v[50:53], v[142:145]
	v_mfma_f32_16x16x32_bf16 v[50:53], v[212:215], v[228:231], v[34:37]
	v_mfma_f32_16x16x32_bf16 v[34:37], v[216:219], v[224:227], v[42:45]
	v_mfma_f32_16x16x32_bf16 v[58:61], v[212:215], v[54:57], v[58:61]
	v_mfma_f32_16x16x32_bf16 v[54:57], v[220:223], v[228:231], v[34:37]
	v_mfma_f32_16x16x32_bf16 v[34:37], v[208:211], v[238:241], v[46:49]
	v_mfma_f32_16x16x32_bf16 v[42:45], v[212:215], v[244:247], v[34:37]
	v_mfma_f32_16x16x32_bf16 v[34:37], v[216:219], v[238:241], v[146:149]
	v_mfma_f32_16x16x32_bf16 v[46:49], v[220:223], v[244:247], v[34:37]
	v_mfma_f32_16x16x32_bf16 v[34:37], v[208:211], v[250:253], v[150:153]
	v_mfma_f32_16x16x32_bf16 v[38:41], v[216:219], v[250:253], v[154:157]
	v_mfma_f32_16x16x32_bf16 v[34:37], v[212:215], v[66:69], v[34:37]
	v_mfma_f32_16x16x32_bf16 v[38:41], v[220:223], v[66:69], v[38:41]
	s_setprio 0
	s_barrier
	s_mov_b32 m0, s45
	s_or_b32 s62, s36, 0x180
	ds_read_b128 v[142:145], v136 offset:49152
	ds_read_b128 v[146:149], v136 offset:50176
	ds_read_b128 v[150:153], v136 offset:51200
	ds_read_b128 v[154:157], v136 offset:52224
	ds_read_b128 v[224:227], v136 offset:53248
	ds_read_b128 v[228:231], v136 offset:54272
	ds_read_b128 v[238:241], v136 offset:55296
	ds_read_b128 v[244:247], v136 offset:56320
	buffer_load_dwordx4 v132, s[0:3], s62 offen lds
	s_mov_b32 m0, s46
	s_nop 0
	buffer_load_dwordx4 v134, s[0:3], s62 offen lds
	s_or_b32 s62, s36, 0x80180
	s_mov_b32 m0, s47
	s_nop 0
	buffer_load_dwordx4 v132, s[0:3], s62 offen lds
	s_mov_b32 m0, s48
	s_nop 0
	buffer_load_dwordx4 v134, s[0:3], s62 offen lds
	s_waitcnt vmcnt(6)
	s_waitcnt lgkmcnt(0)
	s_barrier
	s_setprio 1
	v_mfma_f32_16x16x32_bf16 v[66:69], v[18:21], v[142:145], v[158:161]
	v_mfma_f32_16x16x32_bf16 v[90:93], v[22:25], v[146:149], v[66:69]
	v_mfma_f32_16x16x32_bf16 v[66:69], v[26:29], v[142:145], v[162:165]
	v_mfma_f32_16x16x32_bf16 v[94:97], v[30:33], v[146:149], v[66:69]
	v_mfma_f32_16x16x32_bf16 v[66:69], v[18:21], v[150:153], v[166:169]
	v_mfma_f32_16x16x32_bf16 v[82:85], v[22:25], v[154:157], v[66:69]
	v_mfma_f32_16x16x32_bf16 v[66:69], v[26:29], v[150:153], v[170:173]
	v_mfma_f32_16x16x32_bf16 v[86:89], v[30:33], v[154:157], v[66:69]
	v_mfma_f32_16x16x32_bf16 v[66:69], v[18:21], v[224:227], v[174:177]
	v_mfma_f32_16x16x32_bf16 v[74:77], v[22:25], v[228:231], v[66:69]
	v_mfma_f32_16x16x32_bf16 v[66:69], v[26:29], v[224:227], v[178:181]
	v_mfma_f32_16x16x32_bf16 v[2:5], v[18:21], v[238:241], v[2:5]
	v_mfma_f32_16x16x32_bf16 v[78:81], v[30:33], v[228:231], v[66:69]
	v_mfma_f32_16x16x32_bf16 v[66:69], v[22:25], v[244:247], v[2:5]
	v_mfma_f32_16x16x32_bf16 v[2:5], v[26:29], v[238:241], v[6:9]
	v_mfma_f32_16x16x32_bf16 v[70:73], v[30:33], v[244:247], v[2:5]
	v_mfma_f32_16x16x32_bf16 v[2:5], v[208:211], v[142:145], v[10:13]
	v_mfma_f32_16x16x32_bf16 v[26:29], v[212:215], v[146:149], v[2:5]
	v_mfma_f32_16x16x32_bf16 v[2:5], v[216:219], v[142:145], v[14:17]
	v_mfma_f32_16x16x32_bf16 v[30:33], v[220:223], v[146:149], v[2:5]
	v_mfma_f32_16x16x32_bf16 v[2:5], v[208:211], v[150:153], v[182:185]
	v_mfma_f32_16x16x32_bf16 v[18:21], v[212:215], v[154:157], v[2:5]
	v_mfma_f32_16x16x32_bf16 v[2:5], v[216:219], v[150:153], v[186:189]
	v_mfma_f32_16x16x32_bf16 v[22:25], v[220:223], v[154:157], v[2:5]
	v_mfma_f32_16x16x32_bf16 v[2:5], v[208:211], v[224:227], v[190:193]
	v_mfma_f32_16x16x32_bf16 v[10:13], v[212:215], v[228:231], v[2:5]
	v_mfma_f32_16x16x32_bf16 v[2:5], v[216:219], v[224:227], v[194:197]
	v_mfma_f32_16x16x32_bf16 v[14:17], v[220:223], v[228:231], v[2:5]
	v_mfma_f32_16x16x32_bf16 v[2:5], v[208:211], v[238:241], v[198:201]
	v_mfma_f32_16x16x32_bf16 v[6:9], v[216:219], v[238:241], v[204:207]
	v_mfma_f32_16x16x32_bf16 v[2:5], v[212:215], v[244:247], v[2:5]
	v_mfma_f32_16x16x32_bf16 v[6:9], v[220:223], v[244:247], v[6:9]
	s_setprio 0
	s_barrier
	s_mov_b32 s62, 0
	s_mov_b32 s63, 0
.LBB0_1797:
	ds_read_b128 v[142:145], v137
	ds_read_b128 v[146:149], v137 offset:1024
	ds_read_b128 v[150:153], v137 offset:2048
	ds_read_b128 v[154:157], v137 offset:3072
	ds_read_b128 v[158:161], v138
	ds_read_b128 v[162:165], v138 offset:1024
	ds_read_b128 v[166:169], v138 offset:2048
	ds_read_b128 v[170:173], v138 offset:3072
	s_add_i32 s73, s41, s62
	s_add_i32 s76, s73, 0x100
	s_add_i32 s77, s73, 0x200
	s_add_i32 s72, s59, s62
	s_cmpk_eq_i32 s62, 0xe00
	s_cselect_b32 s72, s61, s72
	s_cselect_b32 s77, s60, s77
	s_addk_i32 s73, 0x180
	s_mov_b32 m0, s49
	ds_read_b128 v[174:177], v136
	ds_read_b128 v[178:181], v136 offset:1024
	ds_read_b128 v[182:185], v136 offset:2048
	ds_read_b128 v[186:189], v136 offset:3072
	ds_read_b128 v[190:193], v136 offset:4096
	ds_read_b128 v[194:197], v136 offset:5120
	ds_read_b128 v[198:201], v136 offset:6144
	ds_read_b128 v[204:207], v136 offset:7168
	buffer_load_dwordx4 v131, s[64:67], s73 offen lds
	s_mov_b32 m0, s51
	s_nop 0
	buffer_load_dwordx4 v133, s[64:67], s73 offen lds
	s_or_b32 s73, s76, 0x80080
	s_mov_b32 m0, s50
	s_nop 0
	buffer_load_dwordx4 v131, s[64:67], s73 offen lds
	s_mov_b32 m0, s52
	s_nop 0
	buffer_load_dwordx4 v133, s[64:67], s73 offen lds
	s_waitcnt vmcnt(8)
	s_waitcnt lgkmcnt(0)
	s_barrier
	s_setprio 1
	v_mfma_f32_16x16x32_bf16 v[122:125], v[142:145], v[174:177], v[122:125]
	v_mfma_f32_16x16x32_bf16 v[126:129], v[150:153], v[174:177], v[126:129]
	v_mfma_f32_16x16x32_bf16 v[114:117], v[142:145], v[182:185], v[114:117]
	v_mfma_f32_16x16x32_bf16 v[118:121], v[150:153], v[182:185], v[118:121]
	v_mfma_f32_16x16x32_bf16 v[110:113], v[142:145], v[190:193], v[110:113]
	v_mfma_f32_16x16x32_bf16 v[106:109], v[150:153], v[190:193], v[106:109]
	v_mfma_f32_16x16x32_bf16 v[98:101], v[142:145], v[198:201], v[98:101]
	v_mfma_f32_16x16x32_bf16 v[102:105], v[150:153], v[198:201], v[102:105]
	v_mfma_f32_16x16x32_bf16 v[58:61], v[158:161], v[174:177], v[58:61]
	v_mfma_f32_16x16x32_bf16 v[62:65], v[166:169], v[174:177], v[62:65]
	v_mfma_f32_16x16x32_bf16 v[50:53], v[158:161], v[182:185], v[50:53]
	v_mfma_f32_16x16x32_bf16 v[54:57], v[166:169], v[182:185], v[54:57]
	v_mfma_f32_16x16x32_bf16 v[42:45], v[158:161], v[190:193], v[42:45]
	v_mfma_f32_16x16x32_bf16 v[46:49], v[166:169], v[190:193], v[46:49]
	v_mfma_f32_16x16x32_bf16 v[34:37], v[158:161], v[198:201], v[34:37]
	v_mfma_f32_16x16x32_bf16 v[38:41], v[166:169], v[198:201], v[38:41]
	v_mfma_f32_16x16x32_bf16 v[122:125], v[146:149], v[178:181], v[122:125]
	v_mfma_f32_16x16x32_bf16 v[126:129], v[154:157], v[178:181], v[126:129]
	v_mfma_f32_16x16x32_bf16 v[114:117], v[146:149], v[186:189], v[114:117]
	v_mfma_f32_16x16x32_bf16 v[118:121], v[154:157], v[186:189], v[118:121]
	v_mfma_f32_16x16x32_bf16 v[110:113], v[146:149], v[194:197], v[110:113]
	v_mfma_f32_16x16x32_bf16 v[106:109], v[154:157], v[194:197], v[106:109]
	v_mfma_f32_16x16x32_bf16 v[98:101], v[146:149], v[204:207], v[98:101]
	v_mfma_f32_16x16x32_bf16 v[102:105], v[154:157], v[204:207], v[102:105]
	v_mfma_f32_16x16x32_bf16 v[58:61], v[162:165], v[178:181], v[58:61]
	v_mfma_f32_16x16x32_bf16 v[62:65], v[170:173], v[178:181], v[62:65]
	v_mfma_f32_16x16x32_bf16 v[50:53], v[162:165], v[186:189], v[50:53]
	v_mfma_f32_16x16x32_bf16 v[54:57], v[170:173], v[186:189], v[54:57]
	v_mfma_f32_16x16x32_bf16 v[42:45], v[162:165], v[194:197], v[42:45]
	v_mfma_f32_16x16x32_bf16 v[46:49], v[170:173], v[194:197], v[46:49]
	v_mfma_f32_16x16x32_bf16 v[34:37], v[162:165], v[204:207], v[34:37]
	v_mfma_f32_16x16x32_bf16 v[38:41], v[170:173], v[204:207], v[38:41]
	s_setprio 0
	s_barrier
	s_mov_b32 m0, s35
	ds_read_b128 v[174:177], v136 offset:16384
	ds_read_b128 v[178:181], v136 offset:17408
	ds_read_b128 v[182:185], v136 offset:18432
	ds_read_b128 v[186:189], v136 offset:19456
	ds_read_b128 v[190:193], v136 offset:20480
	ds_read_b128 v[194:197], v136 offset:21504
	ds_read_b128 v[198:201], v136 offset:22528
	ds_read_b128 v[204:207], v136 offset:23552
	buffer_load_dwordx4 v132, s[0:3], s72 offen lds
	s_mov_b32 m0, s37
	s_or_b32 s73, s72, 0x80000
	buffer_load_dwordx4 v134, s[0:3], s72 offen lds
	s_mov_b32 m0, s38
	s_nop 0
	buffer_load_dwordx4 v132, s[0:3], s73 offen lds
	s_mov_b32 m0, s39
	s_nop 0
	buffer_load_dwordx4 v134, s[0:3], s73 offen lds
	s_waitcnt vmcnt(6)
	s_waitcnt lgkmcnt(0)
	s_barrier
	s_setprio 1
	v_mfma_f32_16x16x32_bf16 v[90:93], v[142:145], v[174:177], v[90:93]
	v_mfma_f32_16x16x32_bf16 v[94:97], v[150:153], v[174:177], v[94:97]
	v_mfma_f32_16x16x32_bf16 v[82:85], v[142:145], v[182:185], v[82:85]
	v_mfma_f32_16x16x32_bf16 v[86:89], v[150:153], v[182:185], v[86:89]
	v_mfma_f32_16x16x32_bf16 v[74:77], v[142:145], v[190:193], v[74:77]
	v_mfma_f32_16x16x32_bf16 v[78:81], v[150:153], v[190:193], v[78:81]
	v_mfma_f32_16x16x32_bf16 v[66:69], v[142:145], v[198:201], v[66:69]
	v_mfma_f32_16x16x32_bf16 v[70:73], v[150:153], v[198:201], v[70:73]
	v_mfma_f32_16x16x32_bf16 v[26:29], v[158:161], v[174:177], v[26:29]
	v_mfma_f32_16x16x32_bf16 v[30:33], v[166:169], v[174:177], v[30:33]
	v_mfma_f32_16x16x32_bf16 v[18:21], v[158:161], v[182:185], v[18:21]
	v_mfma_f32_16x16x32_bf16 v[22:25], v[166:169], v[182:185], v[22:25]
	v_mfma_f32_16x16x32_bf16 v[10:13], v[158:161], v[190:193], v[10:13]
	v_mfma_f32_16x16x32_bf16 v[14:17], v[166:169], v[190:193], v[14:17]
	v_mfma_f32_16x16x32_bf16 v[2:5], v[158:161], v[198:201], v[2:5]
	v_mfma_f32_16x16x32_bf16 v[6:9], v[166:169], v[198:201], v[6:9]
	v_mfma_f32_16x16x32_bf16 v[90:93], v[146:149], v[178:181], v[90:93]
	v_mfma_f32_16x16x32_bf16 v[94:97], v[154:157], v[178:181], v[94:97]
	v_mfma_f32_16x16x32_bf16 v[82:85], v[146:149], v[186:189], v[82:85]
	v_mfma_f32_16x16x32_bf16 v[86:89], v[154:157], v[186:189], v[86:89]
	v_mfma_f32_16x16x32_bf16 v[74:77], v[146:149], v[194:197], v[74:77]
	v_mfma_f32_16x16x32_bf16 v[78:81], v[154:157], v[194:197], v[78:81]
	v_mfma_f32_16x16x32_bf16 v[66:69], v[146:149], v[204:207], v[66:69]
	v_mfma_f32_16x16x32_bf16 v[70:73], v[154:157], v[204:207], v[70:73]
	v_mfma_f32_16x16x32_bf16 v[26:29], v[162:165], v[178:181], v[26:29]
	v_mfma_f32_16x16x32_bf16 v[30:33], v[170:173], v[178:181], v[30:33]
	v_mfma_f32_16x16x32_bf16 v[18:21], v[162:165], v[186:189], v[18:21]
	v_mfma_f32_16x16x32_bf16 v[22:25], v[170:173], v[186:189], v[22:25]
	v_mfma_f32_16x16x32_bf16 v[10:13], v[162:165], v[194:197], v[10:13]
	v_mfma_f32_16x16x32_bf16 v[14:17], v[170:173], v[194:197], v[14:17]
	v_mfma_f32_16x16x32_bf16 v[2:5], v[162:165], v[204:207], v[2:5]
	v_mfma_f32_16x16x32_bf16 v[6:9], v[170:173], v[204:207], v[6:9]
	s_setprio 0
	s_barrier
	ds_read_b128 v[142:145], v139
	ds_read_b128 v[146:149], v139 offset:1024
	ds_read_b128 v[150:153], v139 offset:2048
	ds_read_b128 v[154:157], v139 offset:3072
	ds_read_b128 v[158:161], v140
	ds_read_b128 v[162:165], v140 offset:1024
	ds_read_b128 v[166:169], v140 offset:2048
	ds_read_b128 v[170:173], v140 offset:3072
	s_mov_b32 m0, s34
	ds_read_b128 v[174:177], v136 offset:32768
	ds_read_b128 v[178:181], v136 offset:33792
	ds_read_b128 v[182:185], v136 offset:34816
	ds_read_b128 v[186:189], v136 offset:35840
	ds_read_b128 v[190:193], v136 offset:36864
	ds_read_b128 v[194:197], v136 offset:37888
	ds_read_b128 v[198:201], v136 offset:38912
	ds_read_b128 v[204:207], v136 offset:39936
	buffer_load_dwordx4 v131, s[64:67], s77 offen lds
	s_mov_b32 m0, s40
	s_nop 0
	buffer_load_dwordx4 v133, s[64:67], s77 offen lds
	s_bitset1_b32 s77, 19
	s_mov_b32 m0, s42
	s_nop 0
	buffer_load_dwordx4 v131, s[64:67], s77 offen lds
	s_mov_b32 m0, s43
	s_nop 0
	buffer_load_dwordx4 v133, s[64:67], s77 offen lds
	s_waitcnt vmcnt(8)
	s_waitcnt lgkmcnt(0)
	s_barrier
	s_setprio 1
	v_mfma_f32_16x16x32_bf16 v[122:125], v[142:145], v[174:177], v[122:125]
	v_mfma_f32_16x16x32_bf16 v[126:129], v[150:153], v[174:177], v[126:129]
	v_mfma_f32_16x16x32_bf16 v[114:117], v[142:145], v[182:185], v[114:117]
	v_mfma_f32_16x16x32_bf16 v[118:121], v[150:153], v[182:185], v[118:121]
	v_mfma_f32_16x16x32_bf16 v[110:113], v[142:145], v[190:193], v[110:113]
	v_mfma_f32_16x16x32_bf16 v[106:109], v[150:153], v[190:193], v[106:109]
	v_mfma_f32_16x16x32_bf16 v[98:101], v[142:145], v[198:201], v[98:101]
	v_mfma_f32_16x16x32_bf16 v[102:105], v[150:153], v[198:201], v[102:105]
	v_mfma_f32_16x16x32_bf16 v[58:61], v[158:161], v[174:177], v[58:61]
	v_mfma_f32_16x16x32_bf16 v[62:65], v[166:169], v[174:177], v[62:65]
	v_mfma_f32_16x16x32_bf16 v[50:53], v[158:161], v[182:185], v[50:53]
	v_mfma_f32_16x16x32_bf16 v[54:57], v[166:169], v[182:185], v[54:57]
	v_mfma_f32_16x16x32_bf16 v[42:45], v[158:161], v[190:193], v[42:45]
	v_mfma_f32_16x16x32_bf16 v[46:49], v[166:169], v[190:193], v[46:49]
	v_mfma_f32_16x16x32_bf16 v[34:37], v[158:161], v[198:201], v[34:37]
	v_mfma_f32_16x16x32_bf16 v[38:41], v[166:169], v[198:201], v[38:41]
	v_mfma_f32_16x16x32_bf16 v[122:125], v[146:149], v[178:181], v[122:125]
	v_mfma_f32_16x16x32_bf16 v[126:129], v[154:157], v[178:181], v[126:129]
	v_mfma_f32_16x16x32_bf16 v[114:117], v[146:149], v[186:189], v[114:117]
	v_mfma_f32_16x16x32_bf16 v[118:121], v[154:157], v[186:189], v[118:121]
	v_mfma_f32_16x16x32_bf16 v[110:113], v[146:149], v[194:197], v[110:113]
	v_mfma_f32_16x16x32_bf16 v[106:109], v[154:157], v[194:197], v[106:109]
	v_mfma_f32_16x16x32_bf16 v[98:101], v[146:149], v[204:207], v[98:101]
	v_mfma_f32_16x16x32_bf16 v[102:105], v[154:157], v[204:207], v[102:105]
	v_mfma_f32_16x16x32_bf16 v[58:61], v[162:165], v[178:181], v[58:61]
	v_mfma_f32_16x16x32_bf16 v[62:65], v[170:173], v[178:181], v[62:65]
	v_mfma_f32_16x16x32_bf16 v[50:53], v[162:165], v[186:189], v[50:53]
	v_mfma_f32_16x16x32_bf16 v[54:57], v[170:173], v[186:189], v[54:57]
	v_mfma_f32_16x16x32_bf16 v[42:45], v[162:165], v[194:197], v[42:45]
	v_mfma_f32_16x16x32_bf16 v[46:49], v[170:173], v[194:197], v[46:49]
	v_mfma_f32_16x16x32_bf16 v[34:37], v[162:165], v[204:207], v[34:37]
	v_mfma_f32_16x16x32_bf16 v[38:41], v[170:173], v[204:207], v[38:41]
	s_setprio 0
	s_barrier
	s_mov_b32 m0, s45
	s_or_b32 s73, s72, 0x80
	ds_read_b128 v[174:177], v136 offset:49152
	ds_read_b128 v[178:181], v136 offset:50176
	ds_read_b128 v[182:185], v136 offset:51200
	ds_read_b128 v[186:189], v136 offset:52224
	ds_read_b128 v[190:193], v136 offset:53248
	ds_read_b128 v[194:197], v136 offset:54272
	ds_read_b128 v[198:201], v136 offset:55296
	ds_read_b128 v[204:207], v136 offset:56320
	buffer_load_dwordx4 v132, s[0:3], s73 offen lds
	s_mov_b32 m0, s46
	s_or_b32 s72, s72, 0x80080
	buffer_load_dwordx4 v134, s[0:3], s73 offen lds
	s_mov_b32 m0, s47
	s_nop 0
	buffer_load_dwordx4 v132, s[0:3], s72 offen lds
	s_mov_b32 m0, s48
	s_nop 0
	buffer_load_dwordx4 v134, s[0:3], s72 offen lds
	s_waitcnt vmcnt(6)
	s_waitcnt lgkmcnt(0)
	s_barrier
	s_setprio 1
	v_mfma_f32_16x16x32_bf16 v[90:93], v[142:145], v[174:177], v[90:93]
	v_mfma_f32_16x16x32_bf16 v[94:97], v[150:153], v[174:177], v[94:97]
	v_mfma_f32_16x16x32_bf16 v[82:85], v[142:145], v[182:185], v[82:85]
	v_mfma_f32_16x16x32_bf16 v[86:89], v[150:153], v[182:185], v[86:89]
	v_mfma_f32_16x16x32_bf16 v[74:77], v[142:145], v[190:193], v[74:77]
	v_mfma_f32_16x16x32_bf16 v[78:81], v[150:153], v[190:193], v[78:81]
	v_mfma_f32_16x16x32_bf16 v[66:69], v[142:145], v[198:201], v[66:69]
	v_mfma_f32_16x16x32_bf16 v[70:73], v[150:153], v[198:201], v[70:73]
	v_mfma_f32_16x16x32_bf16 v[26:29], v[158:161], v[174:177], v[26:29]
	v_mfma_f32_16x16x32_bf16 v[30:33], v[166:169], v[174:177], v[30:33]
	v_mfma_f32_16x16x32_bf16 v[18:21], v[158:161], v[182:185], v[18:21]
	v_mfma_f32_16x16x32_bf16 v[22:25], v[166:169], v[182:185], v[22:25]
	v_mfma_f32_16x16x32_bf16 v[10:13], v[158:161], v[190:193], v[10:13]
	v_mfma_f32_16x16x32_bf16 v[14:17], v[166:169], v[190:193], v[14:17]
	v_mfma_f32_16x16x32_bf16 v[2:5], v[158:161], v[198:201], v[2:5]
	v_mfma_f32_16x16x32_bf16 v[6:9], v[166:169], v[198:201], v[6:9]
	v_mfma_f32_16x16x32_bf16 v[90:93], v[146:149], v[178:181], v[90:93]
	v_mfma_f32_16x16x32_bf16 v[94:97], v[154:157], v[178:181], v[94:97]
	v_mfma_f32_16x16x32_bf16 v[82:85], v[146:149], v[186:189], v[82:85]
	v_mfma_f32_16x16x32_bf16 v[86:89], v[154:157], v[186:189], v[86:89]
	v_mfma_f32_16x16x32_bf16 v[74:77], v[146:149], v[194:197], v[74:77]
	v_mfma_f32_16x16x32_bf16 v[78:81], v[154:157], v[194:197], v[78:81]
	v_mfma_f32_16x16x32_bf16 v[66:69], v[146:149], v[204:207], v[66:69]
	v_mfma_f32_16x16x32_bf16 v[70:73], v[154:157], v[204:207], v[70:73]
	v_mfma_f32_16x16x32_bf16 v[26:29], v[162:165], v[178:181], v[26:29]
	v_mfma_f32_16x16x32_bf16 v[30:33], v[170:173], v[178:181], v[30:33]
	v_mfma_f32_16x16x32_bf16 v[18:21], v[162:165], v[186:189], v[18:21]
	v_mfma_f32_16x16x32_bf16 v[22:25], v[170:173], v[186:189], v[22:25]
	v_mfma_f32_16x16x32_bf16 v[10:13], v[162:165], v[194:197], v[10:13]
	v_mfma_f32_16x16x32_bf16 v[14:17], v[170:173], v[194:197], v[14:17]
	v_mfma_f32_16x16x32_bf16 v[2:5], v[162:165], v[204:207], v[2:5]
	v_mfma_f32_16x16x32_bf16 v[6:9], v[170:173], v[204:207], v[6:9]
	s_setprio 0
	s_barrier
	s_add_i32 s63, s63, 2
	s_addk_i32 s62, 0x100
	s_cmp_gt_u32 s63, 29
	s_cbranch_scc0 .LBB0_1797
	s_and_b64 vcc, exec, s[22:23]
	s_cbranch_vccz .LBB0_1793
	s_mov_b32 s31, s54
	s_mov_b32 s18, s55
	s_mov_b32 s36, s58
	s_mov_b32 s41, s57
	s_mov_b32 s53, s56
	s_branch .LBB0_1793

.LBB0_1842:
	v_add_u32_e32 v137, 0x10000, v135
	v_add_u32_e32 v170, 0x14000, v135
	ds_read_b128 v[2:5], v137
	ds_read_b128 v[6:9], v137 offset:1024
	ds_read_b128 v[10:13], v137 offset:2048
	ds_read_b128 v[14:17], v137 offset:3072
	ds_read_b128 v[18:21], v170
	ds_read_b128 v[22:25], v170 offset:1024
	ds_read_b128 v[26:29], v170 offset:2048
	ds_read_b128 v[30:33], v170 offset:3072
	s_lshl_b32 s55, s53, 19
	s_lshl_b32 s56, s52, 19
	s_or_b32 s60, s39, 0x80
	s_or_b32 s61, s34, 0x100
	s_and_b64 s[6:7], s[20:21], exec
	s_cselect_b32 s57, s55, s39
	s_or_b32 s59, s39, 0x100
	s_and_b64 s[6:7], s[20:21], exec
	s_cselect_b32 s58, s56, s34
	s_mov_b32 m0, s47
	ds_read_b128 v[66:69], v136
	ds_read_b128 v[70:73], v136 offset:1024
	ds_read_b128 v[74:77], v136 offset:2048
	ds_read_b128 v[78:81], v136 offset:3072
	ds_read_b128 v[82:85], v136 offset:4096
	ds_read_b128 v[86:89], v136 offset:5120
	ds_read_b128 v[90:93], v136 offset:6144
	ds_read_b128 v[94:97], v136 offset:7168
	buffer_load_dwordx4 v131, s[64:67], s60 offen lds
	s_mov_b32 m0, s49
	s_or_b32 s6, s39, 0x40080
	buffer_load_dwordx4 v133, s[64:67], s60 offen lds
	s_mov_b32 m0, s48
	s_nop 0
	buffer_load_dwordx4 v131, s[64:67], s6 offen lds
	s_mov_b32 m0, s50
	s_nop 0
	buffer_load_dwordx4 v133, s[64:67], s6 offen lds
	s_waitcnt vmcnt(8)
	s_waitcnt lgkmcnt(0)
	s_barrier
	s_setprio 1
	v_mfma_scale_f32_16x16x128_f8f6f4 v[62:65], v[2:9], v[66:73], 0, v237, v237 op_sel_hi:[0,0,0]
	v_mfma_scale_f32_16x16x128_f8f6f4 v[118:121], v[10:17], v[66:73], 0, v237, v237 op_sel_hi:[0,0,0]
	v_mfma_scale_f32_16x16x128_f8f6f4 v[54:57], v[2:9], v[74:81], 0, v237, v237 op_sel_hi:[0,0,0]
	v_mfma_scale_f32_16x16x128_f8f6f4 v[50:53], v[10:17], v[74:81], 0, v237, v237 op_sel_hi:[0,0,0]
	v_mfma_scale_f32_16x16x128_f8f6f4 v[46:49], v[2:9], v[82:89], 0, v237, v237 op_sel_hi:[0,0,0]
	v_mfma_scale_f32_16x16x128_f8f6f4 v[42:45], v[10:17], v[82:89], 0, v237, v237 op_sel_hi:[0,0,0]
	v_mfma_scale_f32_16x16x128_f8f6f4 v[98:101], v[2:9], v[90:97], 0, v237, v237 op_sel_hi:[0,0,0]
	v_mfma_scale_f32_16x16x128_f8f6f4 v[34:37], v[10:17], v[90:97], 0, v237, v237 op_sel_hi:[0,0,0]
	v_mfma_scale_f32_16x16x128_f8f6f4 v[58:61], v[18:25], v[66:73], 0, v237, v237 op_sel_hi:[0,0,0]
	v_mfma_scale_f32_16x16x128_f8f6f4 v[114:117], v[26:33], v[66:73], 0, v237, v237 op_sel_hi:[0,0,0]
	v_mfma_scale_f32_16x16x128_f8f6f4 v[110:113], v[18:25], v[74:81], 0, v237, v237 op_sel_hi:[0,0,0]
	v_mfma_scale_f32_16x16x128_f8f6f4 v[106:109], v[26:33], v[74:81], 0, v237, v237 op_sel_hi:[0,0,0]
	v_mfma_scale_f32_16x16x128_f8f6f4 v[166:169], v[18:25], v[82:89], 0, v237, v237 op_sel_hi:[0,0,0]
	v_mfma_scale_f32_16x16x128_f8f6f4 v[102:105], v[26:33], v[82:89], 0, v237, v237 op_sel_hi:[0,0,0]
	v_mfma_scale_f32_16x16x128_f8f6f4 v[158:161], v[18:25], v[90:97], 0, v237, v237 op_sel_hi:[0,0,0]
	v_mfma_scale_f32_16x16x128_f8f6f4 v[38:41], v[26:33], v[90:97], 0, v237, v237 op_sel_hi:[0,0,0]
	s_setprio 0
	s_barrier
	s_mov_b32 m0, s31
	s_mov_b32 s6, s66
	s_mov_b32 s7, s67
	ds_read_b128 v[122:125], v136 offset:16384
	ds_read_b128 v[126:129], v136 offset:17408
	ds_read_b128 v[138:141], v136 offset:18432
	ds_read_b128 v[142:145], v136 offset:19456
	ds_read_b128 v[172:175], v136 offset:20480
	ds_read_b128 v[176:179], v136 offset:21504
	ds_read_b128 v[180:183], v136 offset:22528
	ds_read_b128 v[184:187], v136 offset:23552
	buffer_load_dwordx4 v132, s[4:7], s61 offen lds
	s_mov_b32 m0, s35
	s_or_b32 s60, s34, 0x40100
	buffer_load_dwordx4 v134, s[4:7], s61 offen lds
	s_mov_b32 m0, s36
	s_nop 0
	buffer_load_dwordx4 v132, s[4:7], s60 offen lds
	s_mov_b32 m0, s37
	s_nop 0
	buffer_load_dwordx4 v134, s[4:7], s60 offen lds
	s_waitcnt vmcnt(6)
	s_waitcnt lgkmcnt(0)
	s_barrier
	s_setprio 1
	v_mfma_scale_f32_16x16x128_f8f6f4 v[90:93], v[2:9], v[122:129], 0, v237, v237 op_sel_hi:[0,0,0]
	v_mfma_scale_f32_16x16x128_f8f6f4 v[94:97], v[10:17], v[122:129], 0, v237, v237 op_sel_hi:[0,0,0]
	v_mfma_scale_f32_16x16x128_f8f6f4 v[82:85], v[2:9], v[138:145], 0, v237, v237 op_sel_hi:[0,0,0]
	v_mfma_scale_f32_16x16x128_f8f6f4 v[86:89], v[10:17], v[138:145], 0, v237, v237 op_sel_hi:[0,0,0]
	v_mfma_scale_f32_16x16x128_f8f6f4 v[74:77], v[2:9], v[172:179], 0, v237, v237 op_sel_hi:[0,0,0]
	v_mfma_scale_f32_16x16x128_f8f6f4 v[78:81], v[10:17], v[172:179], 0, v237, v237 op_sel_hi:[0,0,0]
	v_mfma_scale_f32_16x16x128_f8f6f4 v[66:69], v[2:9], v[180:187], 0, v237, v237 op_sel_hi:[0,0,0]
	v_mfma_scale_f32_16x16x128_f8f6f4 v[70:73], v[10:17], v[180:187], 0, v237, v237 op_sel_hi:[0,0,0]
	v_mfma_scale_f32_16x16x128_f8f6f4 v[162:165], v[18:25], v[122:129], 0, v237, v237 op_sel_hi:[0,0,0]
	v_mfma_scale_f32_16x16x128_f8f6f4 v[154:157], v[26:33], v[122:129], 0, v237, v237 op_sel_hi:[0,0,0]
	v_mfma_scale_f32_16x16x128_f8f6f4 v[150:153], v[18:25], v[138:145], 0, v237, v237 op_sel_hi:[0,0,0]
	v_mfma_scale_f32_16x16x128_f8f6f4 v[146:149], v[26:33], v[138:145], 0, v237, v237 op_sel_hi:[0,0,0]
	v_mfma_scale_f32_16x16x128_f8f6f4 v[142:145], v[18:25], v[172:179], 0, v237, v237 op_sel_hi:[0,0,0]
	v_mfma_scale_f32_16x16x128_f8f6f4 v[138:141], v[26:33], v[172:179], 0, v237, v237 op_sel_hi:[0,0,0]
	v_mfma_scale_f32_16x16x128_f8f6f4 v[126:129], v[18:25], v[180:187], 0, v237, v237 op_sel_hi:[0,0,0]
	v_mfma_scale_f32_16x16x128_f8f6f4 v[122:125], v[26:33], v[180:187], 0, v237, v237 op_sel_hi:[0,0,0]
	s_setprio 0
	s_barrier
	v_add_u32_e32 v171, 0x18000, v135
	v_add_u32_e32 v172, 0x1c000, v135
	ds_read_b128 v[26:29], v171
	ds_read_b128 v[30:33], v171 offset:1024
	ds_read_b128 v[18:21], v171 offset:2048
	ds_read_b128 v[22:25], v171 offset:3072
	ds_read_b128 v[10:13], v172
	ds_read_b128 v[14:17], v172 offset:1024
	ds_read_b128 v[2:5], v172 offset:2048
	ds_read_b128 v[6:9], v172 offset:3072
	s_mov_b32 m0, s30
	ds_read_b128 v[174:177], v136 offset:32768
	ds_read_b128 v[178:181], v136 offset:33792
	ds_read_b128 v[182:185], v136 offset:34816
	ds_read_b128 v[186:189], v136 offset:35840
	ds_read_b128 v[190:193], v136 offset:36864
	ds_read_b128 v[194:197], v136 offset:37888
	ds_read_b128 v[204:207], v136 offset:38912
	ds_read_b128 v[208:211], v136 offset:39936
	buffer_load_dwordx4 v131, s[64:67], s59 offen lds
	s_mov_b32 m0, s38
	s_nop 0
	buffer_load_dwordx4 v133, s[64:67], s59 offen lds
	s_or_b32 s59, s39, 0x40100
	s_mov_b32 m0, s40
	s_nop 0
	buffer_load_dwordx4 v131, s[64:67], s59 offen lds
	s_mov_b32 m0, s41
	s_nop 0
	buffer_load_dwordx4 v133, s[64:67], s59 offen lds
	s_waitcnt vmcnt(8)
	s_waitcnt lgkmcnt(0)
	s_barrier
	s_setprio 1
	v_mfma_scale_f32_16x16x128_f8f6f4 v[62:65], v[26:33], v[174:181], v[62:65], v237, v237 op_sel_hi:[0,0,0]
	v_mfma_scale_f32_16x16x128_f8f6f4 v[118:121], v[18:25], v[174:181], v[118:121], v237, v237 op_sel_hi:[0,0,0]
	v_mfma_scale_f32_16x16x128_f8f6f4 v[54:57], v[26:33], v[182:189], v[54:57], v237, v237 op_sel_hi:[0,0,0]
	v_mfma_scale_f32_16x16x128_f8f6f4 v[50:53], v[18:25], v[182:189], v[50:53], v237, v237 op_sel_hi:[0,0,0]
	v_mfma_scale_f32_16x16x128_f8f6f4 v[46:49], v[26:33], v[190:197], v[46:49], v237, v237 op_sel_hi:[0,0,0]
	v_mfma_scale_f32_16x16x128_f8f6f4 v[42:45], v[18:25], v[190:197], v[42:45], v237, v237 op_sel_hi:[0,0,0]
	v_mfma_scale_f32_16x16x128_f8f6f4 v[98:101], v[26:33], v[204:211], v[98:101], v237, v237 op_sel_hi:[0,0,0]
	v_mfma_scale_f32_16x16x128_f8f6f4 v[34:37], v[18:25], v[204:211], v[34:37], v237, v237 op_sel_hi:[0,0,0]
	v_mfma_scale_f32_16x16x128_f8f6f4 v[58:61], v[10:17], v[174:181], v[58:61], v237, v237 op_sel_hi:[0,0,0]
	v_mfma_scale_f32_16x16x128_f8f6f4 v[114:117], v[2:9], v[174:181], v[114:117], v237, v237 op_sel_hi:[0,0,0]
	v_mfma_scale_f32_16x16x128_f8f6f4 v[110:113], v[10:17], v[182:189], v[110:113], v237, v237 op_sel_hi:[0,0,0]
	v_mfma_scale_f32_16x16x128_f8f6f4 v[106:109], v[2:9], v[182:189], v[106:109], v237, v237 op_sel_hi:[0,0,0]
	v_mfma_scale_f32_16x16x128_f8f6f4 v[166:169], v[10:17], v[190:197], v[166:169], v237, v237 op_sel_hi:[0,0,0]
	v_mfma_scale_f32_16x16x128_f8f6f4 v[102:105], v[2:9], v[190:197], v[102:105], v237, v237 op_sel_hi:[0,0,0]
	v_mfma_scale_f32_16x16x128_f8f6f4 v[158:161], v[10:17], v[204:211], v[158:161], v237, v237 op_sel_hi:[0,0,0]
	v_mfma_scale_f32_16x16x128_f8f6f4 v[38:41], v[2:9], v[204:211], v[38:41], v237, v237 op_sel_hi:[0,0,0]
	s_setprio 0
	s_barrier
	s_mov_b32 m0, s43
	s_or_b32 s59, s34, 0x180
	ds_read_b128 v[174:177], v136 offset:49152
	ds_read_b128 v[178:181], v136 offset:50176
	ds_read_b128 v[182:185], v136 offset:51200
	ds_read_b128 v[186:189], v136 offset:52224
	ds_read_b128 v[190:193], v136 offset:53248
	ds_read_b128 v[194:197], v136 offset:54272
	ds_read_b128 v[204:207], v136 offset:55296
	ds_read_b128 v[208:211], v136 offset:56320
	buffer_load_dwordx4 v132, s[4:7], s59 offen lds
	s_mov_b32 m0, s44
	s_nop 0
	buffer_load_dwordx4 v134, s[4:7], s59 offen lds
	s_or_b32 s59, s34, 0x40180
	s_mov_b32 m0, s45
	s_nop 0
	buffer_load_dwordx4 v132, s[4:7], s59 offen lds
	s_mov_b32 m0, s46
	s_nop 0
	buffer_load_dwordx4 v134, s[4:7], s59 offen lds
	s_waitcnt vmcnt(6)
	s_waitcnt lgkmcnt(0)
	s_barrier
	s_setprio 1
	v_mfma_scale_f32_16x16x128_f8f6f4 v[90:93], v[26:33], v[174:181], v[90:93], v237, v237 op_sel_hi:[0,0,0]
	v_mfma_scale_f32_16x16x128_f8f6f4 v[94:97], v[18:25], v[174:181], v[94:97], v237, v237 op_sel_hi:[0,0,0]
	v_mfma_scale_f32_16x16x128_f8f6f4 v[82:85], v[26:33], v[182:189], v[82:85], v237, v237 op_sel_hi:[0,0,0]
	v_mfma_scale_f32_16x16x128_f8f6f4 v[86:89], v[18:25], v[182:189], v[86:89], v237, v237 op_sel_hi:[0,0,0]
	v_mfma_scale_f32_16x16x128_f8f6f4 v[74:77], v[26:33], v[190:197], v[74:77], v237, v237 op_sel_hi:[0,0,0]
	v_mfma_scale_f32_16x16x128_f8f6f4 v[78:81], v[18:25], v[190:197], v[78:81], v237, v237 op_sel_hi:[0,0,0]
	v_mfma_scale_f32_16x16x128_f8f6f4 v[66:69], v[26:33], v[204:211], v[66:69], v237, v237 op_sel_hi:[0,0,0]
	v_mfma_scale_f32_16x16x128_f8f6f4 v[70:73], v[18:25], v[204:211], v[70:73], v237, v237 op_sel_hi:[0,0,0]
	v_mfma_scale_f32_16x16x128_f8f6f4 v[162:165], v[10:17], v[174:181], v[162:165], v237, v237 op_sel_hi:[0,0,0]
	v_mfma_scale_f32_16x16x128_f8f6f4 v[154:157], v[2:9], v[174:181], v[154:157], v237, v237 op_sel_hi:[0,0,0]
	v_mfma_scale_f32_16x16x128_f8f6f4 v[150:153], v[10:17], v[182:189], v[150:153], v237, v237 op_sel_hi:[0,0,0]
	v_mfma_scale_f32_16x16x128_f8f6f4 v[146:149], v[2:9], v[182:189], v[146:149], v237, v237 op_sel_hi:[0,0,0]
	v_mfma_scale_f32_16x16x128_f8f6f4 v[142:145], v[10:17], v[190:197], v[142:145], v237, v237 op_sel_hi:[0,0,0]
	v_mfma_scale_f32_16x16x128_f8f6f4 v[138:141], v[2:9], v[190:197], v[138:141], v237, v237 op_sel_hi:[0,0,0]
	v_mfma_scale_f32_16x16x128_f8f6f4 v[126:129], v[10:17], v[204:211], v[126:129], v237, v237 op_sel_hi:[0,0,0]
	v_mfma_scale_f32_16x16x128_f8f6f4 v[122:125], v[2:9], v[204:211], v[122:125], v237, v237 op_sel_hi:[0,0,0]
	s_setprio 0
	s_barrier
	s_mov_b32 s59, 0
	s_movk_i32 s60, 0xfa00
.LBB0_1843:
	ds_read_b128 v[2:5], v137
	ds_read_b128 v[6:9], v137 offset:1024
	ds_read_b128 v[10:13], v137 offset:2048
	ds_read_b128 v[14:17], v137 offset:3072
	ds_read_b128 v[18:21], v170
	ds_read_b128 v[22:25], v170 offset:1024
	ds_read_b128 v[26:29], v170 offset:2048
	ds_read_b128 v[30:33], v170 offset:3072
	s_add_i32 s63, s39, s60
	s_add_i32 s61, s34, s60
	s_add_i32 s62, s63, 0x800
	s_addk_i32 s61, 0x800
	s_cmp_eq_u32 s60, 0
	s_cselect_b32 s61, s58, s61
	s_cselect_b32 s62, s57, s62
	s_add_i32 s72, s63, 0x780
	s_mov_b32 m0, s47
	ds_read_b128 v[174:177], v136
	ds_read_b128 v[178:181], v136 offset:1024
	ds_read_b128 v[182:185], v136 offset:2048
	ds_read_b128 v[186:189], v136 offset:3072
	ds_read_b128 v[190:193], v136 offset:4096
	ds_read_b128 v[194:197], v136 offset:5120
	ds_read_b128 v[204:207], v136 offset:6144
	ds_read_b128 v[208:211], v136 offset:7168
	buffer_load_dwordx4 v131, s[64:67], s72 offen lds
	s_mov_b32 m0, s49
	s_add_i32 s63, s63, 0x40780
	buffer_load_dwordx4 v133, s[64:67], s72 offen lds
	s_mov_b32 m0, s48
	s_nop 0
	buffer_load_dwordx4 v131, s[64:67], s63 offen lds
	s_mov_b32 m0, s50
	s_nop 0
	buffer_load_dwordx4 v133, s[64:67], s63 offen lds
	s_waitcnt vmcnt(8)
	s_waitcnt lgkmcnt(0)
	s_barrier
	s_setprio 1
	v_mfma_scale_f32_16x16x128_f8f6f4 v[62:65], v[2:9], v[174:181], v[62:65], v237, v237 op_sel_hi:[0,0,0]
	v_mfma_scale_f32_16x16x128_f8f6f4 v[118:121], v[10:17], v[174:181], v[118:121], v237, v237 op_sel_hi:[0,0,0]
	v_mfma_scale_f32_16x16x128_f8f6f4 v[54:57], v[2:9], v[182:189], v[54:57], v237, v237 op_sel_hi:[0,0,0]
	v_mfma_scale_f32_16x16x128_f8f6f4 v[50:53], v[10:17], v[182:189], v[50:53], v237, v237 op_sel_hi:[0,0,0]
	v_mfma_scale_f32_16x16x128_f8f6f4 v[46:49], v[2:9], v[190:197], v[46:49], v237, v237 op_sel_hi:[0,0,0]
	v_mfma_scale_f32_16x16x128_f8f6f4 v[42:45], v[10:17], v[190:197], v[42:45], v237, v237 op_sel_hi:[0,0,0]
	v_mfma_scale_f32_16x16x128_f8f6f4 v[98:101], v[2:9], v[204:211], v[98:101], v237, v237 op_sel_hi:[0,0,0]
	v_mfma_scale_f32_16x16x128_f8f6f4 v[34:37], v[10:17], v[204:211], v[34:37], v237, v237 op_sel_hi:[0,0,0]
	v_mfma_scale_f32_16x16x128_f8f6f4 v[58:61], v[18:25], v[174:181], v[58:61], v237, v237 op_sel_hi:[0,0,0]
	v_mfma_scale_f32_16x16x128_f8f6f4 v[114:117], v[26:33], v[174:181], v[114:117], v237, v237 op_sel_hi:[0,0,0]
	v_mfma_scale_f32_16x16x128_f8f6f4 v[110:113], v[18:25], v[182:189], v[110:113], v237, v237 op_sel_hi:[0,0,0]
	v_mfma_scale_f32_16x16x128_f8f6f4 v[106:109], v[26:33], v[182:189], v[106:109], v237, v237 op_sel_hi:[0,0,0]
	v_mfma_scale_f32_16x16x128_f8f6f4 v[166:169], v[18:25], v[190:197], v[166:169], v237, v237 op_sel_hi:[0,0,0]
	v_mfma_scale_f32_16x16x128_f8f6f4 v[102:105], v[26:33], v[190:197], v[102:105], v237, v237 op_sel_hi:[0,0,0]
	v_mfma_scale_f32_16x16x128_f8f6f4 v[158:161], v[18:25], v[204:211], v[158:161], v237, v237 op_sel_hi:[0,0,0]
	v_mfma_scale_f32_16x16x128_f8f6f4 v[38:41], v[26:33], v[204:211], v[38:41], v237, v237 op_sel_hi:[0,0,0]
	s_setprio 0
	s_barrier
	s_mov_b32 m0, s31
	ds_read_b128 v[174:177], v136 offset:16384
	ds_read_b128 v[178:181], v136 offset:17408
	ds_read_b128 v[182:185], v136 offset:18432
	ds_read_b128 v[186:189], v136 offset:19456
	ds_read_b128 v[190:193], v136 offset:20480
	ds_read_b128 v[194:197], v136 offset:21504
	ds_read_b128 v[204:207], v136 offset:22528
	ds_read_b128 v[208:211], v136 offset:23552
	buffer_load_dwordx4 v132, s[4:7], s61 offen lds
	s_mov_b32 m0, s35
	s_add_i32 s63, s61, 0x40000
	buffer_load_dwordx4 v134, s[4:7], s61 offen lds
	s_mov_b32 m0, s36
	s_nop 0
	buffer_load_dwordx4 v132, s[4:7], s63 offen lds
	s_mov_b32 m0, s37
	s_nop 0
	buffer_load_dwordx4 v134, s[4:7], s63 offen lds
	s_waitcnt vmcnt(6)
	s_waitcnt lgkmcnt(0)
	s_barrier
	s_setprio 1
	v_mfma_scale_f32_16x16x128_f8f6f4 v[90:93], v[2:9], v[174:181], v[90:93], v237, v237 op_sel_hi:[0,0,0]
	v_mfma_scale_f32_16x16x128_f8f6f4 v[94:97], v[10:17], v[174:181], v[94:97], v237, v237 op_sel_hi:[0,0,0]
	v_mfma_scale_f32_16x16x128_f8f6f4 v[82:85], v[2:9], v[182:189], v[82:85], v237, v237 op_sel_hi:[0,0,0]
	v_mfma_scale_f32_16x16x128_f8f6f4 v[86:89], v[10:17], v[182:189], v[86:89], v237, v237 op_sel_hi:[0,0,0]
	v_mfma_scale_f32_16x16x128_f8f6f4 v[74:77], v[2:9], v[190:197], v[74:77], v237, v237 op_sel_hi:[0,0,0]
	v_mfma_scale_f32_16x16x128_f8f6f4 v[78:81], v[10:17], v[190:197], v[78:81], v237, v237 op_sel_hi:[0,0,0]
	v_mfma_scale_f32_16x16x128_f8f6f4 v[66:69], v[2:9], v[204:211], v[66:69], v237, v237 op_sel_hi:[0,0,0]
	v_mfma_scale_f32_16x16x128_f8f6f4 v[70:73], v[10:17], v[204:211], v[70:73], v237, v237 op_sel_hi:[0,0,0]
	v_mfma_scale_f32_16x16x128_f8f6f4 v[162:165], v[18:25], v[174:181], v[162:165], v237, v237 op_sel_hi:[0,0,0]
	v_mfma_scale_f32_16x16x128_f8f6f4 v[154:157], v[26:33], v[174:181], v[154:157], v237, v237 op_sel_hi:[0,0,0]
	v_mfma_scale_f32_16x16x128_f8f6f4 v[150:153], v[18:25], v[182:189], v[150:153], v237, v237 op_sel_hi:[0,0,0]
	v_mfma_scale_f32_16x16x128_f8f6f4 v[146:149], v[26:33], v[182:189], v[146:149], v237, v237 op_sel_hi:[0,0,0]
	v_mfma_scale_f32_16x16x128_f8f6f4 v[142:145], v[18:25], v[190:197], v[142:145], v237, v237 op_sel_hi:[0,0,0]
	v_mfma_scale_f32_16x16x128_f8f6f4 v[138:141], v[26:33], v[190:197], v[138:141], v237, v237 op_sel_hi:[0,0,0]
	v_mfma_scale_f32_16x16x128_f8f6f4 v[126:129], v[18:25], v[204:211], v[126:129], v237, v237 op_sel_hi:[0,0,0]
	v_mfma_scale_f32_16x16x128_f8f6f4 v[122:125], v[26:33], v[204:211], v[122:125], v237, v237 op_sel_hi:[0,0,0]
	s_setprio 0
	s_barrier
	ds_read_b128 v[18:21], v171
	ds_read_b128 v[22:25], v171 offset:1024
	ds_read_b128 v[26:29], v171 offset:2048
	ds_read_b128 v[30:33], v171 offset:3072
	ds_read_b128 v[10:13], v172
	ds_read_b128 v[14:17], v172 offset:1024
	ds_read_b128 v[2:5], v172 offset:2048
	ds_read_b128 v[6:9], v172 offset:3072
	s_mov_b32 m0, s30
	ds_read_b128 v[174:177], v136 offset:32768
	ds_read_b128 v[178:181], v136 offset:33792
	ds_read_b128 v[182:185], v136 offset:34816
	ds_read_b128 v[186:189], v136 offset:35840
	ds_read_b128 v[190:193], v136 offset:36864
	ds_read_b128 v[194:197], v136 offset:37888
	ds_read_b128 v[204:207], v136 offset:38912
	ds_read_b128 v[208:211], v136 offset:39936
	buffer_load_dwordx4 v131, s[64:67], s62 offen lds
	s_mov_b32 m0, s38
	s_nop 0
	buffer_load_dwordx4 v133, s[64:67], s62 offen lds
	s_add_i32 s62, s62, 0x40000
	s_mov_b32 m0, s40
	s_nop 0
	buffer_load_dwordx4 v131, s[64:67], s62 offen lds
	s_mov_b32 m0, s41
	s_nop 0
	buffer_load_dwordx4 v133, s[64:67], s62 offen lds
	s_waitcnt vmcnt(8)
	s_waitcnt lgkmcnt(0)
	s_barrier
	s_setprio 1
	v_mfma_scale_f32_16x16x128_f8f6f4 v[62:65], v[18:25], v[174:181], v[62:65], v237, v237 op_sel_hi:[0,0,0]
	v_mfma_scale_f32_16x16x128_f8f6f4 v[118:121], v[26:33], v[174:181], v[118:121], v237, v237 op_sel_hi:[0,0,0]
	v_mfma_scale_f32_16x16x128_f8f6f4 v[54:57], v[18:25], v[182:189], v[54:57], v237, v237 op_sel_hi:[0,0,0]
	v_mfma_scale_f32_16x16x128_f8f6f4 v[50:53], v[26:33], v[182:189], v[50:53], v237, v237 op_sel_hi:[0,0,0]
	v_mfma_scale_f32_16x16x128_f8f6f4 v[46:49], v[18:25], v[190:197], v[46:49], v237, v237 op_sel_hi:[0,0,0]
	v_mfma_scale_f32_16x16x128_f8f6f4 v[42:45], v[26:33], v[190:197], v[42:45], v237, v237 op_sel_hi:[0,0,0]
	v_mfma_scale_f32_16x16x128_f8f6f4 v[98:101], v[18:25], v[204:211], v[98:101], v237, v237 op_sel_hi:[0,0,0]
	v_mfma_scale_f32_16x16x128_f8f6f4 v[34:37], v[26:33], v[204:211], v[34:37], v237, v237 op_sel_hi:[0,0,0]
	v_mfma_scale_f32_16x16x128_f8f6f4 v[58:61], v[10:17], v[174:181], v[58:61], v237, v237 op_sel_hi:[0,0,0]
	v_mfma_scale_f32_16x16x128_f8f6f4 v[114:117], v[2:9], v[174:181], v[114:117], v237, v237 op_sel_hi:[0,0,0]
	v_mfma_scale_f32_16x16x128_f8f6f4 v[110:113], v[10:17], v[182:189], v[110:113], v237, v237 op_sel_hi:[0,0,0]
	v_mfma_scale_f32_16x16x128_f8f6f4 v[106:109], v[2:9], v[182:189], v[106:109], v237, v237 op_sel_hi:[0,0,0]
	v_mfma_scale_f32_16x16x128_f8f6f4 v[166:169], v[10:17], v[190:197], v[166:169], v237, v237 op_sel_hi:[0,0,0]
	v_mfma_scale_f32_16x16x128_f8f6f4 v[102:105], v[2:9], v[190:197], v[102:105], v237, v237 op_sel_hi:[0,0,0]
	v_mfma_scale_f32_16x16x128_f8f6f4 v[158:161], v[10:17], v[204:211], v[158:161], v237, v237 op_sel_hi:[0,0,0]
	v_mfma_scale_f32_16x16x128_f8f6f4 v[38:41], v[2:9], v[204:211], v[38:41], v237, v237 op_sel_hi:[0,0,0]
	s_setprio 0
	s_barrier
	s_mov_b32 m0, s43
	s_or_b32 s62, s61, 0x80
	ds_read_b128 v[174:177], v136 offset:49152
	ds_read_b128 v[178:181], v136 offset:50176
	ds_read_b128 v[182:185], v136 offset:51200
	ds_read_b128 v[186:189], v136 offset:52224
	ds_read_b128 v[190:193], v136 offset:53248
	ds_read_b128 v[194:197], v136 offset:54272
	ds_read_b128 v[204:207], v136 offset:55296
	ds_read_b128 v[208:211], v136 offset:56320
	buffer_load_dwordx4 v132, s[4:7], s62 offen lds
	s_mov_b32 m0, s44
	s_add_i32 s61, s61, 0x40080
	buffer_load_dwordx4 v134, s[4:7], s62 offen lds
	s_mov_b32 m0, s45
	s_nop 0
	buffer_load_dwordx4 v132, s[4:7], s61 offen lds
	s_mov_b32 m0, s46
	s_nop 0
	buffer_load_dwordx4 v134, s[4:7], s61 offen lds
	s_waitcnt vmcnt(6)
	s_waitcnt lgkmcnt(0)
	s_barrier
	s_setprio 1
	v_mfma_scale_f32_16x16x128_f8f6f4 v[90:93], v[18:25], v[174:181], v[90:93], v237, v237 op_sel_hi:[0,0,0]
	v_mfma_scale_f32_16x16x128_f8f6f4 v[94:97], v[26:33], v[174:181], v[94:97], v237, v237 op_sel_hi:[0,0,0]
	v_mfma_scale_f32_16x16x128_f8f6f4 v[82:85], v[18:25], v[182:189], v[82:85], v237, v237 op_sel_hi:[0,0,0]
	v_mfma_scale_f32_16x16x128_f8f6f4 v[86:89], v[26:33], v[182:189], v[86:89], v237, v237 op_sel_hi:[0,0,0]
	v_mfma_scale_f32_16x16x128_f8f6f4 v[74:77], v[18:25], v[190:197], v[74:77], v237, v237 op_sel_hi:[0,0,0]
	v_mfma_scale_f32_16x16x128_f8f6f4 v[78:81], v[26:33], v[190:197], v[78:81], v237, v237 op_sel_hi:[0,0,0]
	v_mfma_scale_f32_16x16x128_f8f6f4 v[66:69], v[18:25], v[204:211], v[66:69], v237, v237 op_sel_hi:[0,0,0]
	v_mfma_scale_f32_16x16x128_f8f6f4 v[70:73], v[26:33], v[204:211], v[70:73], v237, v237 op_sel_hi:[0,0,0]
	v_mfma_scale_f32_16x16x128_f8f6f4 v[162:165], v[10:17], v[174:181], v[162:165], v237, v237 op_sel_hi:[0,0,0]
	v_mfma_scale_f32_16x16x128_f8f6f4 v[154:157], v[2:9], v[174:181], v[154:157], v237, v237 op_sel_hi:[0,0,0]
	v_mfma_scale_f32_16x16x128_f8f6f4 v[150:153], v[10:17], v[182:189], v[150:153], v237, v237 op_sel_hi:[0,0,0]
	v_mfma_scale_f32_16x16x128_f8f6f4 v[146:149], v[2:9], v[182:189], v[146:149], v237, v237 op_sel_hi:[0,0,0]
	v_mfma_scale_f32_16x16x128_f8f6f4 v[142:145], v[10:17], v[190:197], v[142:145], v237, v237 op_sel_hi:[0,0,0]
	v_mfma_scale_f32_16x16x128_f8f6f4 v[138:141], v[2:9], v[190:197], v[138:141], v237, v237 op_sel_hi:[0,0,0]
	v_mfma_scale_f32_16x16x128_f8f6f4 v[126:129], v[10:17], v[204:211], v[126:129], v237, v237 op_sel_hi:[0,0,0]
	v_mfma_scale_f32_16x16x128_f8f6f4 v[122:125], v[2:9], v[204:211], v[122:125], v237, v237 op_sel_hi:[0,0,0]
	s_setprio 0
	s_barrier
	s_add_i32 s59, s59, 2
	s_addk_i32 s60, 0x100
	s_cmp_gt_u32 s59, 13
	s_cbranch_scc0 .LBB0_1843
	s_nop 15
	s_nop 15
	s_and_b64 vcc, exec, s[20:21]
	s_cbranch_vccz .LBB0_1839
	s_mov_b32 s29, s52
	s_mov_b32 s0, s53
	s_mov_b32 s34, s56
	s_mov_b32 s39, s55
	s_mov_b32 s51, s54
	s_branch .LBB0_1839
